# v22 variant: both halves of the next B(0,1) piece issued at the top of the heavy phase (light phase 4 loads, vmcnt(6))
# speedup vs baseline: 1.0131x; 1.0002x over previous
;     __device__ __forceinline__ unsigned a_off(const Unit& u, const Gemm& g) const { return (unsigned)u.pm * (unsigned)(BM * 2) * (unsigned)g.K; }
;     __device__ __forceinline__ unsigned b_off(const Unit& u, const Gemm& g) const { return (unsigned)u.pn * (unsigned)(BM * 2) * (unsigned)g.K; }
;     __device__ __forceinline__ bool next(int i, Unit& u) const { return so.next(i, u); }
;     __device__ __forceinline__ unsigned a_off(const Unit& u, const Gemm& g) const { return (unsigned)u.pm * (unsigned)(BM * 2) * (unsigned)g.K; }
; template <class Epi, class Sched, bool ALIGN_EPI = false, bool SP2 = false, bool FP8 = false>
; __device__ __forceinline__ void gemm_phase(LAS unsigned char* lds, const Gemm g, const Sched& S, const Epi& E, int wbase) {
;     ...
;         const bool has_next = S.next(ui + 1, nxt);
;         const unsigned nA = has_next ? S.a_off(nxt, g) : cA, nB = has_next ? S.b_off(nxt, g) : cB;
;         const rsrc_t rAn = (Sched::TWO && has_next) ? (nxt.part ? rA1 : rA0) : rAc, rBn = (Sched::TWO && has_next) ? (nxt.part ? rB1 : rB0) : rBc;
;         float pre_[8] = {0.f, 0.f, 0.f, 0.f, 0.f, 0.f, 0.f, 0.f};
;         if constexpr (Epi::HAS_PRE) E.pre_load(pre_, cur, wr);
;         for (int t = 0; t < nt; t += 2) {
;             const bool last = (t == nt - 2);
;             const unsigned a1 = cA + (unsigned)(t + 1) * kstep;
;             const unsigned a2 = last ? nA : cA + (unsigned)(t + 2) * kstep, b2 = last ? nB : cB + (unsigned)(t + 2) * kstep; const rsrc_t rA2 = (Sched::TWO && last) ? rAn : rAc, rB2 = (Sched::TWO && last) ? rBn : rBc;
;             const unsigned a3 = a2 + kstep, b3 = b2 + kstep;
;             if (last && has_next) S.a_ready(nxt);
;             if constexpr (SP2) {
;             PG8_LDB(B0, 0, 0); PG8_LDB(B1, 0, 1); PG8_SCHED; PG8_LDA(At, 0, 0); PG8_STAGE(PG8_SA(1, 1), rAc, a1 + hstep, voffA);
;             PG8_WAIT_V(8); PG8_WAIT_L(0); PG8_BAR; PG8_MMA(0, 0, At, B0); PG8_MMA(0, 1, At, B1); PG8_BAR; PG8_SCHED;
;             PG8_LDA(At, 0, 1); PG8_STAGE(PG8_SB(0, 0), rB2, b2, voffB); PG8_STAGE(PG8_SB(0, 1), rB2, b2 + hstep, voffB); PG8_STAGE(PG8_SA(0, 0), rA2, a2, voffA);
;             PG8_WAIT_V(8); PG8_WAIT_L(0); PG8_BAR; PG8_MMA(1, 0, At, B0); PG8_MMA(1, 1, At, B1); PG8_BAR; PG8_SCHED;
;             PG8_LDB(B0, 1, 0); PG8_LDB(B1, 1, 1); PG8_SCHED; PG8_LDA(At, 1, 0); PG8_STAGE(PG8_SA(0, 1), rA2, a2 + hstep, voffA);
.LBB0_256:
	s_lshl_b32 s82, s1, 18
	s_andn2_b64 vcc, exec, s[66:67]
	s_lshl_b32 s83, s21, 18
	s_cbranch_vccnz .LBB0_260
	s_and_b64 s[2:3], s[26:27], exec
	s_waitcnt vmcnt(37)
	s_waitcnt vmcnt(36)
	s_waitcnt vmcnt(35)
	s_waitcnt vmcnt(32)
	s_waitcnt vmcnt(31)
	s_waitcnt vmcnt(28)
	s_waitcnt vmcnt(27)
	s_waitcnt vmcnt(24)
	s_waitcnt vmcnt(23)
	s_waitcnt vmcnt(22)
	v_mov_b32_e32 v231, v164
	v_mov_b32_e32 v230, 0xff61b1e6
	v_mov_b32_e32 v175, v233
	s_cselect_b32 s2, s82, s29
	s_cselect_b32 s3, s83, s28
	s_add_i32 s16, s29, 0x80
	s_addk_i32 s28, 0x100
	s_mov_b32 s29, 0
	ds_read_b128 v[128:131], v252
	ds_read_b128 v[132:135], v252 offset:1024
	ds_read_b128 v[136:139], v252 offset:2048
	ds_read_b128 v[140:143], v252 offset:3072
	ds_read_b128 v[144:147], v225
	ds_read_b128 v[148:151], v225 offset:1024
	ds_read_b128 v[152:155], v225 offset:2048
	ds_read_b128 v[156:159], v225 offset:3072
	s_add_i32 s6, s16, 0x80
	s_cmp_eq_u32 s18, s29
	s_cselect_b32 s46, s2, s6
	s_cselect_b32 s31, s3, s28
	s_or_b32 s30, s46, 0x80
	s_add_i32 s6, s41, s16
	s_mov_b32 m0, s19
	ds_read_b128 v[176:179], v172
	ds_read_b128 v[180:183], v172 offset:1024
	ds_read_b128 v[184:187], v172 offset:2048
	ds_read_b128 v[188:191], v172 offset:3072
	ds_read_b128 v[194:197], v172 offset:4096
	ds_read_b128 v[198:201], v172 offset:5120
	ds_read_b128 v[202:205], v172 offset:6144
	ds_read_b128 v[206:209], v172 offset:7168
	buffer_load_dwordx4 v192, s[36:39], s6 offen lds
	s_mov_b32 m0, s20
	s_nop 0
	buffer_load_dwordx4 v223, s[36:39], s6 offen lds
	s_waitcnt vmcnt(8)
	s_waitcnt lgkmcnt(0)
	s_barrier
	s_setprio 1
	v_mfma_f32_16x16x128_f8f6f4 v[124:127], v[128:135], v[176:183], 0
	v_mfma_f32_16x16x128_f8f6f4 v[120:123], v[136:143], v[176:183], 0
	v_mfma_f32_16x16x128_f8f6f4 v[108:111], v[128:135], v[184:191], 0
	v_mfma_f32_16x16x128_f8f6f4 v[104:107], v[136:143], v[184:191], 0
	v_mfma_f32_16x16x128_f8f6f4 v[160:163], v[128:135], v[194:201], 0
	v_mfma_f32_16x16x128_f8f6f4 v[210:213], v[136:143], v[194:201], 0
	v_mfma_f32_16x16x128_f8f6f4 v[214:217], v[128:135], v[202:209], 0
	v_mfma_f32_16x16x128_f8f6f4 v[218:221], v[136:143], v[202:209], 0
	v_mfma_f32_16x16x128_f8f6f4 v[116:119], v[144:151], v[176:183], 0
	v_mfma_f32_16x16x128_f8f6f4 v[112:115], v[152:159], v[176:183], 0
	v_mfma_f32_16x16x128_f8f6f4 v[100:103], v[144:151], v[184:191], 0
	v_mfma_f32_16x16x128_f8f6f4 v[96:99], v[152:159], v[184:191], 0
	v_mfma_f32_16x16x128_f8f6f4 v[176:179], v[144:151], v[194:201], 0
	v_mfma_f32_16x16x128_f8f6f4 v[180:183], v[152:159], v[194:201], 0
	v_mfma_f32_16x16x128_f8f6f4 v[184:187], v[144:151], v[202:209], 0
	v_mfma_f32_16x16x128_f8f6f4 v[188:191], v[152:159], v[202:209], 0
	s_setprio 0
	s_barrier
	s_mov_b32 m0, s43
	s_mov_b32 s6, s38
	s_mov_b32 s7, s39
	s_nop 1
	buffer_load_dwordx4 v222, s[4:7], s31 offen lds
	s_mov_b32 m0, s44
	ds_read_b128 v[64:67], v172 offset:16384
	s_add_i32 s47, s31, s41
	buffer_load_dwordx4 v193, s[4:7], s31 offen lds
	s_mov_b32 m0, s42
	ds_read_b128 v[68:71], v172 offset:17408
	buffer_load_dwordx4 v192, s[36:39], s46 offen lds
	s_mov_b32 m0, s53
	ds_read_b128 v[72:75], v172 offset:18432
	buffer_load_dwordx4 v223, s[36:39], s46 offen lds
	ds_read_b128 v[76:79], v172 offset:19456
	ds_read_b128 v[80:83], v172 offset:20480
	ds_read_b128 v[84:87], v172 offset:21504
	ds_read_b128 v[88:91], v172 offset:22528
	ds_read_b128 v[92:95], v172 offset:23552
	s_waitcnt vmcnt(6)
	s_waitcnt lgkmcnt(0)
	s_barrier
	s_setprio 1
	v_mfma_f32_16x16x128_f8f6f4 v[60:63], v[128:135], v[64:71], 0
	v_mfma_f32_16x16x128_f8f6f4 v[56:59], v[136:143], v[64:71], 0
	v_mfma_f32_16x16x128_f8f6f4 v[194:197], v[128:135], v[72:79], 0
	v_mfma_f32_16x16x128_f8f6f4 v[198:201], v[136:143], v[72:79], 0
	v_mfma_f32_16x16x128_f8f6f4 v[202:205], v[128:135], v[80:87], 0
	v_mfma_f32_16x16x128_f8f6f4 v[206:209], v[136:143], v[80:87], 0
	v_mfma_f32_16x16x128_f8f6f4 v[236:239], v[128:135], v[88:95], 0
	v_mfma_f32_16x16x128_f8f6f4 v[240:243], v[136:143], v[88:95], 0
	v_mfma_f32_16x16x128_f8f6f4 v[52:55], v[144:151], v[64:71], 0
	v_mfma_f32_16x16x128_f8f6f4 v[48:51], v[152:159], v[64:71], 0
	v_mfma_f32_16x16x128_f8f6f4 v[244:247], v[144:151], v[72:79], 0
	v_mfma_f32_16x16x128_f8f6f4 v[248:251], v[152:159], v[72:79], 0
	v_mfma_f32_16x16x128_f8f6f4 v[226:229], v[144:151], v[80:87], 0
	v_mfma_f32_16x16x128_f8f6f4 v[232:235], v[152:159], v[80:87], 0
	v_mfma_f32_16x16x128_f8f6f4 v[164:167], v[144:151], v[88:95], 0
	v_mfma_f32_16x16x128_f8f6f4 v[168:171], v[152:159], v[88:95], 0
	s_setprio 0
	s_barrier
	s_mov_b32 m0, s45
	s_nop 0
	buffer_load_dwordx4 v222, s[4:7], s47 offen lds
	s_mov_b32 m0, s52
	s_nop 0
	buffer_load_dwordx4 v193, s[4:7], s47 offen lds
	s_nop 4
	ds_read_b128 v[0:3], v173
	ds_read_b128 v[4:7], v173 offset:1024
	ds_read_b128 v[16:19], v173 offset:2048
	ds_read_b128 v[20:23], v173 offset:3072
	ds_read_b128 v[128:131], v174
	ds_read_b128 v[132:135], v174 offset:1024
	ds_read_b128 v[136:139], v174 offset:2048
	ds_read_b128 v[140:143], v174 offset:3072
	s_add_i32 s46, s46, s41
	s_mov_b32 m0, s56
	ds_read_b128 v[8:11], v172 offset:32768
	ds_read_b128 v[12:15], v172 offset:33792
	ds_read_b128 v[24:27], v172 offset:34816
	ds_read_b128 v[28:31], v172 offset:35840
	ds_read_b128 v[32:35], v172 offset:36864
	ds_read_b128 v[36:39], v172 offset:37888
	ds_read_b128 v[40:43], v172 offset:38912
	ds_read_b128 v[44:47], v172 offset:39936
	buffer_load_dwordx4 v192, s[36:39], s46 offen lds
	s_mov_b32 m0, s57
	s_nop 0
	buffer_load_dwordx4 v223, s[36:39], s46 offen lds
	s_waitcnt vmcnt(8)
	s_waitcnt lgkmcnt(0)
	s_barrier
; #define PG8_STAGE(bufoff, rs_, soff_, voff) do { _Pragma("unroll") for (int _i = 0; _i < 2; ++_i) \
;         __builtin_amdgcn_raw_ptr_buffer_load_lds(rs_, (LAS void*)(lds + (bufoff) + ldsw + _i * 8192), 16, (int)(voff)[_i], (int)(soff_), 0, 0); } while (0)
; #define PG8_LDA(dst, b, h) do { _Pragma("unroll") for (int m = 0; m < 4; ++m) dst[m] = PG8_LD2(lds + PG8_SA(b, h) + aoff + m * 2048); } while (0)
; #define PG8_LDB(dst, b, h) do { _Pragma("unroll") for (int n = 0; n < 2; ++n) dst[n] = PG8_LD2(lds + PG8_SB(b, h) + boff + n * 2048); } while (0)
; #define PG8_WAIT_V(n) asm volatile("s_waitcnt vmcnt(" #n ")" ::: "memory")
; #define PG8_WAIT_L(n) asm volatile("s_waitcnt lgkmcnt(" #n ")" ::: "memory")
; #define PG8_BAR __builtin_amdgcn_s_barrier()
; #define PG8_SCHED __builtin_amdgcn_sched_barrier(0)
; template <class Epi, class Sched, bool ALIGN_EPI = false, bool SP2 = false, bool FP8 = false>
; __device__ __forceinline__ void gemm_phase(LAS unsigned char* lds, const Gemm g, const Sched& S, const Epi& E, int wbase) {
;     ...
;             PG8_LDB(B0, 0, 0); PG8_LDB(B1, 0, 1); PG8_SCHED; PG8_LDA(At, 0, 0); PG8_STAGE(PG8_SA(1, 1), rAc, a1 + hstep, voffA);
;             PG8_WAIT_V(8); PG8_WAIT_L(0); PG8_BAR; PG8_MMA(0, 0, At, B0); PG8_MMA(0, 1, At, B1); PG8_BAR; PG8_SCHED;
;             PG8_LDA(At, 0, 1); PG8_STAGE(PG8_SB(0, 0), rB2, b2, voffB); PG8_STAGE(PG8_SB(0, 1), rB2, b2 + hstep, voffB); PG8_STAGE(PG8_SA(0, 0), rA2, a2, voffA);
;             PG8_WAIT_V(8); PG8_WAIT_L(0); PG8_BAR; PG8_MMA(1, 0, At, B0); PG8_MMA(1, 1, At, B1); PG8_BAR; PG8_SCHED;
;             PG8_LDB(B0, 1, 0); PG8_LDB(B1, 1, 1); PG8_SCHED; PG8_LDA(At, 1, 0); PG8_STAGE(PG8_SA(0, 1), rA2, a2 + hstep, voffA);
;             PG8_WAIT_V(8); PG8_WAIT_L(0); PG8_BAR; PG8_MMA(0, 0, At, B0); PG8_MMA(0, 1, At, B1); PG8_BAR; PG8_SCHED;
;             PG8_LDA(At, 1, 1); PG8_STAGE(PG8_SB(1, 0), rB2, b3, voffB); PG8_STAGE(PG8_SB(1, 1), rB2, b3 + hstep, voffB); PG8_STAGE(PG8_SA(1, 0), rA2, a3, voffA);
;             PG8_WAIT_V(8); PG8_WAIT_L(0); PG8_BAR; PG8_MMA(1, 0, At, B0); PG8_MMA(1, 1, At, B1); PG8_BAR; PG8_SCHED;
	s_setprio 1
	v_mfma_f32_16x16x128_f8f6f4 v[124:127], v[0:7], v[8:15], v[124:127]
	v_mfma_f32_16x16x128_f8f6f4 v[120:123], v[16:23], v[8:15], v[120:123]
	v_mfma_f32_16x16x128_f8f6f4 v[108:111], v[0:7], v[24:31], v[108:111]
	v_mfma_f32_16x16x128_f8f6f4 v[104:107], v[16:23], v[24:31], v[104:107]
	v_mfma_f32_16x16x128_f8f6f4 v[92:95], v[0:7], v[32:39], v[160:163]
	v_mfma_f32_16x16x128_f8f6f4 v[88:91], v[16:23], v[32:39], v[210:213]
	v_mfma_f32_16x16x128_f8f6f4 v[76:79], v[0:7], v[40:47], v[214:217]
	v_mfma_f32_16x16x128_f8f6f4 v[72:75], v[16:23], v[40:47], v[218:221]
	v_mfma_f32_16x16x128_f8f6f4 v[116:119], v[128:135], v[8:15], v[116:119]
	v_mfma_f32_16x16x128_f8f6f4 v[112:115], v[136:143], v[8:15], v[112:115]
	v_mfma_f32_16x16x128_f8f6f4 v[100:103], v[128:135], v[24:31], v[100:103]
	v_mfma_f32_16x16x128_f8f6f4 v[96:99], v[136:143], v[24:31], v[96:99]
	v_mfma_f32_16x16x128_f8f6f4 v[84:87], v[128:135], v[32:39], v[176:179]
	v_mfma_f32_16x16x128_f8f6f4 v[80:83], v[136:143], v[32:39], v[180:183]
	v_mfma_f32_16x16x128_f8f6f4 v[68:71], v[128:135], v[40:47], v[184:187]
	v_mfma_f32_16x16x128_f8f6f4 v[64:67], v[136:143], v[40:47], v[188:191]
	s_setprio 0
	s_barrier
	s_mov_b32 m0, s58
	s_bitset1_b32 s31, 7
	buffer_load_dwordx4 v222, s[4:7], s31 offen lds
	s_mov_b32 m0, s59
	ds_read_b128 v[32:35], v172 offset:49152
	buffer_load_dwordx4 v193, s[4:7], s31 offen lds
	s_add_i32 s31, s31, s41
	s_mov_b32 m0, s65
	ds_read_b128 v[36:39], v172 offset:50176
	buffer_load_dwordx4 v222, s[4:7], s31 offen lds
	s_mov_b32 m0, s33
	ds_read_b128 v[144:147], v172 offset:51200
	buffer_load_dwordx4 v193, s[4:7], s31 offen lds
	s_mov_b32 m0, s12
	ds_read_b128 v[148:151], v172 offset:52224
	buffer_load_dwordx4 v192, s[36:39], s30 offen lds
	s_mov_b32 m0, s13
	ds_read_b128 v[152:155], v172 offset:53248
	buffer_load_dwordx4 v223, s[36:39], s30 offen lds
	ds_read_b128 v[156:159], v172 offset:54272
	ds_read_b128 v[176:179], v172 offset:55296
	ds_read_b128 v[180:183], v172 offset:56320
	s_waitcnt vmcnt(8)
	s_waitcnt lgkmcnt(0)
	s_barrier
	s_setprio 1
	v_mfma_f32_16x16x128_f8f6f4 v[60:63], v[0:7], v[32:39], v[60:63]
	v_mfma_f32_16x16x128_f8f6f4 v[56:59], v[16:23], v[32:39], v[56:59]
	v_mfma_f32_16x16x128_f8f6f4 v[44:47], v[0:7], v[144:151], v[194:197]
	v_mfma_f32_16x16x128_f8f6f4 v[40:43], v[16:23], v[144:151], v[198:201]
	v_mfma_f32_16x16x128_f8f6f4 v[28:31], v[0:7], v[152:159], v[202:205]
	v_mfma_f32_16x16x128_f8f6f4 v[24:27], v[16:23], v[152:159], v[206:209]
	v_mfma_f32_16x16x128_f8f6f4 v[12:15], v[0:7], v[176:183], v[236:239]
	v_mfma_f32_16x16x128_f8f6f4 v[8:11], v[16:23], v[176:183], v[240:243]
	v_mfma_f32_16x16x128_f8f6f4 v[52:55], v[128:135], v[32:39], v[52:55]
	v_mfma_f32_16x16x128_f8f6f4 v[48:51], v[136:143], v[32:39], v[48:51]
	v_mfma_f32_16x16x128_f8f6f4 v[36:39], v[128:135], v[144:151], v[244:247]
	v_mfma_f32_16x16x128_f8f6f4 v[32:35], v[136:143], v[144:151], v[248:251]
	v_mfma_f32_16x16x128_f8f6f4 v[20:23], v[128:135], v[152:159], v[226:229]
	v_mfma_f32_16x16x128_f8f6f4 v[16:19], v[136:143], v[152:159], v[232:235]
	v_mfma_f32_16x16x128_f8f6f4 v[4:7], v[128:135], v[176:183], v[164:167]
	v_mfma_f32_16x16x128_f8f6f4 v[0:3], v[136:143], v[176:183], v[168:171]
	s_setprio 0
	s_barrier
	s_add_i32 s29, s29, 2
	s_addk_i32 s16, 0x100
	s_addk_i32 s28, 0x100
	s_cmp_ge_i32 s29, s77
	s_cbranch_scc0 .LBB0_258
	s_branch .Lzp_after_258
.LBB0_258:
	ds_read_b128 v[128:131], v252
	ds_read_b128 v[132:135], v252 offset:1024
	ds_read_b128 v[136:139], v252 offset:2048
	ds_read_b128 v[140:143], v252 offset:3072
	ds_read_b128 v[144:147], v225
	ds_read_b128 v[148:151], v225 offset:1024
	ds_read_b128 v[152:155], v225 offset:2048
	ds_read_b128 v[156:159], v225 offset:3072
	s_add_i32 s6, s16, 0x80
	s_cmp_eq_u32 s18, s29
	s_cselect_b32 s46, s2, s6
	s_cselect_b32 s31, s3, s28
	s_or_b32 s30, s46, 0x80
	s_add_i32 s6, s41, s16
	s_mov_b32 m0, s19
	ds_read_b128 v[176:179], v172
	ds_read_b128 v[180:183], v172 offset:1024
	ds_read_b128 v[184:187], v172 offset:2048
	ds_read_b128 v[188:191], v172 offset:3072
	ds_read_b128 v[194:197], v172 offset:4096
	ds_read_b128 v[198:201], v172 offset:5120
	ds_read_b128 v[202:205], v172 offset:6144
	ds_read_b128 v[206:209], v172 offset:7168
	buffer_load_dwordx4 v192, s[36:39], s6 offen lds
	s_mov_b32 m0, s20
	s_nop 0
	buffer_load_dwordx4 v223, s[36:39], s6 offen lds
	s_waitcnt vmcnt(8)
	s_waitcnt lgkmcnt(0)
	s_barrier
	s_setprio 1
	v_mfma_f32_16x16x128_f8f6f4 v[124:127], v[128:135], v[176:183], v[124:127]
	v_mfma_f32_16x16x128_f8f6f4 v[120:123], v[136:143], v[176:183], v[120:123]
	v_mfma_f32_16x16x128_f8f6f4 v[108:111], v[128:135], v[184:191], v[108:111]
	v_mfma_f32_16x16x128_f8f6f4 v[104:107], v[136:143], v[184:191], v[104:107]
	v_mfma_f32_16x16x128_f8f6f4 v[160:163], v[128:135], v[194:201], v[92:95]
	v_mfma_f32_16x16x128_f8f6f4 v[210:213], v[136:143], v[194:201], v[88:91]
	v_mfma_f32_16x16x128_f8f6f4 v[214:217], v[128:135], v[202:209], v[76:79]
	v_mfma_f32_16x16x128_f8f6f4 v[218:221], v[136:143], v[202:209], v[72:75]
	v_mfma_f32_16x16x128_f8f6f4 v[116:119], v[144:151], v[176:183], v[116:119]
	v_mfma_f32_16x16x128_f8f6f4 v[112:115], v[152:159], v[176:183], v[112:115]
	v_mfma_f32_16x16x128_f8f6f4 v[100:103], v[144:151], v[184:191], v[100:103]
	v_mfma_f32_16x16x128_f8f6f4 v[96:99], v[152:159], v[184:191], v[96:99]
	v_mfma_f32_16x16x128_f8f6f4 v[176:179], v[144:151], v[194:201], v[84:87]
	v_mfma_f32_16x16x128_f8f6f4 v[180:183], v[152:159], v[194:201], v[80:83]
	v_mfma_f32_16x16x128_f8f6f4 v[184:187], v[144:151], v[202:209], v[68:71]
	v_mfma_f32_16x16x128_f8f6f4 v[188:191], v[152:159], v[202:209], v[64:67]
	s_setprio 0
	s_barrier
; #define PG8_STAGE(bufoff, rs_, soff_, voff) do { _Pragma("unroll") for (int _i = 0; _i < 2; ++_i) \
;         __builtin_amdgcn_raw_ptr_buffer_load_lds(rs_, (LAS void*)(lds + (bufoff) + ldsw + _i * 8192), 16, (int)(voff)[_i], (int)(soff_), 0, 0); } while (0)
; #define PG8_LDA(dst, b, h) do { _Pragma("unroll") for (int m = 0; m < 4; ++m) dst[m] = PG8_LD2(lds + PG8_SA(b, h) + aoff + m * 2048); } while (0)
; #define PG8_LDB(dst, b, h) do { _Pragma("unroll") for (int n = 0; n < 2; ++n) dst[n] = PG8_LD2(lds + PG8_SB(b, h) + boff + n * 2048); } while (0)
; #define PG8_WAIT_V(n) asm volatile("s_waitcnt vmcnt(" #n ")" ::: "memory")
; #define PG8_WAIT_L(n) asm volatile("s_waitcnt lgkmcnt(" #n ")" ::: "memory")
; #define PG8_BAR __builtin_amdgcn_s_barrier()
; #define PG8_SCHED __builtin_amdgcn_sched_barrier(0)
; template <class Epi, class Sched, bool ALIGN_EPI = false, bool SP2 = false, bool FP8 = false>
; __device__ __forceinline__ void gemm_phase(LAS unsigned char* lds, const Gemm g, const Sched& S, const Epi& E, int wbase) {
;     ...
;             PG8_LDA(At, 0, 1); PG8_STAGE(PG8_SB(0, 0), rB2, b2, voffB); PG8_STAGE(PG8_SB(0, 1), rB2, b2 + hstep, voffB); PG8_STAGE(PG8_SA(0, 0), rA2, a2, voffA);
;             PG8_WAIT_V(8); PG8_WAIT_L(0); PG8_BAR; PG8_MMA(1, 0, At, B0); PG8_MMA(1, 1, At, B1); PG8_BAR; PG8_SCHED;
;             PG8_LDB(B0, 1, 0); PG8_LDB(B1, 1, 1); PG8_SCHED; PG8_LDA(At, 1, 0); PG8_STAGE(PG8_SA(0, 1), rA2, a2 + hstep, voffA);
;             PG8_WAIT_V(8); PG8_WAIT_L(0); PG8_BAR; PG8_MMA(0, 0, At, B0); PG8_MMA(0, 1, At, B1); PG8_BAR; PG8_SCHED;
;             PG8_LDA(At, 1, 1); PG8_STAGE(PG8_SB(1, 0), rB2, b3, voffB); PG8_STAGE(PG8_SB(1, 1), rB2, b3 + hstep, voffB); PG8_STAGE(PG8_SA(1, 0), rA2, a3, voffA);
;             PG8_WAIT_V(8); PG8_WAIT_L(0); PG8_BAR; PG8_MMA(1, 0, At, B0); PG8_MMA(1, 1, At, B1); PG8_BAR; PG8_SCHED;
	s_mov_b32 m0, s43
	s_mov_b32 s6, s38
	s_mov_b32 s7, s39
	s_nop 1
	buffer_load_dwordx4 v222, s[4:7], s31 offen lds
	s_mov_b32 m0, s44
	ds_read_b128 v[64:67], v172 offset:16384
	s_add_i32 s47, s31, s41
	buffer_load_dwordx4 v193, s[4:7], s31 offen lds
	s_mov_b32 m0, s42
	ds_read_b128 v[68:71], v172 offset:17408
	buffer_load_dwordx4 v192, s[36:39], s46 offen lds
	s_mov_b32 m0, s53
	ds_read_b128 v[72:75], v172 offset:18432
	buffer_load_dwordx4 v223, s[36:39], s46 offen lds
	ds_read_b128 v[76:79], v172 offset:19456
	ds_read_b128 v[80:83], v172 offset:20480
	ds_read_b128 v[84:87], v172 offset:21504
	ds_read_b128 v[88:91], v172 offset:22528
	ds_read_b128 v[92:95], v172 offset:23552
	s_waitcnt vmcnt(6)
	s_waitcnt lgkmcnt(0)
	s_barrier
	s_setprio 1
	v_mfma_f32_16x16x128_f8f6f4 v[60:63], v[128:135], v[64:71], v[60:63]
	v_mfma_f32_16x16x128_f8f6f4 v[56:59], v[136:143], v[64:71], v[56:59]
	v_mfma_f32_16x16x128_f8f6f4 v[194:197], v[128:135], v[72:79], v[44:47]
	v_mfma_f32_16x16x128_f8f6f4 v[198:201], v[136:143], v[72:79], v[40:43]
	v_mfma_f32_16x16x128_f8f6f4 v[202:205], v[128:135], v[80:87], v[28:31]
	v_mfma_f32_16x16x128_f8f6f4 v[206:209], v[136:143], v[80:87], v[24:27]
	v_mfma_f32_16x16x128_f8f6f4 v[236:239], v[128:135], v[88:95], v[12:15]
	v_mfma_f32_16x16x128_f8f6f4 v[240:243], v[136:143], v[88:95], v[8:11]
	v_mfma_f32_16x16x128_f8f6f4 v[52:55], v[144:151], v[64:71], v[52:55]
	v_mfma_f32_16x16x128_f8f6f4 v[48:51], v[152:159], v[64:71], v[48:51]
	v_mfma_f32_16x16x128_f8f6f4 v[244:247], v[144:151], v[72:79], v[36:39]
	v_mfma_f32_16x16x128_f8f6f4 v[248:251], v[152:159], v[72:79], v[32:35]
	v_mfma_f32_16x16x128_f8f6f4 v[226:229], v[144:151], v[80:87], v[20:23]
	v_mfma_f32_16x16x128_f8f6f4 v[232:235], v[152:159], v[80:87], v[16:19]
	v_mfma_f32_16x16x128_f8f6f4 v[164:167], v[144:151], v[88:95], v[4:7]
	v_mfma_f32_16x16x128_f8f6f4 v[168:171], v[152:159], v[88:95], v[0:3]
	s_setprio 0
	s_barrier
	s_mov_b32 m0, s45
	s_nop 0
	buffer_load_dwordx4 v222, s[4:7], s47 offen lds
	s_mov_b32 m0, s52
	s_nop 0
	buffer_load_dwordx4 v193, s[4:7], s47 offen lds
	s_nop 4
	ds_read_b128 v[0:3], v173
	ds_read_b128 v[4:7], v173 offset:1024
	ds_read_b128 v[16:19], v173 offset:2048
	ds_read_b128 v[20:23], v173 offset:3072
	ds_read_b128 v[128:131], v174
	ds_read_b128 v[132:135], v174 offset:1024
	ds_read_b128 v[136:139], v174 offset:2048
	ds_read_b128 v[140:143], v174 offset:3072
	s_add_i32 s46, s46, s41
	s_mov_b32 m0, s56
	ds_read_b128 v[8:11], v172 offset:32768
	ds_read_b128 v[12:15], v172 offset:33792
	ds_read_b128 v[24:27], v172 offset:34816
	ds_read_b128 v[28:31], v172 offset:35840
	ds_read_b128 v[32:35], v172 offset:36864
	ds_read_b128 v[36:39], v172 offset:37888
	ds_read_b128 v[40:43], v172 offset:38912
	ds_read_b128 v[44:47], v172 offset:39936
	buffer_load_dwordx4 v192, s[36:39], s46 offen lds
	s_mov_b32 m0, s57
	s_nop 0
	buffer_load_dwordx4 v223, s[36:39], s46 offen lds
	s_waitcnt vmcnt(8)
	s_waitcnt lgkmcnt(0)
	s_barrier
	s_setprio 1
	v_mfma_f32_16x16x128_f8f6f4 v[124:127], v[0:7], v[8:15], v[124:127]
	v_mfma_f32_16x16x128_f8f6f4 v[120:123], v[16:23], v[8:15], v[120:123]
	v_mfma_f32_16x16x128_f8f6f4 v[108:111], v[0:7], v[24:31], v[108:111]
	v_mfma_f32_16x16x128_f8f6f4 v[104:107], v[16:23], v[24:31], v[104:107]
	v_mfma_f32_16x16x128_f8f6f4 v[92:95], v[0:7], v[32:39], v[160:163]
	v_mfma_f32_16x16x128_f8f6f4 v[88:91], v[16:23], v[32:39], v[210:213]
	v_mfma_f32_16x16x128_f8f6f4 v[76:79], v[0:7], v[40:47], v[214:217]
	v_mfma_f32_16x16x128_f8f6f4 v[72:75], v[16:23], v[40:47], v[218:221]
	v_mfma_f32_16x16x128_f8f6f4 v[116:119], v[128:135], v[8:15], v[116:119]
	v_mfma_f32_16x16x128_f8f6f4 v[112:115], v[136:143], v[8:15], v[112:115]
	v_mfma_f32_16x16x128_f8f6f4 v[100:103], v[128:135], v[24:31], v[100:103]
	v_mfma_f32_16x16x128_f8f6f4 v[96:99], v[136:143], v[24:31], v[96:99]
	v_mfma_f32_16x16x128_f8f6f4 v[84:87], v[128:135], v[32:39], v[176:179]
	v_mfma_f32_16x16x128_f8f6f4 v[80:83], v[136:143], v[32:39], v[180:183]
	v_mfma_f32_16x16x128_f8f6f4 v[68:71], v[128:135], v[40:47], v[184:187]
	v_mfma_f32_16x16x128_f8f6f4 v[64:67], v[136:143], v[40:47], v[188:191]
	s_setprio 0
	s_barrier
	s_mov_b32 m0, s58
	s_bitset1_b32 s31, 7
	buffer_load_dwordx4 v222, s[4:7], s31 offen lds
	s_mov_b32 m0, s59
	ds_read_b128 v[32:35], v172 offset:49152
	buffer_load_dwordx4 v193, s[4:7], s31 offen lds
	s_add_i32 s31, s31, s41
	s_mov_b32 m0, s65
	ds_read_b128 v[36:39], v172 offset:50176
	buffer_load_dwordx4 v222, s[4:7], s31 offen lds
	s_mov_b32 m0, s33
	ds_read_b128 v[144:147], v172 offset:51200
	buffer_load_dwordx4 v193, s[4:7], s31 offen lds
	s_mov_b32 m0, s12
	ds_read_b128 v[148:151], v172 offset:52224
	buffer_load_dwordx4 v192, s[36:39], s30 offen lds
	s_mov_b32 m0, s13
	ds_read_b128 v[152:155], v172 offset:53248
	buffer_load_dwordx4 v223, s[36:39], s30 offen lds
	ds_read_b128 v[156:159], v172 offset:54272
	ds_read_b128 v[176:179], v172 offset:55296
	ds_read_b128 v[180:183], v172 offset:56320
	s_waitcnt vmcnt(8)
	s_waitcnt lgkmcnt(0)
	s_barrier
	s_setprio 1
	v_mfma_f32_16x16x128_f8f6f4 v[60:63], v[0:7], v[32:39], v[60:63]
	v_mfma_f32_16x16x128_f8f6f4 v[56:59], v[16:23], v[32:39], v[56:59]
	v_mfma_f32_16x16x128_f8f6f4 v[44:47], v[0:7], v[144:151], v[194:197]
	v_mfma_f32_16x16x128_f8f6f4 v[40:43], v[16:23], v[144:151], v[198:201]
	v_mfma_f32_16x16x128_f8f6f4 v[28:31], v[0:7], v[152:159], v[202:205]
	v_mfma_f32_16x16x128_f8f6f4 v[24:27], v[16:23], v[152:159], v[206:209]
	v_mfma_f32_16x16x128_f8f6f4 v[12:15], v[0:7], v[176:183], v[236:239]
	v_mfma_f32_16x16x128_f8f6f4 v[8:11], v[16:23], v[176:183], v[240:243]
	v_mfma_f32_16x16x128_f8f6f4 v[52:55], v[128:135], v[32:39], v[52:55]
	v_mfma_f32_16x16x128_f8f6f4 v[48:51], v[136:143], v[32:39], v[48:51]
	v_mfma_f32_16x16x128_f8f6f4 v[36:39], v[128:135], v[144:151], v[244:247]
	v_mfma_f32_16x16x128_f8f6f4 v[32:35], v[136:143], v[144:151], v[248:251]
	v_mfma_f32_16x16x128_f8f6f4 v[20:23], v[128:135], v[152:159], v[226:229]
	v_mfma_f32_16x16x128_f8f6f4 v[16:19], v[136:143], v[152:159], v[232:235]
	v_mfma_f32_16x16x128_f8f6f4 v[4:7], v[128:135], v[176:183], v[164:167]
	v_mfma_f32_16x16x128_f8f6f4 v[0:3], v[136:143], v[176:183], v[168:171]
	s_setprio 0
	s_barrier
	s_add_i32 s29, s29, 2
	s_addk_i32 s16, 0x100
	s_addk_i32 s28, 0x100
	s_cmp_ge_i32 s29, s77
	s_cbranch_scc0 .LBB0_258

;     __device__ __forceinline__ unsigned a_off(const Unit& u, const Gemm& g) const { return (unsigned)u.pm * (unsigned)(BM * 2) * (unsigned)g.K; }
; template <class Epi, class Sched, bool ALIGN_EPI = false, bool SP2 = false, bool FP8 = false>
; __device__ __forceinline__ void gemm_phase(LAS unsigned char* lds, const Gemm g, const Sched& S, const Epi& E, int wbase) {
;     ...
;         const bool has_next = S.next(ui + 1, nxt);
;         const unsigned nA = has_next ? S.a_off(nxt, g) : cA, nB = has_next ? S.b_off(nxt, g) : cB;
;         const rsrc_t rAn = (Sched::TWO && has_next) ? (nxt.part ? rA1 : rA0) : rAc, rBn = (Sched::TWO && has_next) ? (nxt.part ? rB1 : rB0) : rBc;
;         float pre_[8] = {0.f, 0.f, 0.f, 0.f, 0.f, 0.f, 0.f, 0.f};
;         if constexpr (Epi::HAS_PRE) E.pre_load(pre_, cur, wr);
;         for (int t = 0; t < nt; t += 2) {
;             const bool last = (t == nt - 2);
;             const unsigned a1 = cA + (unsigned)(t + 1) * kstep;
;             const unsigned a2 = last ? nA : cA + (unsigned)(t + 2) * kstep, b2 = last ? nB : cB + (unsigned)(t + 2) * kstep; const rsrc_t rA2 = (Sched::TWO && last) ? rAn : rAc, rB2 = (Sched::TWO && last) ? rBn : rBc;
;             const unsigned a3 = a2 + kstep, b3 = b2 + kstep;
;             if (last && has_next) S.a_ready(nxt);
;             if constexpr (SP2) {
;             PG8_LDB(B0, 0, 0); PG8_LDB(B1, 0, 1); PG8_SCHED; PG8_LDA(At, 0, 0); PG8_STAGE(PG8_SA(1, 1), rAc, a1 + hstep, voffA);
;             PG8_WAIT_V(8); PG8_WAIT_L(0); PG8_BAR; PG8_MMA(0, 0, At, B0); PG8_MMA(0, 1, At, B1); PG8_BAR; PG8_SCHED;
;             PG8_LDA(At, 0, 1); PG8_STAGE(PG8_SB(0, 0), rB2, b2, voffB); PG8_STAGE(PG8_SB(0, 1), rB2, b2 + hstep, voffB); PG8_STAGE(PG8_SA(0, 0), rA2, a2, voffA);
;             PG8_WAIT_V(8); PG8_WAIT_L(0); PG8_BAR; PG8_MMA(1, 0, At, B0); PG8_MMA(1, 1, At, B1); PG8_BAR; PG8_SCHED;
;             PG8_LDB(B0, 1, 0); PG8_LDB(B1, 1, 1); PG8_SCHED; PG8_LDA(At, 1, 0); PG8_STAGE(PG8_SA(0, 1), rA2, a2 + hstep, voffA);
;             PG8_WAIT_V(8); PG8_WAIT_L(0); PG8_BAR; PG8_MMA(0, 0, At, B0); PG8_MMA(0, 1, At, B1); PG8_BAR; PG8_SCHED;
;             PG8_LDA(At, 1, 1); PG8_STAGE(PG8_SB(1, 0), rB2, b3, voffB); PG8_STAGE(PG8_SB(1, 1), rB2, b3 + hstep, voffB); PG8_STAGE(PG8_SA(1, 0), rA2, a3, voffA);
;             PG8_WAIT_V(8); PG8_WAIT_L(0); PG8_BAR; PG8_MMA(1, 0, At, B0); PG8_MMA(1, 1, At, B1); PG8_BAR; PG8_SCHED;
.LBB0_350:
	s_lshl_b32 s20, s19, 19
	s_andn2_b64 vcc, exec, s[66:67]
	s_lshl_b32 s21, s18, 19
	s_cbranch_vccnz .LBB0_430
	s_and_b64 s[2:3], s[26:27], exec
	s_waitcnt vmcnt(37)
	s_waitcnt vmcnt(36)
	s_waitcnt vmcnt(35)
	s_waitcnt vmcnt(32)
	s_waitcnt vmcnt(31)
	s_waitcnt vmcnt(28)
	s_waitcnt vmcnt(27)
	s_waitcnt vmcnt(24)
	s_waitcnt vmcnt(23)
	s_waitcnt vmcnt(22)
	s_cselect_b32 s2, s20, s29
	s_cselect_b32 s3, s21, s28
	s_add_i32 s16, s29, 0x80
	s_addk_i32 s28, 0x100
	s_mov_b32 s29, 0
	v_add_u32_e32 v140, 0x10000, v170
	v_add_u32_e32 v156, 0x14000, v170
	ds_read_b128 v[128:131], v140
	ds_read_b128 v[132:135], v140 offset:1024
	ds_read_b128 v[136:139], v140 offset:2048
	ds_read_b128 v[140:143], v140 offset:3072
	ds_read_b128 v[144:147], v156
	ds_read_b128 v[148:151], v156 offset:1024
	ds_read_b128 v[152:155], v156 offset:2048
	ds_read_b128 v[156:159], v156 offset:3072
	s_add_i32 s6, s16, 0x80
	s_cmp_eq_u32 s12, s29
	s_cselect_b32 s46, s2, s6
	s_cselect_b32 s31, s3, s28
	s_or_b32 s30, s46, 0x80
	s_add_i32 s6, s33, s16
	s_mov_b32 m0, s13
	ds_read_b128 v[160:163], v171
	ds_read_b128 v[172:175], v171 offset:1024
	ds_read_b128 v[176:179], v171 offset:2048
	ds_read_b128 v[180:183], v171 offset:3072
	ds_read_b128 v[184:187], v171 offset:4096
	ds_read_b128 v[188:191], v171 offset:5120
	ds_read_b128 v[194:197], v171 offset:6144
	ds_read_b128 v[198:201], v171 offset:7168
	buffer_load_dwordx4 v164, s[36:39], s6 offen lds
	s_mov_b32 m0, s83
	s_nop 0
	buffer_load_dwordx4 v166, s[36:39], s6 offen lds
	s_waitcnt vmcnt(8)
	s_waitcnt lgkmcnt(0)
	s_barrier
	s_setprio 1
	v_mfma_f32_16x16x32_bf16 v[124:127], v[128:131], v[160:163], 0
	v_mfma_f32_16x16x32_bf16 v[120:123], v[136:139], v[160:163], 0
	v_mfma_f32_16x16x32_bf16 v[108:111], v[128:131], v[176:179], 0
	v_mfma_f32_16x16x32_bf16 v[104:107], v[136:139], v[176:179], 0
	v_mfma_f32_16x16x32_bf16 v[92:95], v[128:131], v[184:187], 0
	v_mfma_f32_16x16x32_bf16 v[88:91], v[136:139], v[184:187], 0
	v_mfma_f32_16x16x32_bf16 v[76:79], v[128:131], v[194:197], 0
	v_mfma_f32_16x16x32_bf16 v[72:75], v[136:139], v[194:197], 0
	v_mfma_f32_16x16x32_bf16 v[124:127], v[132:135], v[172:175], v[124:127]
	v_mfma_f32_16x16x32_bf16 v[120:123], v[140:143], v[172:175], v[120:123]
	v_mfma_f32_16x16x32_bf16 v[108:111], v[132:135], v[180:183], v[108:111]
	v_mfma_f32_16x16x32_bf16 v[104:107], v[140:143], v[180:183], v[104:107]
	v_mfma_f32_16x16x32_bf16 v[92:95], v[132:135], v[188:191], v[92:95]
	v_mfma_f32_16x16x32_bf16 v[88:91], v[140:143], v[188:191], v[88:91]
	v_mfma_f32_16x16x32_bf16 v[76:79], v[132:135], v[198:201], v[76:79]
	v_mfma_f32_16x16x32_bf16 v[72:75], v[140:143], v[198:201], v[72:75]
	v_mfma_f32_16x16x32_bf16 v[116:119], v[144:147], v[160:163], 0
	v_mfma_f32_16x16x32_bf16 v[112:115], v[152:155], v[160:163], 0
	v_mfma_f32_16x16x32_bf16 v[100:103], v[144:147], v[176:179], 0
	v_mfma_f32_16x16x32_bf16 v[96:99], v[152:155], v[176:179], 0
	v_mfma_f32_16x16x32_bf16 v[84:87], v[144:147], v[184:187], 0
	v_mfma_f32_16x16x32_bf16 v[80:83], v[152:155], v[184:187], 0
	v_mfma_f32_16x16x32_bf16 v[68:71], v[144:147], v[194:197], 0
	v_mfma_f32_16x16x32_bf16 v[64:67], v[152:155], v[194:197], 0
	v_mfma_f32_16x16x32_bf16 v[116:119], v[148:151], v[172:175], v[116:119]
	v_mfma_f32_16x16x32_bf16 v[112:115], v[156:159], v[172:175], v[112:115]
	v_mfma_f32_16x16x32_bf16 v[100:103], v[148:151], v[180:183], v[100:103]
	v_mfma_f32_16x16x32_bf16 v[96:99], v[156:159], v[180:183], v[96:99]
	v_mfma_f32_16x16x32_bf16 v[84:87], v[148:151], v[188:191], v[84:87]
	v_mfma_f32_16x16x32_bf16 v[80:83], v[156:159], v[188:191], v[80:83]
	v_mfma_f32_16x16x32_bf16 v[68:71], v[148:151], v[198:201], v[68:71]
	v_mfma_f32_16x16x32_bf16 v[64:67], v[156:159], v[198:201], v[64:67]
	s_setprio 0
	s_barrier
	s_mov_b32 m0, s42
	s_mov_b32 s6, s38
	s_mov_b32 s7, s39
	buffer_load_dwordx4 v165, s[4:7], s31 offen lds
	s_mov_b32 m0, s43
	ds_read_b128 v[160:163], v171 offset:16384
	s_add_i32 s47, s31, s33
	buffer_load_dwordx4 v167, s[4:7], s31 offen lds
	s_mov_b32 m0, s41
	ds_read_b128 v[172:175], v171 offset:17408
	buffer_load_dwordx4 v164, s[36:39], s46 offen lds
	s_mov_b32 m0, s52
	ds_read_b128 v[176:179], v171 offset:18432
	buffer_load_dwordx4 v166, s[36:39], s46 offen lds
	ds_read_b128 v[180:183], v171 offset:19456
	ds_read_b128 v[184:187], v171 offset:20480
	ds_read_b128 v[188:191], v171 offset:21504
	ds_read_b128 v[194:197], v171 offset:22528
	ds_read_b128 v[198:201], v171 offset:23552
	s_waitcnt vmcnt(6)
	s_waitcnt lgkmcnt(0)
	s_barrier
	s_setprio 1
	v_mfma_f32_16x16x32_bf16 v[60:63], v[128:131], v[160:163], 0
	v_mfma_f32_16x16x32_bf16 v[56:59], v[136:139], v[160:163], 0
	v_mfma_f32_16x16x32_bf16 v[44:47], v[128:131], v[176:179], 0
	v_mfma_f32_16x16x32_bf16 v[40:43], v[136:139], v[176:179], 0
	v_mfma_f32_16x16x32_bf16 v[28:31], v[128:131], v[184:187], 0
	v_mfma_f32_16x16x32_bf16 v[24:27], v[136:139], v[184:187], 0
	v_mfma_f32_16x16x32_bf16 v[12:15], v[128:131], v[194:197], 0
	v_mfma_f32_16x16x32_bf16 v[8:11], v[136:139], v[194:197], 0
	v_mfma_f32_16x16x32_bf16 v[60:63], v[132:135], v[172:175], v[60:63]
	v_mfma_f32_16x16x32_bf16 v[56:59], v[140:143], v[172:175], v[56:59]
	v_mfma_f32_16x16x32_bf16 v[44:47], v[132:135], v[180:183], v[44:47]
	v_mfma_f32_16x16x32_bf16 v[40:43], v[140:143], v[180:183], v[40:43]
	v_mfma_f32_16x16x32_bf16 v[28:31], v[132:135], v[188:191], v[28:31]
	v_mfma_f32_16x16x32_bf16 v[24:27], v[140:143], v[188:191], v[24:27]
	v_mfma_f32_16x16x32_bf16 v[12:15], v[132:135], v[198:201], v[12:15]
	v_mfma_f32_16x16x32_bf16 v[8:11], v[140:143], v[198:201], v[8:11]
	v_mfma_f32_16x16x32_bf16 v[52:55], v[144:147], v[160:163], 0
	v_mfma_f32_16x16x32_bf16 v[48:51], v[152:155], v[160:163], 0
	v_mfma_f32_16x16x32_bf16 v[36:39], v[144:147], v[176:179], 0
	v_mfma_f32_16x16x32_bf16 v[32:35], v[152:155], v[176:179], 0
	v_mfma_f32_16x16x32_bf16 v[20:23], v[144:147], v[184:187], 0
	v_mfma_f32_16x16x32_bf16 v[16:19], v[152:155], v[184:187], 0
	v_mfma_f32_16x16x32_bf16 v[4:7], v[144:147], v[194:197], 0
	v_mfma_f32_16x16x32_bf16 v[0:3], v[152:155], v[194:197], 0
	v_mfma_f32_16x16x32_bf16 v[52:55], v[148:151], v[172:175], v[52:55]
	v_mfma_f32_16x16x32_bf16 v[48:51], v[156:159], v[172:175], v[48:51]
	v_mfma_f32_16x16x32_bf16 v[36:39], v[148:151], v[180:183], v[36:39]
	v_mfma_f32_16x16x32_bf16 v[32:35], v[156:159], v[180:183], v[32:35]
	v_mfma_f32_16x16x32_bf16 v[20:23], v[148:151], v[188:191], v[20:23]
	v_mfma_f32_16x16x32_bf16 v[16:19], v[156:159], v[188:191], v[16:19]
	v_mfma_f32_16x16x32_bf16 v[4:7], v[148:151], v[198:201], v[4:7]
	v_mfma_f32_16x16x32_bf16 v[0:3], v[156:159], v[198:201], v[0:3]
	s_setprio 0
	s_barrier
; #define PG8_STAGE(bufoff, rs_, soff_, voff) do { _Pragma("unroll") for (int _i = 0; _i < 2; ++_i) \
;         __builtin_amdgcn_raw_ptr_buffer_load_lds(rs_, (LAS void*)(lds + (bufoff) + ldsw + _i * 8192), 16, (int)(voff)[_i], (int)(soff_), 0, 0); } while (0)
; #define PG8_LDA(dst, b, h) do { _Pragma("unroll") for (int m = 0; m < 4; ++m) dst[m] = PG8_LD2(lds + PG8_SA(b, h) + aoff + m * 2048); } while (0)
; #define PG8_LDB(dst, b, h) do { _Pragma("unroll") for (int n = 0; n < 2; ++n) dst[n] = PG8_LD2(lds + PG8_SB(b, h) + boff + n * 2048); } while (0)
; #define PG8_WAIT_V(n) asm volatile("s_waitcnt vmcnt(" #n ")" ::: "memory")
; #define PG8_WAIT_L(n) asm volatile("s_waitcnt lgkmcnt(" #n ")" ::: "memory")
; #define PG8_BAR __builtin_amdgcn_s_barrier()
; #define PG8_SCHED __builtin_amdgcn_sched_barrier(0)
; template <class Epi, class Sched, bool ALIGN_EPI = false, bool SP2 = false, bool FP8 = false>
; __device__ __forceinline__ void gemm_phase(LAS unsigned char* lds, const Gemm g, const Sched& S, const Epi& E, int wbase) {
;     ...
;             PG8_LDB(B0, 0, 0); PG8_LDB(B1, 0, 1); PG8_SCHED; PG8_LDA(At, 0, 0); PG8_STAGE(PG8_SA(1, 1), rAc, a1 + hstep, voffA);
;             PG8_WAIT_V(8); PG8_WAIT_L(0); PG8_BAR; PG8_MMA(0, 0, At, B0); PG8_MMA(0, 1, At, B1); PG8_BAR; PG8_SCHED;
;             PG8_LDA(At, 0, 1); PG8_STAGE(PG8_SB(0, 0), rB2, b2, voffB); PG8_STAGE(PG8_SB(0, 1), rB2, b2 + hstep, voffB); PG8_STAGE(PG8_SA(0, 0), rA2, a2, voffA);
;             PG8_WAIT_V(8); PG8_WAIT_L(0); PG8_BAR; PG8_MMA(1, 0, At, B0); PG8_MMA(1, 1, At, B1); PG8_BAR; PG8_SCHED;
;             PG8_LDB(B0, 1, 0); PG8_LDB(B1, 1, 1); PG8_SCHED; PG8_LDA(At, 1, 0); PG8_STAGE(PG8_SA(0, 1), rA2, a2 + hstep, voffA);
;             PG8_WAIT_V(8); PG8_WAIT_L(0); PG8_BAR; PG8_MMA(0, 0, At, B0); PG8_MMA(0, 1, At, B1); PG8_BAR; PG8_SCHED;
;             PG8_LDA(At, 1, 1); PG8_STAGE(PG8_SB(1, 0), rB2, b3, voffB); PG8_STAGE(PG8_SB(1, 1), rB2, b3 + hstep, voffB); PG8_STAGE(PG8_SA(1, 0), rA2, a3, voffA);
;             PG8_WAIT_V(8); PG8_WAIT_L(0); PG8_BAR; PG8_MMA(1, 0, At, B0); PG8_MMA(1, 1, At, B1); PG8_BAR; PG8_SCHED;
	s_mov_b32 m0, s44
	s_nop 0
	buffer_load_dwordx4 v165, s[4:7], s47 offen lds
	s_mov_b32 m0, s45
	s_nop 0
	buffer_load_dwordx4 v167, s[4:7], s47 offen lds
	v_add_u32_e32 v140, 0x18000, v170
	v_add_u32_e32 v156, 0x1c000, v170
	ds_read_b128 v[128:131], v140
	ds_read_b128 v[132:135], v140 offset:1024
	ds_read_b128 v[136:139], v140 offset:2048
	ds_read_b128 v[140:143], v140 offset:3072
	ds_read_b128 v[144:147], v156
	ds_read_b128 v[148:151], v156 offset:1024
	ds_read_b128 v[152:155], v156 offset:2048
	ds_read_b128 v[156:159], v156 offset:3072
	s_add_i32 s46, s46, s33
	s_mov_b32 m0, s53
	ds_read_b128 v[160:163], v171 offset:32768
	ds_read_b128 v[172:175], v171 offset:33792
	ds_read_b128 v[176:179], v171 offset:34816
	ds_read_b128 v[180:183], v171 offset:35840
	ds_read_b128 v[184:187], v171 offset:36864
	ds_read_b128 v[188:191], v171 offset:37888
	ds_read_b128 v[194:197], v171 offset:38912
	ds_read_b128 v[198:201], v171 offset:39936
	buffer_load_dwordx4 v164, s[36:39], s46 offen lds
	s_mov_b32 m0, s1
	s_nop 0
	buffer_load_dwordx4 v166, s[36:39], s46 offen lds
	s_waitcnt vmcnt(8)
	s_waitcnt lgkmcnt(0)
	s_barrier
	s_setprio 1
	v_mfma_f32_16x16x32_bf16 v[124:127], v[128:131], v[160:163], v[124:127]
	v_mfma_f32_16x16x32_bf16 v[120:123], v[136:139], v[160:163], v[120:123]
	v_mfma_f32_16x16x32_bf16 v[108:111], v[128:131], v[176:179], v[108:111]
	v_mfma_f32_16x16x32_bf16 v[104:107], v[136:139], v[176:179], v[104:107]
	v_mfma_f32_16x16x32_bf16 v[92:95], v[128:131], v[184:187], v[92:95]
	v_mfma_f32_16x16x32_bf16 v[88:91], v[136:139], v[184:187], v[88:91]
	v_mfma_f32_16x16x32_bf16 v[76:79], v[128:131], v[194:197], v[76:79]
	v_mfma_f32_16x16x32_bf16 v[72:75], v[136:139], v[194:197], v[72:75]
	v_mfma_f32_16x16x32_bf16 v[124:127], v[132:135], v[172:175], v[124:127]
	v_mfma_f32_16x16x32_bf16 v[120:123], v[140:143], v[172:175], v[120:123]
	v_mfma_f32_16x16x32_bf16 v[108:111], v[132:135], v[180:183], v[108:111]
	v_mfma_f32_16x16x32_bf16 v[104:107], v[140:143], v[180:183], v[104:107]
	v_mfma_f32_16x16x32_bf16 v[92:95], v[132:135], v[188:191], v[92:95]
	v_mfma_f32_16x16x32_bf16 v[88:91], v[140:143], v[188:191], v[88:91]
	v_mfma_f32_16x16x32_bf16 v[76:79], v[132:135], v[198:201], v[76:79]
	v_mfma_f32_16x16x32_bf16 v[72:75], v[140:143], v[198:201], v[72:75]
	v_mfma_f32_16x16x32_bf16 v[116:119], v[144:147], v[160:163], v[116:119]
	v_mfma_f32_16x16x32_bf16 v[112:115], v[152:155], v[160:163], v[112:115]
	v_mfma_f32_16x16x32_bf16 v[100:103], v[144:147], v[176:179], v[100:103]
	v_mfma_f32_16x16x32_bf16 v[96:99], v[152:155], v[176:179], v[96:99]
	v_mfma_f32_16x16x32_bf16 v[84:87], v[144:147], v[184:187], v[84:87]
	v_mfma_f32_16x16x32_bf16 v[80:83], v[152:155], v[184:187], v[80:83]
	v_mfma_f32_16x16x32_bf16 v[68:71], v[144:147], v[194:197], v[68:71]
	v_mfma_f32_16x16x32_bf16 v[64:67], v[152:155], v[194:197], v[64:67]
	v_mfma_f32_16x16x32_bf16 v[116:119], v[148:151], v[172:175], v[116:119]
	v_mfma_f32_16x16x32_bf16 v[112:115], v[156:159], v[172:175], v[112:115]
	v_mfma_f32_16x16x32_bf16 v[100:103], v[148:151], v[180:183], v[100:103]
	v_mfma_f32_16x16x32_bf16 v[96:99], v[156:159], v[180:183], v[96:99]
	v_mfma_f32_16x16x32_bf16 v[84:87], v[148:151], v[188:191], v[84:87]
	v_mfma_f32_16x16x32_bf16 v[80:83], v[156:159], v[188:191], v[80:83]
	v_mfma_f32_16x16x32_bf16 v[68:71], v[148:151], v[198:201], v[68:71]
	v_mfma_f32_16x16x32_bf16 v[64:67], v[156:159], v[198:201], v[64:67]
	s_setprio 0
	s_barrier
	s_mov_b32 m0, s56
	s_bitset1_b32 s31, 7
	buffer_load_dwordx4 v165, s[4:7], s31 offen lds
	s_mov_b32 m0, s57
	ds_read_b128 v[160:163], v171 offset:49152
	buffer_load_dwordx4 v167, s[4:7], s31 offen lds
	s_add_i32 s31, s31, s33
	s_mov_b32 m0, s65
	ds_read_b128 v[172:175], v171 offset:50176
	buffer_load_dwordx4 v165, s[4:7], s31 offen lds
	s_mov_b32 m0, s76
	ds_read_b128 v[176:179], v171 offset:51200
	buffer_load_dwordx4 v167, s[4:7], s31 offen lds
	s_mov_b32 m0, s58
	ds_read_b128 v[180:183], v171 offset:52224
	buffer_load_dwordx4 v164, s[36:39], s30 offen lds
	s_mov_b32 m0, s59
	ds_read_b128 v[184:187], v171 offset:53248
	buffer_load_dwordx4 v166, s[36:39], s30 offen lds
	ds_read_b128 v[188:191], v171 offset:54272
	ds_read_b128 v[194:197], v171 offset:55296
	ds_read_b128 v[198:201], v171 offset:56320
	s_waitcnt vmcnt(8)
	s_waitcnt lgkmcnt(0)
	s_barrier
	s_setprio 1
	v_mfma_f32_16x16x32_bf16 v[60:63], v[128:131], v[160:163], v[60:63]
	v_mfma_f32_16x16x32_bf16 v[56:59], v[136:139], v[160:163], v[56:59]
	v_mfma_f32_16x16x32_bf16 v[44:47], v[128:131], v[176:179], v[44:47]
	v_mfma_f32_16x16x32_bf16 v[40:43], v[136:139], v[176:179], v[40:43]
	v_mfma_f32_16x16x32_bf16 v[28:31], v[128:131], v[184:187], v[28:31]
	v_mfma_f32_16x16x32_bf16 v[24:27], v[136:139], v[184:187], v[24:27]
	v_mfma_f32_16x16x32_bf16 v[12:15], v[128:131], v[194:197], v[12:15]
	v_mfma_f32_16x16x32_bf16 v[8:11], v[136:139], v[194:197], v[8:11]
	v_mfma_f32_16x16x32_bf16 v[60:63], v[132:135], v[172:175], v[60:63]
	v_mfma_f32_16x16x32_bf16 v[56:59], v[140:143], v[172:175], v[56:59]
	v_mfma_f32_16x16x32_bf16 v[44:47], v[132:135], v[180:183], v[44:47]
	v_mfma_f32_16x16x32_bf16 v[40:43], v[140:143], v[180:183], v[40:43]
	v_mfma_f32_16x16x32_bf16 v[28:31], v[132:135], v[188:191], v[28:31]
	v_mfma_f32_16x16x32_bf16 v[24:27], v[140:143], v[188:191], v[24:27]
	v_mfma_f32_16x16x32_bf16 v[12:15], v[132:135], v[198:201], v[12:15]
	v_mfma_f32_16x16x32_bf16 v[8:11], v[140:143], v[198:201], v[8:11]
	v_mfma_f32_16x16x32_bf16 v[52:55], v[144:147], v[160:163], v[52:55]
	v_mfma_f32_16x16x32_bf16 v[48:51], v[152:155], v[160:163], v[48:51]
	v_mfma_f32_16x16x32_bf16 v[36:39], v[144:147], v[176:179], v[36:39]
	v_mfma_f32_16x16x32_bf16 v[32:35], v[152:155], v[176:179], v[32:35]
	v_mfma_f32_16x16x32_bf16 v[20:23], v[144:147], v[184:187], v[20:23]
	v_mfma_f32_16x16x32_bf16 v[16:19], v[152:155], v[184:187], v[16:19]
	v_mfma_f32_16x16x32_bf16 v[4:7], v[144:147], v[194:197], v[4:7]
	v_mfma_f32_16x16x32_bf16 v[0:3], v[152:155], v[194:197], v[0:3]
	v_mfma_f32_16x16x32_bf16 v[52:55], v[148:151], v[172:175], v[52:55]
	v_mfma_f32_16x16x32_bf16 v[48:51], v[156:159], v[172:175], v[48:51]
	v_mfma_f32_16x16x32_bf16 v[36:39], v[148:151], v[180:183], v[36:39]
	v_mfma_f32_16x16x32_bf16 v[32:35], v[156:159], v[180:183], v[32:35]
	v_mfma_f32_16x16x32_bf16 v[20:23], v[148:151], v[188:191], v[20:23]
	v_mfma_f32_16x16x32_bf16 v[16:19], v[156:159], v[188:191], v[16:19]
	v_mfma_f32_16x16x32_bf16 v[4:7], v[148:151], v[198:201], v[4:7]
	v_mfma_f32_16x16x32_bf16 v[0:3], v[156:159], v[198:201], v[0:3]
	s_setprio 0
	s_barrier
	s_add_i32 s29, s29, 2
	s_addk_i32 s16, 0x100
	s_addk_i32 s28, 0x100
	s_cmp_ge_i32 s29, s82
	s_cbranch_scc0 .LBB0_352
	s_branch .Lzp_after_352
; #define PG8_STAGE(bufoff, rs_, soff_, voff) do { _Pragma("unroll") for (int _i = 0; _i < 2; ++_i) \
;         __builtin_amdgcn_raw_ptr_buffer_load_lds(rs_, (LAS void*)(lds + (bufoff) + ldsw + _i * 8192), 16, (int)(voff)[_i], (int)(soff_), 0, 0); } while (0)
; #define PG8_LDA(dst, b, h) do { _Pragma("unroll") for (int m = 0; m < 4; ++m) dst[m] = PG8_LD2(lds + PG8_SA(b, h) + aoff + m * 2048); } while (0)
; #define PG8_LDB(dst, b, h) do { _Pragma("unroll") for (int n = 0; n < 2; ++n) dst[n] = PG8_LD2(lds + PG8_SB(b, h) + boff + n * 2048); } while (0)
; template <class Epi, class Sched, bool ALIGN_EPI = false, bool SP2 = false, bool FP8 = false>
; __device__ __forceinline__ void gemm_phase(LAS unsigned char* lds, const Gemm g, const Sched& S, const Epi& E, int wbase) {
;     ...
;         for (int t = 0; t < nt; t += 2) {
;             const bool last = (t == nt - 2);
;             const unsigned a1 = cA + (unsigned)(t + 1) * kstep;
;             const unsigned a2 = last ? nA : cA + (unsigned)(t + 2) * kstep, b2 = last ? nB : cB + (unsigned)(t + 2) * kstep; const rsrc_t rA2 = (Sched::TWO && last) ? rAn : rAc, rB2 = (Sched::TWO && last) ? rBn : rBc;
;             const unsigned a3 = a2 + kstep, b3 = b2 + kstep;
;             if (last && has_next) S.a_ready(nxt);
;             if constexpr (SP2) {
;             PG8_LDB(B0, 0, 0); PG8_LDB(B1, 0, 1); PG8_SCHED; PG8_LDA(At, 0, 0); PG8_STAGE(PG8_SA(1, 1), rAc, a1 + hstep, voffA);
;             PG8_WAIT_V(8); PG8_WAIT_L(0); PG8_BAR; PG8_MMA(0, 0, At, B0); PG8_MMA(0, 1, At, B1); PG8_BAR; PG8_SCHED;
;             PG8_LDA(At, 0, 1); PG8_STAGE(PG8_SB(0, 0), rB2, b2, voffB); PG8_STAGE(PG8_SB(0, 1), rB2, b2 + hstep, voffB); PG8_STAGE(PG8_SA(0, 0), rA2, a2, voffA);
;             PG8_WAIT_V(8); PG8_WAIT_L(0); PG8_BAR; PG8_MMA(1, 0, At, B0); PG8_MMA(1, 1, At, B1); PG8_BAR; PG8_SCHED;
;             PG8_LDB(B0, 1, 0); PG8_LDB(B1, 1, 1); PG8_SCHED; PG8_LDA(At, 1, 0); PG8_STAGE(PG8_SA(0, 1), rA2, a2 + hstep, voffA);
;             PG8_WAIT_V(8); PG8_WAIT_L(0); PG8_BAR; PG8_MMA(0, 0, At, B0); PG8_MMA(0, 1, At, B1); PG8_BAR; PG8_SCHED;
;             PG8_LDA(At, 1, 1); PG8_STAGE(PG8_SB(1, 0), rB2, b3, voffB); PG8_STAGE(PG8_SB(1, 1), rB2, b3 + hstep, voffB); PG8_STAGE(PG8_SA(1, 0), rA2, a3, voffA);
;             PG8_WAIT_V(8); PG8_WAIT_L(0); PG8_BAR; PG8_MMA(1, 0, At, B0); PG8_MMA(1, 1, At, B1); PG8_BAR; PG8_SCHED;
.LBB0_352:
	v_add_u32_e32 v140, 0x10000, v170
	v_add_u32_e32 v156, 0x14000, v170
	ds_read_b128 v[128:131], v140
	ds_read_b128 v[132:135], v140 offset:1024
	ds_read_b128 v[136:139], v140 offset:2048
	ds_read_b128 v[140:143], v140 offset:3072
	ds_read_b128 v[144:147], v156
	ds_read_b128 v[148:151], v156 offset:1024
	ds_read_b128 v[152:155], v156 offset:2048
	ds_read_b128 v[156:159], v156 offset:3072
	s_add_i32 s6, s16, 0x80
	s_cmp_eq_u32 s12, s29
	s_cselect_b32 s46, s2, s6
	s_cselect_b32 s31, s3, s28
	s_or_b32 s30, s46, 0x80
	s_add_i32 s6, s33, s16
	s_mov_b32 m0, s13
	ds_read_b128 v[160:163], v171
	ds_read_b128 v[172:175], v171 offset:1024
	ds_read_b128 v[176:179], v171 offset:2048
	ds_read_b128 v[180:183], v171 offset:3072
	ds_read_b128 v[184:187], v171 offset:4096
	ds_read_b128 v[188:191], v171 offset:5120
	ds_read_b128 v[194:197], v171 offset:6144
	ds_read_b128 v[198:201], v171 offset:7168
	buffer_load_dwordx4 v164, s[36:39], s6 offen lds
	s_mov_b32 m0, s83
	s_nop 0
	buffer_load_dwordx4 v166, s[36:39], s6 offen lds
	s_waitcnt vmcnt(8)
	s_waitcnt lgkmcnt(0)
	s_barrier
	s_setprio 1
	v_mfma_f32_16x16x32_bf16 v[124:127], v[128:131], v[160:163], v[124:127]
	v_mfma_f32_16x16x32_bf16 v[120:123], v[136:139], v[160:163], v[120:123]
	v_mfma_f32_16x16x32_bf16 v[108:111], v[128:131], v[176:179], v[108:111]
	v_mfma_f32_16x16x32_bf16 v[104:107], v[136:139], v[176:179], v[104:107]
	v_mfma_f32_16x16x32_bf16 v[92:95], v[128:131], v[184:187], v[92:95]
	v_mfma_f32_16x16x32_bf16 v[88:91], v[136:139], v[184:187], v[88:91]
	v_mfma_f32_16x16x32_bf16 v[76:79], v[128:131], v[194:197], v[76:79]
	v_mfma_f32_16x16x32_bf16 v[72:75], v[136:139], v[194:197], v[72:75]
	v_mfma_f32_16x16x32_bf16 v[124:127], v[132:135], v[172:175], v[124:127]
	v_mfma_f32_16x16x32_bf16 v[120:123], v[140:143], v[172:175], v[120:123]
	v_mfma_f32_16x16x32_bf16 v[108:111], v[132:135], v[180:183], v[108:111]
	v_mfma_f32_16x16x32_bf16 v[104:107], v[140:143], v[180:183], v[104:107]
	v_mfma_f32_16x16x32_bf16 v[92:95], v[132:135], v[188:191], v[92:95]
	v_mfma_f32_16x16x32_bf16 v[88:91], v[140:143], v[188:191], v[88:91]
	v_mfma_f32_16x16x32_bf16 v[76:79], v[132:135], v[198:201], v[76:79]
	v_mfma_f32_16x16x32_bf16 v[72:75], v[140:143], v[198:201], v[72:75]
	v_mfma_f32_16x16x32_bf16 v[116:119], v[144:147], v[160:163], v[116:119]
	v_mfma_f32_16x16x32_bf16 v[112:115], v[152:155], v[160:163], v[112:115]
	v_mfma_f32_16x16x32_bf16 v[100:103], v[144:147], v[176:179], v[100:103]
	v_mfma_f32_16x16x32_bf16 v[96:99], v[152:155], v[176:179], v[96:99]
	v_mfma_f32_16x16x32_bf16 v[84:87], v[144:147], v[184:187], v[84:87]
	v_mfma_f32_16x16x32_bf16 v[80:83], v[152:155], v[184:187], v[80:83]
	v_mfma_f32_16x16x32_bf16 v[68:71], v[144:147], v[194:197], v[68:71]
	v_mfma_f32_16x16x32_bf16 v[64:67], v[152:155], v[194:197], v[64:67]
	v_mfma_f32_16x16x32_bf16 v[116:119], v[148:151], v[172:175], v[116:119]
	v_mfma_f32_16x16x32_bf16 v[112:115], v[156:159], v[172:175], v[112:115]
	v_mfma_f32_16x16x32_bf16 v[100:103], v[148:151], v[180:183], v[100:103]
	v_mfma_f32_16x16x32_bf16 v[96:99], v[156:159], v[180:183], v[96:99]
	v_mfma_f32_16x16x32_bf16 v[84:87], v[148:151], v[188:191], v[84:87]
	v_mfma_f32_16x16x32_bf16 v[80:83], v[156:159], v[188:191], v[80:83]
	v_mfma_f32_16x16x32_bf16 v[68:71], v[148:151], v[198:201], v[68:71]
	v_mfma_f32_16x16x32_bf16 v[64:67], v[156:159], v[198:201], v[64:67]
	s_setprio 0
	s_barrier
	s_mov_b32 m0, s42
	s_mov_b32 s6, s38
	s_mov_b32 s7, s39
	buffer_load_dwordx4 v165, s[4:7], s31 offen lds
	s_mov_b32 m0, s43
	ds_read_b128 v[160:163], v171 offset:16384
	s_add_i32 s47, s31, s33
	buffer_load_dwordx4 v167, s[4:7], s31 offen lds
	s_mov_b32 m0, s41
	ds_read_b128 v[172:175], v171 offset:17408
	buffer_load_dwordx4 v164, s[36:39], s46 offen lds
	s_mov_b32 m0, s52
	ds_read_b128 v[176:179], v171 offset:18432
	buffer_load_dwordx4 v166, s[36:39], s46 offen lds
	ds_read_b128 v[180:183], v171 offset:19456
	ds_read_b128 v[184:187], v171 offset:20480
	ds_read_b128 v[188:191], v171 offset:21504
	ds_read_b128 v[194:197], v171 offset:22528
	ds_read_b128 v[198:201], v171 offset:23552
	s_waitcnt vmcnt(6)
	s_waitcnt lgkmcnt(0)
	s_barrier
	s_setprio 1
	v_mfma_f32_16x16x32_bf16 v[60:63], v[128:131], v[160:163], v[60:63]
	v_mfma_f32_16x16x32_bf16 v[56:59], v[136:139], v[160:163], v[56:59]
	v_mfma_f32_16x16x32_bf16 v[44:47], v[128:131], v[176:179], v[44:47]
	v_mfma_f32_16x16x32_bf16 v[40:43], v[136:139], v[176:179], v[40:43]
	v_mfma_f32_16x16x32_bf16 v[28:31], v[128:131], v[184:187], v[28:31]
	v_mfma_f32_16x16x32_bf16 v[24:27], v[136:139], v[184:187], v[24:27]
	v_mfma_f32_16x16x32_bf16 v[12:15], v[128:131], v[194:197], v[12:15]
	v_mfma_f32_16x16x32_bf16 v[8:11], v[136:139], v[194:197], v[8:11]
	v_mfma_f32_16x16x32_bf16 v[60:63], v[132:135], v[172:175], v[60:63]
	v_mfma_f32_16x16x32_bf16 v[56:59], v[140:143], v[172:175], v[56:59]
	v_mfma_f32_16x16x32_bf16 v[44:47], v[132:135], v[180:183], v[44:47]
	v_mfma_f32_16x16x32_bf16 v[40:43], v[140:143], v[180:183], v[40:43]
	v_mfma_f32_16x16x32_bf16 v[28:31], v[132:135], v[188:191], v[28:31]
	v_mfma_f32_16x16x32_bf16 v[24:27], v[140:143], v[188:191], v[24:27]
	v_mfma_f32_16x16x32_bf16 v[12:15], v[132:135], v[198:201], v[12:15]
	v_mfma_f32_16x16x32_bf16 v[8:11], v[140:143], v[198:201], v[8:11]
	v_mfma_f32_16x16x32_bf16 v[52:55], v[144:147], v[160:163], v[52:55]
	v_mfma_f32_16x16x32_bf16 v[48:51], v[152:155], v[160:163], v[48:51]
	v_mfma_f32_16x16x32_bf16 v[36:39], v[144:147], v[176:179], v[36:39]
	v_mfma_f32_16x16x32_bf16 v[32:35], v[152:155], v[176:179], v[32:35]
	v_mfma_f32_16x16x32_bf16 v[20:23], v[144:147], v[184:187], v[20:23]
	v_mfma_f32_16x16x32_bf16 v[16:19], v[152:155], v[184:187], v[16:19]
	v_mfma_f32_16x16x32_bf16 v[4:7], v[144:147], v[194:197], v[4:7]
	v_mfma_f32_16x16x32_bf16 v[0:3], v[152:155], v[194:197], v[0:3]
	v_mfma_f32_16x16x32_bf16 v[52:55], v[148:151], v[172:175], v[52:55]
	v_mfma_f32_16x16x32_bf16 v[48:51], v[156:159], v[172:175], v[48:51]
	v_mfma_f32_16x16x32_bf16 v[36:39], v[148:151], v[180:183], v[36:39]
	v_mfma_f32_16x16x32_bf16 v[32:35], v[156:159], v[180:183], v[32:35]
	v_mfma_f32_16x16x32_bf16 v[20:23], v[148:151], v[188:191], v[20:23]
	v_mfma_f32_16x16x32_bf16 v[16:19], v[156:159], v[188:191], v[16:19]
	v_mfma_f32_16x16x32_bf16 v[4:7], v[148:151], v[198:201], v[4:7]
	v_mfma_f32_16x16x32_bf16 v[0:3], v[156:159], v[198:201], v[0:3]
	s_setprio 0
	s_barrier
; #define PG8_STAGE(bufoff, rs_, soff_, voff) do { _Pragma("unroll") for (int _i = 0; _i < 2; ++_i) \
;         __builtin_amdgcn_raw_ptr_buffer_load_lds(rs_, (LAS void*)(lds + (bufoff) + ldsw + _i * 8192), 16, (int)(voff)[_i], (int)(soff_), 0, 0); } while (0)
; #define PG8_LDA(dst, b, h) do { _Pragma("unroll") for (int m = 0; m < 4; ++m) dst[m] = PG8_LD2(lds + PG8_SA(b, h) + aoff + m * 2048); } while (0)
; #define PG8_LDB(dst, b, h) do { _Pragma("unroll") for (int n = 0; n < 2; ++n) dst[n] = PG8_LD2(lds + PG8_SB(b, h) + boff + n * 2048); } while (0)
; #define PG8_WAIT_V(n) asm volatile("s_waitcnt vmcnt(" #n ")" ::: "memory")
; #define PG8_WAIT_L(n) asm volatile("s_waitcnt lgkmcnt(" #n ")" ::: "memory")
; #define PG8_BAR __builtin_amdgcn_s_barrier()
; #define PG8_SCHED __builtin_amdgcn_sched_barrier(0)
; template <class Epi, class Sched, bool ALIGN_EPI = false, bool SP2 = false, bool FP8 = false>
; __device__ __forceinline__ void gemm_phase(LAS unsigned char* lds, const Gemm g, const Sched& S, const Epi& E, int wbase) {
;     ...
;             PG8_LDB(B0, 0, 0); PG8_LDB(B1, 0, 1); PG8_SCHED; PG8_LDA(At, 0, 0); PG8_STAGE(PG8_SA(1, 1), rAc, a1 + hstep, voffA);
;             PG8_WAIT_V(8); PG8_WAIT_L(0); PG8_BAR; PG8_MMA(0, 0, At, B0); PG8_MMA(0, 1, At, B1); PG8_BAR; PG8_SCHED;
;             PG8_LDA(At, 0, 1); PG8_STAGE(PG8_SB(0, 0), rB2, b2, voffB); PG8_STAGE(PG8_SB(0, 1), rB2, b2 + hstep, voffB); PG8_STAGE(PG8_SA(0, 0), rA2, a2, voffA);
;             PG8_WAIT_V(8); PG8_WAIT_L(0); PG8_BAR; PG8_MMA(1, 0, At, B0); PG8_MMA(1, 1, At, B1); PG8_BAR; PG8_SCHED;
;             PG8_LDB(B0, 1, 0); PG8_LDB(B1, 1, 1); PG8_SCHED; PG8_LDA(At, 1, 0); PG8_STAGE(PG8_SA(0, 1), rA2, a2 + hstep, voffA);
;             PG8_WAIT_V(8); PG8_WAIT_L(0); PG8_BAR; PG8_MMA(0, 0, At, B0); PG8_MMA(0, 1, At, B1); PG8_BAR; PG8_SCHED;
;             PG8_LDA(At, 1, 1); PG8_STAGE(PG8_SB(1, 0), rB2, b3, voffB); PG8_STAGE(PG8_SB(1, 1), rB2, b3 + hstep, voffB); PG8_STAGE(PG8_SA(1, 0), rA2, a3, voffA);
;             PG8_WAIT_V(8); PG8_WAIT_L(0); PG8_BAR; PG8_MMA(1, 0, At, B0); PG8_MMA(1, 1, At, B1); PG8_BAR; PG8_SCHED;
	s_mov_b32 m0, s44
	s_nop 0
	buffer_load_dwordx4 v165, s[4:7], s47 offen lds
	s_mov_b32 m0, s45
	s_nop 0
	buffer_load_dwordx4 v167, s[4:7], s47 offen lds
	v_add_u32_e32 v140, 0x18000, v170
	v_add_u32_e32 v156, 0x1c000, v170
	ds_read_b128 v[128:131], v140
	ds_read_b128 v[132:135], v140 offset:1024
	ds_read_b128 v[136:139], v140 offset:2048
	ds_read_b128 v[140:143], v140 offset:3072
	ds_read_b128 v[144:147], v156
	ds_read_b128 v[148:151], v156 offset:1024
	ds_read_b128 v[152:155], v156 offset:2048
	ds_read_b128 v[156:159], v156 offset:3072
	s_add_i32 s46, s46, s33
	s_mov_b32 m0, s53
	ds_read_b128 v[160:163], v171 offset:32768
	ds_read_b128 v[172:175], v171 offset:33792
	ds_read_b128 v[176:179], v171 offset:34816
	ds_read_b128 v[180:183], v171 offset:35840
	ds_read_b128 v[184:187], v171 offset:36864
	ds_read_b128 v[188:191], v171 offset:37888
	ds_read_b128 v[194:197], v171 offset:38912
	ds_read_b128 v[198:201], v171 offset:39936
	buffer_load_dwordx4 v164, s[36:39], s46 offen lds
	s_mov_b32 m0, s1
	s_nop 0
	buffer_load_dwordx4 v166, s[36:39], s46 offen lds
	s_waitcnt vmcnt(8)
	s_waitcnt lgkmcnt(0)
	s_barrier
	s_setprio 1
	v_mfma_f32_16x16x32_bf16 v[124:127], v[128:131], v[160:163], v[124:127]
	v_mfma_f32_16x16x32_bf16 v[120:123], v[136:139], v[160:163], v[120:123]
	v_mfma_f32_16x16x32_bf16 v[108:111], v[128:131], v[176:179], v[108:111]
	v_mfma_f32_16x16x32_bf16 v[104:107], v[136:139], v[176:179], v[104:107]
	v_mfma_f32_16x16x32_bf16 v[92:95], v[128:131], v[184:187], v[92:95]
	v_mfma_f32_16x16x32_bf16 v[88:91], v[136:139], v[184:187], v[88:91]
	v_mfma_f32_16x16x32_bf16 v[76:79], v[128:131], v[194:197], v[76:79]
	v_mfma_f32_16x16x32_bf16 v[72:75], v[136:139], v[194:197], v[72:75]
	v_mfma_f32_16x16x32_bf16 v[124:127], v[132:135], v[172:175], v[124:127]
	v_mfma_f32_16x16x32_bf16 v[120:123], v[140:143], v[172:175], v[120:123]
	v_mfma_f32_16x16x32_bf16 v[108:111], v[132:135], v[180:183], v[108:111]
	v_mfma_f32_16x16x32_bf16 v[104:107], v[140:143], v[180:183], v[104:107]
	v_mfma_f32_16x16x32_bf16 v[92:95], v[132:135], v[188:191], v[92:95]
	v_mfma_f32_16x16x32_bf16 v[88:91], v[140:143], v[188:191], v[88:91]
	v_mfma_f32_16x16x32_bf16 v[76:79], v[132:135], v[198:201], v[76:79]
	v_mfma_f32_16x16x32_bf16 v[72:75], v[140:143], v[198:201], v[72:75]
	v_mfma_f32_16x16x32_bf16 v[116:119], v[144:147], v[160:163], v[116:119]
	v_mfma_f32_16x16x32_bf16 v[112:115], v[152:155], v[160:163], v[112:115]
	v_mfma_f32_16x16x32_bf16 v[100:103], v[144:147], v[176:179], v[100:103]
	v_mfma_f32_16x16x32_bf16 v[96:99], v[152:155], v[176:179], v[96:99]
	v_mfma_f32_16x16x32_bf16 v[84:87], v[144:147], v[184:187], v[84:87]
	v_mfma_f32_16x16x32_bf16 v[80:83], v[152:155], v[184:187], v[80:83]
	v_mfma_f32_16x16x32_bf16 v[68:71], v[144:147], v[194:197], v[68:71]
	v_mfma_f32_16x16x32_bf16 v[64:67], v[152:155], v[194:197], v[64:67]
	v_mfma_f32_16x16x32_bf16 v[116:119], v[148:151], v[172:175], v[116:119]
	v_mfma_f32_16x16x32_bf16 v[112:115], v[156:159], v[172:175], v[112:115]
	v_mfma_f32_16x16x32_bf16 v[100:103], v[148:151], v[180:183], v[100:103]
	v_mfma_f32_16x16x32_bf16 v[96:99], v[156:159], v[180:183], v[96:99]
	v_mfma_f32_16x16x32_bf16 v[84:87], v[148:151], v[188:191], v[84:87]
	v_mfma_f32_16x16x32_bf16 v[80:83], v[156:159], v[188:191], v[80:83]
	v_mfma_f32_16x16x32_bf16 v[68:71], v[148:151], v[198:201], v[68:71]
	v_mfma_f32_16x16x32_bf16 v[64:67], v[156:159], v[198:201], v[64:67]
	s_setprio 0
	s_barrier
	s_mov_b32 m0, s56
	s_bitset1_b32 s31, 7
	buffer_load_dwordx4 v165, s[4:7], s31 offen lds
	s_mov_b32 m0, s57
	ds_read_b128 v[160:163], v171 offset:49152
	buffer_load_dwordx4 v167, s[4:7], s31 offen lds
	s_add_i32 s31, s31, s33
	s_mov_b32 m0, s65
	ds_read_b128 v[172:175], v171 offset:50176
	buffer_load_dwordx4 v165, s[4:7], s31 offen lds
	s_mov_b32 m0, s76
	ds_read_b128 v[176:179], v171 offset:51200
	buffer_load_dwordx4 v167, s[4:7], s31 offen lds
	s_mov_b32 m0, s58
	ds_read_b128 v[180:183], v171 offset:52224
	buffer_load_dwordx4 v164, s[36:39], s30 offen lds
	s_mov_b32 m0, s59
	ds_read_b128 v[184:187], v171 offset:53248
	buffer_load_dwordx4 v166, s[36:39], s30 offen lds
	ds_read_b128 v[188:191], v171 offset:54272
	ds_read_b128 v[194:197], v171 offset:55296
	ds_read_b128 v[198:201], v171 offset:56320
	s_waitcnt vmcnt(8)
	s_waitcnt lgkmcnt(0)
	s_barrier
	s_setprio 1
	v_mfma_f32_16x16x32_bf16 v[60:63], v[128:131], v[160:163], v[60:63]
	v_mfma_f32_16x16x32_bf16 v[56:59], v[136:139], v[160:163], v[56:59]
	v_mfma_f32_16x16x32_bf16 v[44:47], v[128:131], v[176:179], v[44:47]
	v_mfma_f32_16x16x32_bf16 v[40:43], v[136:139], v[176:179], v[40:43]
	v_mfma_f32_16x16x32_bf16 v[28:31], v[128:131], v[184:187], v[28:31]
	v_mfma_f32_16x16x32_bf16 v[24:27], v[136:139], v[184:187], v[24:27]
	v_mfma_f32_16x16x32_bf16 v[12:15], v[128:131], v[194:197], v[12:15]
	v_mfma_f32_16x16x32_bf16 v[8:11], v[136:139], v[194:197], v[8:11]
	v_mfma_f32_16x16x32_bf16 v[60:63], v[132:135], v[172:175], v[60:63]
	v_mfma_f32_16x16x32_bf16 v[56:59], v[140:143], v[172:175], v[56:59]
	v_mfma_f32_16x16x32_bf16 v[44:47], v[132:135], v[180:183], v[44:47]
	v_mfma_f32_16x16x32_bf16 v[40:43], v[140:143], v[180:183], v[40:43]
	v_mfma_f32_16x16x32_bf16 v[28:31], v[132:135], v[188:191], v[28:31]
	v_mfma_f32_16x16x32_bf16 v[24:27], v[140:143], v[188:191], v[24:27]
	v_mfma_f32_16x16x32_bf16 v[12:15], v[132:135], v[198:201], v[12:15]
	v_mfma_f32_16x16x32_bf16 v[8:11], v[140:143], v[198:201], v[8:11]
	v_mfma_f32_16x16x32_bf16 v[52:55], v[144:147], v[160:163], v[52:55]
	v_mfma_f32_16x16x32_bf16 v[48:51], v[152:155], v[160:163], v[48:51]
	v_mfma_f32_16x16x32_bf16 v[36:39], v[144:147], v[176:179], v[36:39]
	v_mfma_f32_16x16x32_bf16 v[32:35], v[152:155], v[176:179], v[32:35]
	v_mfma_f32_16x16x32_bf16 v[20:23], v[144:147], v[184:187], v[20:23]
	v_mfma_f32_16x16x32_bf16 v[16:19], v[152:155], v[184:187], v[16:19]
	v_mfma_f32_16x16x32_bf16 v[4:7], v[144:147], v[194:197], v[4:7]
	v_mfma_f32_16x16x32_bf16 v[0:3], v[152:155], v[194:197], v[0:3]
	v_mfma_f32_16x16x32_bf16 v[52:55], v[148:151], v[172:175], v[52:55]
	v_mfma_f32_16x16x32_bf16 v[48:51], v[156:159], v[172:175], v[48:51]
	v_mfma_f32_16x16x32_bf16 v[36:39], v[148:151], v[180:183], v[36:39]
	v_mfma_f32_16x16x32_bf16 v[32:35], v[156:159], v[180:183], v[32:35]
	v_mfma_f32_16x16x32_bf16 v[20:23], v[148:151], v[188:191], v[20:23]
	v_mfma_f32_16x16x32_bf16 v[16:19], v[156:159], v[188:191], v[16:19]
	v_mfma_f32_16x16x32_bf16 v[4:7], v[148:151], v[198:201], v[4:7]
	v_mfma_f32_16x16x32_bf16 v[0:3], v[156:159], v[198:201], v[0:3]
	s_setprio 0
	s_barrier
	s_add_i32 s29, s29, 2
	s_addk_i32 s16, 0x100
	s_addk_i32 s28, 0x100
	s_cmp_ge_i32 s29, s82
	s_cbranch_scc0 .LBB0_352

;     __device__ __forceinline__ unsigned a_off(const Unit& u, const Gemm& g) const { return (unsigned)u.pm * (unsigned)(BM * 2) * (unsigned)g.K; }
; template <class Epi, class Sched, bool ALIGN_EPI = false, bool SP2 = false, bool FP8 = false>
; __device__ __forceinline__ void gemm_phase(LAS unsigned char* lds, const Gemm g, const Sched& S, const Epi& E, int wbase) {
;     ...
;         const bool has_next = S.next(ui + 1, nxt);
;         const unsigned nA = has_next ? S.a_off(nxt, g) : cA, nB = has_next ? S.b_off(nxt, g) : cB;
;         const rsrc_t rAn = (Sched::TWO && has_next) ? (nxt.part ? rA1 : rA0) : rAc, rBn = (Sched::TWO && has_next) ? (nxt.part ? rB1 : rB0) : rBc;
;         float pre_[8] = {0.f, 0.f, 0.f, 0.f, 0.f, 0.f, 0.f, 0.f};
;         if constexpr (Epi::HAS_PRE) E.pre_load(pre_, cur, wr);
;         for (int t = 0; t < nt; t += 2) {
;             const bool last = (t == nt - 2);
;             const unsigned a1 = cA + (unsigned)(t + 1) * kstep;
;             const unsigned a2 = last ? nA : cA + (unsigned)(t + 2) * kstep, b2 = last ? nB : cB + (unsigned)(t + 2) * kstep; const rsrc_t rA2 = (Sched::TWO && last) ? rAn : rAc, rB2 = (Sched::TWO && last) ? rBn : rBc;
;             const unsigned a3 = a2 + kstep, b3 = b2 + kstep;
;             if (last && has_next) S.a_ready(nxt);
;             if constexpr (SP2) {
;             PG8_LDB(B0, 0, 0); PG8_LDB(B1, 0, 1); PG8_SCHED; PG8_LDA(At, 0, 0); PG8_STAGE(PG8_SA(1, 1), rAc, a1 + hstep, voffA);
;             PG8_WAIT_V(8); PG8_WAIT_L(0); PG8_BAR; PG8_MMA(0, 0, At, B0); PG8_MMA(0, 1, At, B1); PG8_BAR; PG8_SCHED;
;             PG8_LDA(At, 0, 1); PG8_STAGE(PG8_SB(0, 0), rB2, b2, voffB); PG8_STAGE(PG8_SB(0, 1), rB2, b2 + hstep, voffB); PG8_STAGE(PG8_SA(0, 0), rA2, a2, voffA);
;             PG8_WAIT_V(8); PG8_WAIT_L(0); PG8_BAR; PG8_MMA(1, 0, At, B0); PG8_MMA(1, 1, At, B1); PG8_BAR; PG8_SCHED;
;             PG8_LDB(B0, 1, 0); PG8_LDB(B1, 1, 1); PG8_SCHED; PG8_LDA(At, 1, 0); PG8_STAGE(PG8_SA(0, 1), rA2, a2 + hstep, voffA);
;             PG8_WAIT_V(8); PG8_WAIT_L(0); PG8_BAR; PG8_MMA(0, 0, At, B0); PG8_MMA(0, 1, At, B1); PG8_BAR; PG8_SCHED;
;             PG8_LDA(At, 1, 1); PG8_STAGE(PG8_SB(1, 0), rB2, b3, voffB); PG8_STAGE(PG8_SB(1, 1), rB2, b3 + hstep, voffB); PG8_STAGE(PG8_SA(1, 0), rA2, a3, voffA);
;             PG8_WAIT_V(8); PG8_WAIT_L(0); PG8_BAR; PG8_MMA(1, 0, At, B0); PG8_MMA(1, 1, At, B1); PG8_BAR; PG8_SCHED;
.LBB0_448:
	s_lshl_b32 s48, s47, 17
	s_andn2_b64 vcc, exec, s[10:11]
	s_lshl_b32 s52, s46, 17
	s_cbranch_vccnz .LBB0_456
	s_and_b64 s[6:7], s[16:17], exec
	s_waitcnt vmcnt(37)
	s_waitcnt vmcnt(36)
	s_waitcnt vmcnt(35)
	s_waitcnt vmcnt(32)
	s_waitcnt vmcnt(31)
	s_waitcnt vmcnt(28)
	s_waitcnt vmcnt(27)
	s_waitcnt vmcnt(24)
	s_waitcnt vmcnt(23)
	s_waitcnt vmcnt(22)
	s_cselect_b32 s56, s48, s55
	s_cselect_b32 s57, s52, s54
	s_add_i32 s58, s55, 0x80
	s_add_i32 s59, s54, 0x100
	s_mov_b32 s60, 0
	v_add_u32_e32 v148, 0x10000, v138
	v_add_u32_e32 v164, 0x14000, v138
	ds_read_b128 v[128:131], v148
	ds_read_b128 v[140:143], v148 offset:1024
	ds_read_b128 v[144:147], v148 offset:2048
	ds_read_b128 v[148:151], v148 offset:3072
	ds_read_b128 v[152:155], v164
	ds_read_b128 v[156:159], v164 offset:1024
	ds_read_b128 v[160:163], v164 offset:2048
	ds_read_b128 v[164:167], v164 offset:3072
	s_add_i32 s6, s58, 0x80
	s_cmp_eq_u32 s42, s60
	s_cselect_b32 s61, s56, s6
	s_cselect_b32 s55, s57, s59
	s_or_b32 s54, s61, 0x80
	s_add_i32 s6, s19, s58
	s_mov_b32 m0, s43
	ds_read_b128 v[168:171], v139
	ds_read_b128 v[172:175], v139 offset:1024
	ds_read_b128 v[176:179], v139 offset:2048
	ds_read_b128 v[180:183], v139 offset:3072
	ds_read_b128 v[184:187], v139 offset:4096
	ds_read_b128 v[188:191], v139 offset:5120
	ds_read_b128 v[194:197], v139 offset:6144
	ds_read_b128 v[198:201], v139 offset:7168
	buffer_load_dwordx4 v132, s[36:39], s6 offen lds
	s_mov_b32 m0, s44
	s_nop 0
	buffer_load_dwordx4 v134, s[36:39], s6 offen lds
	s_waitcnt vmcnt(8)
	s_waitcnt lgkmcnt(0)
	s_barrier
	s_setprio 1
	v_mfma_f32_16x16x32_bf16 v[124:127], v[128:131], v[168:171], 0
	v_mfma_f32_16x16x32_bf16 v[120:123], v[144:147], v[168:171], 0
	v_mfma_f32_16x16x32_bf16 v[108:111], v[128:131], v[176:179], 0
	v_mfma_f32_16x16x32_bf16 v[104:107], v[144:147], v[176:179], 0
	v_mfma_f32_16x16x32_bf16 v[92:95], v[128:131], v[184:187], 0
	v_mfma_f32_16x16x32_bf16 v[88:91], v[144:147], v[184:187], 0
	v_mfma_f32_16x16x32_bf16 v[76:79], v[128:131], v[194:197], 0
	v_mfma_f32_16x16x32_bf16 v[72:75], v[144:147], v[194:197], 0
	v_mfma_f32_16x16x32_bf16 v[124:127], v[140:143], v[172:175], v[124:127]
	v_mfma_f32_16x16x32_bf16 v[120:123], v[148:151], v[172:175], v[120:123]
	v_mfma_f32_16x16x32_bf16 v[108:111], v[140:143], v[180:183], v[108:111]
	v_mfma_f32_16x16x32_bf16 v[104:107], v[148:151], v[180:183], v[104:107]
	v_mfma_f32_16x16x32_bf16 v[92:95], v[140:143], v[188:191], v[92:95]
	v_mfma_f32_16x16x32_bf16 v[88:91], v[148:151], v[188:191], v[88:91]
	v_mfma_f32_16x16x32_bf16 v[76:79], v[140:143], v[198:201], v[76:79]
	v_mfma_f32_16x16x32_bf16 v[72:75], v[148:151], v[198:201], v[72:75]
	v_mfma_f32_16x16x32_bf16 v[116:119], v[152:155], v[168:171], 0
	v_mfma_f32_16x16x32_bf16 v[112:115], v[160:163], v[168:171], 0
	v_mfma_f32_16x16x32_bf16 v[100:103], v[152:155], v[176:179], 0
	v_mfma_f32_16x16x32_bf16 v[96:99], v[160:163], v[176:179], 0
	v_mfma_f32_16x16x32_bf16 v[84:87], v[152:155], v[184:187], 0
	v_mfma_f32_16x16x32_bf16 v[80:83], v[160:163], v[184:187], 0
	v_mfma_f32_16x16x32_bf16 v[68:71], v[152:155], v[194:197], 0
	v_mfma_f32_16x16x32_bf16 v[64:67], v[160:163], v[194:197], 0
	v_mfma_f32_16x16x32_bf16 v[116:119], v[156:159], v[172:175], v[116:119]
	v_mfma_f32_16x16x32_bf16 v[112:115], v[164:167], v[172:175], v[112:115]
	v_mfma_f32_16x16x32_bf16 v[100:103], v[156:159], v[180:183], v[100:103]
	v_mfma_f32_16x16x32_bf16 v[96:99], v[164:167], v[180:183], v[96:99]
	v_mfma_f32_16x16x32_bf16 v[84:87], v[156:159], v[188:191], v[84:87]
	v_mfma_f32_16x16x32_bf16 v[80:83], v[164:167], v[188:191], v[80:83]
	v_mfma_f32_16x16x32_bf16 v[68:71], v[156:159], v[198:201], v[68:71]
	v_mfma_f32_16x16x32_bf16 v[64:67], v[164:167], v[198:201], v[64:67]
	s_setprio 0
	s_barrier
	s_mov_b32 m0, s21
	s_mov_b32 s6, s38
	s_mov_b32 s7, s39
	buffer_load_dwordx4 v133, s[4:7], s55 offen lds
	s_mov_b32 m0, s22
	ds_read_b128 v[168:171], v139 offset:16384
	s_add_i32 s62, s55, s19
	buffer_load_dwordx4 v135, s[4:7], s55 offen lds
	s_mov_b32 m0, s20
	ds_read_b128 v[172:175], v139 offset:17408
	buffer_load_dwordx4 v132, s[36:39], s61 offen lds
	s_mov_b32 m0, s25
	ds_read_b128 v[176:179], v139 offset:18432
	buffer_load_dwordx4 v134, s[36:39], s61 offen lds
	ds_read_b128 v[180:183], v139 offset:19456
	ds_read_b128 v[184:187], v139 offset:20480
	ds_read_b128 v[188:191], v139 offset:21504
	ds_read_b128 v[194:197], v139 offset:22528
	ds_read_b128 v[198:201], v139 offset:23552
	s_waitcnt vmcnt(6)
	s_waitcnt lgkmcnt(0)
	s_barrier
	s_setprio 1
	v_mfma_f32_16x16x32_bf16 v[60:63], v[128:131], v[168:171], 0
	v_mfma_f32_16x16x32_bf16 v[56:59], v[144:147], v[168:171], 0
	v_mfma_f32_16x16x32_bf16 v[44:47], v[128:131], v[176:179], 0
	v_mfma_f32_16x16x32_bf16 v[40:43], v[144:147], v[176:179], 0
	v_mfma_f32_16x16x32_bf16 v[28:31], v[128:131], v[184:187], 0
	v_mfma_f32_16x16x32_bf16 v[24:27], v[144:147], v[184:187], 0
	v_mfma_f32_16x16x32_bf16 v[12:15], v[128:131], v[194:197], 0
	v_mfma_f32_16x16x32_bf16 v[8:11], v[144:147], v[194:197], 0
	v_mfma_f32_16x16x32_bf16 v[60:63], v[140:143], v[172:175], v[60:63]
	v_mfma_f32_16x16x32_bf16 v[56:59], v[148:151], v[172:175], v[56:59]
	v_mfma_f32_16x16x32_bf16 v[44:47], v[140:143], v[180:183], v[44:47]
	v_mfma_f32_16x16x32_bf16 v[40:43], v[148:151], v[180:183], v[40:43]
	v_mfma_f32_16x16x32_bf16 v[28:31], v[140:143], v[188:191], v[28:31]
	v_mfma_f32_16x16x32_bf16 v[24:27], v[148:151], v[188:191], v[24:27]
	v_mfma_f32_16x16x32_bf16 v[12:15], v[140:143], v[198:201], v[12:15]
	v_mfma_f32_16x16x32_bf16 v[8:11], v[148:151], v[198:201], v[8:11]
	v_mfma_f32_16x16x32_bf16 v[52:55], v[152:155], v[168:171], 0
	v_mfma_f32_16x16x32_bf16 v[48:51], v[160:163], v[168:171], 0
	v_mfma_f32_16x16x32_bf16 v[36:39], v[152:155], v[176:179], 0
	v_mfma_f32_16x16x32_bf16 v[32:35], v[160:163], v[176:179], 0
	v_mfma_f32_16x16x32_bf16 v[20:23], v[152:155], v[184:187], 0
	v_mfma_f32_16x16x32_bf16 v[16:19], v[160:163], v[184:187], 0
	v_mfma_f32_16x16x32_bf16 v[4:7], v[152:155], v[194:197], 0
	v_mfma_f32_16x16x32_bf16 v[0:3], v[160:163], v[194:197], 0
	v_mfma_f32_16x16x32_bf16 v[52:55], v[156:159], v[172:175], v[52:55]
	v_mfma_f32_16x16x32_bf16 v[48:51], v[164:167], v[172:175], v[48:51]
	v_mfma_f32_16x16x32_bf16 v[36:39], v[156:159], v[180:183], v[36:39]
	v_mfma_f32_16x16x32_bf16 v[32:35], v[164:167], v[180:183], v[32:35]
	v_mfma_f32_16x16x32_bf16 v[20:23], v[156:159], v[188:191], v[20:23]
	v_mfma_f32_16x16x32_bf16 v[16:19], v[164:167], v[188:191], v[16:19]
	v_mfma_f32_16x16x32_bf16 v[4:7], v[156:159], v[198:201], v[4:7]
	v_mfma_f32_16x16x32_bf16 v[0:3], v[164:167], v[198:201], v[0:3]
	s_setprio 0
	s_barrier
; #define PG8_STAGE(bufoff, rs_, soff_, voff) do { _Pragma("unroll") for (int _i = 0; _i < 2; ++_i) \
;         __builtin_amdgcn_raw_ptr_buffer_load_lds(rs_, (LAS void*)(lds + (bufoff) + ldsw + _i * 8192), 16, (int)(voff)[_i], (int)(soff_), 0, 0); } while (0)
; #define PG8_LDA(dst, b, h) do { _Pragma("unroll") for (int m = 0; m < 4; ++m) dst[m] = PG8_LD2(lds + PG8_SA(b, h) + aoff + m * 2048); } while (0)
; #define PG8_LDB(dst, b, h) do { _Pragma("unroll") for (int n = 0; n < 2; ++n) dst[n] = PG8_LD2(lds + PG8_SB(b, h) + boff + n * 2048); } while (0)
; #define PG8_WAIT_V(n) asm volatile("s_waitcnt vmcnt(" #n ")" ::: "memory")
; #define PG8_WAIT_L(n) asm volatile("s_waitcnt lgkmcnt(" #n ")" ::: "memory")
; #define PG8_BAR __builtin_amdgcn_s_barrier()
; #define PG8_SCHED __builtin_amdgcn_sched_barrier(0)
; template <class Epi, class Sched, bool ALIGN_EPI = false, bool SP2 = false, bool FP8 = false>
; __device__ __forceinline__ void gemm_phase(LAS unsigned char* lds, const Gemm g, const Sched& S, const Epi& E, int wbase) {
;     ...
;             PG8_LDB(B0, 0, 0); PG8_LDB(B1, 0, 1); PG8_SCHED; PG8_LDA(At, 0, 0); PG8_STAGE(PG8_SA(1, 1), rAc, a1 + hstep, voffA);
;             PG8_WAIT_V(8); PG8_WAIT_L(0); PG8_BAR; PG8_MMA(0, 0, At, B0); PG8_MMA(0, 1, At, B1); PG8_BAR; PG8_SCHED;
;             PG8_LDA(At, 0, 1); PG8_STAGE(PG8_SB(0, 0), rB2, b2, voffB); PG8_STAGE(PG8_SB(0, 1), rB2, b2 + hstep, voffB); PG8_STAGE(PG8_SA(0, 0), rA2, a2, voffA);
;             PG8_WAIT_V(8); PG8_WAIT_L(0); PG8_BAR; PG8_MMA(1, 0, At, B0); PG8_MMA(1, 1, At, B1); PG8_BAR; PG8_SCHED;
;             PG8_LDB(B0, 1, 0); PG8_LDB(B1, 1, 1); PG8_SCHED; PG8_LDA(At, 1, 0); PG8_STAGE(PG8_SA(0, 1), rA2, a2 + hstep, voffA);
;             PG8_WAIT_V(8); PG8_WAIT_L(0); PG8_BAR; PG8_MMA(0, 0, At, B0); PG8_MMA(0, 1, At, B1); PG8_BAR; PG8_SCHED;
;             PG8_LDA(At, 1, 1); PG8_STAGE(PG8_SB(1, 0), rB2, b3, voffB); PG8_STAGE(PG8_SB(1, 1), rB2, b3 + hstep, voffB); PG8_STAGE(PG8_SA(1, 0), rA2, a3, voffA);
;             PG8_WAIT_V(8); PG8_WAIT_L(0); PG8_BAR; PG8_MMA(1, 0, At, B0); PG8_MMA(1, 1, At, B1); PG8_BAR; PG8_SCHED;
	s_mov_b32 m0, s23
	s_nop 0
	buffer_load_dwordx4 v133, s[4:7], s62 offen lds
	s_mov_b32 m0, s24
	s_nop 0
	buffer_load_dwordx4 v135, s[4:7], s62 offen lds
	v_add_u32_e32 v148, 0x18000, v138
	v_add_u32_e32 v164, 0x1c000, v138
	ds_read_b128 v[128:131], v148
	ds_read_b128 v[140:143], v148 offset:1024
	ds_read_b128 v[144:147], v148 offset:2048
	ds_read_b128 v[148:151], v148 offset:3072
	ds_read_b128 v[152:155], v164
	ds_read_b128 v[156:159], v164 offset:1024
	ds_read_b128 v[160:163], v164 offset:2048
	ds_read_b128 v[164:167], v164 offset:3072
	s_add_i32 s61, s61, s19
	s_mov_b32 m0, s26
	ds_read_b128 v[168:171], v139 offset:32768
	ds_read_b128 v[172:175], v139 offset:33792
	ds_read_b128 v[176:179], v139 offset:34816
	ds_read_b128 v[180:183], v139 offset:35840
	ds_read_b128 v[184:187], v139 offset:36864
	ds_read_b128 v[188:191], v139 offset:37888
	ds_read_b128 v[194:197], v139 offset:38912
	ds_read_b128 v[198:201], v139 offset:39936
	buffer_load_dwordx4 v132, s[36:39], s61 offen lds
	s_mov_b32 m0, s27
	s_nop 0
	buffer_load_dwordx4 v134, s[36:39], s61 offen lds
	s_waitcnt vmcnt(8)
	s_waitcnt lgkmcnt(0)
	s_barrier
	s_setprio 1
	v_mfma_f32_16x16x32_bf16 v[124:127], v[128:131], v[168:171], v[124:127]
	v_mfma_f32_16x16x32_bf16 v[120:123], v[144:147], v[168:171], v[120:123]
	v_mfma_f32_16x16x32_bf16 v[108:111], v[128:131], v[176:179], v[108:111]
	v_mfma_f32_16x16x32_bf16 v[104:107], v[144:147], v[176:179], v[104:107]
	v_mfma_f32_16x16x32_bf16 v[92:95], v[128:131], v[184:187], v[92:95]
	v_mfma_f32_16x16x32_bf16 v[88:91], v[144:147], v[184:187], v[88:91]
	v_mfma_f32_16x16x32_bf16 v[76:79], v[128:131], v[194:197], v[76:79]
	v_mfma_f32_16x16x32_bf16 v[72:75], v[144:147], v[194:197], v[72:75]
	v_mfma_f32_16x16x32_bf16 v[124:127], v[140:143], v[172:175], v[124:127]
	v_mfma_f32_16x16x32_bf16 v[120:123], v[148:151], v[172:175], v[120:123]
	v_mfma_f32_16x16x32_bf16 v[108:111], v[140:143], v[180:183], v[108:111]
	v_mfma_f32_16x16x32_bf16 v[104:107], v[148:151], v[180:183], v[104:107]
	v_mfma_f32_16x16x32_bf16 v[92:95], v[140:143], v[188:191], v[92:95]
	v_mfma_f32_16x16x32_bf16 v[88:91], v[148:151], v[188:191], v[88:91]
	v_mfma_f32_16x16x32_bf16 v[76:79], v[140:143], v[198:201], v[76:79]
	v_mfma_f32_16x16x32_bf16 v[72:75], v[148:151], v[198:201], v[72:75]
	v_mfma_f32_16x16x32_bf16 v[116:119], v[152:155], v[168:171], v[116:119]
	v_mfma_f32_16x16x32_bf16 v[112:115], v[160:163], v[168:171], v[112:115]
	v_mfma_f32_16x16x32_bf16 v[100:103], v[152:155], v[176:179], v[100:103]
	v_mfma_f32_16x16x32_bf16 v[96:99], v[160:163], v[176:179], v[96:99]
	v_mfma_f32_16x16x32_bf16 v[84:87], v[152:155], v[184:187], v[84:87]
	v_mfma_f32_16x16x32_bf16 v[80:83], v[160:163], v[184:187], v[80:83]
	v_mfma_f32_16x16x32_bf16 v[68:71], v[152:155], v[194:197], v[68:71]
	v_mfma_f32_16x16x32_bf16 v[64:67], v[160:163], v[194:197], v[64:67]
	v_mfma_f32_16x16x32_bf16 v[116:119], v[156:159], v[172:175], v[116:119]
	v_mfma_f32_16x16x32_bf16 v[112:115], v[164:167], v[172:175], v[112:115]
	v_mfma_f32_16x16x32_bf16 v[100:103], v[156:159], v[180:183], v[100:103]
	v_mfma_f32_16x16x32_bf16 v[96:99], v[164:167], v[180:183], v[96:99]
	v_mfma_f32_16x16x32_bf16 v[84:87], v[156:159], v[188:191], v[84:87]
	v_mfma_f32_16x16x32_bf16 v[80:83], v[164:167], v[188:191], v[80:83]
	v_mfma_f32_16x16x32_bf16 v[68:71], v[156:159], v[198:201], v[68:71]
	v_mfma_f32_16x16x32_bf16 v[64:67], v[164:167], v[198:201], v[64:67]
	s_setprio 0
	s_barrier
	s_mov_b32 m0, s28
	s_bitset1_b32 s55, 7
	buffer_load_dwordx4 v133, s[4:7], s55 offen lds
	s_mov_b32 m0, s29
	ds_read_b128 v[168:171], v139 offset:49152
	buffer_load_dwordx4 v135, s[4:7], s55 offen lds
	s_add_i32 s55, s55, s19
	s_mov_b32 m0, s33
	ds_read_b128 v[172:175], v139 offset:50176
	buffer_load_dwordx4 v133, s[4:7], s55 offen lds
	s_mov_b32 m0, s34
	ds_read_b128 v[176:179], v139 offset:51200
	buffer_load_dwordx4 v135, s[4:7], s55 offen lds
	s_mov_b32 m0, s30
	ds_read_b128 v[180:183], v139 offset:52224
	buffer_load_dwordx4 v132, s[36:39], s54 offen lds
	s_mov_b32 m0, s31
	ds_read_b128 v[184:187], v139 offset:53248
	buffer_load_dwordx4 v134, s[36:39], s54 offen lds
	ds_read_b128 v[188:191], v139 offset:54272
	ds_read_b128 v[194:197], v139 offset:55296
	ds_read_b128 v[198:201], v139 offset:56320
	s_waitcnt vmcnt(8)
	s_waitcnt lgkmcnt(0)
	s_barrier
	s_setprio 1
	v_mfma_f32_16x16x32_bf16 v[60:63], v[128:131], v[168:171], v[60:63]
	v_mfma_f32_16x16x32_bf16 v[56:59], v[144:147], v[168:171], v[56:59]
	v_mfma_f32_16x16x32_bf16 v[44:47], v[128:131], v[176:179], v[44:47]
	v_mfma_f32_16x16x32_bf16 v[40:43], v[144:147], v[176:179], v[40:43]
	v_mfma_f32_16x16x32_bf16 v[28:31], v[128:131], v[184:187], v[28:31]
	v_mfma_f32_16x16x32_bf16 v[24:27], v[144:147], v[184:187], v[24:27]
	v_mfma_f32_16x16x32_bf16 v[12:15], v[128:131], v[194:197], v[12:15]
	v_mfma_f32_16x16x32_bf16 v[8:11], v[144:147], v[194:197], v[8:11]
	v_mfma_f32_16x16x32_bf16 v[60:63], v[140:143], v[172:175], v[60:63]
	v_mfma_f32_16x16x32_bf16 v[56:59], v[148:151], v[172:175], v[56:59]
	v_mfma_f32_16x16x32_bf16 v[44:47], v[140:143], v[180:183], v[44:47]
	v_mfma_f32_16x16x32_bf16 v[40:43], v[148:151], v[180:183], v[40:43]
	v_mfma_f32_16x16x32_bf16 v[28:31], v[140:143], v[188:191], v[28:31]
	v_mfma_f32_16x16x32_bf16 v[24:27], v[148:151], v[188:191], v[24:27]
	v_mfma_f32_16x16x32_bf16 v[12:15], v[140:143], v[198:201], v[12:15]
	v_mfma_f32_16x16x32_bf16 v[8:11], v[148:151], v[198:201], v[8:11]
	v_mfma_f32_16x16x32_bf16 v[52:55], v[152:155], v[168:171], v[52:55]
	v_mfma_f32_16x16x32_bf16 v[48:51], v[160:163], v[168:171], v[48:51]
	v_mfma_f32_16x16x32_bf16 v[36:39], v[152:155], v[176:179], v[36:39]
	v_mfma_f32_16x16x32_bf16 v[32:35], v[160:163], v[176:179], v[32:35]
	v_mfma_f32_16x16x32_bf16 v[20:23], v[152:155], v[184:187], v[20:23]
	v_mfma_f32_16x16x32_bf16 v[16:19], v[160:163], v[184:187], v[16:19]
	v_mfma_f32_16x16x32_bf16 v[4:7], v[152:155], v[194:197], v[4:7]
	v_mfma_f32_16x16x32_bf16 v[0:3], v[160:163], v[194:197], v[0:3]
	v_mfma_f32_16x16x32_bf16 v[52:55], v[156:159], v[172:175], v[52:55]
	v_mfma_f32_16x16x32_bf16 v[48:51], v[164:167], v[172:175], v[48:51]
	v_mfma_f32_16x16x32_bf16 v[36:39], v[156:159], v[180:183], v[36:39]
	v_mfma_f32_16x16x32_bf16 v[32:35], v[164:167], v[180:183], v[32:35]
	v_mfma_f32_16x16x32_bf16 v[20:23], v[156:159], v[188:191], v[20:23]
	v_mfma_f32_16x16x32_bf16 v[16:19], v[164:167], v[188:191], v[16:19]
	v_mfma_f32_16x16x32_bf16 v[4:7], v[156:159], v[198:201], v[4:7]
	v_mfma_f32_16x16x32_bf16 v[0:3], v[164:167], v[198:201], v[0:3]
	s_setprio 0
	s_barrier
	s_add_i32 s60, s60, 2
	s_addk_i32 s58, 0x100
	s_addk_i32 s59, 0x100
	s_cmp_ge_i32 s60, s35
	s_cbranch_scc0 .LBB0_450
	s_branch .Lzp_after_450
; #define PG8_STAGE(bufoff, rs_, soff_, voff) do { _Pragma("unroll") for (int _i = 0; _i < 2; ++_i) \
;         __builtin_amdgcn_raw_ptr_buffer_load_lds(rs_, (LAS void*)(lds + (bufoff) + ldsw + _i * 8192), 16, (int)(voff)[_i], (int)(soff_), 0, 0); } while (0)
; #define PG8_LDA(dst, b, h) do { _Pragma("unroll") for (int m = 0; m < 4; ++m) dst[m] = PG8_LD2(lds + PG8_SA(b, h) + aoff + m * 2048); } while (0)
; #define PG8_LDB(dst, b, h) do { _Pragma("unroll") for (int n = 0; n < 2; ++n) dst[n] = PG8_LD2(lds + PG8_SB(b, h) + boff + n * 2048); } while (0)
; template <class Epi, class Sched, bool ALIGN_EPI = false, bool SP2 = false, bool FP8 = false>
; __device__ __forceinline__ void gemm_phase(LAS unsigned char* lds, const Gemm g, const Sched& S, const Epi& E, int wbase) {
;     ...
;         for (int t = 0; t < nt; t += 2) {
;             const bool last = (t == nt - 2);
;             const unsigned a1 = cA + (unsigned)(t + 1) * kstep;
;             const unsigned a2 = last ? nA : cA + (unsigned)(t + 2) * kstep, b2 = last ? nB : cB + (unsigned)(t + 2) * kstep; const rsrc_t rA2 = (Sched::TWO && last) ? rAn : rAc, rB2 = (Sched::TWO && last) ? rBn : rBc;
;             const unsigned a3 = a2 + kstep, b3 = b2 + kstep;
;             if (last && has_next) S.a_ready(nxt);
;             if constexpr (SP2) {
;             PG8_LDB(B0, 0, 0); PG8_LDB(B1, 0, 1); PG8_SCHED; PG8_LDA(At, 0, 0); PG8_STAGE(PG8_SA(1, 1), rAc, a1 + hstep, voffA);
;             PG8_WAIT_V(8); PG8_WAIT_L(0); PG8_BAR; PG8_MMA(0, 0, At, B0); PG8_MMA(0, 1, At, B1); PG8_BAR; PG8_SCHED;
;             PG8_LDA(At, 0, 1); PG8_STAGE(PG8_SB(0, 0), rB2, b2, voffB); PG8_STAGE(PG8_SB(0, 1), rB2, b2 + hstep, voffB); PG8_STAGE(PG8_SA(0, 0), rA2, a2, voffA);
;             PG8_WAIT_V(8); PG8_WAIT_L(0); PG8_BAR; PG8_MMA(1, 0, At, B0); PG8_MMA(1, 1, At, B1); PG8_BAR; PG8_SCHED;
;             PG8_LDB(B0, 1, 0); PG8_LDB(B1, 1, 1); PG8_SCHED; PG8_LDA(At, 1, 0); PG8_STAGE(PG8_SA(0, 1), rA2, a2 + hstep, voffA);
;             PG8_WAIT_V(8); PG8_WAIT_L(0); PG8_BAR; PG8_MMA(0, 0, At, B0); PG8_MMA(0, 1, At, B1); PG8_BAR; PG8_SCHED;
;             PG8_LDA(At, 1, 1); PG8_STAGE(PG8_SB(1, 0), rB2, b3, voffB); PG8_STAGE(PG8_SB(1, 1), rB2, b3 + hstep, voffB); PG8_STAGE(PG8_SA(1, 0), rA2, a3, voffA);
;             PG8_WAIT_V(8); PG8_WAIT_L(0); PG8_BAR; PG8_MMA(1, 0, At, B0); PG8_MMA(1, 1, At, B1); PG8_BAR; PG8_SCHED;
.LBB0_450:
	v_add_u32_e32 v148, 0x10000, v138
	v_add_u32_e32 v164, 0x14000, v138
	ds_read_b128 v[128:131], v148
	ds_read_b128 v[140:143], v148 offset:1024
	ds_read_b128 v[144:147], v148 offset:2048
	ds_read_b128 v[148:151], v148 offset:3072
	ds_read_b128 v[152:155], v164
	ds_read_b128 v[156:159], v164 offset:1024
	ds_read_b128 v[160:163], v164 offset:2048
	ds_read_b128 v[164:167], v164 offset:3072
	s_add_i32 s6, s58, 0x80
	s_cmp_eq_u32 s42, s60
	s_cselect_b32 s61, s56, s6
	s_cselect_b32 s55, s57, s59
	s_or_b32 s54, s61, 0x80
	s_add_i32 s6, s19, s58
	s_mov_b32 m0, s43
	ds_read_b128 v[168:171], v139
	ds_read_b128 v[172:175], v139 offset:1024
	ds_read_b128 v[176:179], v139 offset:2048
	ds_read_b128 v[180:183], v139 offset:3072
	ds_read_b128 v[184:187], v139 offset:4096
	ds_read_b128 v[188:191], v139 offset:5120
	ds_read_b128 v[194:197], v139 offset:6144
	ds_read_b128 v[198:201], v139 offset:7168
	buffer_load_dwordx4 v132, s[36:39], s6 offen lds
	s_mov_b32 m0, s44
	s_nop 0
	buffer_load_dwordx4 v134, s[36:39], s6 offen lds
	s_waitcnt vmcnt(8)
	s_waitcnt lgkmcnt(0)
	s_barrier
	s_setprio 1
	v_mfma_f32_16x16x32_bf16 v[124:127], v[128:131], v[168:171], v[124:127]
	v_mfma_f32_16x16x32_bf16 v[120:123], v[144:147], v[168:171], v[120:123]
	v_mfma_f32_16x16x32_bf16 v[108:111], v[128:131], v[176:179], v[108:111]
	v_mfma_f32_16x16x32_bf16 v[104:107], v[144:147], v[176:179], v[104:107]
	v_mfma_f32_16x16x32_bf16 v[92:95], v[128:131], v[184:187], v[92:95]
	v_mfma_f32_16x16x32_bf16 v[88:91], v[144:147], v[184:187], v[88:91]
	v_mfma_f32_16x16x32_bf16 v[76:79], v[128:131], v[194:197], v[76:79]
	v_mfma_f32_16x16x32_bf16 v[72:75], v[144:147], v[194:197], v[72:75]
	v_mfma_f32_16x16x32_bf16 v[124:127], v[140:143], v[172:175], v[124:127]
	v_mfma_f32_16x16x32_bf16 v[120:123], v[148:151], v[172:175], v[120:123]
	v_mfma_f32_16x16x32_bf16 v[108:111], v[140:143], v[180:183], v[108:111]
	v_mfma_f32_16x16x32_bf16 v[104:107], v[148:151], v[180:183], v[104:107]
	v_mfma_f32_16x16x32_bf16 v[92:95], v[140:143], v[188:191], v[92:95]
	v_mfma_f32_16x16x32_bf16 v[88:91], v[148:151], v[188:191], v[88:91]
	v_mfma_f32_16x16x32_bf16 v[76:79], v[140:143], v[198:201], v[76:79]
	v_mfma_f32_16x16x32_bf16 v[72:75], v[148:151], v[198:201], v[72:75]
	v_mfma_f32_16x16x32_bf16 v[116:119], v[152:155], v[168:171], v[116:119]
	v_mfma_f32_16x16x32_bf16 v[112:115], v[160:163], v[168:171], v[112:115]
	v_mfma_f32_16x16x32_bf16 v[100:103], v[152:155], v[176:179], v[100:103]
	v_mfma_f32_16x16x32_bf16 v[96:99], v[160:163], v[176:179], v[96:99]
	v_mfma_f32_16x16x32_bf16 v[84:87], v[152:155], v[184:187], v[84:87]
	v_mfma_f32_16x16x32_bf16 v[80:83], v[160:163], v[184:187], v[80:83]
	v_mfma_f32_16x16x32_bf16 v[68:71], v[152:155], v[194:197], v[68:71]
	v_mfma_f32_16x16x32_bf16 v[64:67], v[160:163], v[194:197], v[64:67]
	v_mfma_f32_16x16x32_bf16 v[116:119], v[156:159], v[172:175], v[116:119]
	v_mfma_f32_16x16x32_bf16 v[112:115], v[164:167], v[172:175], v[112:115]
	v_mfma_f32_16x16x32_bf16 v[100:103], v[156:159], v[180:183], v[100:103]
	v_mfma_f32_16x16x32_bf16 v[96:99], v[164:167], v[180:183], v[96:99]
	v_mfma_f32_16x16x32_bf16 v[84:87], v[156:159], v[188:191], v[84:87]
	v_mfma_f32_16x16x32_bf16 v[80:83], v[164:167], v[188:191], v[80:83]
	v_mfma_f32_16x16x32_bf16 v[68:71], v[156:159], v[198:201], v[68:71]
	v_mfma_f32_16x16x32_bf16 v[64:67], v[164:167], v[198:201], v[64:67]
	s_setprio 0
	s_barrier
	s_mov_b32 m0, s21
	s_mov_b32 s6, s38
	s_mov_b32 s7, s39
	buffer_load_dwordx4 v133, s[4:7], s55 offen lds
	s_mov_b32 m0, s22
	ds_read_b128 v[168:171], v139 offset:16384
	s_add_i32 s62, s55, s19
	buffer_load_dwordx4 v135, s[4:7], s55 offen lds
	s_mov_b32 m0, s20
	ds_read_b128 v[172:175], v139 offset:17408
	buffer_load_dwordx4 v132, s[36:39], s61 offen lds
	s_mov_b32 m0, s25
	ds_read_b128 v[176:179], v139 offset:18432
	buffer_load_dwordx4 v134, s[36:39], s61 offen lds
	ds_read_b128 v[180:183], v139 offset:19456
	ds_read_b128 v[184:187], v139 offset:20480
	ds_read_b128 v[188:191], v139 offset:21504
	ds_read_b128 v[194:197], v139 offset:22528
	ds_read_b128 v[198:201], v139 offset:23552
	s_waitcnt vmcnt(6)
	s_waitcnt lgkmcnt(0)
	s_barrier
	s_setprio 1
	v_mfma_f32_16x16x32_bf16 v[60:63], v[128:131], v[168:171], v[60:63]
	v_mfma_f32_16x16x32_bf16 v[56:59], v[144:147], v[168:171], v[56:59]
	v_mfma_f32_16x16x32_bf16 v[44:47], v[128:131], v[176:179], v[44:47]
	v_mfma_f32_16x16x32_bf16 v[40:43], v[144:147], v[176:179], v[40:43]
	v_mfma_f32_16x16x32_bf16 v[28:31], v[128:131], v[184:187], v[28:31]
	v_mfma_f32_16x16x32_bf16 v[24:27], v[144:147], v[184:187], v[24:27]
	v_mfma_f32_16x16x32_bf16 v[12:15], v[128:131], v[194:197], v[12:15]
	v_mfma_f32_16x16x32_bf16 v[8:11], v[144:147], v[194:197], v[8:11]
	v_mfma_f32_16x16x32_bf16 v[60:63], v[140:143], v[172:175], v[60:63]
	v_mfma_f32_16x16x32_bf16 v[56:59], v[148:151], v[172:175], v[56:59]
	v_mfma_f32_16x16x32_bf16 v[44:47], v[140:143], v[180:183], v[44:47]
	v_mfma_f32_16x16x32_bf16 v[40:43], v[148:151], v[180:183], v[40:43]
	v_mfma_f32_16x16x32_bf16 v[28:31], v[140:143], v[188:191], v[28:31]
	v_mfma_f32_16x16x32_bf16 v[24:27], v[148:151], v[188:191], v[24:27]
	v_mfma_f32_16x16x32_bf16 v[12:15], v[140:143], v[198:201], v[12:15]
	v_mfma_f32_16x16x32_bf16 v[8:11], v[148:151], v[198:201], v[8:11]
	v_mfma_f32_16x16x32_bf16 v[52:55], v[152:155], v[168:171], v[52:55]
	v_mfma_f32_16x16x32_bf16 v[48:51], v[160:163], v[168:171], v[48:51]
	v_mfma_f32_16x16x32_bf16 v[36:39], v[152:155], v[176:179], v[36:39]
	v_mfma_f32_16x16x32_bf16 v[32:35], v[160:163], v[176:179], v[32:35]
	v_mfma_f32_16x16x32_bf16 v[20:23], v[152:155], v[184:187], v[20:23]
	v_mfma_f32_16x16x32_bf16 v[16:19], v[160:163], v[184:187], v[16:19]
	v_mfma_f32_16x16x32_bf16 v[4:7], v[152:155], v[194:197], v[4:7]
	v_mfma_f32_16x16x32_bf16 v[0:3], v[160:163], v[194:197], v[0:3]
	v_mfma_f32_16x16x32_bf16 v[52:55], v[156:159], v[172:175], v[52:55]
	v_mfma_f32_16x16x32_bf16 v[48:51], v[164:167], v[172:175], v[48:51]
	v_mfma_f32_16x16x32_bf16 v[36:39], v[156:159], v[180:183], v[36:39]
	v_mfma_f32_16x16x32_bf16 v[32:35], v[164:167], v[180:183], v[32:35]
	v_mfma_f32_16x16x32_bf16 v[20:23], v[156:159], v[188:191], v[20:23]
	v_mfma_f32_16x16x32_bf16 v[16:19], v[164:167], v[188:191], v[16:19]
	v_mfma_f32_16x16x32_bf16 v[4:7], v[156:159], v[198:201], v[4:7]
	v_mfma_f32_16x16x32_bf16 v[0:3], v[164:167], v[198:201], v[0:3]
	s_setprio 0
	s_barrier
; #define PG8_STAGE(bufoff, rs_, soff_, voff) do { _Pragma("unroll") for (int _i = 0; _i < 2; ++_i) \
;         __builtin_amdgcn_raw_ptr_buffer_load_lds(rs_, (LAS void*)(lds + (bufoff) + ldsw + _i * 8192), 16, (int)(voff)[_i], (int)(soff_), 0, 0); } while (0)
; #define PG8_LDA(dst, b, h) do { _Pragma("unroll") for (int m = 0; m < 4; ++m) dst[m] = PG8_LD2(lds + PG8_SA(b, h) + aoff + m * 2048); } while (0)
; #define PG8_LDB(dst, b, h) do { _Pragma("unroll") for (int n = 0; n < 2; ++n) dst[n] = PG8_LD2(lds + PG8_SB(b, h) + boff + n * 2048); } while (0)
; #define PG8_WAIT_V(n) asm volatile("s_waitcnt vmcnt(" #n ")" ::: "memory")
; #define PG8_WAIT_L(n) asm volatile("s_waitcnt lgkmcnt(" #n ")" ::: "memory")
; #define PG8_BAR __builtin_amdgcn_s_barrier()
; #define PG8_SCHED __builtin_amdgcn_sched_barrier(0)
; template <class Epi, class Sched, bool ALIGN_EPI = false, bool SP2 = false, bool FP8 = false>
; __device__ __forceinline__ void gemm_phase(LAS unsigned char* lds, const Gemm g, const Sched& S, const Epi& E, int wbase) {
;     ...
;             PG8_LDB(B0, 0, 0); PG8_LDB(B1, 0, 1); PG8_SCHED; PG8_LDA(At, 0, 0); PG8_STAGE(PG8_SA(1, 1), rAc, a1 + hstep, voffA);
;             PG8_WAIT_V(8); PG8_WAIT_L(0); PG8_BAR; PG8_MMA(0, 0, At, B0); PG8_MMA(0, 1, At, B1); PG8_BAR; PG8_SCHED;
;             PG8_LDA(At, 0, 1); PG8_STAGE(PG8_SB(0, 0), rB2, b2, voffB); PG8_STAGE(PG8_SB(0, 1), rB2, b2 + hstep, voffB); PG8_STAGE(PG8_SA(0, 0), rA2, a2, voffA);
;             PG8_WAIT_V(8); PG8_WAIT_L(0); PG8_BAR; PG8_MMA(1, 0, At, B0); PG8_MMA(1, 1, At, B1); PG8_BAR; PG8_SCHED;
;             PG8_LDB(B0, 1, 0); PG8_LDB(B1, 1, 1); PG8_SCHED; PG8_LDA(At, 1, 0); PG8_STAGE(PG8_SA(0, 1), rA2, a2 + hstep, voffA);
;             PG8_WAIT_V(8); PG8_WAIT_L(0); PG8_BAR; PG8_MMA(0, 0, At, B0); PG8_MMA(0, 1, At, B1); PG8_BAR; PG8_SCHED;
;             PG8_LDA(At, 1, 1); PG8_STAGE(PG8_SB(1, 0), rB2, b3, voffB); PG8_STAGE(PG8_SB(1, 1), rB2, b3 + hstep, voffB); PG8_STAGE(PG8_SA(1, 0), rA2, a3, voffA);
;             PG8_WAIT_V(8); PG8_WAIT_L(0); PG8_BAR; PG8_MMA(1, 0, At, B0); PG8_MMA(1, 1, At, B1); PG8_BAR; PG8_SCHED;
	s_mov_b32 m0, s23
	s_nop 0
	buffer_load_dwordx4 v133, s[4:7], s62 offen lds
	s_mov_b32 m0, s24
	s_nop 0
	buffer_load_dwordx4 v135, s[4:7], s62 offen lds
	v_add_u32_e32 v148, 0x18000, v138
	v_add_u32_e32 v164, 0x1c000, v138
	ds_read_b128 v[128:131], v148
	ds_read_b128 v[140:143], v148 offset:1024
	ds_read_b128 v[144:147], v148 offset:2048
	ds_read_b128 v[148:151], v148 offset:3072
	ds_read_b128 v[152:155], v164
	ds_read_b128 v[156:159], v164 offset:1024
	ds_read_b128 v[160:163], v164 offset:2048
	ds_read_b128 v[164:167], v164 offset:3072
	s_add_i32 s61, s61, s19
	s_mov_b32 m0, s26
	ds_read_b128 v[168:171], v139 offset:32768
	ds_read_b128 v[172:175], v139 offset:33792
	ds_read_b128 v[176:179], v139 offset:34816
	ds_read_b128 v[180:183], v139 offset:35840
	ds_read_b128 v[184:187], v139 offset:36864
	ds_read_b128 v[188:191], v139 offset:37888
	ds_read_b128 v[194:197], v139 offset:38912
	ds_read_b128 v[198:201], v139 offset:39936
	buffer_load_dwordx4 v132, s[36:39], s61 offen lds
	s_mov_b32 m0, s27
	s_nop 0
	buffer_load_dwordx4 v134, s[36:39], s61 offen lds
	s_waitcnt vmcnt(8)
	s_waitcnt lgkmcnt(0)
	s_barrier
	s_setprio 1
	v_mfma_f32_16x16x32_bf16 v[124:127], v[128:131], v[168:171], v[124:127]
	v_mfma_f32_16x16x32_bf16 v[120:123], v[144:147], v[168:171], v[120:123]
	v_mfma_f32_16x16x32_bf16 v[108:111], v[128:131], v[176:179], v[108:111]
	v_mfma_f32_16x16x32_bf16 v[104:107], v[144:147], v[176:179], v[104:107]
	v_mfma_f32_16x16x32_bf16 v[92:95], v[128:131], v[184:187], v[92:95]
	v_mfma_f32_16x16x32_bf16 v[88:91], v[144:147], v[184:187], v[88:91]
	v_mfma_f32_16x16x32_bf16 v[76:79], v[128:131], v[194:197], v[76:79]
	v_mfma_f32_16x16x32_bf16 v[72:75], v[144:147], v[194:197], v[72:75]
	v_mfma_f32_16x16x32_bf16 v[124:127], v[140:143], v[172:175], v[124:127]
	v_mfma_f32_16x16x32_bf16 v[120:123], v[148:151], v[172:175], v[120:123]
	v_mfma_f32_16x16x32_bf16 v[108:111], v[140:143], v[180:183], v[108:111]
	v_mfma_f32_16x16x32_bf16 v[104:107], v[148:151], v[180:183], v[104:107]
	v_mfma_f32_16x16x32_bf16 v[92:95], v[140:143], v[188:191], v[92:95]
	v_mfma_f32_16x16x32_bf16 v[88:91], v[148:151], v[188:191], v[88:91]
	v_mfma_f32_16x16x32_bf16 v[76:79], v[140:143], v[198:201], v[76:79]
	v_mfma_f32_16x16x32_bf16 v[72:75], v[148:151], v[198:201], v[72:75]
	v_mfma_f32_16x16x32_bf16 v[116:119], v[152:155], v[168:171], v[116:119]
	v_mfma_f32_16x16x32_bf16 v[112:115], v[160:163], v[168:171], v[112:115]
	v_mfma_f32_16x16x32_bf16 v[100:103], v[152:155], v[176:179], v[100:103]
	v_mfma_f32_16x16x32_bf16 v[96:99], v[160:163], v[176:179], v[96:99]
	v_mfma_f32_16x16x32_bf16 v[84:87], v[152:155], v[184:187], v[84:87]
	v_mfma_f32_16x16x32_bf16 v[80:83], v[160:163], v[184:187], v[80:83]
	v_mfma_f32_16x16x32_bf16 v[68:71], v[152:155], v[194:197], v[68:71]
	v_mfma_f32_16x16x32_bf16 v[64:67], v[160:163], v[194:197], v[64:67]
	v_mfma_f32_16x16x32_bf16 v[116:119], v[156:159], v[172:175], v[116:119]
	v_mfma_f32_16x16x32_bf16 v[112:115], v[164:167], v[172:175], v[112:115]
	v_mfma_f32_16x16x32_bf16 v[100:103], v[156:159], v[180:183], v[100:103]
	v_mfma_f32_16x16x32_bf16 v[96:99], v[164:167], v[180:183], v[96:99]
	v_mfma_f32_16x16x32_bf16 v[84:87], v[156:159], v[188:191], v[84:87]
	v_mfma_f32_16x16x32_bf16 v[80:83], v[164:167], v[188:191], v[80:83]
	v_mfma_f32_16x16x32_bf16 v[68:71], v[156:159], v[198:201], v[68:71]
	v_mfma_f32_16x16x32_bf16 v[64:67], v[164:167], v[198:201], v[64:67]
	s_setprio 0
	s_barrier
	s_mov_b32 m0, s28
	s_bitset1_b32 s55, 7
	buffer_load_dwordx4 v133, s[4:7], s55 offen lds
	s_mov_b32 m0, s29
	ds_read_b128 v[168:171], v139 offset:49152
	buffer_load_dwordx4 v135, s[4:7], s55 offen lds
	s_add_i32 s55, s55, s19
	s_mov_b32 m0, s33
	ds_read_b128 v[172:175], v139 offset:50176
	buffer_load_dwordx4 v133, s[4:7], s55 offen lds
	s_mov_b32 m0, s34
	ds_read_b128 v[176:179], v139 offset:51200
	buffer_load_dwordx4 v135, s[4:7], s55 offen lds
	s_mov_b32 m0, s30
	ds_read_b128 v[180:183], v139 offset:52224
	buffer_load_dwordx4 v132, s[36:39], s54 offen lds
	s_mov_b32 m0, s31
	ds_read_b128 v[184:187], v139 offset:53248
	buffer_load_dwordx4 v134, s[36:39], s54 offen lds
	ds_read_b128 v[188:191], v139 offset:54272
	ds_read_b128 v[194:197], v139 offset:55296
	ds_read_b128 v[198:201], v139 offset:56320
	s_waitcnt vmcnt(8)
	s_waitcnt lgkmcnt(0)
	s_barrier
	s_setprio 1
	v_mfma_f32_16x16x32_bf16 v[60:63], v[128:131], v[168:171], v[60:63]
	v_mfma_f32_16x16x32_bf16 v[56:59], v[144:147], v[168:171], v[56:59]
	v_mfma_f32_16x16x32_bf16 v[44:47], v[128:131], v[176:179], v[44:47]
	v_mfma_f32_16x16x32_bf16 v[40:43], v[144:147], v[176:179], v[40:43]
	v_mfma_f32_16x16x32_bf16 v[28:31], v[128:131], v[184:187], v[28:31]
	v_mfma_f32_16x16x32_bf16 v[24:27], v[144:147], v[184:187], v[24:27]
	v_mfma_f32_16x16x32_bf16 v[12:15], v[128:131], v[194:197], v[12:15]
	v_mfma_f32_16x16x32_bf16 v[8:11], v[144:147], v[194:197], v[8:11]
	v_mfma_f32_16x16x32_bf16 v[60:63], v[140:143], v[172:175], v[60:63]
	v_mfma_f32_16x16x32_bf16 v[56:59], v[148:151], v[172:175], v[56:59]
	v_mfma_f32_16x16x32_bf16 v[44:47], v[140:143], v[180:183], v[44:47]
	v_mfma_f32_16x16x32_bf16 v[40:43], v[148:151], v[180:183], v[40:43]
	v_mfma_f32_16x16x32_bf16 v[28:31], v[140:143], v[188:191], v[28:31]
	v_mfma_f32_16x16x32_bf16 v[24:27], v[148:151], v[188:191], v[24:27]
	v_mfma_f32_16x16x32_bf16 v[12:15], v[140:143], v[198:201], v[12:15]
	v_mfma_f32_16x16x32_bf16 v[8:11], v[148:151], v[198:201], v[8:11]
	v_mfma_f32_16x16x32_bf16 v[52:55], v[152:155], v[168:171], v[52:55]
	v_mfma_f32_16x16x32_bf16 v[48:51], v[160:163], v[168:171], v[48:51]
	v_mfma_f32_16x16x32_bf16 v[36:39], v[152:155], v[176:179], v[36:39]
	v_mfma_f32_16x16x32_bf16 v[32:35], v[160:163], v[176:179], v[32:35]
	v_mfma_f32_16x16x32_bf16 v[20:23], v[152:155], v[184:187], v[20:23]
	v_mfma_f32_16x16x32_bf16 v[16:19], v[160:163], v[184:187], v[16:19]
	v_mfma_f32_16x16x32_bf16 v[4:7], v[152:155], v[194:197], v[4:7]
	v_mfma_f32_16x16x32_bf16 v[0:3], v[160:163], v[194:197], v[0:3]
	v_mfma_f32_16x16x32_bf16 v[52:55], v[156:159], v[172:175], v[52:55]
	v_mfma_f32_16x16x32_bf16 v[48:51], v[164:167], v[172:175], v[48:51]
	v_mfma_f32_16x16x32_bf16 v[36:39], v[156:159], v[180:183], v[36:39]
	v_mfma_f32_16x16x32_bf16 v[32:35], v[164:167], v[180:183], v[32:35]
	v_mfma_f32_16x16x32_bf16 v[20:23], v[156:159], v[188:191], v[20:23]
	v_mfma_f32_16x16x32_bf16 v[16:19], v[164:167], v[188:191], v[16:19]
	v_mfma_f32_16x16x32_bf16 v[4:7], v[156:159], v[198:201], v[4:7]
	v_mfma_f32_16x16x32_bf16 v[0:3], v[164:167], v[198:201], v[0:3]
	s_setprio 0
	s_barrier
	s_add_i32 s60, s60, 2
	s_addk_i32 s58, 0x100
	s_addk_i32 s59, 0x100
	s_cmp_ge_i32 s60, s35
	s_cbranch_scc0 .LBB0_450

; #define PG8_STAGE(bufoff, rs_, soff_, voff) do { _Pragma("unroll") for (int _i = 0; _i < 2; ++_i) \
;         __builtin_amdgcn_raw_ptr_buffer_load_lds(rs_, (LAS void*)(lds + (bufoff) + ldsw + _i * 8192), 16, (int)(voff)[_i], (int)(soff_), 0, 0); } while (0)
; #define PG8_LDA(dst, b, h) do { _Pragma("unroll") for (int m = 0; m < 4; ++m) dst[m] = PG8_LD2(lds + PG8_SA(b, h) + aoff + m * 2048); } while (0)
; #define PG8_LDB(dst, b, h) do { _Pragma("unroll") for (int n = 0; n < 2; ++n) dst[n] = PG8_LD2(lds + PG8_SB(b, h) + boff + n * 2048); } while (0)
; template <class Epi, class Sched, bool ALIGN_EPI = false, bool SP2 = false, bool FP8 = false>
; __device__ __forceinline__ void gemm_phase(LAS unsigned char* lds, const Gemm g, const Sched& S, const Epi& E, int wbase) {
;     ...
;         for (int t = 0; t < nt; t += 2) {
;             const bool last = (t == nt - 2);
;             const unsigned a1 = cA + (unsigned)(t + 1) * kstep;
;             const unsigned a2 = last ? nA : cA + (unsigned)(t + 2) * kstep, b2 = last ? nB : cB + (unsigned)(t + 2) * kstep; const rsrc_t rA2 = (Sched::TWO && last) ? rAn : rAc, rB2 = (Sched::TWO && last) ? rBn : rBc;
;             const unsigned a3 = a2 + kstep, b3 = b2 + kstep;
;             if (last && has_next) S.a_ready(nxt);
;             if constexpr (SP2) {
;             PG8_LDB(B0, 0, 0); PG8_LDB(B1, 0, 1); PG8_SCHED; PG8_LDA(At, 0, 0); PG8_STAGE(PG8_SA(1, 1), rAc, a1 + hstep, voffA);
;             PG8_WAIT_V(8); PG8_WAIT_L(0); PG8_BAR; PG8_MMA(0, 0, At, B0); PG8_MMA(0, 1, At, B1); PG8_BAR; PG8_SCHED;
;             PG8_LDA(At, 0, 1); PG8_STAGE(PG8_SB(0, 0), rB2, b2, voffB); PG8_STAGE(PG8_SB(0, 1), rB2, b2 + hstep, voffB); PG8_STAGE(PG8_SA(0, 0), rA2, a2, voffA);
;             PG8_WAIT_V(8); PG8_WAIT_L(0); PG8_BAR; PG8_MMA(1, 0, At, B0); PG8_MMA(1, 1, At, B1); PG8_BAR; PG8_SCHED;
;             PG8_LDB(B0, 1, 0); PG8_LDB(B1, 1, 1); PG8_SCHED; PG8_LDA(At, 1, 0); PG8_STAGE(PG8_SA(0, 1), rA2, a2 + hstep, voffA);
;             PG8_WAIT_V(8); PG8_WAIT_L(0); PG8_BAR; PG8_MMA(0, 0, At, B0); PG8_MMA(0, 1, At, B1); PG8_BAR; PG8_SCHED;
;             PG8_LDA(At, 1, 1); PG8_STAGE(PG8_SB(1, 0), rB2, b3, voffB); PG8_STAGE(PG8_SB(1, 1), rB2, b3 + hstep, voffB); PG8_STAGE(PG8_SA(1, 0), rA2, a3, voffA);
;             PG8_WAIT_V(8); PG8_WAIT_L(0); PG8_BAR; PG8_MMA(1, 0, At, B0); PG8_MMA(1, 1, At, B1); PG8_BAR; PG8_SCHED;
.LBB0_813:
	s_add_i32 s20, vcc_hi, 0x80
	v_add_u32_e32 v140, 0x10000, v240
	v_add_u32_e32 v156, 0x14000, v240
	s_cmp_eq_u32 s41, s78
	ds_read_b128 v[128:131], v140
	ds_read_b128 v[132:135], v140 offset:1024
	ds_read_b128 v[136:139], v140 offset:2048
	ds_read_b128 v[140:143], v140 offset:3072
	ds_read_b128 v[144:147], v156
	ds_read_b128 v[148:151], v156 offset:1024
	ds_read_b128 v[152:155], v156 offset:2048
	ds_read_b128 v[156:159], v156 offset:3072
	s_cselect_b64 s[16:17], -1, 0
	s_and_b64 s[18:19], s[16:17], exec
	s_cselect_b32 s68, s67, s20
	s_cselect_b32 s54, vcc_lo, s3
	s_and_b64 s[20:21], s[44:45], s[16:17]
	s_and_b64 s[16:17], s[20:21], exec
	s_cselect_b32 s18, s52, s14
	s_cselect_b32 s19, s53, s15
	s_cselect_b32 s17, s35, s13
	s_cselect_b32 s16, s34, s12
	s_or_b32 s55, s68, 0x80
	s_and_b64 s[20:21], s[20:21], exec
	s_cselect_b32 s23, s53, s31
	s_cselect_b32 s22, s52, s30
	s_cselect_b32 s21, s11, s59
	s_cselect_b32 s20, s10, s58
	s_add_i32 s69, s46, vcc_hi
	s_mov_b32 m0, s61
	ds_read_b128 v[160:163], v241
	ds_read_b128 v[164:167], v241 offset:1024
	ds_read_b128 v[168:171], v241 offset:2048
	ds_read_b128 v[172:175], v241 offset:3072
	ds_read_b128 v[176:179], v241 offset:4096
	ds_read_b128 v[180:183], v241 offset:5120
	ds_read_b128 v[184:187], v241 offset:6144
	ds_read_b128 v[188:191], v241 offset:7168
	buffer_load_dwordx4 v192, s[12:15], s69 offen lds
	s_mov_b32 m0, s62
	s_nop 0
	buffer_load_dwordx4 v236, s[12:15], s69 offen lds
	s_waitcnt vmcnt(8)
	s_waitcnt lgkmcnt(0)
	s_barrier
	s_setprio 1
	v_mfma_f32_16x16x128_f8f6f4 v[124:127], v[128:135], v[160:167], v[124:127]
	v_mfma_f32_16x16x128_f8f6f4 v[120:123], v[136:143], v[160:167], v[120:123]
	v_mfma_f32_16x16x128_f8f6f4 v[116:119], v[128:135], v[168:175], v[116:119]
	v_mfma_f32_16x16x128_f8f6f4 v[112:115], v[136:143], v[168:175], v[112:115]
	v_mfma_f32_16x16x128_f8f6f4 v[108:111], v[128:135], v[176:183], v[108:111]
	v_mfma_f32_16x16x128_f8f6f4 v[104:107], v[136:143], v[176:183], v[104:107]
	v_mfma_f32_16x16x128_f8f6f4 v[100:103], v[128:135], v[184:191], v[100:103]
	v_mfma_f32_16x16x128_f8f6f4 v[96:99], v[136:143], v[184:191], v[96:99]
	v_mfma_f32_16x16x128_f8f6f4 v[194:197], v[144:151], v[160:167], v[92:95]
	v_mfma_f32_16x16x128_f8f6f4 v[160:163], v[152:159], v[160:167], v[88:91]
	v_mfma_f32_16x16x128_f8f6f4 v[164:167], v[144:151], v[168:175], v[84:87]
	v_mfma_f32_16x16x128_f8f6f4 v[168:171], v[152:159], v[168:175], v[80:83]
	v_mfma_f32_16x16x128_f8f6f4 v[172:175], v[144:151], v[176:183], v[76:79]
	v_mfma_f32_16x16x128_f8f6f4 v[176:179], v[152:159], v[176:183], v[72:75]
	v_mfma_f32_16x16x128_f8f6f4 v[180:183], v[144:151], v[184:191], v[68:71]
	v_mfma_f32_16x16x128_f8f6f4 v[184:187], v[152:159], v[184:191], v[64:67]
	s_setprio 0
	s_barrier
	s_mov_b32 m0, s48
	s_nop 3
	buffer_load_dwordx4 v235, s[20:23], s54 offen lds
	s_mov_b32 m0, s56
	ds_read_b128 v[64:67], v241 offset:16384
	s_add_i32 s69, s54, s46
	buffer_load_dwordx4 v237, s[20:23], s54 offen lds
	s_mov_b32 m0, s47
	ds_read_b128 v[68:71], v241 offset:17408
	buffer_load_dwordx4 v192, s[16:19], s68 offen lds
	s_mov_b32 m0, s76
	ds_read_b128 v[72:75], v241 offset:18432
	buffer_load_dwordx4 v236, s[16:19], s68 offen lds
	ds_read_b128 v[76:79], v241 offset:19456
	ds_read_b128 v[80:83], v241 offset:20480
	ds_read_b128 v[84:87], v241 offset:21504
	ds_read_b128 v[88:91], v241 offset:22528
	ds_read_b128 v[92:95], v241 offset:23552
	s_waitcnt vmcnt(6)
	s_waitcnt lgkmcnt(0)
	s_barrier
	s_setprio 1
	v_mfma_f32_16x16x128_f8f6f4 v[60:63], v[128:135], v[64:71], v[60:63]
	v_mfma_f32_16x16x128_f8f6f4 v[56:59], v[136:143], v[64:71], v[56:59]
	v_mfma_f32_16x16x128_f8f6f4 v[52:55], v[128:135], v[72:79], v[52:55]
	v_mfma_f32_16x16x128_f8f6f4 v[48:51], v[136:143], v[72:79], v[48:51]
	v_mfma_f32_16x16x128_f8f6f4 v[188:191], v[128:135], v[80:87], v[44:47]
	v_mfma_f32_16x16x128_f8f6f4 v[198:201], v[136:143], v[80:87], v[40:43]
	v_mfma_f32_16x16x128_f8f6f4 v[202:205], v[128:135], v[88:95], v[36:39]
	v_mfma_f32_16x16x128_f8f6f4 v[206:209], v[136:143], v[88:95], v[32:35]
	v_mfma_f32_16x16x128_f8f6f4 v[210:213], v[144:151], v[64:71], v[28:31]
	v_mfma_f32_16x16x128_f8f6f4 v[214:217], v[152:159], v[64:71], v[24:27]
	v_mfma_f32_16x16x128_f8f6f4 v[218:221], v[144:151], v[72:79], v[20:23]
	v_mfma_f32_16x16x128_f8f6f4 v[226:229], v[152:159], v[72:79], v[16:19]
	v_mfma_f32_16x16x128_f8f6f4 v[242:245], v[144:151], v[80:87], v[12:15]
	v_mfma_f32_16x16x128_f8f6f4 v[246:249], v[152:159], v[80:87], v[8:11]
	v_mfma_f32_16x16x128_f8f6f4 v[250:253], v[144:151], v[88:95], v[4:7]
	v_mfma_f32_16x16x128_f8f6f4 v[230:233], v[152:159], v[88:95], v[0:3]
	s_setprio 0
	s_barrier
; #define PG8_STAGE(bufoff, rs_, soff_, voff) do { _Pragma("unroll") for (int _i = 0; _i < 2; ++_i) \
;         __builtin_amdgcn_raw_ptr_buffer_load_lds(rs_, (LAS void*)(lds + (bufoff) + ldsw + _i * 8192), 16, (int)(voff)[_i], (int)(soff_), 0, 0); } while (0)
; #define PG8_LDA(dst, b, h) do { _Pragma("unroll") for (int m = 0; m < 4; ++m) dst[m] = PG8_LD2(lds + PG8_SA(b, h) + aoff + m * 2048); } while (0)
; #define PG8_LDB(dst, b, h) do { _Pragma("unroll") for (int n = 0; n < 2; ++n) dst[n] = PG8_LD2(lds + PG8_SB(b, h) + boff + n * 2048); } while (0)
; #define PG8_WAIT_V(n) asm volatile("s_waitcnt vmcnt(" #n ")" ::: "memory")
; #define PG8_WAIT_L(n) asm volatile("s_waitcnt lgkmcnt(" #n ")" ::: "memory")
; #define PG8_BAR __builtin_amdgcn_s_barrier()
; #define PG8_SCHED __builtin_amdgcn_sched_barrier(0)
; template <class Epi, class Sched, bool ALIGN_EPI = false, bool SP2 = false, bool FP8 = false>
; __device__ __forceinline__ void gemm_phase(LAS unsigned char* lds, const Gemm g, const Sched& S, const Epi& E, int wbase) {
;     ...
;             PG8_LDB(B0, 0, 0); PG8_LDB(B1, 0, 1); PG8_SCHED; PG8_LDA(At, 0, 0); PG8_STAGE(PG8_SA(1, 1), rAc, a1 + hstep, voffA);
;             PG8_WAIT_V(8); PG8_WAIT_L(0); PG8_BAR; PG8_MMA(0, 0, At, B0); PG8_MMA(0, 1, At, B1); PG8_BAR; PG8_SCHED;
;             PG8_LDA(At, 0, 1); PG8_STAGE(PG8_SB(0, 0), rB2, b2, voffB); PG8_STAGE(PG8_SB(0, 1), rB2, b2 + hstep, voffB); PG8_STAGE(PG8_SA(0, 0), rA2, a2, voffA);
;             PG8_WAIT_V(8); PG8_WAIT_L(0); PG8_BAR; PG8_MMA(1, 0, At, B0); PG8_MMA(1, 1, At, B1); PG8_BAR; PG8_SCHED;
;             PG8_LDB(B0, 1, 0); PG8_LDB(B1, 1, 1); PG8_SCHED; PG8_LDA(At, 1, 0); PG8_STAGE(PG8_SA(0, 1), rA2, a2 + hstep, voffA);
;             PG8_WAIT_V(8); PG8_WAIT_L(0); PG8_BAR; PG8_MMA(0, 0, At, B0); PG8_MMA(0, 1, At, B1); PG8_BAR; PG8_SCHED;
;             PG8_LDA(At, 1, 1); PG8_STAGE(PG8_SB(1, 0), rB2, b3, voffB); PG8_STAGE(PG8_SB(1, 1), rB2, b3 + hstep, voffB); PG8_STAGE(PG8_SA(1, 0), rA2, a3, voffA);
;             PG8_WAIT_V(8); PG8_WAIT_L(0); PG8_BAR; PG8_MMA(1, 0, At, B0); PG8_MMA(1, 1, At, B1); PG8_BAR; PG8_SCHED;
	s_mov_b32 m0, s57
	s_nop 0
	buffer_load_dwordx4 v235, s[20:23], s69 offen lds
	s_mov_b32 m0, s65
	s_nop 0
	buffer_load_dwordx4 v237, s[20:23], s69 offen lds
	s_nop 1
	v_add_u32_e32 v12, 0x18000, v240
	v_add_u32_e32 v16, 0x1c000, v240
	s_nop 0
	ds_read_b128 v[0:3], v12
	ds_read_b128 v[4:7], v12 offset:1024
	ds_read_b128 v[8:11], v12 offset:2048
	ds_read_b128 v[12:15], v12 offset:3072
	ds_read_b128 v[128:131], v16
	ds_read_b128 v[132:135], v16 offset:1024
	ds_read_b128 v[136:139], v16 offset:2048
	ds_read_b128 v[140:143], v16 offset:3072
	s_add_i32 s68, s68, s46
	s_mov_b32 m0, s77
	ds_read_b128 v[16:19], v241 offset:32768
	ds_read_b128 v[20:23], v241 offset:33792
	ds_read_b128 v[24:27], v241 offset:34816
	ds_read_b128 v[28:31], v241 offset:35840
	ds_read_b128 v[32:35], v241 offset:36864
	ds_read_b128 v[36:39], v241 offset:37888
	ds_read_b128 v[40:43], v241 offset:38912
	ds_read_b128 v[44:47], v241 offset:39936
	buffer_load_dwordx4 v192, s[16:19], s68 offen lds
	s_mov_b32 m0, s79
	s_nop 0
	buffer_load_dwordx4 v236, s[16:19], s68 offen lds
	s_waitcnt vmcnt(8)
	s_waitcnt lgkmcnt(0)
	s_barrier
	s_setprio 1
	v_mfma_f32_16x16x128_f8f6f4 v[124:127], v[0:7], v[16:23], v[124:127]
	v_mfma_f32_16x16x128_f8f6f4 v[120:123], v[8:15], v[16:23], v[120:123]
	v_mfma_f32_16x16x128_f8f6f4 v[116:119], v[0:7], v[24:31], v[116:119]
	v_mfma_f32_16x16x128_f8f6f4 v[112:115], v[8:15], v[24:31], v[112:115]
	v_mfma_f32_16x16x128_f8f6f4 v[108:111], v[0:7], v[32:39], v[108:111]
	v_mfma_f32_16x16x128_f8f6f4 v[104:107], v[8:15], v[32:39], v[104:107]
	v_mfma_f32_16x16x128_f8f6f4 v[100:103], v[0:7], v[40:47], v[100:103]
	v_mfma_f32_16x16x128_f8f6f4 v[96:99], v[8:15], v[40:47], v[96:99]
	v_mfma_f32_16x16x128_f8f6f4 v[92:95], v[128:135], v[16:23], v[194:197]
	v_mfma_f32_16x16x128_f8f6f4 v[88:91], v[136:143], v[16:23], v[160:163]
	v_mfma_f32_16x16x128_f8f6f4 v[84:87], v[128:135], v[24:31], v[164:167]
	v_mfma_f32_16x16x128_f8f6f4 v[80:83], v[136:143], v[24:31], v[168:171]
	v_mfma_f32_16x16x128_f8f6f4 v[76:79], v[128:135], v[32:39], v[172:175]
	v_mfma_f32_16x16x128_f8f6f4 v[72:75], v[136:143], v[32:39], v[176:179]
	v_mfma_f32_16x16x128_f8f6f4 v[68:71], v[128:135], v[40:47], v[180:183]
	v_mfma_f32_16x16x128_f8f6f4 v[64:67], v[136:143], v[40:47], v[184:187]
	s_setprio 0
	s_barrier
	s_mov_b32 m0, s84
	s_bitset1_b32 s54, 7
	buffer_load_dwordx4 v235, s[20:23], s54 offen lds
	s_mov_b32 m0, s85
	ds_read_b128 v[16:19], v241 offset:49152
	buffer_load_dwordx4 v237, s[20:23], s54 offen lds
	s_add_i32 s54, s54, s46
	s_mov_b32 m0, s96
	ds_read_b128 v[20:23], v241 offset:50176
	buffer_load_dwordx4 v235, s[20:23], s54 offen lds
	s_mov_b32 m0, s97
	ds_read_b128 v[144:147], v241 offset:51200
	buffer_load_dwordx4 v237, s[20:23], s54 offen lds
	s_mov_b32 m0, s94
	ds_read_b128 v[148:151], v241 offset:52224
	buffer_load_dwordx4 v192, s[16:19], s55 offen lds
	s_mov_b32 m0, s95
	ds_read_b128 v[152:155], v241 offset:53248
	buffer_load_dwordx4 v236, s[16:19], s55 offen lds
	ds_read_b128 v[156:159], v241 offset:54272
	ds_read_b128 v[160:163], v241 offset:55296
	ds_read_b128 v[164:167], v241 offset:56320
	s_waitcnt vmcnt(8)
	s_waitcnt lgkmcnt(0)
	s_barrier
	s_setprio 1
	v_mfma_f32_16x16x128_f8f6f4 v[60:63], v[0:7], v[16:23], v[60:63]
	v_mfma_f32_16x16x128_f8f6f4 v[56:59], v[8:15], v[16:23], v[56:59]
	v_mfma_f32_16x16x128_f8f6f4 v[52:55], v[0:7], v[144:151], v[52:55]
	v_mfma_f32_16x16x128_f8f6f4 v[48:51], v[8:15], v[144:151], v[48:51]
	v_mfma_f32_16x16x128_f8f6f4 v[44:47], v[0:7], v[152:159], v[188:191]
	v_mfma_f32_16x16x128_f8f6f4 v[40:43], v[8:15], v[152:159], v[198:201]
	v_mfma_f32_16x16x128_f8f6f4 v[36:39], v[0:7], v[160:167], v[202:205]
	v_mfma_f32_16x16x128_f8f6f4 v[32:35], v[8:15], v[160:167], v[206:209]
	v_mfma_f32_16x16x128_f8f6f4 v[28:31], v[128:135], v[16:23], v[210:213]
	v_mfma_f32_16x16x128_f8f6f4 v[24:27], v[136:143], v[16:23], v[214:217]
	v_mfma_f32_16x16x128_f8f6f4 v[20:23], v[128:135], v[144:151], v[218:221]
	v_mfma_f32_16x16x128_f8f6f4 v[16:19], v[136:143], v[144:151], v[226:229]
	v_mfma_f32_16x16x128_f8f6f4 v[12:15], v[128:135], v[152:159], v[242:245]
	v_mfma_f32_16x16x128_f8f6f4 v[8:11], v[136:143], v[152:159], v[246:249]
	v_mfma_f32_16x16x128_f8f6f4 v[4:7], v[128:135], v[160:167], v[250:253]
	v_mfma_f32_16x16x128_f8f6f4 v[0:3], v[136:143], v[160:167], v[230:233]
	s_setprio 0
	s_barrier
	s_add_i32 s78, s78, 2
	s_addk_i32 vcc_hi, 0x100
	s_addk_i32 s3, 0x100
	s_cmp_ge_i32 s78, s60
	s_cbranch_scc0 .LBB0_813
	v_readlane_b32 s68, v255, 22
	v_readlane_b32 s54, v255, 25
	v_readlane_b32 s69, v255, 23
	v_readlane_b32 s55, v255, 26
	v_mov_b32_e32 v230, v193
	v_mov_b32_e32 v231, v222

; #define PG8_STAGE(bufoff, rs_, soff_, voff) do { _Pragma("unroll") for (int _i = 0; _i < 2; ++_i) \
;         __builtin_amdgcn_raw_ptr_buffer_load_lds(rs_, (LAS void*)(lds + (bufoff) + ldsw + _i * 8192), 16, (int)(voff)[_i], (int)(soff_), 0, 0); } while (0)
; #define PG8_LDA(dst, b, h) do { _Pragma("unroll") for (int m = 0; m < 4; ++m) dst[m] = PG8_LD2(lds + PG8_SA(b, h) + aoff + m * 2048); } while (0)
; #define PG8_LDB(dst, b, h) do { _Pragma("unroll") for (int n = 0; n < 2; ++n) dst[n] = PG8_LD2(lds + PG8_SB(b, h) + boff + n * 2048); } while (0)
; template <class Epi, class Sched, bool ALIGN_EPI = false, bool SP2 = false, bool FP8 = false>
; __device__ __forceinline__ void gemm_phase(LAS unsigned char* lds, const Gemm g, const Sched& S, const Epi& E, int wbase) {
;     ...
;         for (int t = 0; t < nt; t += 2) {
;             const bool last = (t == nt - 2);
;             const unsigned a1 = cA + (unsigned)(t + 1) * kstep;
;             const unsigned a2 = last ? nA : cA + (unsigned)(t + 2) * kstep, b2 = last ? nB : cB + (unsigned)(t + 2) * kstep; const rsrc_t rA2 = (Sched::TWO && last) ? rAn : rAc, rB2 = (Sched::TWO && last) ? rBn : rBc;
;             const unsigned a3 = a2 + kstep, b3 = b2 + kstep;
;             if (last && has_next) S.a_ready(nxt);
;             if constexpr (SP2) {
;             PG8_LDB(B0, 0, 0); PG8_LDB(B1, 0, 1); PG8_SCHED; PG8_LDA(At, 0, 0); PG8_STAGE(PG8_SA(1, 1), rAc, a1 + hstep, voffA);
;             PG8_WAIT_V(8); PG8_WAIT_L(0); PG8_BAR; PG8_MMA(0, 0, At, B0); PG8_MMA(0, 1, At, B1); PG8_BAR; PG8_SCHED;
;             PG8_LDA(At, 0, 1); PG8_STAGE(PG8_SB(0, 0), rB2, b2, voffB); PG8_STAGE(PG8_SB(0, 1), rB2, b2 + hstep, voffB); PG8_STAGE(PG8_SA(0, 0), rA2, a2, voffA);
;             PG8_WAIT_V(8); PG8_WAIT_L(0); PG8_BAR; PG8_MMA(1, 0, At, B0); PG8_MMA(1, 1, At, B1); PG8_BAR; PG8_SCHED;
;             PG8_LDB(B0, 1, 0); PG8_LDB(B1, 1, 1); PG8_SCHED; PG8_LDA(At, 1, 0); PG8_STAGE(PG8_SA(0, 1), rA2, a2 + hstep, voffA);
;             PG8_WAIT_V(8); PG8_WAIT_L(0); PG8_BAR; PG8_MMA(0, 0, At, B0); PG8_MMA(0, 1, At, B1); PG8_BAR; PG8_SCHED;
;             PG8_LDA(At, 1, 1); PG8_STAGE(PG8_SB(1, 0), rB2, b3, voffB); PG8_STAGE(PG8_SB(1, 1), rB2, b3 + hstep, voffB); PG8_STAGE(PG8_SA(1, 0), rA2, a3, voffA);
;             PG8_WAIT_V(8); PG8_WAIT_L(0); PG8_BAR; PG8_MMA(1, 0, At, B0); PG8_MMA(1, 1, At, B1); PG8_BAR; PG8_SCHED;
.LBB0_847:
	s_add_i32 s20, vcc_lo, 0x80
	v_add_u32_e32 v140, 0x10000, v238
	v_add_u32_e32 v156, 0x14000, v238
	s_cmp_eq_u32 s88, s85
	ds_read_b128 v[128:131], v140
	ds_read_b128 v[132:135], v140 offset:1024
	ds_read_b128 v[136:139], v140 offset:2048
	ds_read_b128 v[140:143], v140 offset:3072
	ds_read_b128 v[144:147], v156
	ds_read_b128 v[148:151], v156 offset:1024
	ds_read_b128 v[152:155], v156 offset:2048
	ds_read_b128 v[156:159], v156 offset:3072
	s_cselect_b64 s[16:17], -1, 0
	s_and_b64 s[18:19], s[16:17], exec
	s_cselect_b32 s68, s67, s20
	s_cselect_b32 s54, s78, vcc_hi
	s_and_b64 s[20:21], s[58:59], s[16:17]
	s_and_b64 s[16:17], s[20:21], exec
	s_cselect_b32 s18, s30, s14
	s_cselect_b32 s19, s31, s15
	s_cselect_b32 s17, s35, s13
	s_cselect_b32 s16, s34, s12
	s_or_b32 s55, s68, 0x80
	s_and_b64 s[20:21], s[20:21], exec
	s_cselect_b32 s23, s31, s53
	s_cselect_b32 s22, s30, s52
	s_cselect_b32 s21, s45, s11
	s_cselect_b32 s20, s44, s10
	s_add_i32 s69, s41, vcc_lo
	s_mov_b32 m0, s89
	ds_read_b128 v[160:163], v239
	ds_read_b128 v[164:167], v239 offset:1024
	ds_read_b128 v[168:171], v239 offset:2048
	ds_read_b128 v[172:175], v239 offset:3072
	ds_read_b128 v[176:179], v239 offset:4096
	ds_read_b128 v[180:183], v239 offset:5120
	ds_read_b128 v[184:187], v239 offset:6144
	ds_read_b128 v[188:191], v239 offset:7168
	buffer_load_dwordx4 v192, s[12:15], s69 offen lds
	s_mov_b32 m0, s92
	s_nop 0
	buffer_load_dwordx4 v223, s[12:15], s69 offen lds
	s_waitcnt vmcnt(8)
	s_waitcnt lgkmcnt(0)
	s_barrier
	s_setprio 1
	v_mfma_f32_16x16x32_bf16 v[124:127], v[128:131], v[160:163], v[124:127]
	v_mfma_f32_16x16x32_bf16 v[120:123], v[136:139], v[160:163], v[120:123]
	v_mfma_f32_16x16x32_bf16 v[116:119], v[128:131], v[168:171], v[116:119]
	v_mfma_f32_16x16x32_bf16 v[112:115], v[136:139], v[168:171], v[112:115]
	v_mfma_f32_16x16x32_bf16 v[108:111], v[128:131], v[176:179], v[108:111]
	v_mfma_f32_16x16x32_bf16 v[104:107], v[136:139], v[176:179], v[104:107]
	v_mfma_f32_16x16x32_bf16 v[100:103], v[128:131], v[184:187], v[100:103]
	v_mfma_f32_16x16x32_bf16 v[96:99], v[136:139], v[184:187], v[96:99]
	v_mfma_f32_16x16x32_bf16 v[124:127], v[132:135], v[164:167], v[124:127]
	v_mfma_f32_16x16x32_bf16 v[120:123], v[140:143], v[164:167], v[120:123]
	v_mfma_f32_16x16x32_bf16 v[116:119], v[132:135], v[172:175], v[116:119]
	v_mfma_f32_16x16x32_bf16 v[112:115], v[140:143], v[172:175], v[112:115]
	v_mfma_f32_16x16x32_bf16 v[108:111], v[132:135], v[180:183], v[108:111]
	v_mfma_f32_16x16x32_bf16 v[104:107], v[140:143], v[180:183], v[104:107]
	v_mfma_f32_16x16x32_bf16 v[100:103], v[132:135], v[188:191], v[100:103]
	v_mfma_f32_16x16x32_bf16 v[96:99], v[140:143], v[188:191], v[96:99]
	v_mfma_f32_16x16x32_bf16 v[92:95], v[144:147], v[160:163], v[92:95]
	v_mfma_f32_16x16x32_bf16 v[88:91], v[152:155], v[160:163], v[88:91]
	v_mfma_f32_16x16x32_bf16 v[84:87], v[144:147], v[168:171], v[84:87]
	v_mfma_f32_16x16x32_bf16 v[80:83], v[152:155], v[168:171], v[80:83]
	v_mfma_f32_16x16x32_bf16 v[76:79], v[144:147], v[176:179], v[76:79]
	v_mfma_f32_16x16x32_bf16 v[72:75], v[152:155], v[176:179], v[72:75]
	v_mfma_f32_16x16x32_bf16 v[68:71], v[144:147], v[184:187], v[68:71]
	v_mfma_f32_16x16x32_bf16 v[64:67], v[152:155], v[184:187], v[64:67]
	v_mfma_f32_16x16x32_bf16 v[92:95], v[148:151], v[164:167], v[92:95]
	v_mfma_f32_16x16x32_bf16 v[88:91], v[156:159], v[164:167], v[88:91]
	v_mfma_f32_16x16x32_bf16 v[84:87], v[148:151], v[172:175], v[84:87]
	v_mfma_f32_16x16x32_bf16 v[80:83], v[156:159], v[172:175], v[80:83]
	v_mfma_f32_16x16x32_bf16 v[76:79], v[148:151], v[180:183], v[76:79]
	v_mfma_f32_16x16x32_bf16 v[72:75], v[156:159], v[180:183], v[72:75]
	v_mfma_f32_16x16x32_bf16 v[68:71], v[148:151], v[188:191], v[68:71]
	v_mfma_f32_16x16x32_bf16 v[64:67], v[156:159], v[188:191], v[64:67]
	s_setprio 0
	s_barrier
	s_mov_b32 m0, s43
	ds_read_b128 v[160:163], v239 offset:16384
	buffer_load_dwordx4 v222, s[20:23], s54 offen lds
	s_mov_b32 m0, s46
	ds_read_b128 v[164:167], v239 offset:17408
	s_add_i32 s69, s54, s41
	buffer_load_dwordx4 v235, s[20:23], s54 offen lds
	s_mov_b32 m0, s42
	ds_read_b128 v[168:171], v239 offset:18432
	buffer_load_dwordx4 v192, s[16:19], s68 offen lds
	s_mov_b32 m0, s56
	ds_read_b128 v[172:175], v239 offset:19456
	buffer_load_dwordx4 v223, s[16:19], s68 offen lds
	ds_read_b128 v[176:179], v239 offset:20480
	ds_read_b128 v[180:183], v239 offset:21504
	ds_read_b128 v[184:187], v239 offset:22528
	ds_read_b128 v[188:191], v239 offset:23552
	s_waitcnt vmcnt(6)
	s_waitcnt lgkmcnt(0)
	s_barrier
	s_setprio 1
	v_mfma_f32_16x16x32_bf16 v[60:63], v[128:131], v[160:163], v[60:63]
	v_mfma_f32_16x16x32_bf16 v[56:59], v[136:139], v[160:163], v[56:59]
	v_mfma_f32_16x16x32_bf16 v[52:55], v[128:131], v[168:171], v[52:55]
	v_mfma_f32_16x16x32_bf16 v[48:51], v[136:139], v[168:171], v[48:51]
	v_mfma_f32_16x16x32_bf16 v[44:47], v[128:131], v[176:179], v[44:47]
	v_mfma_f32_16x16x32_bf16 v[40:43], v[136:139], v[176:179], v[40:43]
	v_mfma_f32_16x16x32_bf16 v[36:39], v[128:131], v[184:187], v[36:39]
	v_mfma_f32_16x16x32_bf16 v[32:35], v[136:139], v[184:187], v[32:35]
	v_mfma_f32_16x16x32_bf16 v[60:63], v[132:135], v[164:167], v[60:63]
	v_mfma_f32_16x16x32_bf16 v[56:59], v[140:143], v[164:167], v[56:59]
	v_mfma_f32_16x16x32_bf16 v[52:55], v[132:135], v[172:175], v[52:55]
	v_mfma_f32_16x16x32_bf16 v[48:51], v[140:143], v[172:175], v[48:51]
	v_mfma_f32_16x16x32_bf16 v[44:47], v[132:135], v[180:183], v[44:47]
	v_mfma_f32_16x16x32_bf16 v[40:43], v[140:143], v[180:183], v[40:43]
	v_mfma_f32_16x16x32_bf16 v[36:39], v[132:135], v[188:191], v[36:39]
	v_mfma_f32_16x16x32_bf16 v[32:35], v[140:143], v[188:191], v[32:35]
	v_mfma_f32_16x16x32_bf16 v[28:31], v[144:147], v[160:163], v[28:31]
	v_mfma_f32_16x16x32_bf16 v[24:27], v[152:155], v[160:163], v[24:27]
	v_mfma_f32_16x16x32_bf16 v[20:23], v[144:147], v[168:171], v[20:23]
	v_mfma_f32_16x16x32_bf16 v[16:19], v[152:155], v[168:171], v[16:19]
	v_mfma_f32_16x16x32_bf16 v[12:15], v[144:147], v[176:179], v[12:15]
	v_mfma_f32_16x16x32_bf16 v[8:11], v[152:155], v[176:179], v[8:11]
	v_mfma_f32_16x16x32_bf16 v[4:7], v[144:147], v[184:187], v[4:7]
	v_mfma_f32_16x16x32_bf16 v[0:3], v[152:155], v[184:187], v[0:3]
	v_mfma_f32_16x16x32_bf16 v[28:31], v[148:151], v[164:167], v[28:31]
	v_mfma_f32_16x16x32_bf16 v[24:27], v[156:159], v[164:167], v[24:27]
	v_mfma_f32_16x16x32_bf16 v[20:23], v[148:151], v[172:175], v[20:23]
	v_mfma_f32_16x16x32_bf16 v[16:19], v[156:159], v[172:175], v[16:19]
	v_mfma_f32_16x16x32_bf16 v[12:15], v[148:151], v[180:183], v[12:15]
	v_mfma_f32_16x16x32_bf16 v[8:11], v[156:159], v[180:183], v[8:11]
	v_mfma_f32_16x16x32_bf16 v[4:7], v[148:151], v[188:191], v[4:7]
	v_mfma_f32_16x16x32_bf16 v[0:3], v[156:159], v[188:191], v[0:3]
	s_setprio 0
	s_barrier
; #define PG8_STAGE(bufoff, rs_, soff_, voff) do { _Pragma("unroll") for (int _i = 0; _i < 2; ++_i) \
;         __builtin_amdgcn_raw_ptr_buffer_load_lds(rs_, (LAS void*)(lds + (bufoff) + ldsw + _i * 8192), 16, (int)(voff)[_i], (int)(soff_), 0, 0); } while (0)
; #define PG8_LDA(dst, b, h) do { _Pragma("unroll") for (int m = 0; m < 4; ++m) dst[m] = PG8_LD2(lds + PG8_SA(b, h) + aoff + m * 2048); } while (0)
; #define PG8_LDB(dst, b, h) do { _Pragma("unroll") for (int n = 0; n < 2; ++n) dst[n] = PG8_LD2(lds + PG8_SB(b, h) + boff + n * 2048); } while (0)
; #define PG8_WAIT_V(n) asm volatile("s_waitcnt vmcnt(" #n ")" ::: "memory")
; #define PG8_WAIT_L(n) asm volatile("s_waitcnt lgkmcnt(" #n ")" ::: "memory")
; #define PG8_BAR __builtin_amdgcn_s_barrier()
; #define PG8_SCHED __builtin_amdgcn_sched_barrier(0)
; template <class Epi, class Sched, bool ALIGN_EPI = false, bool SP2 = false, bool FP8 = false>
; __device__ __forceinline__ void gemm_phase(LAS unsigned char* lds, const Gemm g, const Sched& S, const Epi& E, int wbase) {
;     ...
;             PG8_LDB(B0, 0, 0); PG8_LDB(B1, 0, 1); PG8_SCHED; PG8_LDA(At, 0, 0); PG8_STAGE(PG8_SA(1, 1), rAc, a1 + hstep, voffA);
;             PG8_WAIT_V(8); PG8_WAIT_L(0); PG8_BAR; PG8_MMA(0, 0, At, B0); PG8_MMA(0, 1, At, B1); PG8_BAR; PG8_SCHED;
;             PG8_LDA(At, 0, 1); PG8_STAGE(PG8_SB(0, 0), rB2, b2, voffB); PG8_STAGE(PG8_SB(0, 1), rB2, b2 + hstep, voffB); PG8_STAGE(PG8_SA(0, 0), rA2, a2, voffA);
;             PG8_WAIT_V(8); PG8_WAIT_L(0); PG8_BAR; PG8_MMA(1, 0, At, B0); PG8_MMA(1, 1, At, B1); PG8_BAR; PG8_SCHED;
;             PG8_LDB(B0, 1, 0); PG8_LDB(B1, 1, 1); PG8_SCHED; PG8_LDA(At, 1, 0); PG8_STAGE(PG8_SA(0, 1), rA2, a2 + hstep, voffA);
;             PG8_WAIT_V(8); PG8_WAIT_L(0); PG8_BAR; PG8_MMA(0, 0, At, B0); PG8_MMA(0, 1, At, B1); PG8_BAR; PG8_SCHED;
;             PG8_LDA(At, 1, 1); PG8_STAGE(PG8_SB(1, 0), rB2, b3, voffB); PG8_STAGE(PG8_SB(1, 1), rB2, b3 + hstep, voffB); PG8_STAGE(PG8_SA(1, 0), rA2, a3, voffA);
;             PG8_WAIT_V(8); PG8_WAIT_L(0); PG8_BAR; PG8_MMA(1, 0, At, B0); PG8_MMA(1, 1, At, B1); PG8_BAR; PG8_SCHED;
	s_mov_b32 m0, s47
	s_nop 0
	buffer_load_dwordx4 v222, s[20:23], s69 offen lds
	s_mov_b32 m0, s48
	s_nop 0
	buffer_load_dwordx4 v235, s[20:23], s69 offen lds
	v_add_u32_e32 v140, 0x18000, v238
	v_add_u32_e32 v156, 0x1c000, v238
	ds_read_b128 v[128:131], v140
	ds_read_b128 v[132:135], v140 offset:1024
	ds_read_b128 v[136:139], v140 offset:2048
	ds_read_b128 v[140:143], v140 offset:3072
	ds_read_b128 v[144:147], v156
	ds_read_b128 v[148:151], v156 offset:1024
	ds_read_b128 v[152:155], v156 offset:2048
	ds_read_b128 v[156:159], v156 offset:3072
	s_add_i32 s68, s68, s41
	s_mov_b32 m0, s57
	ds_read_b128 v[160:163], v239 offset:32768
	ds_read_b128 v[164:167], v239 offset:33792
	ds_read_b128 v[168:171], v239 offset:34816
	ds_read_b128 v[172:175], v239 offset:35840
	ds_read_b128 v[176:179], v239 offset:36864
	ds_read_b128 v[180:183], v239 offset:37888
	ds_read_b128 v[184:187], v239 offset:38912
	ds_read_b128 v[188:191], v239 offset:39936
	buffer_load_dwordx4 v192, s[16:19], s68 offen lds
	s_mov_b32 m0, s60
	s_nop 0
	buffer_load_dwordx4 v223, s[16:19], s68 offen lds
	s_waitcnt vmcnt(8)
	s_waitcnt lgkmcnt(0)
	s_barrier
	s_setprio 1
	v_mfma_f32_16x16x32_bf16 v[124:127], v[128:131], v[160:163], v[124:127]
	v_mfma_f32_16x16x32_bf16 v[120:123], v[136:139], v[160:163], v[120:123]
	v_mfma_f32_16x16x32_bf16 v[116:119], v[128:131], v[168:171], v[116:119]
	v_mfma_f32_16x16x32_bf16 v[112:115], v[136:139], v[168:171], v[112:115]
	v_mfma_f32_16x16x32_bf16 v[108:111], v[128:131], v[176:179], v[108:111]
	v_mfma_f32_16x16x32_bf16 v[104:107], v[136:139], v[176:179], v[104:107]
	v_mfma_f32_16x16x32_bf16 v[100:103], v[128:131], v[184:187], v[100:103]
	v_mfma_f32_16x16x32_bf16 v[96:99], v[136:139], v[184:187], v[96:99]
	v_mfma_f32_16x16x32_bf16 v[124:127], v[132:135], v[164:167], v[124:127]
	v_mfma_f32_16x16x32_bf16 v[120:123], v[140:143], v[164:167], v[120:123]
	v_mfma_f32_16x16x32_bf16 v[116:119], v[132:135], v[172:175], v[116:119]
	v_mfma_f32_16x16x32_bf16 v[112:115], v[140:143], v[172:175], v[112:115]
	v_mfma_f32_16x16x32_bf16 v[108:111], v[132:135], v[180:183], v[108:111]
	v_mfma_f32_16x16x32_bf16 v[104:107], v[140:143], v[180:183], v[104:107]
	v_mfma_f32_16x16x32_bf16 v[100:103], v[132:135], v[188:191], v[100:103]
	v_mfma_f32_16x16x32_bf16 v[96:99], v[140:143], v[188:191], v[96:99]
	v_mfma_f32_16x16x32_bf16 v[92:95], v[144:147], v[160:163], v[92:95]
	v_mfma_f32_16x16x32_bf16 v[88:91], v[152:155], v[160:163], v[88:91]
	v_mfma_f32_16x16x32_bf16 v[84:87], v[144:147], v[168:171], v[84:87]
	v_mfma_f32_16x16x32_bf16 v[80:83], v[152:155], v[168:171], v[80:83]
	v_mfma_f32_16x16x32_bf16 v[76:79], v[144:147], v[176:179], v[76:79]
	v_mfma_f32_16x16x32_bf16 v[72:75], v[152:155], v[176:179], v[72:75]
	v_mfma_f32_16x16x32_bf16 v[68:71], v[144:147], v[184:187], v[68:71]
	v_mfma_f32_16x16x32_bf16 v[64:67], v[152:155], v[184:187], v[64:67]
	v_mfma_f32_16x16x32_bf16 v[92:95], v[148:151], v[164:167], v[92:95]
	v_mfma_f32_16x16x32_bf16 v[88:91], v[156:159], v[164:167], v[88:91]
	v_mfma_f32_16x16x32_bf16 v[84:87], v[148:151], v[172:175], v[84:87]
	v_mfma_f32_16x16x32_bf16 v[80:83], v[156:159], v[172:175], v[80:83]
	v_mfma_f32_16x16x32_bf16 v[76:79], v[148:151], v[180:183], v[76:79]
	v_mfma_f32_16x16x32_bf16 v[72:75], v[156:159], v[180:183], v[72:75]
	v_mfma_f32_16x16x32_bf16 v[68:71], v[148:151], v[188:191], v[68:71]
	v_mfma_f32_16x16x32_bf16 v[64:67], v[156:159], v[188:191], v[64:67]
	s_setprio 0
	s_barrier
	s_mov_b32 m0, s63
	s_bitset1_b32 s54, 7
	buffer_load_dwordx4 v222, s[20:23], s54 offen lds
	s_mov_b32 m0, s65
	ds_read_b128 v[160:163], v239 offset:49152
	buffer_load_dwordx4 v235, s[20:23], s54 offen lds
	s_add_i32 s54, s54, s41
	s_mov_b32 m0, s79
	ds_read_b128 v[164:167], v239 offset:50176
	buffer_load_dwordx4 v222, s[20:23], s54 offen lds
	s_mov_b32 m0, s80
	ds_read_b128 v[168:171], v239 offset:51200
	buffer_load_dwordx4 v235, s[20:23], s54 offen lds
	s_mov_b32 m0, s76
	ds_read_b128 v[172:175], v239 offset:52224
	buffer_load_dwordx4 v192, s[16:19], s55 offen lds
	s_mov_b32 m0, s77
	ds_read_b128 v[176:179], v239 offset:53248
	buffer_load_dwordx4 v223, s[16:19], s55 offen lds
	ds_read_b128 v[180:183], v239 offset:54272
	ds_read_b128 v[184:187], v239 offset:55296
	ds_read_b128 v[188:191], v239 offset:56320
	s_waitcnt vmcnt(8)
	s_waitcnt lgkmcnt(0)
	s_barrier
	s_setprio 1
	v_mfma_f32_16x16x32_bf16 v[60:63], v[128:131], v[160:163], v[60:63]
	v_mfma_f32_16x16x32_bf16 v[56:59], v[136:139], v[160:163], v[56:59]
	v_mfma_f32_16x16x32_bf16 v[52:55], v[128:131], v[168:171], v[52:55]
	v_mfma_f32_16x16x32_bf16 v[48:51], v[136:139], v[168:171], v[48:51]
	v_mfma_f32_16x16x32_bf16 v[44:47], v[128:131], v[176:179], v[44:47]
	v_mfma_f32_16x16x32_bf16 v[40:43], v[136:139], v[176:179], v[40:43]
	v_mfma_f32_16x16x32_bf16 v[36:39], v[128:131], v[184:187], v[36:39]
	v_mfma_f32_16x16x32_bf16 v[32:35], v[136:139], v[184:187], v[32:35]
	v_mfma_f32_16x16x32_bf16 v[60:63], v[132:135], v[164:167], v[60:63]
	v_mfma_f32_16x16x32_bf16 v[56:59], v[140:143], v[164:167], v[56:59]
	v_mfma_f32_16x16x32_bf16 v[52:55], v[132:135], v[172:175], v[52:55]
	v_mfma_f32_16x16x32_bf16 v[48:51], v[140:143], v[172:175], v[48:51]
	v_mfma_f32_16x16x32_bf16 v[44:47], v[132:135], v[180:183], v[44:47]
	v_mfma_f32_16x16x32_bf16 v[40:43], v[140:143], v[180:183], v[40:43]
	v_mfma_f32_16x16x32_bf16 v[36:39], v[132:135], v[188:191], v[36:39]
	v_mfma_f32_16x16x32_bf16 v[32:35], v[140:143], v[188:191], v[32:35]
	v_mfma_f32_16x16x32_bf16 v[28:31], v[144:147], v[160:163], v[28:31]
	v_mfma_f32_16x16x32_bf16 v[24:27], v[152:155], v[160:163], v[24:27]
	v_mfma_f32_16x16x32_bf16 v[20:23], v[144:147], v[168:171], v[20:23]
	v_mfma_f32_16x16x32_bf16 v[16:19], v[152:155], v[168:171], v[16:19]
	v_mfma_f32_16x16x32_bf16 v[12:15], v[144:147], v[176:179], v[12:15]
	v_mfma_f32_16x16x32_bf16 v[8:11], v[152:155], v[176:179], v[8:11]
	v_mfma_f32_16x16x32_bf16 v[4:7], v[144:147], v[184:187], v[4:7]
	v_mfma_f32_16x16x32_bf16 v[0:3], v[152:155], v[184:187], v[0:3]
	v_mfma_f32_16x16x32_bf16 v[28:31], v[148:151], v[164:167], v[28:31]
	v_mfma_f32_16x16x32_bf16 v[24:27], v[156:159], v[164:167], v[24:27]
	v_mfma_f32_16x16x32_bf16 v[20:23], v[148:151], v[172:175], v[20:23]
	v_mfma_f32_16x16x32_bf16 v[16:19], v[156:159], v[172:175], v[16:19]
	v_mfma_f32_16x16x32_bf16 v[12:15], v[148:151], v[180:183], v[12:15]
	v_mfma_f32_16x16x32_bf16 v[8:11], v[156:159], v[180:183], v[8:11]
	v_mfma_f32_16x16x32_bf16 v[4:7], v[148:151], v[188:191], v[4:7]
	v_mfma_f32_16x16x32_bf16 v[0:3], v[156:159], v[188:191], v[0:3]
	s_setprio 0
	s_barrier
	s_add_i32 s85, s85, 2
	s_addk_i32 vcc_lo, 0x100
	s_addk_i32 vcc_hi, 0x100
	s_cmp_ge_i32 s85, s81
	s_cbranch_scc0 .LBB0_847
	v_readlane_b32 s68, v255, 22
	v_readlane_b32 s54, v255, 25
	v_readlane_b32 s69, v255, 23
	v_readlane_b32 s55, v255, 26

;     __device__ __forceinline__ unsigned a_off(const Unit& u, const Gemm& g) const { return (unsigned)u.pm * (unsigned)(BM * 2) * (unsigned)g.K; }
; template <class Epi, class Sched, bool ALIGN_EPI = false, bool SP2 = false, bool FP8 = false>
; __device__ __forceinline__ void gemm_phase(LAS unsigned char* lds, const Gemm g, const Sched& S, const Epi& E, int wbase) {
;     ...
;         const bool has_next = S.next(ui + 1, nxt);
;         const unsigned nA = has_next ? S.a_off(nxt, g) : cA, nB = has_next ? S.b_off(nxt, g) : cB;
;         const rsrc_t rAn = (Sched::TWO && has_next) ? (nxt.part ? rA1 : rA0) : rAc, rBn = (Sched::TWO && has_next) ? (nxt.part ? rB1 : rB0) : rBc;
;         float pre_[8] = {0.f, 0.f, 0.f, 0.f, 0.f, 0.f, 0.f, 0.f};
;         if constexpr (Epi::HAS_PRE) E.pre_load(pre_, cur, wr);
;         for (int t = 0; t < nt; t += 2) {
;             const bool last = (t == nt - 2);
;             const unsigned a1 = cA + (unsigned)(t + 1) * kstep;
;             const unsigned a2 = last ? nA : cA + (unsigned)(t + 2) * kstep, b2 = last ? nB : cB + (unsigned)(t + 2) * kstep; const rsrc_t rA2 = (Sched::TWO && last) ? rAn : rAc, rB2 = (Sched::TWO && last) ? rBn : rBc;
;             const unsigned a3 = a2 + kstep, b3 = b2 + kstep;
;             if (last && has_next) S.a_ready(nxt);
;             if constexpr (SP2) {
;             PG8_LDB(B0, 0, 0); PG8_LDB(B1, 0, 1); PG8_SCHED; PG8_LDA(At, 0, 0); PG8_STAGE(PG8_SA(1, 1), rAc, a1 + hstep, voffA);
;             PG8_WAIT_V(8); PG8_WAIT_L(0); PG8_BAR; PG8_MMA(0, 0, At, B0); PG8_MMA(0, 1, At, B1); PG8_BAR; PG8_SCHED;
;             PG8_LDA(At, 0, 1); PG8_STAGE(PG8_SB(0, 0), rB2, b2, voffB); PG8_STAGE(PG8_SB(0, 1), rB2, b2 + hstep, voffB); PG8_STAGE(PG8_SA(0, 0), rA2, a2, voffA);
;             PG8_WAIT_V(8); PG8_WAIT_L(0); PG8_BAR; PG8_MMA(1, 0, At, B0); PG8_MMA(1, 1, At, B1); PG8_BAR; PG8_SCHED;
;             PG8_LDB(B0, 1, 0); PG8_LDB(B1, 1, 1); PG8_SCHED; PG8_LDA(At, 1, 0); PG8_STAGE(PG8_SA(0, 1), rA2, a2 + hstep, voffA);
;             PG8_WAIT_V(8); PG8_WAIT_L(0); PG8_BAR; PG8_MMA(0, 0, At, B0); PG8_MMA(0, 1, At, B1); PG8_BAR; PG8_SCHED;
;             PG8_LDA(At, 1, 1); PG8_STAGE(PG8_SB(1, 0), rB2, b3, voffB); PG8_STAGE(PG8_SB(1, 1), rB2, b3 + hstep, voffB); PG8_STAGE(PG8_SA(1, 0), rA2, a3, voffA);
;             PG8_WAIT_V(8); PG8_WAIT_L(0); PG8_BAR; PG8_MMA(1, 0, At, B0); PG8_MMA(1, 1, At, B1); PG8_BAR; PG8_SCHED;
.LBB0_924:
	s_lshl_b32 s79, s77, 18
	s_andn2_b64 vcc, exec, s[22:23]
	s_lshl_b32 s80, s76, 18
	s_cbranch_vccnz .LBB0_928
	s_and_b64 s[2:3], s[26:27], exec
	s_waitcnt vmcnt(37)
	s_waitcnt vmcnt(36)
	s_waitcnt vmcnt(35)
	s_waitcnt vmcnt(32)
	s_waitcnt vmcnt(31)
	s_waitcnt vmcnt(28)
	s_waitcnt vmcnt(27)
	s_waitcnt vmcnt(24)
	s_waitcnt vmcnt(23)
	v_mov_b32_e32 v159, v233
	s_cselect_b32 s2, s79, s4
	s_cselect_b32 s3, s80, s5
	s_addk_i32 s4, 0x80
	s_addk_i32 s5, 0x100
	s_mov_b32 s11, 0
	s_waitcnt vmcnt(0)
	v_add_u32_e32 v120, 0x10000, v160
	ds_read_b128 v[132:135], v120
	ds_read_b128 v[136:139], v120 offset:1024
	ds_read_b128 v[140:143], v120 offset:2048
	ds_read_b128 v[144:147], v120 offset:3072
	v_add_u32_e32 v120, 0x14000, v160
	ds_read_b128 v[162:165], v120
	ds_read_b128 v[166:169], v120 offset:1024
	ds_read_b128 v[170:173], v120 offset:2048
	ds_read_b128 v[174:177], v120 offset:3072
	s_add_i32 s14, s4, 0x80
	s_cmp_eq_u32 s60, s11
	s_cselect_b32 s66, s2, s14
	s_cselect_b32 s55, s3, s5
	s_or_b32 s54, s66, 0x80
	s_add_i32 s14, s30, s4
	s_mov_b32 m0, s61
	ds_read_b128 v[178:181], v161
	ds_read_b128 v[182:185], v161 offset:1024
	ds_read_b128 v[194:197], v161 offset:2048
	ds_read_b128 v[198:201], v161 offset:3072
	ds_read_b128 v[202:205], v161 offset:4096
	ds_read_b128 v[206:209], v161 offset:5120
	ds_read_b128 v[210:213], v161 offset:6144
	ds_read_b128 v[214:217], v161 offset:7168
	buffer_load_dwordx4 v222, s[36:39], s14 offen lds
	s_mov_b32 m0, s62
	s_nop 0
	buffer_load_dwordx4 v156, s[36:39], s14 offen lds
	s_waitcnt vmcnt(8)
	s_waitcnt lgkmcnt(0)
	s_barrier
	s_setprio 1
	v_mfma_f32_16x16x128_f8f6f4 v[124:127], v[140:147], v[178:185], 0
	v_mfma_f32_16x16x128_f8f6f4 v[108:111], v[132:139], v[194:201], 0
	v_mfma_f32_16x16x128_f8f6f4 v[104:107], v[140:147], v[194:201], 0
	v_mfma_f32_16x16x128_f8f6f4 v[120:123], v[132:139], v[178:185], 0
	v_mfma_f32_16x16x128_f8f6f4 v[148:151], v[132:139], v[202:209], 0
	v_mfma_f32_16x16x128_f8f6f4 v[186:189], v[140:147], v[202:209], 0
	v_mfma_f32_16x16x128_f8f6f4 v[218:221], v[132:139], v[210:217], 0
	v_mfma_f32_16x16x128_f8f6f4 v[226:229], v[140:147], v[210:217], 0
	v_mfma_f32_16x16x128_f8f6f4 v[116:119], v[162:169], v[178:185], 0
	v_mfma_f32_16x16x128_f8f6f4 v[112:115], v[170:177], v[178:185], 0
	v_mfma_f32_16x16x128_f8f6f4 v[100:103], v[162:169], v[194:201], 0
	v_mfma_f32_16x16x128_f8f6f4 v[96:99], v[170:177], v[194:201], 0
	v_mfma_f32_16x16x128_f8f6f4 v[178:181], v[162:169], v[202:209], 0
	v_mfma_f32_16x16x128_f8f6f4 v[182:185], v[170:177], v[202:209], 0
	v_mfma_f32_16x16x128_f8f6f4 v[194:197], v[162:169], v[210:217], 0
	v_mfma_f32_16x16x128_f8f6f4 v[198:201], v[170:177], v[210:217], 0
	s_setprio 0
	s_barrier
	s_mov_b32 m0, s33
	s_mov_b32 s14, s38
	s_mov_b32 s15, s39
	s_nop 1
	buffer_load_dwordx4 v223, s[12:15], s55 offen lds
	s_mov_b32 m0, s34
	ds_read_b128 v[64:67], v161 offset:16384
	s_add_i32 s67, s55, s30
	buffer_load_dwordx4 v157, s[12:15], s55 offen lds
	s_mov_b32 m0, s31
	ds_read_b128 v[68:71], v161 offset:17408
	buffer_load_dwordx4 v222, s[36:39], s66 offen lds
	s_mov_b32 m0, s42
	ds_read_b128 v[72:75], v161 offset:18432
	buffer_load_dwordx4 v156, s[36:39], s66 offen lds
	ds_read_b128 v[76:79], v161 offset:19456
	ds_read_b128 v[80:83], v161 offset:20480
	ds_read_b128 v[84:87], v161 offset:21504
	ds_read_b128 v[88:91], v161 offset:22528
	ds_read_b128 v[92:95], v161 offset:23552
	s_waitcnt vmcnt(6)
	s_waitcnt lgkmcnt(0)
	s_barrier
	s_setprio 1
	v_mfma_f32_16x16x128_f8f6f4 v[60:63], v[132:139], v[64:71], 0
	v_mfma_f32_16x16x128_f8f6f4 v[56:59], v[140:147], v[64:71], 0
	v_mfma_f32_16x16x128_f8f6f4 v[202:205], v[132:139], v[72:79], 0
	v_mfma_f32_16x16x128_f8f6f4 v[206:209], v[140:147], v[72:79], 0
	v_mfma_f32_16x16x128_f8f6f4 v[210:213], v[132:139], v[80:87], 0
	v_mfma_f32_16x16x128_f8f6f4 v[214:217], v[140:147], v[80:87], 0
	v_mfma_f32_16x16x128_f8f6f4 v[230:233], v[132:139], v[88:95], 0
	v_mfma_f32_16x16x128_f8f6f4 v[234:237], v[140:147], v[88:95], 0
	v_mfma_f32_16x16x128_f8f6f4 v[52:55], v[162:169], v[64:71], 0
	v_mfma_f32_16x16x128_f8f6f4 v[48:51], v[170:177], v[64:71], 0
	v_mfma_f32_16x16x128_f8f6f4 v[238:241], v[162:169], v[72:79], 0
	v_mfma_f32_16x16x128_f8f6f4 v[242:245], v[170:177], v[72:79], 0
	v_mfma_f32_16x16x128_f8f6f4 v[246:249], v[162:169], v[80:87], 0
	v_mfma_f32_16x16x128_f8f6f4 v[250:253], v[170:177], v[80:87], 0
	v_mfma_f32_16x16x128_f8f6f4 v[190:193], v[162:169], v[88:95], 0
	v_mfma_f32_16x16x128_f8f6f4 v[152:155], v[170:177], v[88:95], 0
	s_setprio 0
	s_barrier
	s_mov_b32 m0, s35
	s_nop 0
	buffer_load_dwordx4 v223, s[12:15], s67 offen lds
	s_mov_b32 m0, s41
	s_nop 0
	buffer_load_dwordx4 v157, s[12:15], s67 offen lds
	v_add_u32_e32 v8, 0x18000, v160
	s_nop 3
	ds_read_b128 v[0:3], v8
	ds_read_b128 v[4:7], v8 offset:1024
	ds_read_b128 v[16:19], v8 offset:2048
	ds_read_b128 v[20:23], v8 offset:3072
	v_add_u32_e32 v8, 0x1c000, v160
	ds_read_b128 v[132:135], v8
	ds_read_b128 v[136:139], v8 offset:1024
	ds_read_b128 v[140:143], v8 offset:2048
	ds_read_b128 v[144:147], v8 offset:3072
	s_add_i32 s66, s66, s30
	s_mov_b32 m0, s43
	ds_read_b128 v[8:11], v161 offset:32768
	ds_read_b128 v[12:15], v161 offset:33792
	ds_read_b128 v[24:27], v161 offset:34816
	ds_read_b128 v[28:31], v161 offset:35840
	ds_read_b128 v[32:35], v161 offset:36864
	ds_read_b128 v[36:39], v161 offset:37888
	ds_read_b128 v[40:43], v161 offset:38912
	ds_read_b128 v[44:47], v161 offset:39936
	buffer_load_dwordx4 v222, s[36:39], s66 offen lds
	s_mov_b32 m0, s44
	s_nop 0
	buffer_load_dwordx4 v156, s[36:39], s66 offen lds
	s_waitcnt vmcnt(8)
	s_waitcnt lgkmcnt(0)
	s_barrier
; #define PG8_STAGE(bufoff, rs_, soff_, voff) do { _Pragma("unroll") for (int _i = 0; _i < 2; ++_i) \
;         __builtin_amdgcn_raw_ptr_buffer_load_lds(rs_, (LAS void*)(lds + (bufoff) + ldsw + _i * 8192), 16, (int)(voff)[_i], (int)(soff_), 0, 0); } while (0)
; #define PG8_LDA(dst, b, h) do { _Pragma("unroll") for (int m = 0; m < 4; ++m) dst[m] = PG8_LD2(lds + PG8_SA(b, h) + aoff + m * 2048); } while (0)
; #define PG8_LDB(dst, b, h) do { _Pragma("unroll") for (int n = 0; n < 2; ++n) dst[n] = PG8_LD2(lds + PG8_SB(b, h) + boff + n * 2048); } while (0)
; template <class Epi, class Sched, bool ALIGN_EPI = false, bool SP2 = false, bool FP8 = false>
; __device__ __forceinline__ void gemm_phase(LAS unsigned char* lds, const Gemm g, const Sched& S, const Epi& E, int wbase) {
;     ...
;         for (int t = 0; t < nt; t += 2) {
;             const bool last = (t == nt - 2);
;             const unsigned a1 = cA + (unsigned)(t + 1) * kstep;
;             const unsigned a2 = last ? nA : cA + (unsigned)(t + 2) * kstep, b2 = last ? nB : cB + (unsigned)(t + 2) * kstep; const rsrc_t rA2 = (Sched::TWO && last) ? rAn : rAc, rB2 = (Sched::TWO && last) ? rBn : rBc;
;             const unsigned a3 = a2 + kstep, b3 = b2 + kstep;
;             if (last && has_next) S.a_ready(nxt);
;             if constexpr (SP2) {
;             PG8_LDB(B0, 0, 0); PG8_LDB(B1, 0, 1); PG8_SCHED; PG8_LDA(At, 0, 0); PG8_STAGE(PG8_SA(1, 1), rAc, a1 + hstep, voffA);
;             PG8_WAIT_V(8); PG8_WAIT_L(0); PG8_BAR; PG8_MMA(0, 0, At, B0); PG8_MMA(0, 1, At, B1); PG8_BAR; PG8_SCHED;
;             PG8_LDA(At, 0, 1); PG8_STAGE(PG8_SB(0, 0), rB2, b2, voffB); PG8_STAGE(PG8_SB(0, 1), rB2, b2 + hstep, voffB); PG8_STAGE(PG8_SA(0, 0), rA2, a2, voffA);
;             PG8_WAIT_V(8); PG8_WAIT_L(0); PG8_BAR; PG8_MMA(1, 0, At, B0); PG8_MMA(1, 1, At, B1); PG8_BAR; PG8_SCHED;
;             PG8_LDB(B0, 1, 0); PG8_LDB(B1, 1, 1); PG8_SCHED; PG8_LDA(At, 1, 0); PG8_STAGE(PG8_SA(0, 1), rA2, a2 + hstep, voffA);
;             PG8_WAIT_V(8); PG8_WAIT_L(0); PG8_BAR; PG8_MMA(0, 0, At, B0); PG8_MMA(0, 1, At, B1); PG8_BAR; PG8_SCHED;
;             PG8_LDA(At, 1, 1); PG8_STAGE(PG8_SB(1, 0), rB2, b3, voffB); PG8_STAGE(PG8_SB(1, 1), rB2, b3 + hstep, voffB); PG8_STAGE(PG8_SA(1, 0), rA2, a3, voffA);
;             PG8_WAIT_V(8); PG8_WAIT_L(0); PG8_BAR; PG8_MMA(1, 0, At, B0); PG8_MMA(1, 1, At, B1); PG8_BAR; PG8_SCHED;
	s_setprio 1
	v_mfma_f32_16x16x128_f8f6f4 v[128:131], v[0:7], v[8:15], v[120:123]
	v_mfma_f32_16x16x128_f8f6f4 v[124:127], v[16:23], v[8:15], v[124:127]
	v_mfma_f32_16x16x128_f8f6f4 v[108:111], v[0:7], v[24:31], v[108:111]
	v_mfma_f32_16x16x128_f8f6f4 v[104:107], v[16:23], v[24:31], v[104:107]
	v_mfma_f32_16x16x128_f8f6f4 v[92:95], v[0:7], v[32:39], v[148:151]
	v_mfma_f32_16x16x128_f8f6f4 v[88:91], v[16:23], v[32:39], v[186:189]
	v_mfma_f32_16x16x128_f8f6f4 v[76:79], v[0:7], v[40:47], v[218:221]
	v_mfma_f32_16x16x128_f8f6f4 v[72:75], v[16:23], v[40:47], v[226:229]
	v_mfma_f32_16x16x128_f8f6f4 v[116:119], v[132:139], v[8:15], v[116:119]
	v_mfma_f32_16x16x128_f8f6f4 v[112:115], v[140:147], v[8:15], v[112:115]
	v_mfma_f32_16x16x128_f8f6f4 v[100:103], v[132:139], v[24:31], v[100:103]
	v_mfma_f32_16x16x128_f8f6f4 v[96:99], v[140:147], v[24:31], v[96:99]
	v_mfma_f32_16x16x128_f8f6f4 v[84:87], v[132:139], v[32:39], v[178:181]
	v_mfma_f32_16x16x128_f8f6f4 v[80:83], v[140:147], v[32:39], v[182:185]
	v_mfma_f32_16x16x128_f8f6f4 v[68:71], v[132:139], v[40:47], v[194:197]
	v_mfma_f32_16x16x128_f8f6f4 v[64:67], v[140:147], v[40:47], v[198:201]
	s_setprio 0
	s_barrier
	s_mov_b32 m0, s45
	s_bitset1_b32 s55, 7
	buffer_load_dwordx4 v223, s[12:15], s55 offen lds
	s_mov_b32 m0, s46
	ds_read_b128 v[32:35], v161 offset:49152
	buffer_load_dwordx4 v157, s[12:15], s55 offen lds
	s_add_i32 s55, s55, s30
	s_mov_b32 m0, s52
	ds_read_b128 v[36:39], v161 offset:50176
	buffer_load_dwordx4 v223, s[12:15], s55 offen lds
	s_mov_b32 m0, s53
	ds_read_b128 v[162:165], v161 offset:51200
	buffer_load_dwordx4 v157, s[12:15], s55 offen lds
	s_mov_b32 m0, s47
	ds_read_b128 v[166:169], v161 offset:52224
	buffer_load_dwordx4 v222, s[36:39], s54 offen lds
	s_mov_b32 m0, s48
	ds_read_b128 v[170:173], v161 offset:53248
	buffer_load_dwordx4 v156, s[36:39], s54 offen lds
	ds_read_b128 v[174:177], v161 offset:54272
	ds_read_b128 v[178:181], v161 offset:55296
	ds_read_b128 v[182:185], v161 offset:56320
	s_waitcnt vmcnt(8)
	s_waitcnt lgkmcnt(0)
	s_barrier
	s_setprio 1
	v_mfma_f32_16x16x128_f8f6f4 v[60:63], v[0:7], v[32:39], v[60:63]
	v_mfma_f32_16x16x128_f8f6f4 v[56:59], v[16:23], v[32:39], v[56:59]
	v_mfma_f32_16x16x128_f8f6f4 v[44:47], v[0:7], v[162:169], v[202:205]
	v_mfma_f32_16x16x128_f8f6f4 v[40:43], v[16:23], v[162:169], v[206:209]
	v_mfma_f32_16x16x128_f8f6f4 v[28:31], v[0:7], v[170:177], v[210:213]
	v_mfma_f32_16x16x128_f8f6f4 v[24:27], v[16:23], v[170:177], v[214:217]
	v_mfma_f32_16x16x128_f8f6f4 v[12:15], v[0:7], v[178:185], v[230:233]
	v_mfma_f32_16x16x128_f8f6f4 v[8:11], v[16:23], v[178:185], v[234:237]
	v_mfma_f32_16x16x128_f8f6f4 v[52:55], v[132:139], v[32:39], v[52:55]
	v_mfma_f32_16x16x128_f8f6f4 v[48:51], v[140:147], v[32:39], v[48:51]
	v_mfma_f32_16x16x128_f8f6f4 v[36:39], v[132:139], v[162:169], v[238:241]
	v_mfma_f32_16x16x128_f8f6f4 v[32:35], v[140:147], v[162:169], v[242:245]
	v_mfma_f32_16x16x128_f8f6f4 v[20:23], v[132:139], v[170:177], v[246:249]
	v_mfma_f32_16x16x128_f8f6f4 v[16:19], v[140:147], v[170:177], v[250:253]
	v_mfma_f32_16x16x128_f8f6f4 v[4:7], v[132:139], v[178:185], v[190:193]
	v_mfma_f32_16x16x128_f8f6f4 v[0:3], v[140:147], v[178:185], v[152:155]
	s_setprio 0
	s_barrier
	s_add_i32 s11, s11, 2
	s_addk_i32 s4, 0x100
	s_addk_i32 s5, 0x100
	s_cmp_ge_i32 s11, s58
	s_cbranch_scc0 .LBB0_926
	s_branch .Lzp_after_926
.LBB0_926:
	v_add_u32_e32 v120, 0x10000, v160
	ds_read_b128 v[132:135], v120
	ds_read_b128 v[136:139], v120 offset:1024
	ds_read_b128 v[140:143], v120 offset:2048
	ds_read_b128 v[144:147], v120 offset:3072
	v_add_u32_e32 v120, 0x14000, v160
	ds_read_b128 v[162:165], v120
	ds_read_b128 v[166:169], v120 offset:1024
	ds_read_b128 v[170:173], v120 offset:2048
	ds_read_b128 v[174:177], v120 offset:3072
	s_add_i32 s14, s4, 0x80
	s_cmp_eq_u32 s60, s11
	s_cselect_b32 s66, s2, s14
	s_cselect_b32 s55, s3, s5
	s_or_b32 s54, s66, 0x80
	s_add_i32 s14, s30, s4
	s_mov_b32 m0, s61
	ds_read_b128 v[178:181], v161
	ds_read_b128 v[182:185], v161 offset:1024
	ds_read_b128 v[194:197], v161 offset:2048
	ds_read_b128 v[198:201], v161 offset:3072
	ds_read_b128 v[202:205], v161 offset:4096
	ds_read_b128 v[206:209], v161 offset:5120
	ds_read_b128 v[210:213], v161 offset:6144
	ds_read_b128 v[214:217], v161 offset:7168
	buffer_load_dwordx4 v222, s[36:39], s14 offen lds
	s_mov_b32 m0, s62
	s_nop 0
	buffer_load_dwordx4 v156, s[36:39], s14 offen lds
	s_waitcnt vmcnt(8)
	s_waitcnt lgkmcnt(0)
	s_barrier
	s_setprio 1
	v_mfma_f32_16x16x128_f8f6f4 v[124:127], v[140:147], v[178:185], v[124:127]
	v_mfma_f32_16x16x128_f8f6f4 v[108:111], v[132:139], v[194:201], v[108:111]
	v_mfma_f32_16x16x128_f8f6f4 v[104:107], v[140:147], v[194:201], v[104:107]
	v_mfma_f32_16x16x128_f8f6f4 v[120:123], v[132:139], v[178:185], v[128:131]
	v_mfma_f32_16x16x128_f8f6f4 v[148:151], v[132:139], v[202:209], v[92:95]
	v_mfma_f32_16x16x128_f8f6f4 v[186:189], v[140:147], v[202:209], v[88:91]
	v_mfma_f32_16x16x128_f8f6f4 v[218:221], v[132:139], v[210:217], v[76:79]
	v_mfma_f32_16x16x128_f8f6f4 v[226:229], v[140:147], v[210:217], v[72:75]
	v_mfma_f32_16x16x128_f8f6f4 v[116:119], v[162:169], v[178:185], v[116:119]
	v_mfma_f32_16x16x128_f8f6f4 v[112:115], v[170:177], v[178:185], v[112:115]
	v_mfma_f32_16x16x128_f8f6f4 v[100:103], v[162:169], v[194:201], v[100:103]
	v_mfma_f32_16x16x128_f8f6f4 v[96:99], v[170:177], v[194:201], v[96:99]
	v_mfma_f32_16x16x128_f8f6f4 v[178:181], v[162:169], v[202:209], v[84:87]
	v_mfma_f32_16x16x128_f8f6f4 v[182:185], v[170:177], v[202:209], v[80:83]
	v_mfma_f32_16x16x128_f8f6f4 v[194:197], v[162:169], v[210:217], v[68:71]
	v_mfma_f32_16x16x128_f8f6f4 v[198:201], v[170:177], v[210:217], v[64:67]
	s_setprio 0
	s_barrier
; #define PG8_STAGE(bufoff, rs_, soff_, voff) do { _Pragma("unroll") for (int _i = 0; _i < 2; ++_i) \
;         __builtin_amdgcn_raw_ptr_buffer_load_lds(rs_, (LAS void*)(lds + (bufoff) + ldsw + _i * 8192), 16, (int)(voff)[_i], (int)(soff_), 0, 0); } while (0)
; #define PG8_LDA(dst, b, h) do { _Pragma("unroll") for (int m = 0; m < 4; ++m) dst[m] = PG8_LD2(lds + PG8_SA(b, h) + aoff + m * 2048); } while (0)
; #define PG8_LDB(dst, b, h) do { _Pragma("unroll") for (int n = 0; n < 2; ++n) dst[n] = PG8_LD2(lds + PG8_SB(b, h) + boff + n * 2048); } while (0)
; template <class Epi, class Sched, bool ALIGN_EPI = false, bool SP2 = false, bool FP8 = false>
; __device__ __forceinline__ void gemm_phase(LAS unsigned char* lds, const Gemm g, const Sched& S, const Epi& E, int wbase) {
;     ...
;         for (int t = 0; t < nt; t += 2) {
;             const bool last = (t == nt - 2);
;             const unsigned a1 = cA + (unsigned)(t + 1) * kstep;
;             const unsigned a2 = last ? nA : cA + (unsigned)(t + 2) * kstep, b2 = last ? nB : cB + (unsigned)(t + 2) * kstep; const rsrc_t rA2 = (Sched::TWO && last) ? rAn : rAc, rB2 = (Sched::TWO && last) ? rBn : rBc;
;             const unsigned a3 = a2 + kstep, b3 = b2 + kstep;
;             if (last && has_next) S.a_ready(nxt);
;             if constexpr (SP2) {
;             PG8_LDB(B0, 0, 0); PG8_LDB(B1, 0, 1); PG8_SCHED; PG8_LDA(At, 0, 0); PG8_STAGE(PG8_SA(1, 1), rAc, a1 + hstep, voffA);
;             PG8_WAIT_V(8); PG8_WAIT_L(0); PG8_BAR; PG8_MMA(0, 0, At, B0); PG8_MMA(0, 1, At, B1); PG8_BAR; PG8_SCHED;
;             PG8_LDA(At, 0, 1); PG8_STAGE(PG8_SB(0, 0), rB2, b2, voffB); PG8_STAGE(PG8_SB(0, 1), rB2, b2 + hstep, voffB); PG8_STAGE(PG8_SA(0, 0), rA2, a2, voffA);
;             PG8_WAIT_V(8); PG8_WAIT_L(0); PG8_BAR; PG8_MMA(1, 0, At, B0); PG8_MMA(1, 1, At, B1); PG8_BAR; PG8_SCHED;
;             PG8_LDB(B0, 1, 0); PG8_LDB(B1, 1, 1); PG8_SCHED; PG8_LDA(At, 1, 0); PG8_STAGE(PG8_SA(0, 1), rA2, a2 + hstep, voffA);
;             PG8_WAIT_V(8); PG8_WAIT_L(0); PG8_BAR; PG8_MMA(0, 0, At, B0); PG8_MMA(0, 1, At, B1); PG8_BAR; PG8_SCHED;
;             PG8_LDA(At, 1, 1); PG8_STAGE(PG8_SB(1, 0), rB2, b3, voffB); PG8_STAGE(PG8_SB(1, 1), rB2, b3 + hstep, voffB); PG8_STAGE(PG8_SA(1, 0), rA2, a3, voffA);
;             PG8_WAIT_V(8); PG8_WAIT_L(0); PG8_BAR; PG8_MMA(1, 0, At, B0); PG8_MMA(1, 1, At, B1); PG8_BAR; PG8_SCHED;
	s_mov_b32 m0, s33
	s_mov_b32 s14, s38
	s_mov_b32 s15, s39
	s_nop 1
	buffer_load_dwordx4 v223, s[12:15], s55 offen lds
	s_mov_b32 m0, s34
	ds_read_b128 v[64:67], v161 offset:16384
	s_add_i32 s67, s55, s30
	buffer_load_dwordx4 v157, s[12:15], s55 offen lds
	s_mov_b32 m0, s31
	ds_read_b128 v[68:71], v161 offset:17408
	buffer_load_dwordx4 v222, s[36:39], s66 offen lds
	s_mov_b32 m0, s42
	ds_read_b128 v[72:75], v161 offset:18432
	buffer_load_dwordx4 v156, s[36:39], s66 offen lds
	ds_read_b128 v[76:79], v161 offset:19456
	ds_read_b128 v[80:83], v161 offset:20480
	ds_read_b128 v[84:87], v161 offset:21504
	ds_read_b128 v[88:91], v161 offset:22528
	ds_read_b128 v[92:95], v161 offset:23552
	s_waitcnt vmcnt(6)
	s_waitcnt lgkmcnt(0)
	s_barrier
	s_setprio 1
	v_mfma_f32_16x16x128_f8f6f4 v[60:63], v[132:139], v[64:71], v[60:63]
	v_mfma_f32_16x16x128_f8f6f4 v[56:59], v[140:147], v[64:71], v[56:59]
	v_mfma_f32_16x16x128_f8f6f4 v[202:205], v[132:139], v[72:79], v[44:47]
	v_mfma_f32_16x16x128_f8f6f4 v[206:209], v[140:147], v[72:79], v[40:43]
	v_mfma_f32_16x16x128_f8f6f4 v[210:213], v[132:139], v[80:87], v[28:31]
	v_mfma_f32_16x16x128_f8f6f4 v[214:217], v[140:147], v[80:87], v[24:27]
	v_mfma_f32_16x16x128_f8f6f4 v[230:233], v[132:139], v[88:95], v[12:15]
	v_mfma_f32_16x16x128_f8f6f4 v[234:237], v[140:147], v[88:95], v[8:11]
	v_mfma_f32_16x16x128_f8f6f4 v[52:55], v[162:169], v[64:71], v[52:55]
	v_mfma_f32_16x16x128_f8f6f4 v[48:51], v[170:177], v[64:71], v[48:51]
	v_mfma_f32_16x16x128_f8f6f4 v[238:241], v[162:169], v[72:79], v[36:39]
	v_mfma_f32_16x16x128_f8f6f4 v[242:245], v[170:177], v[72:79], v[32:35]
	v_mfma_f32_16x16x128_f8f6f4 v[246:249], v[162:169], v[80:87], v[20:23]
	v_mfma_f32_16x16x128_f8f6f4 v[250:253], v[170:177], v[80:87], v[16:19]
	v_mfma_f32_16x16x128_f8f6f4 v[190:193], v[162:169], v[88:95], v[4:7]
	v_mfma_f32_16x16x128_f8f6f4 v[152:155], v[170:177], v[88:95], v[0:3]
	s_setprio 0
	s_barrier
	s_mov_b32 m0, s35
	s_nop 0
	buffer_load_dwordx4 v223, s[12:15], s67 offen lds
	s_mov_b32 m0, s41
	s_nop 0
	buffer_load_dwordx4 v157, s[12:15], s67 offen lds
	v_add_u32_e32 v8, 0x18000, v160
	s_nop 3
	ds_read_b128 v[0:3], v8
	ds_read_b128 v[4:7], v8 offset:1024
	ds_read_b128 v[16:19], v8 offset:2048
	ds_read_b128 v[20:23], v8 offset:3072
	v_add_u32_e32 v8, 0x1c000, v160
	ds_read_b128 v[132:135], v8
	ds_read_b128 v[136:139], v8 offset:1024
	ds_read_b128 v[140:143], v8 offset:2048
	ds_read_b128 v[144:147], v8 offset:3072
	s_add_i32 s66, s66, s30
	s_mov_b32 m0, s43
	ds_read_b128 v[8:11], v161 offset:32768
	ds_read_b128 v[12:15], v161 offset:33792
	ds_read_b128 v[24:27], v161 offset:34816
	ds_read_b128 v[28:31], v161 offset:35840
	ds_read_b128 v[32:35], v161 offset:36864
	ds_read_b128 v[36:39], v161 offset:37888
	ds_read_b128 v[40:43], v161 offset:38912
	ds_read_b128 v[44:47], v161 offset:39936
	buffer_load_dwordx4 v222, s[36:39], s66 offen lds
	s_mov_b32 m0, s44
	s_nop 0
	buffer_load_dwordx4 v156, s[36:39], s66 offen lds
	s_waitcnt vmcnt(8)
	s_waitcnt lgkmcnt(0)
	s_barrier
	s_setprio 1
	v_mfma_f32_16x16x128_f8f6f4 v[128:131], v[0:7], v[8:15], v[120:123]
	v_mfma_f32_16x16x128_f8f6f4 v[124:127], v[16:23], v[8:15], v[124:127]
	v_mfma_f32_16x16x128_f8f6f4 v[108:111], v[0:7], v[24:31], v[108:111]
	v_mfma_f32_16x16x128_f8f6f4 v[104:107], v[16:23], v[24:31], v[104:107]
	v_mfma_f32_16x16x128_f8f6f4 v[92:95], v[0:7], v[32:39], v[148:151]
	v_mfma_f32_16x16x128_f8f6f4 v[88:91], v[16:23], v[32:39], v[186:189]
	v_mfma_f32_16x16x128_f8f6f4 v[76:79], v[0:7], v[40:47], v[218:221]
	v_mfma_f32_16x16x128_f8f6f4 v[72:75], v[16:23], v[40:47], v[226:229]
	v_mfma_f32_16x16x128_f8f6f4 v[116:119], v[132:139], v[8:15], v[116:119]
	v_mfma_f32_16x16x128_f8f6f4 v[112:115], v[140:147], v[8:15], v[112:115]
	v_mfma_f32_16x16x128_f8f6f4 v[100:103], v[132:139], v[24:31], v[100:103]
	v_mfma_f32_16x16x128_f8f6f4 v[96:99], v[140:147], v[24:31], v[96:99]
	v_mfma_f32_16x16x128_f8f6f4 v[84:87], v[132:139], v[32:39], v[178:181]
	v_mfma_f32_16x16x128_f8f6f4 v[80:83], v[140:147], v[32:39], v[182:185]
	v_mfma_f32_16x16x128_f8f6f4 v[68:71], v[132:139], v[40:47], v[194:197]
	v_mfma_f32_16x16x128_f8f6f4 v[64:67], v[140:147], v[40:47], v[198:201]
	s_setprio 0
	s_barrier
	s_mov_b32 m0, s45
	s_bitset1_b32 s55, 7
	buffer_load_dwordx4 v223, s[12:15], s55 offen lds
	s_mov_b32 m0, s46
	ds_read_b128 v[32:35], v161 offset:49152
	buffer_load_dwordx4 v157, s[12:15], s55 offen lds
	s_add_i32 s55, s55, s30
	s_mov_b32 m0, s52
	ds_read_b128 v[36:39], v161 offset:50176
	buffer_load_dwordx4 v223, s[12:15], s55 offen lds
	s_mov_b32 m0, s53
	ds_read_b128 v[162:165], v161 offset:51200
	buffer_load_dwordx4 v157, s[12:15], s55 offen lds
	s_mov_b32 m0, s47
	ds_read_b128 v[166:169], v161 offset:52224
	buffer_load_dwordx4 v222, s[36:39], s54 offen lds
	s_mov_b32 m0, s48
	ds_read_b128 v[170:173], v161 offset:53248
	buffer_load_dwordx4 v156, s[36:39], s54 offen lds
	ds_read_b128 v[174:177], v161 offset:54272
	ds_read_b128 v[178:181], v161 offset:55296
	ds_read_b128 v[182:185], v161 offset:56320
	s_waitcnt vmcnt(8)
	s_waitcnt lgkmcnt(0)
	s_barrier
	s_setprio 1
	v_mfma_f32_16x16x128_f8f6f4 v[60:63], v[0:7], v[32:39], v[60:63]
	v_mfma_f32_16x16x128_f8f6f4 v[56:59], v[16:23], v[32:39], v[56:59]
	v_mfma_f32_16x16x128_f8f6f4 v[44:47], v[0:7], v[162:169], v[202:205]
	v_mfma_f32_16x16x128_f8f6f4 v[40:43], v[16:23], v[162:169], v[206:209]
	v_mfma_f32_16x16x128_f8f6f4 v[28:31], v[0:7], v[170:177], v[210:213]
	v_mfma_f32_16x16x128_f8f6f4 v[24:27], v[16:23], v[170:177], v[214:217]
	v_mfma_f32_16x16x128_f8f6f4 v[12:15], v[0:7], v[178:185], v[230:233]
	v_mfma_f32_16x16x128_f8f6f4 v[8:11], v[16:23], v[178:185], v[234:237]
	v_mfma_f32_16x16x128_f8f6f4 v[52:55], v[132:139], v[32:39], v[52:55]
	v_mfma_f32_16x16x128_f8f6f4 v[48:51], v[140:147], v[32:39], v[48:51]
	v_mfma_f32_16x16x128_f8f6f4 v[36:39], v[132:139], v[162:169], v[238:241]
	v_mfma_f32_16x16x128_f8f6f4 v[32:35], v[140:147], v[162:169], v[242:245]
	v_mfma_f32_16x16x128_f8f6f4 v[20:23], v[132:139], v[170:177], v[246:249]
	v_mfma_f32_16x16x128_f8f6f4 v[16:19], v[140:147], v[170:177], v[250:253]
	v_mfma_f32_16x16x128_f8f6f4 v[4:7], v[132:139], v[178:185], v[190:193]
	v_mfma_f32_16x16x128_f8f6f4 v[0:3], v[140:147], v[178:185], v[152:155]
	s_setprio 0
	s_barrier
	s_add_i32 s11, s11, 2
	s_addk_i32 s4, 0x100
	s_addk_i32 s5, 0x100
	s_cmp_ge_i32 s11, s58
	s_cbranch_scc0 .LBB0_926

;     __device__ __forceinline__ unsigned a_off(const Unit& u, const Gemm& g) const { return (unsigned)u.pm * (unsigned)(BM * 2) * (unsigned)g.K; }
; template <class Epi, class Sched, bool ALIGN_EPI = false, bool SP2 = false, bool FP8 = false>
; __device__ __forceinline__ void gemm_phase(LAS unsigned char* lds, const Gemm g, const Sched& S, const Epi& E, int wbase) {
;     ...
;         const bool has_next = S.next(ui + 1, nxt);
;         const unsigned nA = has_next ? S.a_off(nxt, g) : cA, nB = has_next ? S.b_off(nxt, g) : cB;
;         const rsrc_t rAn = (Sched::TWO && has_next) ? (nxt.part ? rA1 : rA0) : rAc, rBn = (Sched::TWO && has_next) ? (nxt.part ? rB1 : rB0) : rBc;
;         float pre_[8] = {0.f, 0.f, 0.f, 0.f, 0.f, 0.f, 0.f, 0.f};
;         if constexpr (Epi::HAS_PRE) E.pre_load(pre_, cur, wr);
;         for (int t = 0; t < nt; t += 2) {
;             const bool last = (t == nt - 2);
;             const unsigned a1 = cA + (unsigned)(t + 1) * kstep;
;             const unsigned a2 = last ? nA : cA + (unsigned)(t + 2) * kstep, b2 = last ? nB : cB + (unsigned)(t + 2) * kstep; const rsrc_t rA2 = (Sched::TWO && last) ? rAn : rAc, rB2 = (Sched::TWO && last) ? rBn : rBc;
;             const unsigned a3 = a2 + kstep, b3 = b2 + kstep;
;             if (last && has_next) S.a_ready(nxt);
;             if constexpr (SP2) {
;             PG8_LDB(B0, 0, 0); PG8_LDB(B1, 0, 1); PG8_SCHED; PG8_LDA(At, 0, 0); PG8_STAGE(PG8_SA(1, 1), rAc, a1 + hstep, voffA);
;             PG8_WAIT_V(8); PG8_WAIT_L(0); PG8_BAR; PG8_MMA(0, 0, At, B0); PG8_MMA(0, 1, At, B1); PG8_BAR; PG8_SCHED;
;             PG8_LDA(At, 0, 1); PG8_STAGE(PG8_SB(0, 0), rB2, b2, voffB); PG8_STAGE(PG8_SB(0, 1), rB2, b2 + hstep, voffB); PG8_STAGE(PG8_SA(0, 0), rA2, a2, voffA);
;             PG8_WAIT_V(8); PG8_WAIT_L(0); PG8_BAR; PG8_MMA(1, 0, At, B0); PG8_MMA(1, 1, At, B1); PG8_BAR; PG8_SCHED;
;             PG8_LDB(B0, 1, 0); PG8_LDB(B1, 1, 1); PG8_SCHED; PG8_LDA(At, 1, 0); PG8_STAGE(PG8_SA(0, 1), rA2, a2 + hstep, voffA);
;             PG8_WAIT_V(8); PG8_WAIT_L(0); PG8_BAR; PG8_MMA(0, 0, At, B0); PG8_MMA(0, 1, At, B1); PG8_BAR; PG8_SCHED;
;             PG8_LDA(At, 1, 1); PG8_STAGE(PG8_SB(1, 0), rB2, b3, voffB); PG8_STAGE(PG8_SB(1, 1), rB2, b3 + hstep, voffB); PG8_STAGE(PG8_SA(1, 0), rA2, a3, voffA);
;             PG8_WAIT_V(8); PG8_WAIT_L(0); PG8_BAR; PG8_MMA(1, 0, At, B0); PG8_MMA(1, 1, At, B1); PG8_BAR; PG8_SCHED;
.LBB0_1002:
	s_lshl_b32 s81, s80, 19
	s_andn2_b64 vcc, exec, s[24:25]
	s_lshl_b32 s82, s79, 19
	s_cbranch_vccnz .LBB0_1058
	s_and_b64 s[2:3], s[28:29], exec
	s_waitcnt vmcnt(37)
	s_waitcnt vmcnt(36)
	s_waitcnt vmcnt(35)
	s_waitcnt vmcnt(32)
	s_waitcnt vmcnt(31)
	s_waitcnt vmcnt(27)
	s_waitcnt vmcnt(26)
	s_waitcnt vmcnt(24)
	s_waitcnt vmcnt(23)
	s_cselect_b32 s2, s81, s4
	s_cselect_b32 s3, s82, s5
	s_addk_i32 s4, 0x80
	s_addk_i32 s5, 0x100
	s_mov_b32 s11, 0
	s_waitcnt vmcnt(0)
	v_add_u32_e32 v132, 0x10000, v180
	v_add_u32_e32 v156, 0x14000, v180
	ds_read_b128 v[96:99], v132
	ds_read_b128 v[108:111], v132 offset:1024
	ds_read_b128 v[120:123], v132 offset:2048
	ds_read_b128 v[132:135], v132 offset:3072
	ds_read_b128 v[136:139], v156
	ds_read_b128 v[144:147], v156 offset:1024
	ds_read_b128 v[152:155], v156 offset:2048
	ds_read_b128 v[156:159], v156 offset:3072
	s_add_i32 s14, s4, 0x80
	s_cmp_eq_u32 s62, s11
	s_cselect_b32 s66, s2, s14
	s_cselect_b32 s55, s3, s5
	s_or_b32 s54, s66, 0x80
	s_add_i32 s14, s33, s4
	s_mov_b32 m0, s63
	ds_read_b128 v[160:163], v181
	ds_read_b128 v[164:167], v181 offset:1024
	ds_read_b128 v[168:171], v181 offset:2048
	ds_read_b128 v[182:185], v181 offset:3072
	ds_read_b128 v[186:189], v181 offset:4096
	ds_read_b128 v[190:193], v181 offset:5120
	ds_read_b128 v[194:197], v181 offset:6144
	ds_read_b128 v[198:201], v181 offset:7168
	buffer_load_dwordx4 v174, s[36:39], s14 offen lds
	s_mov_b32 m0, s65
	s_nop 0
	buffer_load_dwordx4 v176, s[36:39], s14 offen lds
	s_waitcnt vmcnt(8)
	s_waitcnt lgkmcnt(0)
	s_barrier
	s_setprio 1
	v_mfma_f32_16x16x32_bf16 v[148:151], v[96:99], v[160:163], 0
	v_mfma_f32_16x16x32_bf16 v[140:143], v[120:123], v[160:163], 0
	v_mfma_f32_16x16x32_bf16 v[116:119], v[96:99], v[168:171], 0
	v_mfma_f32_16x16x32_bf16 v[112:115], v[120:123], v[168:171], 0
	v_mfma_f32_16x16x32_bf16 v[92:95], v[96:99], v[186:189], 0
	v_mfma_f32_16x16x32_bf16 v[88:91], v[120:123], v[186:189], 0
	v_mfma_f32_16x16x32_bf16 v[76:79], v[96:99], v[194:197], 0
	v_mfma_f32_16x16x32_bf16 v[72:75], v[120:123], v[194:197], 0
	v_mfma_f32_16x16x32_bf16 v[148:151], v[108:111], v[164:167], v[148:151]
	v_mfma_f32_16x16x32_bf16 v[140:143], v[132:135], v[164:167], v[140:143]
	v_mfma_f32_16x16x32_bf16 v[116:119], v[108:111], v[182:185], v[116:119]
	v_mfma_f32_16x16x32_bf16 v[112:115], v[132:135], v[182:185], v[112:115]
	v_mfma_f32_16x16x32_bf16 v[92:95], v[108:111], v[190:193], v[92:95]
	v_mfma_f32_16x16x32_bf16 v[88:91], v[132:135], v[190:193], v[88:91]
	v_mfma_f32_16x16x32_bf16 v[76:79], v[108:111], v[198:201], v[76:79]
	v_mfma_f32_16x16x32_bf16 v[72:75], v[132:135], v[198:201], v[72:75]
	v_mfma_f32_16x16x32_bf16 v[128:131], v[136:139], v[160:163], 0
	v_mfma_f32_16x16x32_bf16 v[124:127], v[152:155], v[160:163], 0
	v_mfma_f32_16x16x32_bf16 v[104:107], v[136:139], v[168:171], 0
	v_mfma_f32_16x16x32_bf16 v[100:103], v[152:155], v[168:171], 0
	v_mfma_f32_16x16x32_bf16 v[84:87], v[136:139], v[186:189], 0
	v_mfma_f32_16x16x32_bf16 v[80:83], v[152:155], v[186:189], 0
	v_mfma_f32_16x16x32_bf16 v[68:71], v[136:139], v[194:197], 0
	v_mfma_f32_16x16x32_bf16 v[64:67], v[152:155], v[194:197], 0
	v_mfma_f32_16x16x32_bf16 v[128:131], v[144:147], v[164:167], v[128:131]
	v_mfma_f32_16x16x32_bf16 v[124:127], v[156:159], v[164:167], v[124:127]
	v_mfma_f32_16x16x32_bf16 v[104:107], v[144:147], v[182:185], v[104:107]
	v_mfma_f32_16x16x32_bf16 v[100:103], v[156:159], v[182:185], v[100:103]
	v_mfma_f32_16x16x32_bf16 v[84:87], v[144:147], v[190:193], v[84:87]
	v_mfma_f32_16x16x32_bf16 v[80:83], v[156:159], v[190:193], v[80:83]
	v_mfma_f32_16x16x32_bf16 v[68:71], v[144:147], v[198:201], v[68:71]
	v_mfma_f32_16x16x32_bf16 v[64:67], v[156:159], v[198:201], v[64:67]
	s_setprio 0
	s_barrier
	s_mov_b32 m0, s35
	s_mov_b32 s14, s38
	s_mov_b32 s15, s39
	buffer_load_dwordx4 v175, s[12:15], s55 offen lds
	s_mov_b32 m0, s41
	ds_read_b128 v[160:163], v181 offset:16384
	s_add_i32 s67, s55, s33
	buffer_load_dwordx4 v177, s[12:15], s55 offen lds
	s_mov_b32 m0, s34
	ds_read_b128 v[164:167], v181 offset:17408
	buffer_load_dwordx4 v174, s[36:39], s66 offen lds
	s_mov_b32 m0, s44
	ds_read_b128 v[168:171], v181 offset:18432
	buffer_load_dwordx4 v176, s[36:39], s66 offen lds
	ds_read_b128 v[182:185], v181 offset:19456
	ds_read_b128 v[186:189], v181 offset:20480
	ds_read_b128 v[190:193], v181 offset:21504
	ds_read_b128 v[194:197], v181 offset:22528
	ds_read_b128 v[198:201], v181 offset:23552
	s_waitcnt vmcnt(6)
	s_waitcnt lgkmcnt(0)
	s_barrier
	s_setprio 1
	v_mfma_f32_16x16x32_bf16 v[60:63], v[96:99], v[160:163], 0
	v_mfma_f32_16x16x32_bf16 v[56:59], v[120:123], v[160:163], 0
	v_mfma_f32_16x16x32_bf16 v[44:47], v[96:99], v[168:171], 0
	v_mfma_f32_16x16x32_bf16 v[40:43], v[120:123], v[168:171], 0
	v_mfma_f32_16x16x32_bf16 v[28:31], v[96:99], v[186:189], 0
	v_mfma_f32_16x16x32_bf16 v[24:27], v[120:123], v[186:189], 0
	v_mfma_f32_16x16x32_bf16 v[12:15], v[96:99], v[194:197], 0
	v_mfma_f32_16x16x32_bf16 v[8:11], v[120:123], v[194:197], 0
	v_mfma_f32_16x16x32_bf16 v[60:63], v[108:111], v[164:167], v[60:63]
	v_mfma_f32_16x16x32_bf16 v[56:59], v[132:135], v[164:167], v[56:59]
	v_mfma_f32_16x16x32_bf16 v[44:47], v[108:111], v[182:185], v[44:47]
	v_mfma_f32_16x16x32_bf16 v[40:43], v[132:135], v[182:185], v[40:43]
	v_mfma_f32_16x16x32_bf16 v[28:31], v[108:111], v[190:193], v[28:31]
	v_mfma_f32_16x16x32_bf16 v[24:27], v[132:135], v[190:193], v[24:27]
	v_mfma_f32_16x16x32_bf16 v[12:15], v[108:111], v[198:201], v[12:15]
	v_mfma_f32_16x16x32_bf16 v[8:11], v[132:135], v[198:201], v[8:11]
	v_mfma_f32_16x16x32_bf16 v[52:55], v[136:139], v[160:163], 0
	v_mfma_f32_16x16x32_bf16 v[48:51], v[152:155], v[160:163], 0
	v_mfma_f32_16x16x32_bf16 v[36:39], v[136:139], v[168:171], 0
	v_mfma_f32_16x16x32_bf16 v[32:35], v[152:155], v[168:171], 0
	v_mfma_f32_16x16x32_bf16 v[20:23], v[136:139], v[186:189], 0
	v_mfma_f32_16x16x32_bf16 v[16:19], v[152:155], v[186:189], 0
	v_mfma_f32_16x16x32_bf16 v[4:7], v[136:139], v[194:197], 0
	v_mfma_f32_16x16x32_bf16 v[0:3], v[152:155], v[194:197], 0
	v_mfma_f32_16x16x32_bf16 v[52:55], v[144:147], v[164:167], v[52:55]
	v_mfma_f32_16x16x32_bf16 v[48:51], v[156:159], v[164:167], v[48:51]
	v_mfma_f32_16x16x32_bf16 v[36:39], v[144:147], v[182:185], v[36:39]
	v_mfma_f32_16x16x32_bf16 v[32:35], v[156:159], v[182:185], v[32:35]
	v_mfma_f32_16x16x32_bf16 v[20:23], v[144:147], v[190:193], v[20:23]
	v_mfma_f32_16x16x32_bf16 v[16:19], v[156:159], v[190:193], v[16:19]
	v_mfma_f32_16x16x32_bf16 v[4:7], v[144:147], v[198:201], v[4:7]
	v_mfma_f32_16x16x32_bf16 v[0:3], v[156:159], v[198:201], v[0:3]
	s_setprio 0
	s_barrier
; #define PG8_STAGE(bufoff, rs_, soff_, voff) do { _Pragma("unroll") for (int _i = 0; _i < 2; ++_i) \
;         __builtin_amdgcn_raw_ptr_buffer_load_lds(rs_, (LAS void*)(lds + (bufoff) + ldsw + _i * 8192), 16, (int)(voff)[_i], (int)(soff_), 0, 0); } while (0)
; #define PG8_LDA(dst, b, h) do { _Pragma("unroll") for (int m = 0; m < 4; ++m) dst[m] = PG8_LD2(lds + PG8_SA(b, h) + aoff + m * 2048); } while (0)
; #define PG8_LDB(dst, b, h) do { _Pragma("unroll") for (int n = 0; n < 2; ++n) dst[n] = PG8_LD2(lds + PG8_SB(b, h) + boff + n * 2048); } while (0)
; #define PG8_WAIT_V(n) asm volatile("s_waitcnt vmcnt(" #n ")" ::: "memory")
; #define PG8_WAIT_L(n) asm volatile("s_waitcnt lgkmcnt(" #n ")" ::: "memory")
; #define PG8_BAR __builtin_amdgcn_s_barrier()
; #define PG8_SCHED __builtin_amdgcn_sched_barrier(0)
; template <class Epi, class Sched, bool ALIGN_EPI = false, bool SP2 = false, bool FP8 = false>
; __device__ __forceinline__ void gemm_phase(LAS unsigned char* lds, const Gemm g, const Sched& S, const Epi& E, int wbase) {
;     ...
;             PG8_LDB(B0, 0, 0); PG8_LDB(B1, 0, 1); PG8_SCHED; PG8_LDA(At, 0, 0); PG8_STAGE(PG8_SA(1, 1), rAc, a1 + hstep, voffA);
;             PG8_WAIT_V(8); PG8_WAIT_L(0); PG8_BAR; PG8_MMA(0, 0, At, B0); PG8_MMA(0, 1, At, B1); PG8_BAR; PG8_SCHED;
;             PG8_LDA(At, 0, 1); PG8_STAGE(PG8_SB(0, 0), rB2, b2, voffB); PG8_STAGE(PG8_SB(0, 1), rB2, b2 + hstep, voffB); PG8_STAGE(PG8_SA(0, 0), rA2, a2, voffA);
;             PG8_WAIT_V(8); PG8_WAIT_L(0); PG8_BAR; PG8_MMA(1, 0, At, B0); PG8_MMA(1, 1, At, B1); PG8_BAR; PG8_SCHED;
;             PG8_LDB(B0, 1, 0); PG8_LDB(B1, 1, 1); PG8_SCHED; PG8_LDA(At, 1, 0); PG8_STAGE(PG8_SA(0, 1), rA2, a2 + hstep, voffA);
;             PG8_WAIT_V(8); PG8_WAIT_L(0); PG8_BAR; PG8_MMA(0, 0, At, B0); PG8_MMA(0, 1, At, B1); PG8_BAR; PG8_SCHED;
;             PG8_LDA(At, 1, 1); PG8_STAGE(PG8_SB(1, 0), rB2, b3, voffB); PG8_STAGE(PG8_SB(1, 1), rB2, b3 + hstep, voffB); PG8_STAGE(PG8_SA(1, 0), rA2, a3, voffA);
;             PG8_WAIT_V(8); PG8_WAIT_L(0); PG8_BAR; PG8_MMA(1, 0, At, B0); PG8_MMA(1, 1, At, B1); PG8_BAR; PG8_SCHED;
	s_mov_b32 m0, s42
	s_nop 0
	buffer_load_dwordx4 v175, s[12:15], s67 offen lds
	s_mov_b32 m0, s43
	s_nop 0
	buffer_load_dwordx4 v177, s[12:15], s67 offen lds
	v_add_u32_e32 v132, 0x18000, v180
	v_add_u32_e32 v156, 0x1c000, v180
	ds_read_b128 v[96:99], v132
	ds_read_b128 v[108:111], v132 offset:1024
	ds_read_b128 v[120:123], v132 offset:2048
	ds_read_b128 v[132:135], v132 offset:3072
	ds_read_b128 v[136:139], v156
	ds_read_b128 v[144:147], v156 offset:1024
	ds_read_b128 v[152:155], v156 offset:2048
	ds_read_b128 v[156:159], v156 offset:3072
	s_add_i32 s66, s66, s33
	s_mov_b32 m0, s45
	ds_read_b128 v[160:163], v181 offset:32768
	ds_read_b128 v[164:167], v181 offset:33792
	ds_read_b128 v[168:171], v181 offset:34816
	ds_read_b128 v[182:185], v181 offset:35840
	ds_read_b128 v[186:189], v181 offset:36864
	ds_read_b128 v[190:193], v181 offset:37888
	ds_read_b128 v[194:197], v181 offset:38912
	ds_read_b128 v[198:201], v181 offset:39936
	buffer_load_dwordx4 v174, s[36:39], s66 offen lds
	s_mov_b32 m0, s46
	s_nop 0
	buffer_load_dwordx4 v176, s[36:39], s66 offen lds
	s_waitcnt vmcnt(8)
	s_waitcnt lgkmcnt(0)
	s_barrier
	s_setprio 1
	v_mfma_f32_16x16x32_bf16 v[148:151], v[96:99], v[160:163], v[148:151]
	v_mfma_f32_16x16x32_bf16 v[140:143], v[120:123], v[160:163], v[140:143]
	v_mfma_f32_16x16x32_bf16 v[116:119], v[96:99], v[168:171], v[116:119]
	v_mfma_f32_16x16x32_bf16 v[112:115], v[120:123], v[168:171], v[112:115]
	v_mfma_f32_16x16x32_bf16 v[92:95], v[96:99], v[186:189], v[92:95]
	v_mfma_f32_16x16x32_bf16 v[88:91], v[120:123], v[186:189], v[88:91]
	v_mfma_f32_16x16x32_bf16 v[76:79], v[96:99], v[194:197], v[76:79]
	v_mfma_f32_16x16x32_bf16 v[72:75], v[120:123], v[194:197], v[72:75]
	v_mfma_f32_16x16x32_bf16 v[148:151], v[108:111], v[164:167], v[148:151]
	v_mfma_f32_16x16x32_bf16 v[140:143], v[132:135], v[164:167], v[140:143]
	v_mfma_f32_16x16x32_bf16 v[116:119], v[108:111], v[182:185], v[116:119]
	v_mfma_f32_16x16x32_bf16 v[112:115], v[132:135], v[182:185], v[112:115]
	v_mfma_f32_16x16x32_bf16 v[92:95], v[108:111], v[190:193], v[92:95]
	v_mfma_f32_16x16x32_bf16 v[88:91], v[132:135], v[190:193], v[88:91]
	v_mfma_f32_16x16x32_bf16 v[76:79], v[108:111], v[198:201], v[76:79]
	v_mfma_f32_16x16x32_bf16 v[72:75], v[132:135], v[198:201], v[72:75]
	v_mfma_f32_16x16x32_bf16 v[128:131], v[136:139], v[160:163], v[128:131]
	v_mfma_f32_16x16x32_bf16 v[124:127], v[152:155], v[160:163], v[124:127]
	v_mfma_f32_16x16x32_bf16 v[104:107], v[136:139], v[168:171], v[104:107]
	v_mfma_f32_16x16x32_bf16 v[100:103], v[152:155], v[168:171], v[100:103]
	v_mfma_f32_16x16x32_bf16 v[84:87], v[136:139], v[186:189], v[84:87]
	v_mfma_f32_16x16x32_bf16 v[80:83], v[152:155], v[186:189], v[80:83]
	v_mfma_f32_16x16x32_bf16 v[68:71], v[136:139], v[194:197], v[68:71]
	v_mfma_f32_16x16x32_bf16 v[64:67], v[152:155], v[194:197], v[64:67]
	v_mfma_f32_16x16x32_bf16 v[128:131], v[144:147], v[164:167], v[128:131]
	v_mfma_f32_16x16x32_bf16 v[124:127], v[156:159], v[164:167], v[124:127]
	v_mfma_f32_16x16x32_bf16 v[104:107], v[144:147], v[182:185], v[104:107]
	v_mfma_f32_16x16x32_bf16 v[100:103], v[156:159], v[182:185], v[100:103]
	v_mfma_f32_16x16x32_bf16 v[84:87], v[144:147], v[190:193], v[84:87]
	v_mfma_f32_16x16x32_bf16 v[80:83], v[156:159], v[190:193], v[80:83]
	v_mfma_f32_16x16x32_bf16 v[68:71], v[144:147], v[198:201], v[68:71]
	v_mfma_f32_16x16x32_bf16 v[64:67], v[156:159], v[198:201], v[64:67]
	s_setprio 0
	s_barrier
	s_mov_b32 m0, s47
	s_bitset1_b32 s55, 7
	buffer_load_dwordx4 v175, s[12:15], s55 offen lds
	s_mov_b32 m0, s48
	ds_read_b128 v[160:163], v181 offset:49152
	buffer_load_dwordx4 v177, s[12:15], s55 offen lds
	s_add_i32 s55, s55, s33
	s_mov_b32 m0, s56
	ds_read_b128 v[164:167], v181 offset:50176
	buffer_load_dwordx4 v175, s[12:15], s55 offen lds
	s_mov_b32 m0, s57
	ds_read_b128 v[168:171], v181 offset:51200
	buffer_load_dwordx4 v177, s[12:15], s55 offen lds
	s_mov_b32 m0, s52
	ds_read_b128 v[182:185], v181 offset:52224
	buffer_load_dwordx4 v174, s[36:39], s54 offen lds
	s_mov_b32 m0, s53
	ds_read_b128 v[186:189], v181 offset:53248
	buffer_load_dwordx4 v176, s[36:39], s54 offen lds
	ds_read_b128 v[190:193], v181 offset:54272
	ds_read_b128 v[194:197], v181 offset:55296
	ds_read_b128 v[198:201], v181 offset:56320
	s_waitcnt vmcnt(8)
	s_waitcnt lgkmcnt(0)
	s_barrier
	s_setprio 1
	v_mfma_f32_16x16x32_bf16 v[60:63], v[96:99], v[160:163], v[60:63]
	v_mfma_f32_16x16x32_bf16 v[56:59], v[120:123], v[160:163], v[56:59]
	v_mfma_f32_16x16x32_bf16 v[44:47], v[96:99], v[168:171], v[44:47]
	v_mfma_f32_16x16x32_bf16 v[40:43], v[120:123], v[168:171], v[40:43]
	v_mfma_f32_16x16x32_bf16 v[28:31], v[96:99], v[186:189], v[28:31]
	v_mfma_f32_16x16x32_bf16 v[24:27], v[120:123], v[186:189], v[24:27]
	v_mfma_f32_16x16x32_bf16 v[12:15], v[96:99], v[194:197], v[12:15]
	v_mfma_f32_16x16x32_bf16 v[8:11], v[120:123], v[194:197], v[8:11]
	v_mfma_f32_16x16x32_bf16 v[60:63], v[108:111], v[164:167], v[60:63]
	v_mfma_f32_16x16x32_bf16 v[56:59], v[132:135], v[164:167], v[56:59]
	v_mfma_f32_16x16x32_bf16 v[44:47], v[108:111], v[182:185], v[44:47]
	v_mfma_f32_16x16x32_bf16 v[40:43], v[132:135], v[182:185], v[40:43]
	v_mfma_f32_16x16x32_bf16 v[28:31], v[108:111], v[190:193], v[28:31]
	v_mfma_f32_16x16x32_bf16 v[24:27], v[132:135], v[190:193], v[24:27]
	v_mfma_f32_16x16x32_bf16 v[12:15], v[108:111], v[198:201], v[12:15]
	v_mfma_f32_16x16x32_bf16 v[8:11], v[132:135], v[198:201], v[8:11]
	v_mfma_f32_16x16x32_bf16 v[52:55], v[136:139], v[160:163], v[52:55]
	v_mfma_f32_16x16x32_bf16 v[48:51], v[152:155], v[160:163], v[48:51]
	v_mfma_f32_16x16x32_bf16 v[36:39], v[136:139], v[168:171], v[36:39]
	v_mfma_f32_16x16x32_bf16 v[32:35], v[152:155], v[168:171], v[32:35]
	v_mfma_f32_16x16x32_bf16 v[20:23], v[136:139], v[186:189], v[20:23]
	v_mfma_f32_16x16x32_bf16 v[16:19], v[152:155], v[186:189], v[16:19]
	v_mfma_f32_16x16x32_bf16 v[4:7], v[136:139], v[194:197], v[4:7]
	v_mfma_f32_16x16x32_bf16 v[0:3], v[152:155], v[194:197], v[0:3]
	v_mfma_f32_16x16x32_bf16 v[52:55], v[144:147], v[164:167], v[52:55]
	v_mfma_f32_16x16x32_bf16 v[48:51], v[156:159], v[164:167], v[48:51]
	v_mfma_f32_16x16x32_bf16 v[36:39], v[144:147], v[182:185], v[36:39]
	v_mfma_f32_16x16x32_bf16 v[32:35], v[156:159], v[182:185], v[32:35]
	v_mfma_f32_16x16x32_bf16 v[20:23], v[144:147], v[190:193], v[20:23]
	v_mfma_f32_16x16x32_bf16 v[16:19], v[156:159], v[190:193], v[16:19]
	v_mfma_f32_16x16x32_bf16 v[4:7], v[144:147], v[198:201], v[4:7]
	v_mfma_f32_16x16x32_bf16 v[0:3], v[156:159], v[198:201], v[0:3]
	s_setprio 0
	s_barrier
	s_add_i32 s11, s11, 2
	s_addk_i32 s4, 0x100
	s_addk_i32 s5, 0x100
	s_cmp_ge_i32 s11, s60
	s_cbranch_scc0 .LBB0_1004
	s_branch .Lzp_after_1004
; #define PG8_STAGE(bufoff, rs_, soff_, voff) do { _Pragma("unroll") for (int _i = 0; _i < 2; ++_i) \
;         __builtin_amdgcn_raw_ptr_buffer_load_lds(rs_, (LAS void*)(lds + (bufoff) + ldsw + _i * 8192), 16, (int)(voff)[_i], (int)(soff_), 0, 0); } while (0)
; #define PG8_LDA(dst, b, h) do { _Pragma("unroll") for (int m = 0; m < 4; ++m) dst[m] = PG8_LD2(lds + PG8_SA(b, h) + aoff + m * 2048); } while (0)
; #define PG8_LDB(dst, b, h) do { _Pragma("unroll") for (int n = 0; n < 2; ++n) dst[n] = PG8_LD2(lds + PG8_SB(b, h) + boff + n * 2048); } while (0)
; template <class Epi, class Sched, bool ALIGN_EPI = false, bool SP2 = false, bool FP8 = false>
; __device__ __forceinline__ void gemm_phase(LAS unsigned char* lds, const Gemm g, const Sched& S, const Epi& E, int wbase) {
;     ...
;         for (int t = 0; t < nt; t += 2) {
;             const bool last = (t == nt - 2);
;             const unsigned a1 = cA + (unsigned)(t + 1) * kstep;
;             const unsigned a2 = last ? nA : cA + (unsigned)(t + 2) * kstep, b2 = last ? nB : cB + (unsigned)(t + 2) * kstep; const rsrc_t rA2 = (Sched::TWO && last) ? rAn : rAc, rB2 = (Sched::TWO && last) ? rBn : rBc;
;             const unsigned a3 = a2 + kstep, b3 = b2 + kstep;
;             if (last && has_next) S.a_ready(nxt);
;             if constexpr (SP2) {
;             PG8_LDB(B0, 0, 0); PG8_LDB(B1, 0, 1); PG8_SCHED; PG8_LDA(At, 0, 0); PG8_STAGE(PG8_SA(1, 1), rAc, a1 + hstep, voffA);
;             PG8_WAIT_V(8); PG8_WAIT_L(0); PG8_BAR; PG8_MMA(0, 0, At, B0); PG8_MMA(0, 1, At, B1); PG8_BAR; PG8_SCHED;
;             PG8_LDA(At, 0, 1); PG8_STAGE(PG8_SB(0, 0), rB2, b2, voffB); PG8_STAGE(PG8_SB(0, 1), rB2, b2 + hstep, voffB); PG8_STAGE(PG8_SA(0, 0), rA2, a2, voffA);
;             PG8_WAIT_V(8); PG8_WAIT_L(0); PG8_BAR; PG8_MMA(1, 0, At, B0); PG8_MMA(1, 1, At, B1); PG8_BAR; PG8_SCHED;
;             PG8_LDB(B0, 1, 0); PG8_LDB(B1, 1, 1); PG8_SCHED; PG8_LDA(At, 1, 0); PG8_STAGE(PG8_SA(0, 1), rA2, a2 + hstep, voffA);
;             PG8_WAIT_V(8); PG8_WAIT_L(0); PG8_BAR; PG8_MMA(0, 0, At, B0); PG8_MMA(0, 1, At, B1); PG8_BAR; PG8_SCHED;
;             PG8_LDA(At, 1, 1); PG8_STAGE(PG8_SB(1, 0), rB2, b3, voffB); PG8_STAGE(PG8_SB(1, 1), rB2, b3 + hstep, voffB); PG8_STAGE(PG8_SA(1, 0), rA2, a3, voffA);
;             PG8_WAIT_V(8); PG8_WAIT_L(0); PG8_BAR; PG8_MMA(1, 0, At, B0); PG8_MMA(1, 1, At, B1); PG8_BAR; PG8_SCHED;
.LBB0_1004:
	v_add_u32_e32 v132, 0x10000, v180
	v_add_u32_e32 v156, 0x14000, v180
	ds_read_b128 v[96:99], v132
	ds_read_b128 v[108:111], v132 offset:1024
	ds_read_b128 v[120:123], v132 offset:2048
	ds_read_b128 v[132:135], v132 offset:3072
	ds_read_b128 v[136:139], v156
	ds_read_b128 v[144:147], v156 offset:1024
	ds_read_b128 v[152:155], v156 offset:2048
	ds_read_b128 v[156:159], v156 offset:3072
	s_add_i32 s14, s4, 0x80
	s_cmp_eq_u32 s62, s11
	s_cselect_b32 s66, s2, s14
	s_cselect_b32 s55, s3, s5
	s_or_b32 s54, s66, 0x80
	s_add_i32 s14, s33, s4
	s_mov_b32 m0, s63
	ds_read_b128 v[160:163], v181
	ds_read_b128 v[164:167], v181 offset:1024
	ds_read_b128 v[168:171], v181 offset:2048
	ds_read_b128 v[182:185], v181 offset:3072
	ds_read_b128 v[186:189], v181 offset:4096
	ds_read_b128 v[190:193], v181 offset:5120
	ds_read_b128 v[194:197], v181 offset:6144
	ds_read_b128 v[198:201], v181 offset:7168
	buffer_load_dwordx4 v174, s[36:39], s14 offen lds
	s_mov_b32 m0, s65
	s_nop 0
	buffer_load_dwordx4 v176, s[36:39], s14 offen lds
	s_waitcnt vmcnt(8)
	s_waitcnt lgkmcnt(0)
	s_barrier
	s_setprio 1
	v_mfma_f32_16x16x32_bf16 v[148:151], v[96:99], v[160:163], v[148:151]
	v_mfma_f32_16x16x32_bf16 v[140:143], v[120:123], v[160:163], v[140:143]
	v_mfma_f32_16x16x32_bf16 v[116:119], v[96:99], v[168:171], v[116:119]
	v_mfma_f32_16x16x32_bf16 v[112:115], v[120:123], v[168:171], v[112:115]
	v_mfma_f32_16x16x32_bf16 v[92:95], v[96:99], v[186:189], v[92:95]
	v_mfma_f32_16x16x32_bf16 v[88:91], v[120:123], v[186:189], v[88:91]
	v_mfma_f32_16x16x32_bf16 v[76:79], v[96:99], v[194:197], v[76:79]
	v_mfma_f32_16x16x32_bf16 v[72:75], v[120:123], v[194:197], v[72:75]
	v_mfma_f32_16x16x32_bf16 v[148:151], v[108:111], v[164:167], v[148:151]
	v_mfma_f32_16x16x32_bf16 v[140:143], v[132:135], v[164:167], v[140:143]
	v_mfma_f32_16x16x32_bf16 v[116:119], v[108:111], v[182:185], v[116:119]
	v_mfma_f32_16x16x32_bf16 v[112:115], v[132:135], v[182:185], v[112:115]
	v_mfma_f32_16x16x32_bf16 v[92:95], v[108:111], v[190:193], v[92:95]
	v_mfma_f32_16x16x32_bf16 v[88:91], v[132:135], v[190:193], v[88:91]
	v_mfma_f32_16x16x32_bf16 v[76:79], v[108:111], v[198:201], v[76:79]
	v_mfma_f32_16x16x32_bf16 v[72:75], v[132:135], v[198:201], v[72:75]
	v_mfma_f32_16x16x32_bf16 v[128:131], v[136:139], v[160:163], v[128:131]
	v_mfma_f32_16x16x32_bf16 v[124:127], v[152:155], v[160:163], v[124:127]
	v_mfma_f32_16x16x32_bf16 v[104:107], v[136:139], v[168:171], v[104:107]
	v_mfma_f32_16x16x32_bf16 v[100:103], v[152:155], v[168:171], v[100:103]
	v_mfma_f32_16x16x32_bf16 v[84:87], v[136:139], v[186:189], v[84:87]
	v_mfma_f32_16x16x32_bf16 v[80:83], v[152:155], v[186:189], v[80:83]
	v_mfma_f32_16x16x32_bf16 v[68:71], v[136:139], v[194:197], v[68:71]
	v_mfma_f32_16x16x32_bf16 v[64:67], v[152:155], v[194:197], v[64:67]
	v_mfma_f32_16x16x32_bf16 v[128:131], v[144:147], v[164:167], v[128:131]
	v_mfma_f32_16x16x32_bf16 v[124:127], v[156:159], v[164:167], v[124:127]
	v_mfma_f32_16x16x32_bf16 v[104:107], v[144:147], v[182:185], v[104:107]
	v_mfma_f32_16x16x32_bf16 v[100:103], v[156:159], v[182:185], v[100:103]
	v_mfma_f32_16x16x32_bf16 v[84:87], v[144:147], v[190:193], v[84:87]
	v_mfma_f32_16x16x32_bf16 v[80:83], v[156:159], v[190:193], v[80:83]
	v_mfma_f32_16x16x32_bf16 v[68:71], v[144:147], v[198:201], v[68:71]
	v_mfma_f32_16x16x32_bf16 v[64:67], v[156:159], v[198:201], v[64:67]
	s_setprio 0
	s_barrier
	s_mov_b32 m0, s35
	s_mov_b32 s14, s38
	s_mov_b32 s15, s39
	buffer_load_dwordx4 v175, s[12:15], s55 offen lds
	s_mov_b32 m0, s41
	ds_read_b128 v[160:163], v181 offset:16384
	s_add_i32 s67, s55, s33
	buffer_load_dwordx4 v177, s[12:15], s55 offen lds
	s_mov_b32 m0, s34
	ds_read_b128 v[164:167], v181 offset:17408
	buffer_load_dwordx4 v174, s[36:39], s66 offen lds
	s_mov_b32 m0, s44
	ds_read_b128 v[168:171], v181 offset:18432
	buffer_load_dwordx4 v176, s[36:39], s66 offen lds
	ds_read_b128 v[182:185], v181 offset:19456
	ds_read_b128 v[186:189], v181 offset:20480
	ds_read_b128 v[190:193], v181 offset:21504
	ds_read_b128 v[194:197], v181 offset:22528
	ds_read_b128 v[198:201], v181 offset:23552
	s_waitcnt vmcnt(6)
	s_waitcnt lgkmcnt(0)
	s_barrier
	s_setprio 1
	v_mfma_f32_16x16x32_bf16 v[60:63], v[96:99], v[160:163], v[60:63]
	v_mfma_f32_16x16x32_bf16 v[56:59], v[120:123], v[160:163], v[56:59]
	v_mfma_f32_16x16x32_bf16 v[44:47], v[96:99], v[168:171], v[44:47]
	v_mfma_f32_16x16x32_bf16 v[40:43], v[120:123], v[168:171], v[40:43]
	v_mfma_f32_16x16x32_bf16 v[28:31], v[96:99], v[186:189], v[28:31]
	v_mfma_f32_16x16x32_bf16 v[24:27], v[120:123], v[186:189], v[24:27]
	v_mfma_f32_16x16x32_bf16 v[12:15], v[96:99], v[194:197], v[12:15]
	v_mfma_f32_16x16x32_bf16 v[8:11], v[120:123], v[194:197], v[8:11]
	v_mfma_f32_16x16x32_bf16 v[60:63], v[108:111], v[164:167], v[60:63]
	v_mfma_f32_16x16x32_bf16 v[56:59], v[132:135], v[164:167], v[56:59]
	v_mfma_f32_16x16x32_bf16 v[44:47], v[108:111], v[182:185], v[44:47]
	v_mfma_f32_16x16x32_bf16 v[40:43], v[132:135], v[182:185], v[40:43]
	v_mfma_f32_16x16x32_bf16 v[28:31], v[108:111], v[190:193], v[28:31]
	v_mfma_f32_16x16x32_bf16 v[24:27], v[132:135], v[190:193], v[24:27]
	v_mfma_f32_16x16x32_bf16 v[12:15], v[108:111], v[198:201], v[12:15]
	v_mfma_f32_16x16x32_bf16 v[8:11], v[132:135], v[198:201], v[8:11]
	v_mfma_f32_16x16x32_bf16 v[52:55], v[136:139], v[160:163], v[52:55]
	v_mfma_f32_16x16x32_bf16 v[48:51], v[152:155], v[160:163], v[48:51]
	v_mfma_f32_16x16x32_bf16 v[36:39], v[136:139], v[168:171], v[36:39]
	v_mfma_f32_16x16x32_bf16 v[32:35], v[152:155], v[168:171], v[32:35]
	v_mfma_f32_16x16x32_bf16 v[20:23], v[136:139], v[186:189], v[20:23]
	v_mfma_f32_16x16x32_bf16 v[16:19], v[152:155], v[186:189], v[16:19]
	v_mfma_f32_16x16x32_bf16 v[4:7], v[136:139], v[194:197], v[4:7]
	v_mfma_f32_16x16x32_bf16 v[0:3], v[152:155], v[194:197], v[0:3]
	v_mfma_f32_16x16x32_bf16 v[52:55], v[144:147], v[164:167], v[52:55]
	v_mfma_f32_16x16x32_bf16 v[48:51], v[156:159], v[164:167], v[48:51]
	v_mfma_f32_16x16x32_bf16 v[36:39], v[144:147], v[182:185], v[36:39]
	v_mfma_f32_16x16x32_bf16 v[32:35], v[156:159], v[182:185], v[32:35]
	v_mfma_f32_16x16x32_bf16 v[20:23], v[144:147], v[190:193], v[20:23]
	v_mfma_f32_16x16x32_bf16 v[16:19], v[156:159], v[190:193], v[16:19]
	v_mfma_f32_16x16x32_bf16 v[4:7], v[144:147], v[198:201], v[4:7]
	v_mfma_f32_16x16x32_bf16 v[0:3], v[156:159], v[198:201], v[0:3]
	s_setprio 0
	s_barrier
; #define PG8_STAGE(bufoff, rs_, soff_, voff) do { _Pragma("unroll") for (int _i = 0; _i < 2; ++_i) \
;         __builtin_amdgcn_raw_ptr_buffer_load_lds(rs_, (LAS void*)(lds + (bufoff) + ldsw + _i * 8192), 16, (int)(voff)[_i], (int)(soff_), 0, 0); } while (0)
; #define PG8_LDA(dst, b, h) do { _Pragma("unroll") for (int m = 0; m < 4; ++m) dst[m] = PG8_LD2(lds + PG8_SA(b, h) + aoff + m * 2048); } while (0)
; #define PG8_LDB(dst, b, h) do { _Pragma("unroll") for (int n = 0; n < 2; ++n) dst[n] = PG8_LD2(lds + PG8_SB(b, h) + boff + n * 2048); } while (0)
; #define PG8_WAIT_V(n) asm volatile("s_waitcnt vmcnt(" #n ")" ::: "memory")
; #define PG8_WAIT_L(n) asm volatile("s_waitcnt lgkmcnt(" #n ")" ::: "memory")
; #define PG8_BAR __builtin_amdgcn_s_barrier()
; #define PG8_SCHED __builtin_amdgcn_sched_barrier(0)
; template <class Epi, class Sched, bool ALIGN_EPI = false, bool SP2 = false, bool FP8 = false>
; __device__ __forceinline__ void gemm_phase(LAS unsigned char* lds, const Gemm g, const Sched& S, const Epi& E, int wbase) {
;     ...
;             PG8_LDB(B0, 0, 0); PG8_LDB(B1, 0, 1); PG8_SCHED; PG8_LDA(At, 0, 0); PG8_STAGE(PG8_SA(1, 1), rAc, a1 + hstep, voffA);
;             PG8_WAIT_V(8); PG8_WAIT_L(0); PG8_BAR; PG8_MMA(0, 0, At, B0); PG8_MMA(0, 1, At, B1); PG8_BAR; PG8_SCHED;
;             PG8_LDA(At, 0, 1); PG8_STAGE(PG8_SB(0, 0), rB2, b2, voffB); PG8_STAGE(PG8_SB(0, 1), rB2, b2 + hstep, voffB); PG8_STAGE(PG8_SA(0, 0), rA2, a2, voffA);
;             PG8_WAIT_V(8); PG8_WAIT_L(0); PG8_BAR; PG8_MMA(1, 0, At, B0); PG8_MMA(1, 1, At, B1); PG8_BAR; PG8_SCHED;
;             PG8_LDB(B0, 1, 0); PG8_LDB(B1, 1, 1); PG8_SCHED; PG8_LDA(At, 1, 0); PG8_STAGE(PG8_SA(0, 1), rA2, a2 + hstep, voffA);
;             PG8_WAIT_V(8); PG8_WAIT_L(0); PG8_BAR; PG8_MMA(0, 0, At, B0); PG8_MMA(0, 1, At, B1); PG8_BAR; PG8_SCHED;
;             PG8_LDA(At, 1, 1); PG8_STAGE(PG8_SB(1, 0), rB2, b3, voffB); PG8_STAGE(PG8_SB(1, 1), rB2, b3 + hstep, voffB); PG8_STAGE(PG8_SA(1, 0), rA2, a3, voffA);
;             PG8_WAIT_V(8); PG8_WAIT_L(0); PG8_BAR; PG8_MMA(1, 0, At, B0); PG8_MMA(1, 1, At, B1); PG8_BAR; PG8_SCHED;
	s_mov_b32 m0, s42
	s_nop 0
	buffer_load_dwordx4 v175, s[12:15], s67 offen lds
	s_mov_b32 m0, s43
	s_nop 0
	buffer_load_dwordx4 v177, s[12:15], s67 offen lds
	v_add_u32_e32 v132, 0x18000, v180
	v_add_u32_e32 v156, 0x1c000, v180
	ds_read_b128 v[96:99], v132
	ds_read_b128 v[108:111], v132 offset:1024
	ds_read_b128 v[120:123], v132 offset:2048
	ds_read_b128 v[132:135], v132 offset:3072
	ds_read_b128 v[136:139], v156
	ds_read_b128 v[144:147], v156 offset:1024
	ds_read_b128 v[152:155], v156 offset:2048
	ds_read_b128 v[156:159], v156 offset:3072
	s_add_i32 s66, s66, s33
	s_mov_b32 m0, s45
	ds_read_b128 v[160:163], v181 offset:32768
	ds_read_b128 v[164:167], v181 offset:33792
	ds_read_b128 v[168:171], v181 offset:34816
	ds_read_b128 v[182:185], v181 offset:35840
	ds_read_b128 v[186:189], v181 offset:36864
	ds_read_b128 v[190:193], v181 offset:37888
	ds_read_b128 v[194:197], v181 offset:38912
	ds_read_b128 v[198:201], v181 offset:39936
	buffer_load_dwordx4 v174, s[36:39], s66 offen lds
	s_mov_b32 m0, s46
	s_nop 0
	buffer_load_dwordx4 v176, s[36:39], s66 offen lds
	s_waitcnt vmcnt(8)
	s_waitcnt lgkmcnt(0)
	s_barrier
	s_setprio 1
	v_mfma_f32_16x16x32_bf16 v[148:151], v[96:99], v[160:163], v[148:151]
	v_mfma_f32_16x16x32_bf16 v[140:143], v[120:123], v[160:163], v[140:143]
	v_mfma_f32_16x16x32_bf16 v[116:119], v[96:99], v[168:171], v[116:119]
	v_mfma_f32_16x16x32_bf16 v[112:115], v[120:123], v[168:171], v[112:115]
	v_mfma_f32_16x16x32_bf16 v[92:95], v[96:99], v[186:189], v[92:95]
	v_mfma_f32_16x16x32_bf16 v[88:91], v[120:123], v[186:189], v[88:91]
	v_mfma_f32_16x16x32_bf16 v[76:79], v[96:99], v[194:197], v[76:79]
	v_mfma_f32_16x16x32_bf16 v[72:75], v[120:123], v[194:197], v[72:75]
	v_mfma_f32_16x16x32_bf16 v[148:151], v[108:111], v[164:167], v[148:151]
	v_mfma_f32_16x16x32_bf16 v[140:143], v[132:135], v[164:167], v[140:143]
	v_mfma_f32_16x16x32_bf16 v[116:119], v[108:111], v[182:185], v[116:119]
	v_mfma_f32_16x16x32_bf16 v[112:115], v[132:135], v[182:185], v[112:115]
	v_mfma_f32_16x16x32_bf16 v[92:95], v[108:111], v[190:193], v[92:95]
	v_mfma_f32_16x16x32_bf16 v[88:91], v[132:135], v[190:193], v[88:91]
	v_mfma_f32_16x16x32_bf16 v[76:79], v[108:111], v[198:201], v[76:79]
	v_mfma_f32_16x16x32_bf16 v[72:75], v[132:135], v[198:201], v[72:75]
	v_mfma_f32_16x16x32_bf16 v[128:131], v[136:139], v[160:163], v[128:131]
	v_mfma_f32_16x16x32_bf16 v[124:127], v[152:155], v[160:163], v[124:127]
	v_mfma_f32_16x16x32_bf16 v[104:107], v[136:139], v[168:171], v[104:107]
	v_mfma_f32_16x16x32_bf16 v[100:103], v[152:155], v[168:171], v[100:103]
	v_mfma_f32_16x16x32_bf16 v[84:87], v[136:139], v[186:189], v[84:87]
	v_mfma_f32_16x16x32_bf16 v[80:83], v[152:155], v[186:189], v[80:83]
	v_mfma_f32_16x16x32_bf16 v[68:71], v[136:139], v[194:197], v[68:71]
	v_mfma_f32_16x16x32_bf16 v[64:67], v[152:155], v[194:197], v[64:67]
	v_mfma_f32_16x16x32_bf16 v[128:131], v[144:147], v[164:167], v[128:131]
	v_mfma_f32_16x16x32_bf16 v[124:127], v[156:159], v[164:167], v[124:127]
	v_mfma_f32_16x16x32_bf16 v[104:107], v[144:147], v[182:185], v[104:107]
	v_mfma_f32_16x16x32_bf16 v[100:103], v[156:159], v[182:185], v[100:103]
	v_mfma_f32_16x16x32_bf16 v[84:87], v[144:147], v[190:193], v[84:87]
	v_mfma_f32_16x16x32_bf16 v[80:83], v[156:159], v[190:193], v[80:83]
	v_mfma_f32_16x16x32_bf16 v[68:71], v[144:147], v[198:201], v[68:71]
	v_mfma_f32_16x16x32_bf16 v[64:67], v[156:159], v[198:201], v[64:67]
	s_setprio 0
	s_barrier
	s_mov_b32 m0, s47
	s_bitset1_b32 s55, 7
	buffer_load_dwordx4 v175, s[12:15], s55 offen lds
	s_mov_b32 m0, s48
	ds_read_b128 v[160:163], v181 offset:49152
	buffer_load_dwordx4 v177, s[12:15], s55 offen lds
	s_add_i32 s55, s55, s33
	s_mov_b32 m0, s56
	ds_read_b128 v[164:167], v181 offset:50176
	buffer_load_dwordx4 v175, s[12:15], s55 offen lds
	s_mov_b32 m0, s57
	ds_read_b128 v[168:171], v181 offset:51200
	buffer_load_dwordx4 v177, s[12:15], s55 offen lds
	s_mov_b32 m0, s52
	ds_read_b128 v[182:185], v181 offset:52224
	buffer_load_dwordx4 v174, s[36:39], s54 offen lds
	s_mov_b32 m0, s53
	ds_read_b128 v[186:189], v181 offset:53248
	buffer_load_dwordx4 v176, s[36:39], s54 offen lds
	ds_read_b128 v[190:193], v181 offset:54272
	ds_read_b128 v[194:197], v181 offset:55296
	ds_read_b128 v[198:201], v181 offset:56320
	s_waitcnt vmcnt(8)
	s_waitcnt lgkmcnt(0)
	s_barrier
	s_setprio 1
	v_mfma_f32_16x16x32_bf16 v[60:63], v[96:99], v[160:163], v[60:63]
	v_mfma_f32_16x16x32_bf16 v[56:59], v[120:123], v[160:163], v[56:59]
	v_mfma_f32_16x16x32_bf16 v[44:47], v[96:99], v[168:171], v[44:47]
	v_mfma_f32_16x16x32_bf16 v[40:43], v[120:123], v[168:171], v[40:43]
	v_mfma_f32_16x16x32_bf16 v[28:31], v[96:99], v[186:189], v[28:31]
	v_mfma_f32_16x16x32_bf16 v[24:27], v[120:123], v[186:189], v[24:27]
	v_mfma_f32_16x16x32_bf16 v[12:15], v[96:99], v[194:197], v[12:15]
	v_mfma_f32_16x16x32_bf16 v[8:11], v[120:123], v[194:197], v[8:11]
	v_mfma_f32_16x16x32_bf16 v[60:63], v[108:111], v[164:167], v[60:63]
	v_mfma_f32_16x16x32_bf16 v[56:59], v[132:135], v[164:167], v[56:59]
	v_mfma_f32_16x16x32_bf16 v[44:47], v[108:111], v[182:185], v[44:47]
	v_mfma_f32_16x16x32_bf16 v[40:43], v[132:135], v[182:185], v[40:43]
	v_mfma_f32_16x16x32_bf16 v[28:31], v[108:111], v[190:193], v[28:31]
	v_mfma_f32_16x16x32_bf16 v[24:27], v[132:135], v[190:193], v[24:27]
	v_mfma_f32_16x16x32_bf16 v[12:15], v[108:111], v[198:201], v[12:15]
	v_mfma_f32_16x16x32_bf16 v[8:11], v[132:135], v[198:201], v[8:11]
	v_mfma_f32_16x16x32_bf16 v[52:55], v[136:139], v[160:163], v[52:55]
	v_mfma_f32_16x16x32_bf16 v[48:51], v[152:155], v[160:163], v[48:51]
	v_mfma_f32_16x16x32_bf16 v[36:39], v[136:139], v[168:171], v[36:39]
	v_mfma_f32_16x16x32_bf16 v[32:35], v[152:155], v[168:171], v[32:35]
	v_mfma_f32_16x16x32_bf16 v[20:23], v[136:139], v[186:189], v[20:23]
	v_mfma_f32_16x16x32_bf16 v[16:19], v[152:155], v[186:189], v[16:19]
	v_mfma_f32_16x16x32_bf16 v[4:7], v[136:139], v[194:197], v[4:7]
	v_mfma_f32_16x16x32_bf16 v[0:3], v[152:155], v[194:197], v[0:3]
	v_mfma_f32_16x16x32_bf16 v[52:55], v[144:147], v[164:167], v[52:55]
	v_mfma_f32_16x16x32_bf16 v[48:51], v[156:159], v[164:167], v[48:51]
	v_mfma_f32_16x16x32_bf16 v[36:39], v[144:147], v[182:185], v[36:39]
	v_mfma_f32_16x16x32_bf16 v[32:35], v[156:159], v[182:185], v[32:35]
	v_mfma_f32_16x16x32_bf16 v[20:23], v[144:147], v[190:193], v[20:23]
	v_mfma_f32_16x16x32_bf16 v[16:19], v[156:159], v[190:193], v[16:19]
	v_mfma_f32_16x16x32_bf16 v[4:7], v[144:147], v[198:201], v[4:7]
	v_mfma_f32_16x16x32_bf16 v[0:3], v[156:159], v[198:201], v[0:3]
	s_setprio 0
	s_barrier
	s_add_i32 s11, s11, 2
	s_addk_i32 s4, 0x100
	s_addk_i32 s5, 0x100
	s_cmp_ge_i32 s11, s60
	s_cbranch_scc0 .LBB0_1004

; #define PG8_STAGE(bufoff, rs_, soff_, voff) do { _Pragma("unroll") for (int _i = 0; _i < 2; ++_i) \
;         __builtin_amdgcn_raw_ptr_buffer_load_lds(rs_, (LAS void*)(lds + (bufoff) + ldsw + _i * 8192), 16, (int)(voff)[_i], (int)(soff_), 0, 0); } while (0)
; #define PG8_LDA(dst, b, h) do { _Pragma("unroll") for (int m = 0; m < 4; ++m) dst[m] = PG8_LD2(lds + PG8_SA(b, h) + aoff + m * 2048); } while (0)
; #define PG8_LDB(dst, b, h) do { _Pragma("unroll") for (int n = 0; n < 2; ++n) dst[n] = PG8_LD2(lds + PG8_SB(b, h) + boff + n * 2048); } while (0)
; #define PG8_WAIT_V(n) asm volatile("s_waitcnt vmcnt(" #n ")" ::: "memory")
; #define PG8_WAIT_L(n) asm volatile("s_waitcnt lgkmcnt(" #n ")" ::: "memory")
; #define PG8_BAR __builtin_amdgcn_s_barrier()
; #define PG8_SCHED __builtin_amdgcn_sched_barrier(0)
; template <class Epi, class Sched, bool ALIGN_EPI = false, bool SP2 = false, bool FP8 = false>
; __device__ __forceinline__ void gemm_phase(LAS unsigned char* lds, const Gemm g, const Sched& S, const Epi& E, int wbase) {
;     ...
;         for (int t = 0; t < nt; t += 2) {
;             const bool last = (t == nt - 2);
;             const unsigned a1 = cA + (unsigned)(t + 1) * kstep;
;             const unsigned a2 = last ? nA : cA + (unsigned)(t + 2) * kstep, b2 = last ? nB : cB + (unsigned)(t + 2) * kstep; const rsrc_t rA2 = (Sched::TWO && last) ? rAn : rAc, rB2 = (Sched::TWO && last) ? rBn : rBc;
;             const unsigned a3 = a2 + kstep, b3 = b2 + kstep;
;             if (last && has_next) S.a_ready(nxt);
;             if constexpr (SP2) {
;             PG8_LDB(B0, 0, 0); PG8_LDB(B1, 0, 1); PG8_SCHED; PG8_LDA(At, 0, 0); PG8_STAGE(PG8_SA(1, 1), rAc, a1 + hstep, voffA);
;             PG8_WAIT_V(8); PG8_WAIT_L(0); PG8_BAR; PG8_MMA(0, 0, At, B0); PG8_MMA(0, 1, At, B1); PG8_BAR; PG8_SCHED;
;             PG8_LDA(At, 0, 1); PG8_STAGE(PG8_SB(0, 0), rB2, b2, voffB); PG8_STAGE(PG8_SB(0, 1), rB2, b2 + hstep, voffB); PG8_STAGE(PG8_SA(0, 0), rA2, a2, voffA);
;             PG8_WAIT_V(8); PG8_WAIT_L(0); PG8_BAR; PG8_MMA(1, 0, At, B0); PG8_MMA(1, 1, At, B1); PG8_BAR; PG8_SCHED;
.LBB0_1348:
	v_add_u32_e32 v12, 0x10000, v199
	v_add_u32_e32 v28, 0x14000, v199
	ds_read_b128 v[0:3], v12
	ds_read_b128 v[4:7], v12 offset:1024
	ds_read_b128 v[8:11], v12 offset:2048
	ds_read_b128 v[12:15], v12 offset:3072
	ds_read_b128 v[16:19], v28
	ds_read_b128 v[20:23], v28 offset:1024
	ds_read_b128 v[24:27], v28 offset:2048
	ds_read_b128 v[28:31], v28 offset:3072
	s_add_i32 s6, s67, 0x80
	s_cmp_eq_u32 s65, s85
	s_cselect_b32 s54, s66, s6
	s_cselect_b64 vcc, -1, 0
	v_cndmask_b32_e32 v211, v210, v201, vcc
	s_or_b32 s78, s54, 0x80
	s_add_i32 s6, s41, s67
	s_mov_b32 m0, s76
	ds_read_b128 v[32:35], v200
	ds_read_b128 v[36:39], v200 offset:1024
	ds_read_b128 v[40:43], v200 offset:2048
	ds_read_b128 v[44:47], v200 offset:3072
	ds_read_b128 v[48:51], v200 offset:4096
	ds_read_b128 v[52:55], v200 offset:5120
	ds_read_b128 v[56:59], v200 offset:6144
	ds_read_b128 v[60:63], v200 offset:7168
	v_readfirstlane_b32 s55, v211
	s_add_i32 s20, s55, s41
	buffer_load_dwordx4 v192, s[36:39], s6 offen lds
	s_mov_b32 m0, s77
	s_nop 0
	buffer_load_dwordx4 v195, s[36:39], s6 offen lds
	s_waitcnt vmcnt(8)
	s_waitcnt lgkmcnt(0)
	s_barrier
	s_setprio 1
	v_mfma_f32_16x16x128_f8f6f4 v[184:187], v[0:7], v[32:39], v[184:187]
	v_mfma_f32_16x16x128_f8f6f4 v[188:191], v[8:15], v[32:39], v[188:191]
	v_mfma_f32_16x16x128_f8f6f4 v[168:171], v[0:7], v[40:47], v[168:171]
	v_mfma_f32_16x16x128_f8f6f4 v[172:175], v[8:15], v[40:47], v[172:175]
	v_mfma_f32_16x16x128_f8f6f4 v[152:155], v[0:7], v[48:55], v[152:155]
	v_mfma_f32_16x16x128_f8f6f4 v[156:159], v[8:15], v[48:55], v[156:159]
	v_mfma_f32_16x16x128_f8f6f4 v[136:139], v[0:7], v[56:63], v[136:139]
	v_mfma_f32_16x16x128_f8f6f4 v[140:143], v[8:15], v[56:63], v[140:143]
	v_mfma_f32_16x16x128_f8f6f4 v[176:179], v[16:23], v[32:39], v[176:179]
	v_mfma_f32_16x16x128_f8f6f4 v[180:183], v[24:31], v[32:39], v[180:183]
	v_mfma_f32_16x16x128_f8f6f4 v[160:163], v[16:23], v[40:47], v[160:163]
	v_mfma_f32_16x16x128_f8f6f4 v[164:167], v[24:31], v[40:47], v[164:167]
	v_mfma_f32_16x16x128_f8f6f4 v[144:147], v[16:23], v[48:55], v[144:147]
	v_mfma_f32_16x16x128_f8f6f4 v[148:151], v[24:31], v[48:55], v[148:151]
	v_mfma_f32_16x16x128_f8f6f4 v[128:131], v[16:23], v[56:63], v[128:131]
	v_mfma_f32_16x16x128_f8f6f4 v[132:135], v[24:31], v[56:63], v[132:135]
	s_setprio 0
	s_barrier
	s_mov_b32 s6, s38
	s_mov_b32 s7, s39
	s_mov_b32 m0, s43
	ds_read_b128 v[32:35], v200 offset:16384
	buffer_load_dwordx4 v194, s[4:7], s55 offen lds
	s_mov_b32 m0, s44
	ds_read_b128 v[36:39], v200 offset:17408
	buffer_load_dwordx4 v196, s[4:7], s55 offen lds
	s_mov_b32 m0, s42
	ds_read_b128 v[40:43], v200 offset:18432
	buffer_load_dwordx4 v192, s[36:39], s54 offen lds
	s_mov_b32 m0, s47
	ds_read_b128 v[44:47], v200 offset:19456
	buffer_load_dwordx4 v195, s[36:39], s54 offen lds
	ds_read_b128 v[48:51], v200 offset:20480
	ds_read_b128 v[52:55], v200 offset:21504
	ds_read_b128 v[56:59], v200 offset:22528
	ds_read_b128 v[60:63], v200 offset:23552
	s_waitcnt vmcnt(6)
	s_waitcnt lgkmcnt(0)
	s_barrier
	s_setprio 1
	v_mfma_f32_16x16x128_f8f6f4 v[120:123], v[0:7], v[32:39], v[120:123]
	v_mfma_f32_16x16x128_f8f6f4 v[124:127], v[8:15], v[32:39], v[124:127]
	v_mfma_f32_16x16x128_f8f6f4 v[104:107], v[0:7], v[40:47], v[104:107]
	v_mfma_f32_16x16x128_f8f6f4 v[108:111], v[8:15], v[40:47], v[108:111]
	v_mfma_f32_16x16x128_f8f6f4 v[88:91], v[0:7], v[48:55], v[88:91]
	v_mfma_f32_16x16x128_f8f6f4 v[92:95], v[8:15], v[48:55], v[92:95]
	v_mfma_f32_16x16x128_f8f6f4 v[72:75], v[0:7], v[56:63], v[72:75]
	v_mfma_f32_16x16x128_f8f6f4 v[76:79], v[8:15], v[56:63], v[76:79]
	v_mfma_f32_16x16x128_f8f6f4 v[112:115], v[16:23], v[32:39], v[112:115]
	v_mfma_f32_16x16x128_f8f6f4 v[116:119], v[24:31], v[32:39], v[116:119]
	v_mfma_f32_16x16x128_f8f6f4 v[96:99], v[16:23], v[40:47], v[96:99]
	v_mfma_f32_16x16x128_f8f6f4 v[100:103], v[24:31], v[40:47], v[100:103]
	v_mfma_f32_16x16x128_f8f6f4 v[80:83], v[16:23], v[48:55], v[80:83]
	v_mfma_f32_16x16x128_f8f6f4 v[84:87], v[24:31], v[48:55], v[84:87]
	v_mfma_f32_16x16x128_f8f6f4 v[68:71], v[16:23], v[56:63], v[68:71]
	v_mfma_f32_16x16x128_f8f6f4 v[64:67], v[24:31], v[56:63], v[64:67]
	s_setprio 0
	s_barrier
; #define PG8_STAGE(bufoff, rs_, soff_, voff) do { _Pragma("unroll") for (int _i = 0; _i < 2; ++_i) \
;         __builtin_amdgcn_raw_ptr_buffer_load_lds(rs_, (LAS void*)(lds + (bufoff) + ldsw + _i * 8192), 16, (int)(voff)[_i], (int)(soff_), 0, 0); } while (0)
; #define PG8_LDA(dst, b, h) do { _Pragma("unroll") for (int m = 0; m < 4; ++m) dst[m] = PG8_LD2(lds + PG8_SA(b, h) + aoff + m * 2048); } while (0)
; #define PG8_LDB(dst, b, h) do { _Pragma("unroll") for (int n = 0; n < 2; ++n) dst[n] = PG8_LD2(lds + PG8_SB(b, h) + boff + n * 2048); } while (0)
; #define PG8_WAIT_V(n) asm volatile("s_waitcnt vmcnt(" #n ")" ::: "memory")
; #define PG8_WAIT_L(n) asm volatile("s_waitcnt lgkmcnt(" #n ")" ::: "memory")
; #define PG8_BAR __builtin_amdgcn_s_barrier()
; #define PG8_SCHED __builtin_amdgcn_sched_barrier(0)
; template <class Epi, class Sched, bool ALIGN_EPI = false, bool SP2 = false, bool FP8 = false>
; __device__ __forceinline__ void gemm_phase(LAS unsigned char* lds, const Gemm g, const Sched& S, const Epi& E, int wbase) {
;     ...
;             PG8_LDB(B0, 1, 0); PG8_LDB(B1, 1, 1); PG8_SCHED; PG8_LDA(At, 1, 0); PG8_STAGE(PG8_SA(0, 1), rA2, a2 + hstep, voffA);
;             PG8_WAIT_V(8); PG8_WAIT_L(0); PG8_BAR; PG8_MMA(0, 0, At, B0); PG8_MMA(0, 1, At, B1); PG8_BAR; PG8_SCHED;
;             PG8_LDA(At, 1, 1); PG8_STAGE(PG8_SB(1, 0), rB2, b3, voffB); PG8_STAGE(PG8_SB(1, 1), rB2, b3 + hstep, voffB); PG8_STAGE(PG8_SA(1, 0), rA2, a3, voffA);
;             PG8_WAIT_V(8); PG8_WAIT_L(0); PG8_BAR; PG8_MMA(1, 0, At, B0); PG8_MMA(1, 1, At, B1); PG8_BAR; PG8_SCHED;
	s_mov_b32 m0, s45
	s_nop 0
	buffer_load_dwordx4 v194, s[4:7], s20 offen lds
	s_mov_b32 m0, s46
	s_nop 0
	buffer_load_dwordx4 v196, s[4:7], s20 offen lds
	v_add_u32_e32 v12, 0x18000, v199
	v_add_u32_e32 v28, 0x1c000, v199
	ds_read_b128 v[0:3], v12
	ds_read_b128 v[4:7], v12 offset:1024
	ds_read_b128 v[8:11], v12 offset:2048
	ds_read_b128 v[12:15], v12 offset:3072
	ds_read_b128 v[16:19], v28
	ds_read_b128 v[20:23], v28 offset:1024
	ds_read_b128 v[24:27], v28 offset:2048
	ds_read_b128 v[28:31], v28 offset:3072
	s_add_i32 s54, s54, s41
	s_mov_b32 m0, s48
	ds_read_b128 v[32:35], v200 offset:32768
	ds_read_b128 v[36:39], v200 offset:33792
	ds_read_b128 v[40:43], v200 offset:34816
	ds_read_b128 v[44:47], v200 offset:35840
	ds_read_b128 v[48:51], v200 offset:36864
	ds_read_b128 v[52:55], v200 offset:37888
	ds_read_b128 v[56:59], v200 offset:38912
	ds_read_b128 v[60:63], v200 offset:39936
	buffer_load_dwordx4 v192, s[36:39], s54 offen lds
	s_mov_b32 m0, s52
	s_nop 0
	buffer_load_dwordx4 v195, s[36:39], s54 offen lds
	s_waitcnt vmcnt(8)
	s_waitcnt lgkmcnt(0)
	s_barrier
	s_setprio 1
	v_mfma_f32_16x16x128_f8f6f4 v[184:187], v[0:7], v[32:39], v[184:187]
	v_mfma_f32_16x16x128_f8f6f4 v[188:191], v[8:15], v[32:39], v[188:191]
	v_mfma_f32_16x16x128_f8f6f4 v[168:171], v[0:7], v[40:47], v[168:171]
	v_mfma_f32_16x16x128_f8f6f4 v[172:175], v[8:15], v[40:47], v[172:175]
	v_mfma_f32_16x16x128_f8f6f4 v[152:155], v[0:7], v[48:55], v[152:155]
	v_mfma_f32_16x16x128_f8f6f4 v[156:159], v[8:15], v[48:55], v[156:159]
	v_mfma_f32_16x16x128_f8f6f4 v[136:139], v[0:7], v[56:63], v[136:139]
	v_mfma_f32_16x16x128_f8f6f4 v[140:143], v[8:15], v[56:63], v[140:143]
	v_mfma_f32_16x16x128_f8f6f4 v[176:179], v[16:23], v[32:39], v[176:179]
	v_mfma_f32_16x16x128_f8f6f4 v[180:183], v[24:31], v[32:39], v[180:183]
	v_mfma_f32_16x16x128_f8f6f4 v[160:163], v[16:23], v[40:47], v[160:163]
	v_mfma_f32_16x16x128_f8f6f4 v[164:167], v[24:31], v[40:47], v[164:167]
	v_mfma_f32_16x16x128_f8f6f4 v[144:147], v[16:23], v[48:55], v[144:147]
	v_mfma_f32_16x16x128_f8f6f4 v[148:151], v[24:31], v[48:55], v[148:151]
	v_mfma_f32_16x16x128_f8f6f4 v[128:131], v[16:23], v[56:63], v[128:131]
	v_mfma_f32_16x16x128_f8f6f4 v[132:135], v[24:31], v[56:63], v[132:135]
	s_setprio 0
	s_barrier
	s_addk_i32 s55, 0x80
	s_addk_i32 s20, 0x80
	s_mov_b32 m0, s57
	ds_read_b128 v[32:35], v200 offset:49152
	buffer_load_dwordx4 v194, s[4:7], s55 offen lds
	s_mov_b32 m0, s58
	ds_read_b128 v[36:39], v200 offset:50176
	buffer_load_dwordx4 v196, s[4:7], s55 offen lds
	s_mov_b32 m0, s61
	ds_read_b128 v[40:43], v200 offset:51200
	buffer_load_dwordx4 v194, s[4:7], s20 offen lds
	s_mov_b32 m0, s62
	ds_read_b128 v[44:47], v200 offset:52224
	buffer_load_dwordx4 v196, s[4:7], s20 offen lds
	s_mov_b32 m0, s59
	ds_read_b128 v[48:51], v200 offset:53248
	buffer_load_dwordx4 v192, s[36:39], s78 offen lds
	s_mov_b32 m0, s60
	ds_read_b128 v[52:55], v200 offset:54272
	buffer_load_dwordx4 v195, s[36:39], s78 offen lds
	ds_read_b128 v[56:59], v200 offset:55296
	ds_read_b128 v[60:63], v200 offset:56320
	s_waitcnt vmcnt(8)
	s_waitcnt lgkmcnt(0)
	s_barrier
	s_setprio 1
	v_mfma_f32_16x16x128_f8f6f4 v[120:123], v[0:7], v[32:39], v[120:123]
	v_mfma_f32_16x16x128_f8f6f4 v[124:127], v[8:15], v[32:39], v[124:127]
	v_mfma_f32_16x16x128_f8f6f4 v[104:107], v[0:7], v[40:47], v[104:107]
	v_mfma_f32_16x16x128_f8f6f4 v[108:111], v[8:15], v[40:47], v[108:111]
	v_mfma_f32_16x16x128_f8f6f4 v[88:91], v[0:7], v[48:55], v[88:91]
	v_mfma_f32_16x16x128_f8f6f4 v[92:95], v[8:15], v[48:55], v[92:95]
	v_mfma_f32_16x16x128_f8f6f4 v[72:75], v[0:7], v[56:63], v[72:75]
	v_mfma_f32_16x16x128_f8f6f4 v[76:79], v[8:15], v[56:63], v[76:79]
	v_mfma_f32_16x16x128_f8f6f4 v[112:115], v[16:23], v[32:39], v[112:115]
	v_mfma_f32_16x16x128_f8f6f4 v[116:119], v[24:31], v[32:39], v[116:119]
	v_mfma_f32_16x16x128_f8f6f4 v[96:99], v[16:23], v[40:47], v[96:99]
	v_mfma_f32_16x16x128_f8f6f4 v[100:103], v[24:31], v[40:47], v[100:103]
	v_mfma_f32_16x16x128_f8f6f4 v[80:83], v[16:23], v[48:55], v[80:83]
	v_mfma_f32_16x16x128_f8f6f4 v[84:87], v[24:31], v[48:55], v[84:87]
	v_mfma_f32_16x16x128_f8f6f4 v[68:71], v[16:23], v[56:63], v[68:71]
	v_mfma_f32_16x16x128_f8f6f4 v[64:67], v[24:31], v[56:63], v[64:67]
	s_setprio 0
	s_barrier
	s_add_i32 s85, s85, 2
	s_addk_i32 s67, 0x100
	s_cmp_ge_i32 s85, s53
	v_add_u32_e32 v210, 0x100, v210
	s_cbranch_scc0 .LBB0_1348
	v_readlane_b32 s54, v255, 25
	v_readlane_b32 s55, v255, 26
	s_and_b64 vcc, exec, s[18:19]
	s_cbranch_vccnz .LBB0_1367
	s_branch .LBB0_1368

;     __device__ __forceinline__ unsigned a_off(const Unit& u, const Gemm& g) const { return (unsigned)u.pm * (unsigned)(BM * 2) * (unsigned)g.K; }
;     __device__ __forceinline__ unsigned b_off(const Unit& u, const Gemm& g) const { return (unsigned)u.pn * (unsigned)(BM * 2) * (unsigned)g.K; }
;     __device__ __forceinline__ bool next(int i, Unit& u) const { return so.next(i, u); }
;     __device__ __forceinline__ unsigned a_off(const Unit& u, const Gemm& g) const { return (unsigned)u.pm * (unsigned)(BM * 2) * (unsigned)g.K; }
; #define PG8_WAIT_V(n) asm volatile("s_waitcnt vmcnt(" #n ")" ::: "memory")
; #define PG8_BAR __builtin_amdgcn_s_barrier()
; template <class Epi, class Sched, bool ALIGN_EPI = false, bool SP2 = false, bool FP8 = false>
; __device__ __forceinline__ void gemm_phase(LAS unsigned char* lds, const Gemm g, const Sched& S, const Epi& E, int wbase) {
;     ...
;     for (;;) {
;         const bool has_next = S.next(ui + 1, nxt);
;         const unsigned nA = has_next ? S.a_off(nxt, g) : cA, nB = has_next ? S.b_off(nxt, g) : cB;
;         const rsrc_t rAn = (Sched::TWO && has_next) ? (nxt.part ? rA1 : rA0) : rAc, rBn = (Sched::TWO && has_next) ? (nxt.part ? rB1 : rB0) : rBc;
;         float pre_[8] = {0.f, 0.f, 0.f, 0.f, 0.f, 0.f, 0.f, 0.f};
;         if constexpr (Epi::HAS_PRE) E.pre_load(pre_, cur, wr);
;         for (int t = 0; t < nt; t += 2) {
;             const bool last = (t == nt - 2);
;             const unsigned a1 = cA + (unsigned)(t + 1) * kstep;
;             const unsigned a2 = last ? nA : cA + (unsigned)(t + 2) * kstep, b2 = last ? nB : cB + (unsigned)(t + 2) * kstep; const rsrc_t rA2 = (Sched::TWO && last) ? rAn : rAc, rB2 = (Sched::TWO && last) ? rBn : rBc;
;             const unsigned a3 = a2 + kstep, b3 = b2 + kstep;
;             if (last && has_next) S.a_ready(nxt);
;             if constexpr (SP2) {
;             PG8_LDB(B0, 0, 0); PG8_LDB(B1, 0, 1); PG8_SCHED; PG8_LDA(At, 0, 0); PG8_STAGE(PG8_SA(1, 1), rAc, a1 + hstep, voffA);
;             PG8_WAIT_V(8); PG8_WAIT_L(0); PG8_BAR; PG8_MMA(0, 0, At, B0); PG8_MMA(0, 1, At, B1); PG8_BAR; PG8_SCHED;
;             PG8_LDA(At, 0, 1); PG8_STAGE(PG8_SB(0, 0), rB2, b2, voffB); PG8_STAGE(PG8_SB(0, 1), rB2, b2 + hstep, voffB); PG8_STAGE(PG8_SA(0, 0), rA2, a2, voffA);
;             PG8_WAIT_V(8); PG8_WAIT_L(0); PG8_BAR; PG8_MMA(1, 0, At, B0); PG8_MMA(1, 1, At, B1); PG8_BAR; PG8_SCHED;
.LBB0_1626:
	s_lshl_b32 s56, s53, 19
	s_andn2_b64 vcc, exec, s[12:13]
	s_lshl_b32 s57, s52, 19
	s_cbranch_vccnz .LBB0_1634
	s_and_b64 s[6:7], s[18:19], exec
	s_waitcnt vmcnt(37)
	s_waitcnt vmcnt(35)
	s_waitcnt vmcnt(31)
	s_waitcnt vmcnt(27)
	s_waitcnt vmcnt(23)
	s_waitcnt vmcnt(22)
	s_cselect_b32 s59, s56, s55
	s_cselect_b32 s60, s57, s54
	s_add_i32 s61, s55, 0x80
	s_add_i32 s62, s54, 0x100
	s_mov_b32 s63, 0
	v_add_u32_e32 v136, 0x10000, v161
	ds_read_b128 v[128:131], v136
	ds_read_b128 v[132:135], v136 offset:1024
	ds_read_b128 v[164:167], v136 offset:2048
	ds_read_b128 v[168:171], v136 offset:3072
	v_add_u32_e32 v136, 0x14000, v161
	ds_read_b128 v[172:175], v136
	ds_read_b128 v[176:179], v136 offset:1024
	ds_read_b128 v[180:183], v136 offset:2048
	ds_read_b128 v[184:187], v136 offset:3072
	s_add_i32 s6, s61, 0x80
	s_cmp_eq_u32 s46, s63
	s_cselect_b32 s65, s59, s6
	s_cselect_b32 s55, s60, s62
	s_or_b32 s54, s65, 0x80
	s_add_i32 s6, s22, s61
	s_mov_b32 m0, s47
	ds_read_b128 v[188:191], v162
	ds_read_b128 v[192:195], v162 offset:1024
	ds_read_b128 v[196:199], v162 offset:2048
	ds_read_b128 v[200:203], v162 offset:3072
	ds_read_b128 v[204:207], v162 offset:4096
	ds_read_b128 v[208:211], v162 offset:5120
	ds_read_b128 v[212:215], v162 offset:6144
	ds_read_b128 v[216:219], v162 offset:7168
	buffer_load_dwordx4 v137, s[36:39], s6 offen lds
	s_mov_b32 m0, s48
	s_nop 0
	buffer_load_dwordx4 v145, s[36:39], s6 offen lds
	s_waitcnt vmcnt(8)
	s_waitcnt lgkmcnt(0)
	s_barrier
	s_setprio 1
	v_mfma_f32_16x16x32_bf16 v[120:123], v[128:131], v[188:191], 0
	v_mfma_f32_16x16x32_bf16 v[124:127], v[164:167], v[188:191], 0
	v_mfma_f32_16x16x32_bf16 v[104:107], v[128:131], v[196:199], 0
	v_mfma_f32_16x16x32_bf16 v[108:111], v[164:167], v[196:199], 0
	v_mfma_f32_16x16x32_bf16 v[88:91], v[128:131], v[204:207], 0
	v_mfma_f32_16x16x32_bf16 v[92:95], v[164:167], v[204:207], 0
	v_mfma_f32_16x16x32_bf16 v[72:75], v[128:131], v[212:215], 0
	v_mfma_f32_16x16x32_bf16 v[76:79], v[164:167], v[212:215], 0
	v_mfma_f32_16x16x32_bf16 v[120:123], v[132:135], v[192:195], v[120:123]
	v_mfma_f32_16x16x32_bf16 v[124:127], v[168:171], v[192:195], v[124:127]
	v_mfma_f32_16x16x32_bf16 v[104:107], v[132:135], v[200:203], v[104:107]
	v_mfma_f32_16x16x32_bf16 v[108:111], v[168:171], v[200:203], v[108:111]
	v_mfma_f32_16x16x32_bf16 v[88:91], v[132:135], v[208:211], v[88:91]
	v_mfma_f32_16x16x32_bf16 v[92:95], v[168:171], v[208:211], v[92:95]
	v_mfma_f32_16x16x32_bf16 v[72:75], v[132:135], v[216:219], v[72:75]
	v_mfma_f32_16x16x32_bf16 v[76:79], v[168:171], v[216:219], v[76:79]
	v_mfma_f32_16x16x32_bf16 v[112:115], v[172:175], v[188:191], 0
	v_mfma_f32_16x16x32_bf16 v[116:119], v[180:183], v[188:191], 0
	v_mfma_f32_16x16x32_bf16 v[96:99], v[172:175], v[196:199], 0
	v_mfma_f32_16x16x32_bf16 v[100:103], v[180:183], v[196:199], 0
	v_mfma_f32_16x16x32_bf16 v[80:83], v[172:175], v[204:207], 0
	v_mfma_f32_16x16x32_bf16 v[84:87], v[180:183], v[204:207], 0
	v_mfma_f32_16x16x32_bf16 v[64:67], v[172:175], v[212:215], 0
	v_mfma_f32_16x16x32_bf16 v[68:71], v[180:183], v[212:215], 0
	v_mfma_f32_16x16x32_bf16 v[112:115], v[176:179], v[192:195], v[112:115]
	v_mfma_f32_16x16x32_bf16 v[116:119], v[184:187], v[192:195], v[116:119]
	v_mfma_f32_16x16x32_bf16 v[96:99], v[176:179], v[200:203], v[96:99]
	v_mfma_f32_16x16x32_bf16 v[100:103], v[184:187], v[200:203], v[100:103]
	v_mfma_f32_16x16x32_bf16 v[80:83], v[176:179], v[208:211], v[80:83]
	v_mfma_f32_16x16x32_bf16 v[84:87], v[184:187], v[208:211], v[84:87]
	v_mfma_f32_16x16x32_bf16 v[64:67], v[176:179], v[216:219], v[64:67]
	v_mfma_f32_16x16x32_bf16 v[68:71], v[184:187], v[216:219], v[68:71]
	s_setprio 0
	s_barrier
	s_mov_b32 m0, s24
	s_mov_b32 s6, s38
	s_mov_b32 s7, s39
	buffer_load_dwordx4 v141, s[4:7], s55 offen lds
	s_mov_b32 m0, s25
	ds_read_b128 v[188:191], v162 offset:16384
	s_add_i32 s66, s55, s22
	buffer_load_dwordx4 v149, s[4:7], s55 offen lds
	s_mov_b32 m0, s23
	ds_read_b128 v[192:195], v162 offset:17408
	buffer_load_dwordx4 v137, s[36:39], s65 offen lds
	s_mov_b32 m0, s28
	ds_read_b128 v[196:199], v162 offset:18432
	buffer_load_dwordx4 v145, s[36:39], s65 offen lds
	ds_read_b128 v[200:203], v162 offset:19456
	ds_read_b128 v[204:207], v162 offset:20480
	ds_read_b128 v[208:211], v162 offset:21504
	ds_read_b128 v[212:215], v162 offset:22528
	ds_read_b128 v[216:219], v162 offset:23552
	s_waitcnt vmcnt(6)
	s_waitcnt lgkmcnt(0)
	s_barrier
	s_setprio 1
	v_mfma_f32_16x16x32_bf16 v[56:59], v[128:131], v[188:191], 0
	v_mfma_f32_16x16x32_bf16 v[60:63], v[164:167], v[188:191], 0
	v_mfma_f32_16x16x32_bf16 v[40:43], v[128:131], v[196:199], 0
	v_mfma_f32_16x16x32_bf16 v[44:47], v[164:167], v[196:199], 0
	v_mfma_f32_16x16x32_bf16 v[24:27], v[128:131], v[204:207], 0
	v_mfma_f32_16x16x32_bf16 v[28:31], v[164:167], v[204:207], 0
	v_mfma_f32_16x16x32_bf16 v[8:11], v[128:131], v[212:215], 0
	v_mfma_f32_16x16x32_bf16 v[12:15], v[164:167], v[212:215], 0
	v_mfma_f32_16x16x32_bf16 v[56:59], v[132:135], v[192:195], v[56:59]
	v_mfma_f32_16x16x32_bf16 v[60:63], v[168:171], v[192:195], v[60:63]
	v_mfma_f32_16x16x32_bf16 v[40:43], v[132:135], v[200:203], v[40:43]
	v_mfma_f32_16x16x32_bf16 v[44:47], v[168:171], v[200:203], v[44:47]
	v_mfma_f32_16x16x32_bf16 v[24:27], v[132:135], v[208:211], v[24:27]
	v_mfma_f32_16x16x32_bf16 v[28:31], v[168:171], v[208:211], v[28:31]
	v_mfma_f32_16x16x32_bf16 v[8:11], v[132:135], v[216:219], v[8:11]
	v_mfma_f32_16x16x32_bf16 v[12:15], v[168:171], v[216:219], v[12:15]
	v_mfma_f32_16x16x32_bf16 v[48:51], v[172:175], v[188:191], 0
	v_mfma_f32_16x16x32_bf16 v[52:55], v[180:183], v[188:191], 0
	v_mfma_f32_16x16x32_bf16 v[32:35], v[172:175], v[196:199], 0
	v_mfma_f32_16x16x32_bf16 v[36:39], v[180:183], v[196:199], 0
	v_mfma_f32_16x16x32_bf16 v[16:19], v[172:175], v[204:207], 0
	v_mfma_f32_16x16x32_bf16 v[20:23], v[180:183], v[204:207], 0
	v_mfma_f32_16x16x32_bf16 v[4:7], v[172:175], v[212:215], 0
	v_mfma_f32_16x16x32_bf16 v[0:3], v[180:183], v[212:215], 0
	v_mfma_f32_16x16x32_bf16 v[48:51], v[176:179], v[192:195], v[48:51]
	v_mfma_f32_16x16x32_bf16 v[52:55], v[184:187], v[192:195], v[52:55]
	v_mfma_f32_16x16x32_bf16 v[32:35], v[176:179], v[200:203], v[32:35]
	v_mfma_f32_16x16x32_bf16 v[36:39], v[184:187], v[200:203], v[36:39]
	v_mfma_f32_16x16x32_bf16 v[16:19], v[176:179], v[208:211], v[16:19]
	v_mfma_f32_16x16x32_bf16 v[20:23], v[184:187], v[208:211], v[20:23]
	v_mfma_f32_16x16x32_bf16 v[4:7], v[176:179], v[216:219], v[4:7]
	v_mfma_f32_16x16x32_bf16 v[0:3], v[184:187], v[216:219], v[0:3]
	s_setprio 0
	s_barrier
; #define PG8_STAGE(bufoff, rs_, soff_, voff) do { _Pragma("unroll") for (int _i = 0; _i < 2; ++_i) \
;         __builtin_amdgcn_raw_ptr_buffer_load_lds(rs_, (LAS void*)(lds + (bufoff) + ldsw + _i * 8192), 16, (int)(voff)[_i], (int)(soff_), 0, 0); } while (0)
; #define PG8_LDA(dst, b, h) do { _Pragma("unroll") for (int m = 0; m < 4; ++m) dst[m] = PG8_LD2(lds + PG8_SA(b, h) + aoff + m * 2048); } while (0)
; #define PG8_LDB(dst, b, h) do { _Pragma("unroll") for (int n = 0; n < 2; ++n) dst[n] = PG8_LD2(lds + PG8_SB(b, h) + boff + n * 2048); } while (0)
; #define PG8_WAIT_V(n) asm volatile("s_waitcnt vmcnt(" #n ")" ::: "memory")
; #define PG8_WAIT_L(n) asm volatile("s_waitcnt lgkmcnt(" #n ")" ::: "memory")
; #define PG8_BAR __builtin_amdgcn_s_barrier()
; #define PG8_SCHED __builtin_amdgcn_sched_barrier(0)
; template <class Epi, class Sched, bool ALIGN_EPI = false, bool SP2 = false, bool FP8 = false>
; __device__ __forceinline__ void gemm_phase(LAS unsigned char* lds, const Gemm g, const Sched& S, const Epi& E, int wbase) {
;     ...
;             PG8_LDB(B0, 1, 0); PG8_LDB(B1, 1, 1); PG8_SCHED; PG8_LDA(At, 1, 0); PG8_STAGE(PG8_SA(0, 1), rA2, a2 + hstep, voffA);
;             PG8_WAIT_V(8); PG8_WAIT_L(0); PG8_BAR; PG8_MMA(0, 0, At, B0); PG8_MMA(0, 1, At, B1); PG8_BAR; PG8_SCHED;
;             PG8_LDA(At, 1, 1); PG8_STAGE(PG8_SB(1, 0), rB2, b3, voffB); PG8_STAGE(PG8_SB(1, 1), rB2, b3 + hstep, voffB); PG8_STAGE(PG8_SA(1, 0), rA2, a3, voffA);
;             PG8_WAIT_V(8); PG8_WAIT_L(0); PG8_BAR; PG8_MMA(1, 0, At, B0); PG8_MMA(1, 1, At, B1); PG8_BAR; PG8_SCHED;
	s_mov_b32 m0, s26
	s_nop 0
	buffer_load_dwordx4 v141, s[4:7], s66 offen lds
	s_mov_b32 m0, s27
	s_nop 0
	buffer_load_dwordx4 v149, s[4:7], s66 offen lds
	v_add_u32_e32 v136, 0x18000, v161
	ds_read_b128 v[128:131], v136
	ds_read_b128 v[132:135], v136 offset:1024
	ds_read_b128 v[164:167], v136 offset:2048
	ds_read_b128 v[168:171], v136 offset:3072
	v_add_u32_e32 v136, 0x1c000, v161
	ds_read_b128 v[172:175], v136
	ds_read_b128 v[176:179], v136 offset:1024
	ds_read_b128 v[180:183], v136 offset:2048
	ds_read_b128 v[184:187], v136 offset:3072
	s_add_i32 s65, s65, s22
	s_mov_b32 m0, s29
	ds_read_b128 v[188:191], v162 offset:32768
	ds_read_b128 v[192:195], v162 offset:33792
	ds_read_b128 v[196:199], v162 offset:34816
	ds_read_b128 v[200:203], v162 offset:35840
	ds_read_b128 v[204:207], v162 offset:36864
	ds_read_b128 v[208:211], v162 offset:37888
	ds_read_b128 v[212:215], v162 offset:38912
	ds_read_b128 v[216:219], v162 offset:39936
	buffer_load_dwordx4 v137, s[36:39], s65 offen lds
	s_mov_b32 m0, s30
	s_nop 0
	buffer_load_dwordx4 v145, s[36:39], s65 offen lds
	s_waitcnt vmcnt(8)
	s_waitcnt lgkmcnt(0)
	s_barrier
	s_setprio 1
	v_mfma_f32_16x16x32_bf16 v[120:123], v[128:131], v[188:191], v[120:123]
	v_mfma_f32_16x16x32_bf16 v[124:127], v[164:167], v[188:191], v[124:127]
	v_mfma_f32_16x16x32_bf16 v[104:107], v[128:131], v[196:199], v[104:107]
	v_mfma_f32_16x16x32_bf16 v[108:111], v[164:167], v[196:199], v[108:111]
	v_mfma_f32_16x16x32_bf16 v[88:91], v[128:131], v[204:207], v[88:91]
	v_mfma_f32_16x16x32_bf16 v[92:95], v[164:167], v[204:207], v[92:95]
	v_mfma_f32_16x16x32_bf16 v[72:75], v[128:131], v[212:215], v[72:75]
	v_mfma_f32_16x16x32_bf16 v[76:79], v[164:167], v[212:215], v[76:79]
	v_mfma_f32_16x16x32_bf16 v[120:123], v[132:135], v[192:195], v[120:123]
	v_mfma_f32_16x16x32_bf16 v[124:127], v[168:171], v[192:195], v[124:127]
	v_mfma_f32_16x16x32_bf16 v[104:107], v[132:135], v[200:203], v[104:107]
	v_mfma_f32_16x16x32_bf16 v[108:111], v[168:171], v[200:203], v[108:111]
	v_mfma_f32_16x16x32_bf16 v[88:91], v[132:135], v[208:211], v[88:91]
	v_mfma_f32_16x16x32_bf16 v[92:95], v[168:171], v[208:211], v[92:95]
	v_mfma_f32_16x16x32_bf16 v[72:75], v[132:135], v[216:219], v[72:75]
	v_mfma_f32_16x16x32_bf16 v[76:79], v[168:171], v[216:219], v[76:79]
	v_mfma_f32_16x16x32_bf16 v[112:115], v[172:175], v[188:191], v[112:115]
	v_mfma_f32_16x16x32_bf16 v[116:119], v[180:183], v[188:191], v[116:119]
	v_mfma_f32_16x16x32_bf16 v[96:99], v[172:175], v[196:199], v[96:99]
	v_mfma_f32_16x16x32_bf16 v[100:103], v[180:183], v[196:199], v[100:103]
	v_mfma_f32_16x16x32_bf16 v[80:83], v[172:175], v[204:207], v[80:83]
	v_mfma_f32_16x16x32_bf16 v[84:87], v[180:183], v[204:207], v[84:87]
	v_mfma_f32_16x16x32_bf16 v[64:67], v[172:175], v[212:215], v[64:67]
	v_mfma_f32_16x16x32_bf16 v[68:71], v[180:183], v[212:215], v[68:71]
	v_mfma_f32_16x16x32_bf16 v[112:115], v[176:179], v[192:195], v[112:115]
	v_mfma_f32_16x16x32_bf16 v[116:119], v[184:187], v[192:195], v[116:119]
	v_mfma_f32_16x16x32_bf16 v[96:99], v[176:179], v[200:203], v[96:99]
	v_mfma_f32_16x16x32_bf16 v[100:103], v[184:187], v[200:203], v[100:103]
	v_mfma_f32_16x16x32_bf16 v[80:83], v[176:179], v[208:211], v[80:83]
	v_mfma_f32_16x16x32_bf16 v[84:87], v[184:187], v[208:211], v[84:87]
	v_mfma_f32_16x16x32_bf16 v[64:67], v[176:179], v[216:219], v[64:67]
	v_mfma_f32_16x16x32_bf16 v[68:71], v[184:187], v[216:219], v[68:71]
	s_setprio 0
	s_barrier
	s_mov_b32 m0, s31
	s_bitset1_b32 s55, 7
	buffer_load_dwordx4 v141, s[4:7], s55 offen lds
	s_mov_b32 m0, s33
	ds_read_b128 v[188:191], v162 offset:49152
	buffer_load_dwordx4 v149, s[4:7], s55 offen lds
	s_add_i32 s55, s55, s22
	s_mov_b32 m0, s41
	ds_read_b128 v[192:195], v162 offset:50176
	buffer_load_dwordx4 v141, s[4:7], s55 offen lds
	s_mov_b32 m0, s42
	ds_read_b128 v[196:199], v162 offset:51200
	buffer_load_dwordx4 v149, s[4:7], s55 offen lds
	s_mov_b32 m0, s34
	ds_read_b128 v[200:203], v162 offset:52224
	buffer_load_dwordx4 v137, s[36:39], s54 offen lds
	s_mov_b32 m0, s35
	ds_read_b128 v[204:207], v162 offset:53248
	buffer_load_dwordx4 v145, s[36:39], s54 offen lds
	ds_read_b128 v[208:211], v162 offset:54272
	ds_read_b128 v[212:215], v162 offset:55296
	ds_read_b128 v[216:219], v162 offset:56320
	s_waitcnt vmcnt(8)
	s_waitcnt lgkmcnt(0)
	s_barrier
	s_setprio 1
	v_mfma_f32_16x16x32_bf16 v[56:59], v[128:131], v[188:191], v[56:59]
	v_mfma_f32_16x16x32_bf16 v[60:63], v[164:167], v[188:191], v[60:63]
	v_mfma_f32_16x16x32_bf16 v[40:43], v[128:131], v[196:199], v[40:43]
	v_mfma_f32_16x16x32_bf16 v[44:47], v[164:167], v[196:199], v[44:47]
	v_mfma_f32_16x16x32_bf16 v[24:27], v[128:131], v[204:207], v[24:27]
	v_mfma_f32_16x16x32_bf16 v[28:31], v[164:167], v[204:207], v[28:31]
	v_mfma_f32_16x16x32_bf16 v[8:11], v[128:131], v[212:215], v[8:11]
	v_mfma_f32_16x16x32_bf16 v[12:15], v[164:167], v[212:215], v[12:15]
	v_mfma_f32_16x16x32_bf16 v[56:59], v[132:135], v[192:195], v[56:59]
	v_mfma_f32_16x16x32_bf16 v[60:63], v[168:171], v[192:195], v[60:63]
	v_mfma_f32_16x16x32_bf16 v[40:43], v[132:135], v[200:203], v[40:43]
	v_mfma_f32_16x16x32_bf16 v[44:47], v[168:171], v[200:203], v[44:47]
	v_mfma_f32_16x16x32_bf16 v[24:27], v[132:135], v[208:211], v[24:27]
	v_mfma_f32_16x16x32_bf16 v[28:31], v[168:171], v[208:211], v[28:31]
	v_mfma_f32_16x16x32_bf16 v[8:11], v[132:135], v[216:219], v[8:11]
	v_mfma_f32_16x16x32_bf16 v[12:15], v[168:171], v[216:219], v[12:15]
	v_mfma_f32_16x16x32_bf16 v[48:51], v[172:175], v[188:191], v[48:51]
	v_mfma_f32_16x16x32_bf16 v[52:55], v[180:183], v[188:191], v[52:55]
	v_mfma_f32_16x16x32_bf16 v[32:35], v[172:175], v[196:199], v[32:35]
	v_mfma_f32_16x16x32_bf16 v[36:39], v[180:183], v[196:199], v[36:39]
	v_mfma_f32_16x16x32_bf16 v[16:19], v[172:175], v[204:207], v[16:19]
	v_mfma_f32_16x16x32_bf16 v[20:23], v[180:183], v[204:207], v[20:23]
	v_mfma_f32_16x16x32_bf16 v[4:7], v[172:175], v[212:215], v[4:7]
	v_mfma_f32_16x16x32_bf16 v[0:3], v[180:183], v[212:215], v[0:3]
	v_mfma_f32_16x16x32_bf16 v[48:51], v[176:179], v[192:195], v[48:51]
	v_mfma_f32_16x16x32_bf16 v[52:55], v[184:187], v[192:195], v[52:55]
	v_mfma_f32_16x16x32_bf16 v[32:35], v[176:179], v[200:203], v[32:35]
	v_mfma_f32_16x16x32_bf16 v[36:39], v[184:187], v[200:203], v[36:39]
	v_mfma_f32_16x16x32_bf16 v[16:19], v[176:179], v[208:211], v[16:19]
	v_mfma_f32_16x16x32_bf16 v[20:23], v[184:187], v[208:211], v[20:23]
	v_mfma_f32_16x16x32_bf16 v[4:7], v[176:179], v[216:219], v[4:7]
	v_mfma_f32_16x16x32_bf16 v[0:3], v[184:187], v[216:219], v[0:3]
	s_setprio 0
	s_barrier
	s_add_i32 s63, s63, 2
	s_addk_i32 s61, 0x100
	s_addk_i32 s62, 0x100
	s_cmp_ge_i32 s63, s44
	s_cbranch_scc0 .LBB0_1628
	s_branch .Lzp_after_1628
; #define PG8_STAGE(bufoff, rs_, soff_, voff) do { _Pragma("unroll") for (int _i = 0; _i < 2; ++_i) \
;         __builtin_amdgcn_raw_ptr_buffer_load_lds(rs_, (LAS void*)(lds + (bufoff) + ldsw + _i * 8192), 16, (int)(voff)[_i], (int)(soff_), 0, 0); } while (0)
; #define PG8_LDA(dst, b, h) do { _Pragma("unroll") for (int m = 0; m < 4; ++m) dst[m] = PG8_LD2(lds + PG8_SA(b, h) + aoff + m * 2048); } while (0)
; #define PG8_LDB(dst, b, h) do { _Pragma("unroll") for (int n = 0; n < 2; ++n) dst[n] = PG8_LD2(lds + PG8_SB(b, h) + boff + n * 2048); } while (0)
; #define PG8_WAIT_V(n) asm volatile("s_waitcnt vmcnt(" #n ")" ::: "memory")
; #define PG8_WAIT_L(n) asm volatile("s_waitcnt lgkmcnt(" #n ")" ::: "memory")
; #define PG8_BAR __builtin_amdgcn_s_barrier()
; #define PG8_SCHED __builtin_amdgcn_sched_barrier(0)
; template <class Epi, class Sched, bool ALIGN_EPI = false, bool SP2 = false, bool FP8 = false>
; __device__ __forceinline__ void gemm_phase(LAS unsigned char* lds, const Gemm g, const Sched& S, const Epi& E, int wbase) {
;     ...
;         for (int t = 0; t < nt; t += 2) {
;             const bool last = (t == nt - 2);
;             const unsigned a1 = cA + (unsigned)(t + 1) * kstep;
;             const unsigned a2 = last ? nA : cA + (unsigned)(t + 2) * kstep, b2 = last ? nB : cB + (unsigned)(t + 2) * kstep; const rsrc_t rA2 = (Sched::TWO && last) ? rAn : rAc, rB2 = (Sched::TWO && last) ? rBn : rBc;
;             const unsigned a3 = a2 + kstep, b3 = b2 + kstep;
;             if (last && has_next) S.a_ready(nxt);
;             if constexpr (SP2) {
;             PG8_LDB(B0, 0, 0); PG8_LDB(B1, 0, 1); PG8_SCHED; PG8_LDA(At, 0, 0); PG8_STAGE(PG8_SA(1, 1), rAc, a1 + hstep, voffA);
;             PG8_WAIT_V(8); PG8_WAIT_L(0); PG8_BAR; PG8_MMA(0, 0, At, B0); PG8_MMA(0, 1, At, B1); PG8_BAR; PG8_SCHED;
;             PG8_LDA(At, 0, 1); PG8_STAGE(PG8_SB(0, 0), rB2, b2, voffB); PG8_STAGE(PG8_SB(0, 1), rB2, b2 + hstep, voffB); PG8_STAGE(PG8_SA(0, 0), rA2, a2, voffA);
;             PG8_WAIT_V(8); PG8_WAIT_L(0); PG8_BAR; PG8_MMA(1, 0, At, B0); PG8_MMA(1, 1, At, B1); PG8_BAR; PG8_SCHED;
.LBB0_1628:
	v_add_u32_e32 v136, 0x10000, v161
	ds_read_b128 v[128:131], v136
	ds_read_b128 v[132:135], v136 offset:1024
	ds_read_b128 v[164:167], v136 offset:2048
	ds_read_b128 v[168:171], v136 offset:3072
	v_add_u32_e32 v136, 0x14000, v161
	ds_read_b128 v[172:175], v136
	ds_read_b128 v[176:179], v136 offset:1024
	ds_read_b128 v[180:183], v136 offset:2048
	ds_read_b128 v[184:187], v136 offset:3072
	s_add_i32 s6, s61, 0x80
	s_cmp_eq_u32 s46, s63
	s_cselect_b32 s65, s59, s6
	s_cselect_b32 s55, s60, s62
	s_or_b32 s54, s65, 0x80
	s_add_i32 s6, s22, s61
	s_mov_b32 m0, s47
	ds_read_b128 v[188:191], v162
	ds_read_b128 v[192:195], v162 offset:1024
	ds_read_b128 v[196:199], v162 offset:2048
	ds_read_b128 v[200:203], v162 offset:3072
	ds_read_b128 v[204:207], v162 offset:4096
	ds_read_b128 v[208:211], v162 offset:5120
	ds_read_b128 v[212:215], v162 offset:6144
	ds_read_b128 v[216:219], v162 offset:7168
	buffer_load_dwordx4 v137, s[36:39], s6 offen lds
	s_mov_b32 m0, s48
	s_nop 0
	buffer_load_dwordx4 v145, s[36:39], s6 offen lds
	s_waitcnt vmcnt(8)
	s_waitcnt lgkmcnt(0)
	s_barrier
	s_setprio 1
	v_mfma_f32_16x16x32_bf16 v[120:123], v[128:131], v[188:191], v[120:123]
	v_mfma_f32_16x16x32_bf16 v[124:127], v[164:167], v[188:191], v[124:127]
	v_mfma_f32_16x16x32_bf16 v[104:107], v[128:131], v[196:199], v[104:107]
	v_mfma_f32_16x16x32_bf16 v[108:111], v[164:167], v[196:199], v[108:111]
	v_mfma_f32_16x16x32_bf16 v[88:91], v[128:131], v[204:207], v[88:91]
	v_mfma_f32_16x16x32_bf16 v[92:95], v[164:167], v[204:207], v[92:95]
	v_mfma_f32_16x16x32_bf16 v[72:75], v[128:131], v[212:215], v[72:75]
	v_mfma_f32_16x16x32_bf16 v[76:79], v[164:167], v[212:215], v[76:79]
	v_mfma_f32_16x16x32_bf16 v[120:123], v[132:135], v[192:195], v[120:123]
	v_mfma_f32_16x16x32_bf16 v[124:127], v[168:171], v[192:195], v[124:127]
	v_mfma_f32_16x16x32_bf16 v[104:107], v[132:135], v[200:203], v[104:107]
	v_mfma_f32_16x16x32_bf16 v[108:111], v[168:171], v[200:203], v[108:111]
	v_mfma_f32_16x16x32_bf16 v[88:91], v[132:135], v[208:211], v[88:91]
	v_mfma_f32_16x16x32_bf16 v[92:95], v[168:171], v[208:211], v[92:95]
	v_mfma_f32_16x16x32_bf16 v[72:75], v[132:135], v[216:219], v[72:75]
	v_mfma_f32_16x16x32_bf16 v[76:79], v[168:171], v[216:219], v[76:79]
	v_mfma_f32_16x16x32_bf16 v[112:115], v[172:175], v[188:191], v[112:115]
	v_mfma_f32_16x16x32_bf16 v[116:119], v[180:183], v[188:191], v[116:119]
	v_mfma_f32_16x16x32_bf16 v[96:99], v[172:175], v[196:199], v[96:99]
	v_mfma_f32_16x16x32_bf16 v[100:103], v[180:183], v[196:199], v[100:103]
	v_mfma_f32_16x16x32_bf16 v[80:83], v[172:175], v[204:207], v[80:83]
	v_mfma_f32_16x16x32_bf16 v[84:87], v[180:183], v[204:207], v[84:87]
	v_mfma_f32_16x16x32_bf16 v[64:67], v[172:175], v[212:215], v[64:67]
	v_mfma_f32_16x16x32_bf16 v[68:71], v[180:183], v[212:215], v[68:71]
	v_mfma_f32_16x16x32_bf16 v[112:115], v[176:179], v[192:195], v[112:115]
	v_mfma_f32_16x16x32_bf16 v[116:119], v[184:187], v[192:195], v[116:119]
	v_mfma_f32_16x16x32_bf16 v[96:99], v[176:179], v[200:203], v[96:99]
	v_mfma_f32_16x16x32_bf16 v[100:103], v[184:187], v[200:203], v[100:103]
	v_mfma_f32_16x16x32_bf16 v[80:83], v[176:179], v[208:211], v[80:83]
	v_mfma_f32_16x16x32_bf16 v[84:87], v[184:187], v[208:211], v[84:87]
	v_mfma_f32_16x16x32_bf16 v[64:67], v[176:179], v[216:219], v[64:67]
	v_mfma_f32_16x16x32_bf16 v[68:71], v[184:187], v[216:219], v[68:71]
	s_setprio 0
	s_barrier
	s_mov_b32 m0, s24
	s_mov_b32 s6, s38
	s_mov_b32 s7, s39
	buffer_load_dwordx4 v141, s[4:7], s55 offen lds
	s_mov_b32 m0, s25
	ds_read_b128 v[188:191], v162 offset:16384
	s_add_i32 s66, s55, s22
	buffer_load_dwordx4 v149, s[4:7], s55 offen lds
	s_mov_b32 m0, s23
	ds_read_b128 v[192:195], v162 offset:17408
	buffer_load_dwordx4 v137, s[36:39], s65 offen lds
	s_mov_b32 m0, s28
	ds_read_b128 v[196:199], v162 offset:18432
	buffer_load_dwordx4 v145, s[36:39], s65 offen lds
	ds_read_b128 v[200:203], v162 offset:19456
	ds_read_b128 v[204:207], v162 offset:20480
	ds_read_b128 v[208:211], v162 offset:21504
	ds_read_b128 v[212:215], v162 offset:22528
	ds_read_b128 v[216:219], v162 offset:23552
	s_waitcnt vmcnt(6)
	s_waitcnt lgkmcnt(0)
	s_barrier
	s_setprio 1
	v_mfma_f32_16x16x32_bf16 v[56:59], v[128:131], v[188:191], v[56:59]
	v_mfma_f32_16x16x32_bf16 v[60:63], v[164:167], v[188:191], v[60:63]
	v_mfma_f32_16x16x32_bf16 v[40:43], v[128:131], v[196:199], v[40:43]
	v_mfma_f32_16x16x32_bf16 v[44:47], v[164:167], v[196:199], v[44:47]
	v_mfma_f32_16x16x32_bf16 v[24:27], v[128:131], v[204:207], v[24:27]
	v_mfma_f32_16x16x32_bf16 v[28:31], v[164:167], v[204:207], v[28:31]
	v_mfma_f32_16x16x32_bf16 v[8:11], v[128:131], v[212:215], v[8:11]
	v_mfma_f32_16x16x32_bf16 v[12:15], v[164:167], v[212:215], v[12:15]
	v_mfma_f32_16x16x32_bf16 v[56:59], v[132:135], v[192:195], v[56:59]
	v_mfma_f32_16x16x32_bf16 v[60:63], v[168:171], v[192:195], v[60:63]
	v_mfma_f32_16x16x32_bf16 v[40:43], v[132:135], v[200:203], v[40:43]
	v_mfma_f32_16x16x32_bf16 v[44:47], v[168:171], v[200:203], v[44:47]
	v_mfma_f32_16x16x32_bf16 v[24:27], v[132:135], v[208:211], v[24:27]
	v_mfma_f32_16x16x32_bf16 v[28:31], v[168:171], v[208:211], v[28:31]
	v_mfma_f32_16x16x32_bf16 v[8:11], v[132:135], v[216:219], v[8:11]
	v_mfma_f32_16x16x32_bf16 v[12:15], v[168:171], v[216:219], v[12:15]
	v_mfma_f32_16x16x32_bf16 v[48:51], v[172:175], v[188:191], v[48:51]
	v_mfma_f32_16x16x32_bf16 v[52:55], v[180:183], v[188:191], v[52:55]
	v_mfma_f32_16x16x32_bf16 v[32:35], v[172:175], v[196:199], v[32:35]
	v_mfma_f32_16x16x32_bf16 v[36:39], v[180:183], v[196:199], v[36:39]
	v_mfma_f32_16x16x32_bf16 v[16:19], v[172:175], v[204:207], v[16:19]
	v_mfma_f32_16x16x32_bf16 v[20:23], v[180:183], v[204:207], v[20:23]
	v_mfma_f32_16x16x32_bf16 v[4:7], v[172:175], v[212:215], v[4:7]
	v_mfma_f32_16x16x32_bf16 v[0:3], v[180:183], v[212:215], v[0:3]
	v_mfma_f32_16x16x32_bf16 v[48:51], v[176:179], v[192:195], v[48:51]
	v_mfma_f32_16x16x32_bf16 v[52:55], v[184:187], v[192:195], v[52:55]
	v_mfma_f32_16x16x32_bf16 v[32:35], v[176:179], v[200:203], v[32:35]
	v_mfma_f32_16x16x32_bf16 v[36:39], v[184:187], v[200:203], v[36:39]
	v_mfma_f32_16x16x32_bf16 v[16:19], v[176:179], v[208:211], v[16:19]
	v_mfma_f32_16x16x32_bf16 v[20:23], v[184:187], v[208:211], v[20:23]
	v_mfma_f32_16x16x32_bf16 v[4:7], v[176:179], v[216:219], v[4:7]
	v_mfma_f32_16x16x32_bf16 v[0:3], v[184:187], v[216:219], v[0:3]
	s_setprio 0
	s_barrier
; #define PG8_STAGE(bufoff, rs_, soff_, voff) do { _Pragma("unroll") for (int _i = 0; _i < 2; ++_i) \
;         __builtin_amdgcn_raw_ptr_buffer_load_lds(rs_, (LAS void*)(lds + (bufoff) + ldsw + _i * 8192), 16, (int)(voff)[_i], (int)(soff_), 0, 0); } while (0)
; #define PG8_LDA(dst, b, h) do { _Pragma("unroll") for (int m = 0; m < 4; ++m) dst[m] = PG8_LD2(lds + PG8_SA(b, h) + aoff + m * 2048); } while (0)
; #define PG8_LDB(dst, b, h) do { _Pragma("unroll") for (int n = 0; n < 2; ++n) dst[n] = PG8_LD2(lds + PG8_SB(b, h) + boff + n * 2048); } while (0)
; #define PG8_WAIT_V(n) asm volatile("s_waitcnt vmcnt(" #n ")" ::: "memory")
; #define PG8_WAIT_L(n) asm volatile("s_waitcnt lgkmcnt(" #n ")" ::: "memory")
; #define PG8_BAR __builtin_amdgcn_s_barrier()
; #define PG8_SCHED __builtin_amdgcn_sched_barrier(0)
; template <class Epi, class Sched, bool ALIGN_EPI = false, bool SP2 = false, bool FP8 = false>
; __device__ __forceinline__ void gemm_phase(LAS unsigned char* lds, const Gemm g, const Sched& S, const Epi& E, int wbase) {
;     ...
;         for (int t = 0; t < nt; t += 2) {
;     ...
;             PG8_LDB(B0, 1, 0); PG8_LDB(B1, 1, 1); PG8_SCHED; PG8_LDA(At, 1, 0); PG8_STAGE(PG8_SA(0, 1), rA2, a2 + hstep, voffA);
;             PG8_WAIT_V(8); PG8_WAIT_L(0); PG8_BAR; PG8_MMA(0, 0, At, B0); PG8_MMA(0, 1, At, B1); PG8_BAR; PG8_SCHED;
;             PG8_LDA(At, 1, 1); PG8_STAGE(PG8_SB(1, 0), rB2, b3, voffB); PG8_STAGE(PG8_SB(1, 1), rB2, b3 + hstep, voffB); PG8_STAGE(PG8_SA(1, 0), rA2, a3, voffA);
;             PG8_WAIT_V(8); PG8_WAIT_L(0); PG8_BAR; PG8_MMA(1, 0, At, B0); PG8_MMA(1, 1, At, B1); PG8_BAR; PG8_SCHED;
	s_mov_b32 m0, s26
	s_nop 0
	buffer_load_dwordx4 v141, s[4:7], s66 offen lds
	s_mov_b32 m0, s27
	s_nop 0
	buffer_load_dwordx4 v149, s[4:7], s66 offen lds
	v_add_u32_e32 v136, 0x18000, v161
	ds_read_b128 v[128:131], v136
	ds_read_b128 v[132:135], v136 offset:1024
	ds_read_b128 v[164:167], v136 offset:2048
	ds_read_b128 v[168:171], v136 offset:3072
	v_add_u32_e32 v136, 0x1c000, v161
	ds_read_b128 v[172:175], v136
	ds_read_b128 v[176:179], v136 offset:1024
	ds_read_b128 v[180:183], v136 offset:2048
	ds_read_b128 v[184:187], v136 offset:3072
	s_add_i32 s65, s65, s22
	s_mov_b32 m0, s29
	ds_read_b128 v[188:191], v162 offset:32768
	ds_read_b128 v[192:195], v162 offset:33792
	ds_read_b128 v[196:199], v162 offset:34816
	ds_read_b128 v[200:203], v162 offset:35840
	ds_read_b128 v[204:207], v162 offset:36864
	ds_read_b128 v[208:211], v162 offset:37888
	ds_read_b128 v[212:215], v162 offset:38912
	ds_read_b128 v[216:219], v162 offset:39936
	buffer_load_dwordx4 v137, s[36:39], s65 offen lds
	s_mov_b32 m0, s30
	s_nop 0
	buffer_load_dwordx4 v145, s[36:39], s65 offen lds
	s_waitcnt vmcnt(8)
	s_waitcnt lgkmcnt(0)
	s_barrier
	s_setprio 1
	v_mfma_f32_16x16x32_bf16 v[120:123], v[128:131], v[188:191], v[120:123]
	v_mfma_f32_16x16x32_bf16 v[124:127], v[164:167], v[188:191], v[124:127]
	v_mfma_f32_16x16x32_bf16 v[104:107], v[128:131], v[196:199], v[104:107]
	v_mfma_f32_16x16x32_bf16 v[108:111], v[164:167], v[196:199], v[108:111]
	v_mfma_f32_16x16x32_bf16 v[88:91], v[128:131], v[204:207], v[88:91]
	v_mfma_f32_16x16x32_bf16 v[92:95], v[164:167], v[204:207], v[92:95]
	v_mfma_f32_16x16x32_bf16 v[72:75], v[128:131], v[212:215], v[72:75]
	v_mfma_f32_16x16x32_bf16 v[76:79], v[164:167], v[212:215], v[76:79]
	v_mfma_f32_16x16x32_bf16 v[120:123], v[132:135], v[192:195], v[120:123]
	v_mfma_f32_16x16x32_bf16 v[124:127], v[168:171], v[192:195], v[124:127]
	v_mfma_f32_16x16x32_bf16 v[104:107], v[132:135], v[200:203], v[104:107]
	v_mfma_f32_16x16x32_bf16 v[108:111], v[168:171], v[200:203], v[108:111]
	v_mfma_f32_16x16x32_bf16 v[88:91], v[132:135], v[208:211], v[88:91]
	v_mfma_f32_16x16x32_bf16 v[92:95], v[168:171], v[208:211], v[92:95]
	v_mfma_f32_16x16x32_bf16 v[72:75], v[132:135], v[216:219], v[72:75]
	v_mfma_f32_16x16x32_bf16 v[76:79], v[168:171], v[216:219], v[76:79]
	v_mfma_f32_16x16x32_bf16 v[112:115], v[172:175], v[188:191], v[112:115]
	v_mfma_f32_16x16x32_bf16 v[116:119], v[180:183], v[188:191], v[116:119]
	v_mfma_f32_16x16x32_bf16 v[96:99], v[172:175], v[196:199], v[96:99]
	v_mfma_f32_16x16x32_bf16 v[100:103], v[180:183], v[196:199], v[100:103]
	v_mfma_f32_16x16x32_bf16 v[80:83], v[172:175], v[204:207], v[80:83]
	v_mfma_f32_16x16x32_bf16 v[84:87], v[180:183], v[204:207], v[84:87]
	v_mfma_f32_16x16x32_bf16 v[64:67], v[172:175], v[212:215], v[64:67]
	v_mfma_f32_16x16x32_bf16 v[68:71], v[180:183], v[212:215], v[68:71]
	v_mfma_f32_16x16x32_bf16 v[112:115], v[176:179], v[192:195], v[112:115]
	v_mfma_f32_16x16x32_bf16 v[116:119], v[184:187], v[192:195], v[116:119]
	v_mfma_f32_16x16x32_bf16 v[96:99], v[176:179], v[200:203], v[96:99]
	v_mfma_f32_16x16x32_bf16 v[100:103], v[184:187], v[200:203], v[100:103]
	v_mfma_f32_16x16x32_bf16 v[80:83], v[176:179], v[208:211], v[80:83]
	v_mfma_f32_16x16x32_bf16 v[84:87], v[184:187], v[208:211], v[84:87]
	v_mfma_f32_16x16x32_bf16 v[64:67], v[176:179], v[216:219], v[64:67]
	v_mfma_f32_16x16x32_bf16 v[68:71], v[184:187], v[216:219], v[68:71]
	s_setprio 0
	s_barrier
	s_mov_b32 m0, s31
	s_bitset1_b32 s55, 7
	buffer_load_dwordx4 v141, s[4:7], s55 offen lds
	s_mov_b32 m0, s33
	ds_read_b128 v[188:191], v162 offset:49152
	buffer_load_dwordx4 v149, s[4:7], s55 offen lds
	s_add_i32 s55, s55, s22
	s_mov_b32 m0, s41
	ds_read_b128 v[192:195], v162 offset:50176
	buffer_load_dwordx4 v141, s[4:7], s55 offen lds
	s_mov_b32 m0, s42
	ds_read_b128 v[196:199], v162 offset:51200
	buffer_load_dwordx4 v149, s[4:7], s55 offen lds
	s_mov_b32 m0, s34
	ds_read_b128 v[200:203], v162 offset:52224
	buffer_load_dwordx4 v137, s[36:39], s54 offen lds
	s_mov_b32 m0, s35
	ds_read_b128 v[204:207], v162 offset:53248
	buffer_load_dwordx4 v145, s[36:39], s54 offen lds
	ds_read_b128 v[208:211], v162 offset:54272
	ds_read_b128 v[212:215], v162 offset:55296
	ds_read_b128 v[216:219], v162 offset:56320
	s_waitcnt vmcnt(8)
	s_waitcnt lgkmcnt(0)
	s_barrier
	s_setprio 1
	v_mfma_f32_16x16x32_bf16 v[56:59], v[128:131], v[188:191], v[56:59]
	v_mfma_f32_16x16x32_bf16 v[60:63], v[164:167], v[188:191], v[60:63]
	v_mfma_f32_16x16x32_bf16 v[40:43], v[128:131], v[196:199], v[40:43]
	v_mfma_f32_16x16x32_bf16 v[44:47], v[164:167], v[196:199], v[44:47]
	v_mfma_f32_16x16x32_bf16 v[24:27], v[128:131], v[204:207], v[24:27]
	v_mfma_f32_16x16x32_bf16 v[28:31], v[164:167], v[204:207], v[28:31]
	v_mfma_f32_16x16x32_bf16 v[8:11], v[128:131], v[212:215], v[8:11]
	v_mfma_f32_16x16x32_bf16 v[12:15], v[164:167], v[212:215], v[12:15]
	v_mfma_f32_16x16x32_bf16 v[56:59], v[132:135], v[192:195], v[56:59]
	v_mfma_f32_16x16x32_bf16 v[60:63], v[168:171], v[192:195], v[60:63]
	v_mfma_f32_16x16x32_bf16 v[40:43], v[132:135], v[200:203], v[40:43]
	v_mfma_f32_16x16x32_bf16 v[44:47], v[168:171], v[200:203], v[44:47]
	v_mfma_f32_16x16x32_bf16 v[24:27], v[132:135], v[208:211], v[24:27]
	v_mfma_f32_16x16x32_bf16 v[28:31], v[168:171], v[208:211], v[28:31]
	v_mfma_f32_16x16x32_bf16 v[8:11], v[132:135], v[216:219], v[8:11]
	v_mfma_f32_16x16x32_bf16 v[12:15], v[168:171], v[216:219], v[12:15]
	v_mfma_f32_16x16x32_bf16 v[48:51], v[172:175], v[188:191], v[48:51]
	v_mfma_f32_16x16x32_bf16 v[52:55], v[180:183], v[188:191], v[52:55]
	v_mfma_f32_16x16x32_bf16 v[32:35], v[172:175], v[196:199], v[32:35]
	v_mfma_f32_16x16x32_bf16 v[36:39], v[180:183], v[196:199], v[36:39]
	v_mfma_f32_16x16x32_bf16 v[16:19], v[172:175], v[204:207], v[16:19]
	v_mfma_f32_16x16x32_bf16 v[20:23], v[180:183], v[204:207], v[20:23]
	v_mfma_f32_16x16x32_bf16 v[4:7], v[172:175], v[212:215], v[4:7]
	v_mfma_f32_16x16x32_bf16 v[0:3], v[180:183], v[212:215], v[0:3]
	v_mfma_f32_16x16x32_bf16 v[48:51], v[176:179], v[192:195], v[48:51]
	v_mfma_f32_16x16x32_bf16 v[52:55], v[184:187], v[192:195], v[52:55]
	v_mfma_f32_16x16x32_bf16 v[32:35], v[176:179], v[200:203], v[32:35]
	v_mfma_f32_16x16x32_bf16 v[36:39], v[184:187], v[200:203], v[36:39]
	v_mfma_f32_16x16x32_bf16 v[16:19], v[176:179], v[208:211], v[16:19]
	v_mfma_f32_16x16x32_bf16 v[20:23], v[184:187], v[208:211], v[20:23]
	v_mfma_f32_16x16x32_bf16 v[4:7], v[176:179], v[216:219], v[4:7]
	v_mfma_f32_16x16x32_bf16 v[0:3], v[184:187], v[216:219], v[0:3]
	s_setprio 0
	s_barrier
	s_add_i32 s63, s63, 2
	s_addk_i32 s61, 0x100
	s_addk_i32 s62, 0x100
	s_cmp_ge_i32 s63, s44
	s_cbranch_scc0 .LBB0_1628

;     __device__ __forceinline__ unsigned a_off(const Unit& u, const Gemm& g) const { return (unsigned)u.pm * (unsigned)(BM * 2) * (unsigned)g.K; }
;     __device__ __forceinline__ unsigned b_off(const Unit& u, const Gemm& g) const { return (unsigned)u.pn * (unsigned)(BM * 2) * (unsigned)g.K; }
;     __device__ __forceinline__ bool next(int i, Unit& u) const { return so.next(i, u); }
;     __device__ __forceinline__ unsigned a_off(const Unit& u, const Gemm& g) const { return (unsigned)u.pm * (unsigned)(BM * 2) * (unsigned)g.K; }
; #define PG8_WAIT_V(n) asm volatile("s_waitcnt vmcnt(" #n ")" ::: "memory")
; #define PG8_BAR __builtin_amdgcn_s_barrier()
; template <class Epi, class Sched, bool ALIGN_EPI = false, bool SP2 = false, bool FP8 = false>
; __device__ __forceinline__ void gemm_phase(LAS unsigned char* lds, const Gemm g, const Sched& S, const Epi& E, int wbase) {
;     ...
;     for (;;) {
;         const bool has_next = S.next(ui + 1, nxt);
;         const unsigned nA = has_next ? S.a_off(nxt, g) : cA, nB = has_next ? S.b_off(nxt, g) : cB;
;         const rsrc_t rAn = (Sched::TWO && has_next) ? (nxt.part ? rA1 : rA0) : rAc, rBn = (Sched::TWO && has_next) ? (nxt.part ? rB1 : rB0) : rBc;
;         float pre_[8] = {0.f, 0.f, 0.f, 0.f, 0.f, 0.f, 0.f, 0.f};
;         if constexpr (Epi::HAS_PRE) E.pre_load(pre_, cur, wr);
;         for (int t = 0; t < nt; t += 2) {
;             const bool last = (t == nt - 2);
;             const unsigned a1 = cA + (unsigned)(t + 1) * kstep;
;             const unsigned a2 = last ? nA : cA + (unsigned)(t + 2) * kstep, b2 = last ? nB : cB + (unsigned)(t + 2) * kstep; const rsrc_t rA2 = (Sched::TWO && last) ? rAn : rAc, rB2 = (Sched::TWO && last) ? rBn : rBc;
;             const unsigned a3 = a2 + kstep, b3 = b2 + kstep;
;             if (last && has_next) S.a_ready(nxt);
;             if constexpr (SP2) {
;             PG8_LDB(B0, 0, 0); PG8_LDB(B1, 0, 1); PG8_SCHED; PG8_LDA(At, 0, 0); PG8_STAGE(PG8_SA(1, 1), rAc, a1 + hstep, voffA);
;             PG8_WAIT_V(8); PG8_WAIT_L(0); PG8_BAR; PG8_MMA(0, 0, At, B0); PG8_MMA(0, 1, At, B1); PG8_BAR; PG8_SCHED;
;             PG8_LDA(At, 0, 1); PG8_STAGE(PG8_SB(0, 0), rB2, b2, voffB); PG8_STAGE(PG8_SB(0, 1), rB2, b2 + hstep, voffB); PG8_STAGE(PG8_SA(0, 0), rA2, a2, voffA);
;             PG8_WAIT_V(8); PG8_WAIT_L(0); PG8_BAR; PG8_MMA(1, 0, At, B0); PG8_MMA(1, 1, At, B1); PG8_BAR; PG8_SCHED;
.LBB0_1699:
	s_mul_i32 s61, s60, 0x1c0000
	s_andn2_b64 vcc, exec, s[14:15]
	s_mul_i32 s62, s59, 0x1c0000
	s_cbranch_vccnz .LBB0_1703
	s_and_b64 s[6:7], s[18:19], exec
	s_waitcnt vmcnt(37)
	s_waitcnt vmcnt(36)
	s_waitcnt vmcnt(35)
	s_waitcnt vmcnt(32)
	s_waitcnt vmcnt(31)
	s_waitcnt vmcnt(28)
	s_waitcnt vmcnt(27)
	s_waitcnt vmcnt(23)
	s_waitcnt vmcnt(22)
	s_cselect_b32 s21, s61, s55
	s_cselect_b32 s63, s62, s54
	s_add_i32 s65, s55, 0x80
	s_add_i32 s66, s54, 0x100
	s_mov_b32 s67, 0
	v_add_u32_e32 v140, 0x10000, v176
	v_add_u32_e32 v156, 0x14000, v176
	ds_read_b128 v[112:115], v140
	ds_read_b128 v[124:127], v140 offset:1024
	ds_read_b128 v[136:139], v140 offset:2048
	ds_read_b128 v[140:143], v140 offset:3072
	ds_read_b128 v[144:147], v156
	ds_read_b128 v[148:151], v156 offset:1024
	ds_read_b128 v[152:155], v156 offset:2048
	ds_read_b128 v[156:159], v156 offset:3072
	s_add_i32 s6, s65, 0x80
	s_cmp_eq_u32 s52, s67
	s_cselect_b32 s68, s21, s6
	s_cselect_b32 s55, s63, s66
	s_or_b32 s54, s68, 0x80
	s_add_i32 s6, s25, s65
	s_mov_b32 m0, s53
	ds_read_b128 v[160:163], v177
	ds_read_b128 v[164:167], v177 offset:1024
	ds_read_b128 v[178:181], v177 offset:2048
	ds_read_b128 v[182:185], v177 offset:3072
	ds_read_b128 v[186:189], v177 offset:4096
	ds_read_b128 v[190:193], v177 offset:5120
	ds_read_b128 v[194:197], v177 offset:6144
	ds_read_b128 v[198:201], v177 offset:7168
	buffer_load_dwordx4 v170, s[36:39], s6 offen lds
	s_mov_b32 m0, s56
	s_nop 0
	buffer_load_dwordx4 v172, s[36:39], s6 offen lds
	s_waitcnt vmcnt(8)
	s_waitcnt lgkmcnt(0)
	s_barrier
	s_setprio 1
	v_mfma_f32_16x16x32_bf16 v[132:135], v[112:115], v[160:163], 0
	v_mfma_f32_16x16x32_bf16 v[128:131], v[136:139], v[160:163], 0
	v_mfma_f32_16x16x32_bf16 v[108:111], v[112:115], v[178:181], 0
	v_mfma_f32_16x16x32_bf16 v[104:107], v[136:139], v[178:181], 0
	v_mfma_f32_16x16x32_bf16 v[92:95], v[112:115], v[186:189], 0
	v_mfma_f32_16x16x32_bf16 v[88:91], v[136:139], v[186:189], 0
	v_mfma_f32_16x16x32_bf16 v[76:79], v[112:115], v[194:197], 0
	v_mfma_f32_16x16x32_bf16 v[72:75], v[136:139], v[194:197], 0
	v_mfma_f32_16x16x32_bf16 v[132:135], v[124:127], v[164:167], v[132:135]
	v_mfma_f32_16x16x32_bf16 v[128:131], v[140:143], v[164:167], v[128:131]
	v_mfma_f32_16x16x32_bf16 v[108:111], v[124:127], v[182:185], v[108:111]
	v_mfma_f32_16x16x32_bf16 v[104:107], v[140:143], v[182:185], v[104:107]
	v_mfma_f32_16x16x32_bf16 v[92:95], v[124:127], v[190:193], v[92:95]
	v_mfma_f32_16x16x32_bf16 v[88:91], v[140:143], v[190:193], v[88:91]
	v_mfma_f32_16x16x32_bf16 v[76:79], v[124:127], v[198:201], v[76:79]
	v_mfma_f32_16x16x32_bf16 v[72:75], v[140:143], v[198:201], v[72:75]
	v_mfma_f32_16x16x32_bf16 v[120:123], v[144:147], v[160:163], 0
	v_mfma_f32_16x16x32_bf16 v[116:119], v[152:155], v[160:163], 0
	v_mfma_f32_16x16x32_bf16 v[100:103], v[144:147], v[178:181], 0
	v_mfma_f32_16x16x32_bf16 v[96:99], v[152:155], v[178:181], 0
	v_mfma_f32_16x16x32_bf16 v[84:87], v[144:147], v[186:189], 0
	v_mfma_f32_16x16x32_bf16 v[80:83], v[152:155], v[186:189], 0
	v_mfma_f32_16x16x32_bf16 v[68:71], v[144:147], v[194:197], 0
	v_mfma_f32_16x16x32_bf16 v[64:67], v[152:155], v[194:197], 0
	v_mfma_f32_16x16x32_bf16 v[120:123], v[148:151], v[164:167], v[120:123]
	v_mfma_f32_16x16x32_bf16 v[116:119], v[156:159], v[164:167], v[116:119]
	v_mfma_f32_16x16x32_bf16 v[100:103], v[148:151], v[182:185], v[100:103]
	v_mfma_f32_16x16x32_bf16 v[96:99], v[156:159], v[182:185], v[96:99]
	v_mfma_f32_16x16x32_bf16 v[84:87], v[148:151], v[190:193], v[84:87]
	v_mfma_f32_16x16x32_bf16 v[80:83], v[156:159], v[190:193], v[80:83]
	v_mfma_f32_16x16x32_bf16 v[68:71], v[148:151], v[198:201], v[68:71]
	v_mfma_f32_16x16x32_bf16 v[64:67], v[156:159], v[198:201], v[64:67]
	s_setprio 0
	s_barrier
	s_mov_b32 m0, s27
	s_mov_b32 s6, s38
	s_mov_b32 s7, s39
	buffer_load_dwordx4 v171, s[4:7], s55 offen lds
	s_mov_b32 m0, s28
	ds_read_b128 v[160:163], v177 offset:16384
	s_add_i32 s69, s55, s25
	buffer_load_dwordx4 v173, s[4:7], s55 offen lds
	s_mov_b32 m0, s26
	ds_read_b128 v[164:167], v177 offset:17408
	buffer_load_dwordx4 v170, s[36:39], s68 offen lds
	s_mov_b32 m0, s31
	ds_read_b128 v[178:181], v177 offset:18432
	buffer_load_dwordx4 v172, s[36:39], s68 offen lds
	ds_read_b128 v[182:185], v177 offset:19456
	ds_read_b128 v[186:189], v177 offset:20480
	ds_read_b128 v[190:193], v177 offset:21504
	ds_read_b128 v[194:197], v177 offset:22528
	ds_read_b128 v[198:201], v177 offset:23552
	s_waitcnt vmcnt(6)
	s_waitcnt lgkmcnt(0)
	s_barrier
	s_setprio 1
	v_mfma_f32_16x16x32_bf16 v[60:63], v[112:115], v[160:163], 0
	v_mfma_f32_16x16x32_bf16 v[56:59], v[136:139], v[160:163], 0
	v_mfma_f32_16x16x32_bf16 v[44:47], v[112:115], v[178:181], 0
	v_mfma_f32_16x16x32_bf16 v[40:43], v[136:139], v[178:181], 0
	v_mfma_f32_16x16x32_bf16 v[28:31], v[112:115], v[186:189], 0
	v_mfma_f32_16x16x32_bf16 v[24:27], v[136:139], v[186:189], 0
	v_mfma_f32_16x16x32_bf16 v[12:15], v[112:115], v[194:197], 0
	v_mfma_f32_16x16x32_bf16 v[8:11], v[136:139], v[194:197], 0
	v_mfma_f32_16x16x32_bf16 v[60:63], v[124:127], v[164:167], v[60:63]
	v_mfma_f32_16x16x32_bf16 v[56:59], v[140:143], v[164:167], v[56:59]
	v_mfma_f32_16x16x32_bf16 v[44:47], v[124:127], v[182:185], v[44:47]
	v_mfma_f32_16x16x32_bf16 v[40:43], v[140:143], v[182:185], v[40:43]
	v_mfma_f32_16x16x32_bf16 v[28:31], v[124:127], v[190:193], v[28:31]
	v_mfma_f32_16x16x32_bf16 v[24:27], v[140:143], v[190:193], v[24:27]
	v_mfma_f32_16x16x32_bf16 v[12:15], v[124:127], v[198:201], v[12:15]
	v_mfma_f32_16x16x32_bf16 v[8:11], v[140:143], v[198:201], v[8:11]
	v_mfma_f32_16x16x32_bf16 v[52:55], v[144:147], v[160:163], 0
	v_mfma_f32_16x16x32_bf16 v[48:51], v[152:155], v[160:163], 0
	v_mfma_f32_16x16x32_bf16 v[36:39], v[144:147], v[178:181], 0
	v_mfma_f32_16x16x32_bf16 v[32:35], v[152:155], v[178:181], 0
	v_mfma_f32_16x16x32_bf16 v[20:23], v[144:147], v[186:189], 0
	v_mfma_f32_16x16x32_bf16 v[16:19], v[152:155], v[186:189], 0
	v_mfma_f32_16x16x32_bf16 v[4:7], v[144:147], v[194:197], 0
	v_mfma_f32_16x16x32_bf16 v[0:3], v[152:155], v[194:197], 0
	v_mfma_f32_16x16x32_bf16 v[52:55], v[148:151], v[164:167], v[52:55]
	v_mfma_f32_16x16x32_bf16 v[48:51], v[156:159], v[164:167], v[48:51]
	v_mfma_f32_16x16x32_bf16 v[36:39], v[148:151], v[182:185], v[36:39]
	v_mfma_f32_16x16x32_bf16 v[32:35], v[156:159], v[182:185], v[32:35]
	v_mfma_f32_16x16x32_bf16 v[20:23], v[148:151], v[190:193], v[20:23]
	v_mfma_f32_16x16x32_bf16 v[16:19], v[156:159], v[190:193], v[16:19]
	v_mfma_f32_16x16x32_bf16 v[4:7], v[148:151], v[198:201], v[4:7]
	v_mfma_f32_16x16x32_bf16 v[0:3], v[156:159], v[198:201], v[0:3]
	s_setprio 0
	s_barrier
; #define PG8_STAGE(bufoff, rs_, soff_, voff) do { _Pragma("unroll") for (int _i = 0; _i < 2; ++_i) \
;         __builtin_amdgcn_raw_ptr_buffer_load_lds(rs_, (LAS void*)(lds + (bufoff) + ldsw + _i * 8192), 16, (int)(voff)[_i], (int)(soff_), 0, 0); } while (0)
; #define PG8_LDA(dst, b, h) do { _Pragma("unroll") for (int m = 0; m < 4; ++m) dst[m] = PG8_LD2(lds + PG8_SA(b, h) + aoff + m * 2048); } while (0)
; #define PG8_LDB(dst, b, h) do { _Pragma("unroll") for (int n = 0; n < 2; ++n) dst[n] = PG8_LD2(lds + PG8_SB(b, h) + boff + n * 2048); } while (0)
; #define PG8_WAIT_V(n) asm volatile("s_waitcnt vmcnt(" #n ")" ::: "memory")
; #define PG8_WAIT_L(n) asm volatile("s_waitcnt lgkmcnt(" #n ")" ::: "memory")
; #define PG8_BAR __builtin_amdgcn_s_barrier()
; #define PG8_SCHED __builtin_amdgcn_sched_barrier(0)
; template <class Epi, class Sched, bool ALIGN_EPI = false, bool SP2 = false, bool FP8 = false>
; __device__ __forceinline__ void gemm_phase(LAS unsigned char* lds, const Gemm g, const Sched& S, const Epi& E, int wbase) {
;     ...
;             PG8_LDB(B0, 1, 0); PG8_LDB(B1, 1, 1); PG8_SCHED; PG8_LDA(At, 1, 0); PG8_STAGE(PG8_SA(0, 1), rA2, a2 + hstep, voffA);
;             PG8_WAIT_V(8); PG8_WAIT_L(0); PG8_BAR; PG8_MMA(0, 0, At, B0); PG8_MMA(0, 1, At, B1); PG8_BAR; PG8_SCHED;
;             PG8_LDA(At, 1, 1); PG8_STAGE(PG8_SB(1, 0), rB2, b3, voffB); PG8_STAGE(PG8_SB(1, 1), rB2, b3 + hstep, voffB); PG8_STAGE(PG8_SA(1, 0), rA2, a3, voffA);
;             PG8_WAIT_V(8); PG8_WAIT_L(0); PG8_BAR; PG8_MMA(1, 0, At, B0); PG8_MMA(1, 1, At, B1); PG8_BAR; PG8_SCHED;
	s_mov_b32 m0, s29
	s_nop 0
	buffer_load_dwordx4 v171, s[4:7], s69 offen lds
	s_mov_b32 m0, s30
	s_nop 0
	buffer_load_dwordx4 v173, s[4:7], s69 offen lds
	v_add_u32_e32 v140, 0x18000, v176
	v_add_u32_e32 v156, 0x1c000, v176
	ds_read_b128 v[112:115], v140
	ds_read_b128 v[124:127], v140 offset:1024
	ds_read_b128 v[136:139], v140 offset:2048
	ds_read_b128 v[140:143], v140 offset:3072
	ds_read_b128 v[144:147], v156
	ds_read_b128 v[148:151], v156 offset:1024
	ds_read_b128 v[152:155], v156 offset:2048
	ds_read_b128 v[156:159], v156 offset:3072
	s_add_i32 s68, s68, s25
	s_mov_b32 m0, s33
	ds_read_b128 v[160:163], v177 offset:32768
	ds_read_b128 v[164:167], v177 offset:33792
	ds_read_b128 v[178:181], v177 offset:34816
	ds_read_b128 v[182:185], v177 offset:35840
	ds_read_b128 v[186:189], v177 offset:36864
	ds_read_b128 v[190:193], v177 offset:37888
	ds_read_b128 v[194:197], v177 offset:38912
	ds_read_b128 v[198:201], v177 offset:39936
	buffer_load_dwordx4 v170, s[36:39], s68 offen lds
	s_mov_b32 m0, s34
	s_nop 0
	buffer_load_dwordx4 v172, s[36:39], s68 offen lds
	s_waitcnt vmcnt(8)
	s_waitcnt lgkmcnt(0)
	s_barrier
	s_setprio 1
	v_mfma_f32_16x16x32_bf16 v[132:135], v[112:115], v[160:163], v[132:135]
	v_mfma_f32_16x16x32_bf16 v[128:131], v[136:139], v[160:163], v[128:131]
	v_mfma_f32_16x16x32_bf16 v[108:111], v[112:115], v[178:181], v[108:111]
	v_mfma_f32_16x16x32_bf16 v[104:107], v[136:139], v[178:181], v[104:107]
	v_mfma_f32_16x16x32_bf16 v[92:95], v[112:115], v[186:189], v[92:95]
	v_mfma_f32_16x16x32_bf16 v[88:91], v[136:139], v[186:189], v[88:91]
	v_mfma_f32_16x16x32_bf16 v[76:79], v[112:115], v[194:197], v[76:79]
	v_mfma_f32_16x16x32_bf16 v[72:75], v[136:139], v[194:197], v[72:75]
	v_mfma_f32_16x16x32_bf16 v[132:135], v[124:127], v[164:167], v[132:135]
	v_mfma_f32_16x16x32_bf16 v[128:131], v[140:143], v[164:167], v[128:131]
	v_mfma_f32_16x16x32_bf16 v[108:111], v[124:127], v[182:185], v[108:111]
	v_mfma_f32_16x16x32_bf16 v[104:107], v[140:143], v[182:185], v[104:107]
	v_mfma_f32_16x16x32_bf16 v[92:95], v[124:127], v[190:193], v[92:95]
	v_mfma_f32_16x16x32_bf16 v[88:91], v[140:143], v[190:193], v[88:91]
	v_mfma_f32_16x16x32_bf16 v[76:79], v[124:127], v[198:201], v[76:79]
	v_mfma_f32_16x16x32_bf16 v[72:75], v[140:143], v[198:201], v[72:75]
	v_mfma_f32_16x16x32_bf16 v[120:123], v[144:147], v[160:163], v[120:123]
	v_mfma_f32_16x16x32_bf16 v[116:119], v[152:155], v[160:163], v[116:119]
	v_mfma_f32_16x16x32_bf16 v[100:103], v[144:147], v[178:181], v[100:103]
	v_mfma_f32_16x16x32_bf16 v[96:99], v[152:155], v[178:181], v[96:99]
	v_mfma_f32_16x16x32_bf16 v[84:87], v[144:147], v[186:189], v[84:87]
	v_mfma_f32_16x16x32_bf16 v[80:83], v[152:155], v[186:189], v[80:83]
	v_mfma_f32_16x16x32_bf16 v[68:71], v[144:147], v[194:197], v[68:71]
	v_mfma_f32_16x16x32_bf16 v[64:67], v[152:155], v[194:197], v[64:67]
	v_mfma_f32_16x16x32_bf16 v[120:123], v[148:151], v[164:167], v[120:123]
	v_mfma_f32_16x16x32_bf16 v[116:119], v[156:159], v[164:167], v[116:119]
	v_mfma_f32_16x16x32_bf16 v[100:103], v[148:151], v[182:185], v[100:103]
	v_mfma_f32_16x16x32_bf16 v[96:99], v[156:159], v[182:185], v[96:99]
	v_mfma_f32_16x16x32_bf16 v[84:87], v[148:151], v[190:193], v[84:87]
	v_mfma_f32_16x16x32_bf16 v[80:83], v[156:159], v[190:193], v[80:83]
	v_mfma_f32_16x16x32_bf16 v[68:71], v[148:151], v[198:201], v[68:71]
	v_mfma_f32_16x16x32_bf16 v[64:67], v[156:159], v[198:201], v[64:67]
	s_setprio 0
	s_barrier
	s_mov_b32 m0, s1
	s_bitset1_b32 s55, 7
	buffer_load_dwordx4 v171, s[4:7], s55 offen lds
	s_mov_b32 m0, s35
	ds_read_b128 v[160:163], v177 offset:49152
	buffer_load_dwordx4 v173, s[4:7], s55 offen lds
	s_add_i32 s55, s55, s25
	s_mov_b32 m0, s43
	ds_read_b128 v[164:167], v177 offset:50176
	buffer_load_dwordx4 v171, s[4:7], s55 offen lds
	s_mov_b32 m0, s44
	ds_read_b128 v[178:181], v177 offset:51200
	buffer_load_dwordx4 v173, s[4:7], s55 offen lds
	s_mov_b32 m0, s41
	ds_read_b128 v[182:185], v177 offset:52224
	buffer_load_dwordx4 v170, s[36:39], s54 offen lds
	s_mov_b32 m0, s42
	ds_read_b128 v[186:189], v177 offset:53248
	buffer_load_dwordx4 v172, s[36:39], s54 offen lds
	ds_read_b128 v[190:193], v177 offset:54272
	ds_read_b128 v[194:197], v177 offset:55296
	ds_read_b128 v[198:201], v177 offset:56320
	s_waitcnt vmcnt(8)
	s_waitcnt lgkmcnt(0)
	s_barrier
	s_setprio 1
	v_mfma_f32_16x16x32_bf16 v[60:63], v[112:115], v[160:163], v[60:63]
	v_mfma_f32_16x16x32_bf16 v[56:59], v[136:139], v[160:163], v[56:59]
	v_mfma_f32_16x16x32_bf16 v[44:47], v[112:115], v[178:181], v[44:47]
	v_mfma_f32_16x16x32_bf16 v[40:43], v[136:139], v[178:181], v[40:43]
	v_mfma_f32_16x16x32_bf16 v[28:31], v[112:115], v[186:189], v[28:31]
	v_mfma_f32_16x16x32_bf16 v[24:27], v[136:139], v[186:189], v[24:27]
	v_mfma_f32_16x16x32_bf16 v[12:15], v[112:115], v[194:197], v[12:15]
	v_mfma_f32_16x16x32_bf16 v[8:11], v[136:139], v[194:197], v[8:11]
	v_mfma_f32_16x16x32_bf16 v[60:63], v[124:127], v[164:167], v[60:63]
	v_mfma_f32_16x16x32_bf16 v[56:59], v[140:143], v[164:167], v[56:59]
	v_mfma_f32_16x16x32_bf16 v[44:47], v[124:127], v[182:185], v[44:47]
	v_mfma_f32_16x16x32_bf16 v[40:43], v[140:143], v[182:185], v[40:43]
	v_mfma_f32_16x16x32_bf16 v[28:31], v[124:127], v[190:193], v[28:31]
	v_mfma_f32_16x16x32_bf16 v[24:27], v[140:143], v[190:193], v[24:27]
	v_mfma_f32_16x16x32_bf16 v[12:15], v[124:127], v[198:201], v[12:15]
	v_mfma_f32_16x16x32_bf16 v[8:11], v[140:143], v[198:201], v[8:11]
	v_mfma_f32_16x16x32_bf16 v[52:55], v[144:147], v[160:163], v[52:55]
	v_mfma_f32_16x16x32_bf16 v[48:51], v[152:155], v[160:163], v[48:51]
	v_mfma_f32_16x16x32_bf16 v[36:39], v[144:147], v[178:181], v[36:39]
	v_mfma_f32_16x16x32_bf16 v[32:35], v[152:155], v[178:181], v[32:35]
	v_mfma_f32_16x16x32_bf16 v[20:23], v[144:147], v[186:189], v[20:23]
	v_mfma_f32_16x16x32_bf16 v[16:19], v[152:155], v[186:189], v[16:19]
	v_mfma_f32_16x16x32_bf16 v[4:7], v[144:147], v[194:197], v[4:7]
	v_mfma_f32_16x16x32_bf16 v[0:3], v[152:155], v[194:197], v[0:3]
	v_mfma_f32_16x16x32_bf16 v[52:55], v[148:151], v[164:167], v[52:55]
	v_mfma_f32_16x16x32_bf16 v[48:51], v[156:159], v[164:167], v[48:51]
	v_mfma_f32_16x16x32_bf16 v[36:39], v[148:151], v[182:185], v[36:39]
	v_mfma_f32_16x16x32_bf16 v[32:35], v[156:159], v[182:185], v[32:35]
	v_mfma_f32_16x16x32_bf16 v[20:23], v[148:151], v[190:193], v[20:23]
	v_mfma_f32_16x16x32_bf16 v[16:19], v[156:159], v[190:193], v[16:19]
	v_mfma_f32_16x16x32_bf16 v[4:7], v[148:151], v[198:201], v[4:7]
	v_mfma_f32_16x16x32_bf16 v[0:3], v[156:159], v[198:201], v[0:3]
	s_setprio 0
	s_barrier
	s_add_i32 s67, s67, 2
	s_addk_i32 s65, 0x100
	s_addk_i32 s66, 0x100
	s_cmp_ge_i32 s67, s47
	s_cbranch_scc0 .LBB0_1701
	s_branch .Lzp_after_1701
; #define PG8_STAGE(bufoff, rs_, soff_, voff) do { _Pragma("unroll") for (int _i = 0; _i < 2; ++_i) \
;         __builtin_amdgcn_raw_ptr_buffer_load_lds(rs_, (LAS void*)(lds + (bufoff) + ldsw + _i * 8192), 16, (int)(voff)[_i], (int)(soff_), 0, 0); } while (0)
; #define PG8_LDA(dst, b, h) do { _Pragma("unroll") for (int m = 0; m < 4; ++m) dst[m] = PG8_LD2(lds + PG8_SA(b, h) + aoff + m * 2048); } while (0)
; #define PG8_LDB(dst, b, h) do { _Pragma("unroll") for (int n = 0; n < 2; ++n) dst[n] = PG8_LD2(lds + PG8_SB(b, h) + boff + n * 2048); } while (0)
; #define PG8_WAIT_V(n) asm volatile("s_waitcnt vmcnt(" #n ")" ::: "memory")
; #define PG8_WAIT_L(n) asm volatile("s_waitcnt lgkmcnt(" #n ")" ::: "memory")
; #define PG8_BAR __builtin_amdgcn_s_barrier()
; #define PG8_SCHED __builtin_amdgcn_sched_barrier(0)
; template <class Epi, class Sched, bool ALIGN_EPI = false, bool SP2 = false, bool FP8 = false>
; __device__ __forceinline__ void gemm_phase(LAS unsigned char* lds, const Gemm g, const Sched& S, const Epi& E, int wbase) {
;     ...
;         for (int t = 0; t < nt; t += 2) {
;             const bool last = (t == nt - 2);
;             const unsigned a1 = cA + (unsigned)(t + 1) * kstep;
;             const unsigned a2 = last ? nA : cA + (unsigned)(t + 2) * kstep, b2 = last ? nB : cB + (unsigned)(t + 2) * kstep; const rsrc_t rA2 = (Sched::TWO && last) ? rAn : rAc, rB2 = (Sched::TWO && last) ? rBn : rBc;
;             const unsigned a3 = a2 + kstep, b3 = b2 + kstep;
;             if (last && has_next) S.a_ready(nxt);
;             if constexpr (SP2) {
;             PG8_LDB(B0, 0, 0); PG8_LDB(B1, 0, 1); PG8_SCHED; PG8_LDA(At, 0, 0); PG8_STAGE(PG8_SA(1, 1), rAc, a1 + hstep, voffA);
;             PG8_WAIT_V(8); PG8_WAIT_L(0); PG8_BAR; PG8_MMA(0, 0, At, B0); PG8_MMA(0, 1, At, B1); PG8_BAR; PG8_SCHED;
;             PG8_LDA(At, 0, 1); PG8_STAGE(PG8_SB(0, 0), rB2, b2, voffB); PG8_STAGE(PG8_SB(0, 1), rB2, b2 + hstep, voffB); PG8_STAGE(PG8_SA(0, 0), rA2, a2, voffA);
;             PG8_WAIT_V(8); PG8_WAIT_L(0); PG8_BAR; PG8_MMA(1, 0, At, B0); PG8_MMA(1, 1, At, B1); PG8_BAR; PG8_SCHED;
.LBB0_1701:
	v_add_u32_e32 v140, 0x10000, v176
	v_add_u32_e32 v156, 0x14000, v176
	ds_read_b128 v[112:115], v140
	ds_read_b128 v[124:127], v140 offset:1024
	ds_read_b128 v[136:139], v140 offset:2048
	ds_read_b128 v[140:143], v140 offset:3072
	ds_read_b128 v[144:147], v156
	ds_read_b128 v[148:151], v156 offset:1024
	ds_read_b128 v[152:155], v156 offset:2048
	ds_read_b128 v[156:159], v156 offset:3072
	s_add_i32 s6, s65, 0x80
	s_cmp_eq_u32 s52, s67
	s_cselect_b32 s68, s21, s6
	s_cselect_b32 s55, s63, s66
	s_or_b32 s54, s68, 0x80
	s_add_i32 s6, s25, s65
	s_mov_b32 m0, s53
	ds_read_b128 v[160:163], v177
	ds_read_b128 v[164:167], v177 offset:1024
	ds_read_b128 v[178:181], v177 offset:2048
	ds_read_b128 v[182:185], v177 offset:3072
	ds_read_b128 v[186:189], v177 offset:4096
	ds_read_b128 v[190:193], v177 offset:5120
	ds_read_b128 v[194:197], v177 offset:6144
	ds_read_b128 v[198:201], v177 offset:7168
	buffer_load_dwordx4 v170, s[36:39], s6 offen lds
	s_mov_b32 m0, s56
	s_nop 0
	buffer_load_dwordx4 v172, s[36:39], s6 offen lds
	s_waitcnt vmcnt(8)
	s_waitcnt lgkmcnt(0)
	s_barrier
	s_setprio 1
	v_mfma_f32_16x16x32_bf16 v[132:135], v[112:115], v[160:163], v[132:135]
	v_mfma_f32_16x16x32_bf16 v[128:131], v[136:139], v[160:163], v[128:131]
	v_mfma_f32_16x16x32_bf16 v[108:111], v[112:115], v[178:181], v[108:111]
	v_mfma_f32_16x16x32_bf16 v[104:107], v[136:139], v[178:181], v[104:107]
	v_mfma_f32_16x16x32_bf16 v[92:95], v[112:115], v[186:189], v[92:95]
	v_mfma_f32_16x16x32_bf16 v[88:91], v[136:139], v[186:189], v[88:91]
	v_mfma_f32_16x16x32_bf16 v[76:79], v[112:115], v[194:197], v[76:79]
	v_mfma_f32_16x16x32_bf16 v[72:75], v[136:139], v[194:197], v[72:75]
	v_mfma_f32_16x16x32_bf16 v[132:135], v[124:127], v[164:167], v[132:135]
	v_mfma_f32_16x16x32_bf16 v[128:131], v[140:143], v[164:167], v[128:131]
	v_mfma_f32_16x16x32_bf16 v[108:111], v[124:127], v[182:185], v[108:111]
	v_mfma_f32_16x16x32_bf16 v[104:107], v[140:143], v[182:185], v[104:107]
	v_mfma_f32_16x16x32_bf16 v[92:95], v[124:127], v[190:193], v[92:95]
	v_mfma_f32_16x16x32_bf16 v[88:91], v[140:143], v[190:193], v[88:91]
	v_mfma_f32_16x16x32_bf16 v[76:79], v[124:127], v[198:201], v[76:79]
	v_mfma_f32_16x16x32_bf16 v[72:75], v[140:143], v[198:201], v[72:75]
	v_mfma_f32_16x16x32_bf16 v[120:123], v[144:147], v[160:163], v[120:123]
	v_mfma_f32_16x16x32_bf16 v[116:119], v[152:155], v[160:163], v[116:119]
	v_mfma_f32_16x16x32_bf16 v[100:103], v[144:147], v[178:181], v[100:103]
	v_mfma_f32_16x16x32_bf16 v[96:99], v[152:155], v[178:181], v[96:99]
	v_mfma_f32_16x16x32_bf16 v[84:87], v[144:147], v[186:189], v[84:87]
	v_mfma_f32_16x16x32_bf16 v[80:83], v[152:155], v[186:189], v[80:83]
	v_mfma_f32_16x16x32_bf16 v[68:71], v[144:147], v[194:197], v[68:71]
	v_mfma_f32_16x16x32_bf16 v[64:67], v[152:155], v[194:197], v[64:67]
	v_mfma_f32_16x16x32_bf16 v[120:123], v[148:151], v[164:167], v[120:123]
	v_mfma_f32_16x16x32_bf16 v[116:119], v[156:159], v[164:167], v[116:119]
	v_mfma_f32_16x16x32_bf16 v[100:103], v[148:151], v[182:185], v[100:103]
	v_mfma_f32_16x16x32_bf16 v[96:99], v[156:159], v[182:185], v[96:99]
	v_mfma_f32_16x16x32_bf16 v[84:87], v[148:151], v[190:193], v[84:87]
	v_mfma_f32_16x16x32_bf16 v[80:83], v[156:159], v[190:193], v[80:83]
	v_mfma_f32_16x16x32_bf16 v[68:71], v[148:151], v[198:201], v[68:71]
	v_mfma_f32_16x16x32_bf16 v[64:67], v[156:159], v[198:201], v[64:67]
	s_setprio 0
	s_barrier
	s_mov_b32 m0, s27
	s_mov_b32 s6, s38
	s_mov_b32 s7, s39
	buffer_load_dwordx4 v171, s[4:7], s55 offen lds
	s_mov_b32 m0, s28
	ds_read_b128 v[160:163], v177 offset:16384
	s_add_i32 s69, s55, s25
	buffer_load_dwordx4 v173, s[4:7], s55 offen lds
	s_mov_b32 m0, s26
	ds_read_b128 v[164:167], v177 offset:17408
	buffer_load_dwordx4 v170, s[36:39], s68 offen lds
	s_mov_b32 m0, s31
	ds_read_b128 v[178:181], v177 offset:18432
	buffer_load_dwordx4 v172, s[36:39], s68 offen lds
	ds_read_b128 v[182:185], v177 offset:19456
	ds_read_b128 v[186:189], v177 offset:20480
	ds_read_b128 v[190:193], v177 offset:21504
	ds_read_b128 v[194:197], v177 offset:22528
	ds_read_b128 v[198:201], v177 offset:23552
	s_waitcnt vmcnt(6)
	s_waitcnt lgkmcnt(0)
	s_barrier
	s_setprio 1
	v_mfma_f32_16x16x32_bf16 v[60:63], v[112:115], v[160:163], v[60:63]
	v_mfma_f32_16x16x32_bf16 v[56:59], v[136:139], v[160:163], v[56:59]
	v_mfma_f32_16x16x32_bf16 v[44:47], v[112:115], v[178:181], v[44:47]
	v_mfma_f32_16x16x32_bf16 v[40:43], v[136:139], v[178:181], v[40:43]
	v_mfma_f32_16x16x32_bf16 v[28:31], v[112:115], v[186:189], v[28:31]
	v_mfma_f32_16x16x32_bf16 v[24:27], v[136:139], v[186:189], v[24:27]
	v_mfma_f32_16x16x32_bf16 v[12:15], v[112:115], v[194:197], v[12:15]
	v_mfma_f32_16x16x32_bf16 v[8:11], v[136:139], v[194:197], v[8:11]
	v_mfma_f32_16x16x32_bf16 v[60:63], v[124:127], v[164:167], v[60:63]
	v_mfma_f32_16x16x32_bf16 v[56:59], v[140:143], v[164:167], v[56:59]
	v_mfma_f32_16x16x32_bf16 v[44:47], v[124:127], v[182:185], v[44:47]
	v_mfma_f32_16x16x32_bf16 v[40:43], v[140:143], v[182:185], v[40:43]
	v_mfma_f32_16x16x32_bf16 v[28:31], v[124:127], v[190:193], v[28:31]
	v_mfma_f32_16x16x32_bf16 v[24:27], v[140:143], v[190:193], v[24:27]
	v_mfma_f32_16x16x32_bf16 v[12:15], v[124:127], v[198:201], v[12:15]
	v_mfma_f32_16x16x32_bf16 v[8:11], v[140:143], v[198:201], v[8:11]
	v_mfma_f32_16x16x32_bf16 v[52:55], v[144:147], v[160:163], v[52:55]
	v_mfma_f32_16x16x32_bf16 v[48:51], v[152:155], v[160:163], v[48:51]
	v_mfma_f32_16x16x32_bf16 v[36:39], v[144:147], v[178:181], v[36:39]
	v_mfma_f32_16x16x32_bf16 v[32:35], v[152:155], v[178:181], v[32:35]
	v_mfma_f32_16x16x32_bf16 v[20:23], v[144:147], v[186:189], v[20:23]
	v_mfma_f32_16x16x32_bf16 v[16:19], v[152:155], v[186:189], v[16:19]
	v_mfma_f32_16x16x32_bf16 v[4:7], v[144:147], v[194:197], v[4:7]
	v_mfma_f32_16x16x32_bf16 v[0:3], v[152:155], v[194:197], v[0:3]
	v_mfma_f32_16x16x32_bf16 v[52:55], v[148:151], v[164:167], v[52:55]
	v_mfma_f32_16x16x32_bf16 v[48:51], v[156:159], v[164:167], v[48:51]
	v_mfma_f32_16x16x32_bf16 v[36:39], v[148:151], v[182:185], v[36:39]
	v_mfma_f32_16x16x32_bf16 v[32:35], v[156:159], v[182:185], v[32:35]
	v_mfma_f32_16x16x32_bf16 v[20:23], v[148:151], v[190:193], v[20:23]
	v_mfma_f32_16x16x32_bf16 v[16:19], v[156:159], v[190:193], v[16:19]
	v_mfma_f32_16x16x32_bf16 v[4:7], v[148:151], v[198:201], v[4:7]
	v_mfma_f32_16x16x32_bf16 v[0:3], v[156:159], v[198:201], v[0:3]
	s_setprio 0
	s_barrier
; #define PG8_STAGE(bufoff, rs_, soff_, voff) do { _Pragma("unroll") for (int _i = 0; _i < 2; ++_i) \
;         __builtin_amdgcn_raw_ptr_buffer_load_lds(rs_, (LAS void*)(lds + (bufoff) + ldsw + _i * 8192), 16, (int)(voff)[_i], (int)(soff_), 0, 0); } while (0)
; #define PG8_LDA(dst, b, h) do { _Pragma("unroll") for (int m = 0; m < 4; ++m) dst[m] = PG8_LD2(lds + PG8_SA(b, h) + aoff + m * 2048); } while (0)
; #define PG8_LDB(dst, b, h) do { _Pragma("unroll") for (int n = 0; n < 2; ++n) dst[n] = PG8_LD2(lds + PG8_SB(b, h) + boff + n * 2048); } while (0)
; #define PG8_WAIT_V(n) asm volatile("s_waitcnt vmcnt(" #n ")" ::: "memory")
; #define PG8_WAIT_L(n) asm volatile("s_waitcnt lgkmcnt(" #n ")" ::: "memory")
; #define PG8_BAR __builtin_amdgcn_s_barrier()
; #define PG8_SCHED __builtin_amdgcn_sched_barrier(0)
; template <class Epi, class Sched, bool ALIGN_EPI = false, bool SP2 = false, bool FP8 = false>
; __device__ __forceinline__ void gemm_phase(LAS unsigned char* lds, const Gemm g, const Sched& S, const Epi& E, int wbase) {
;     ...
;         for (int t = 0; t < nt; t += 2) {
;     ...
;             PG8_LDB(B0, 1, 0); PG8_LDB(B1, 1, 1); PG8_SCHED; PG8_LDA(At, 1, 0); PG8_STAGE(PG8_SA(0, 1), rA2, a2 + hstep, voffA);
;             PG8_WAIT_V(8); PG8_WAIT_L(0); PG8_BAR; PG8_MMA(0, 0, At, B0); PG8_MMA(0, 1, At, B1); PG8_BAR; PG8_SCHED;
;             PG8_LDA(At, 1, 1); PG8_STAGE(PG8_SB(1, 0), rB2, b3, voffB); PG8_STAGE(PG8_SB(1, 1), rB2, b3 + hstep, voffB); PG8_STAGE(PG8_SA(1, 0), rA2, a3, voffA);
;             PG8_WAIT_V(8); PG8_WAIT_L(0); PG8_BAR; PG8_MMA(1, 0, At, B0); PG8_MMA(1, 1, At, B1); PG8_BAR; PG8_SCHED;
	s_mov_b32 m0, s29
	s_nop 0
	buffer_load_dwordx4 v171, s[4:7], s69 offen lds
	s_mov_b32 m0, s30
	s_nop 0
	buffer_load_dwordx4 v173, s[4:7], s69 offen lds
	v_add_u32_e32 v140, 0x18000, v176
	v_add_u32_e32 v156, 0x1c000, v176
	ds_read_b128 v[112:115], v140
	ds_read_b128 v[124:127], v140 offset:1024
	ds_read_b128 v[136:139], v140 offset:2048
	ds_read_b128 v[140:143], v140 offset:3072
	ds_read_b128 v[144:147], v156
	ds_read_b128 v[148:151], v156 offset:1024
	ds_read_b128 v[152:155], v156 offset:2048
	ds_read_b128 v[156:159], v156 offset:3072
	s_add_i32 s68, s68, s25
	s_mov_b32 m0, s33
	ds_read_b128 v[160:163], v177 offset:32768
	ds_read_b128 v[164:167], v177 offset:33792
	ds_read_b128 v[178:181], v177 offset:34816
	ds_read_b128 v[182:185], v177 offset:35840
	ds_read_b128 v[186:189], v177 offset:36864
	ds_read_b128 v[190:193], v177 offset:37888
	ds_read_b128 v[194:197], v177 offset:38912
	ds_read_b128 v[198:201], v177 offset:39936
	buffer_load_dwordx4 v170, s[36:39], s68 offen lds
	s_mov_b32 m0, s34
	s_nop 0
	buffer_load_dwordx4 v172, s[36:39], s68 offen lds
	s_waitcnt vmcnt(8)
	s_waitcnt lgkmcnt(0)
	s_barrier
	s_setprio 1
	v_mfma_f32_16x16x32_bf16 v[132:135], v[112:115], v[160:163], v[132:135]
	v_mfma_f32_16x16x32_bf16 v[128:131], v[136:139], v[160:163], v[128:131]
	v_mfma_f32_16x16x32_bf16 v[108:111], v[112:115], v[178:181], v[108:111]
	v_mfma_f32_16x16x32_bf16 v[104:107], v[136:139], v[178:181], v[104:107]
	v_mfma_f32_16x16x32_bf16 v[92:95], v[112:115], v[186:189], v[92:95]
	v_mfma_f32_16x16x32_bf16 v[88:91], v[136:139], v[186:189], v[88:91]
	v_mfma_f32_16x16x32_bf16 v[76:79], v[112:115], v[194:197], v[76:79]
	v_mfma_f32_16x16x32_bf16 v[72:75], v[136:139], v[194:197], v[72:75]
	v_mfma_f32_16x16x32_bf16 v[132:135], v[124:127], v[164:167], v[132:135]
	v_mfma_f32_16x16x32_bf16 v[128:131], v[140:143], v[164:167], v[128:131]
	v_mfma_f32_16x16x32_bf16 v[108:111], v[124:127], v[182:185], v[108:111]
	v_mfma_f32_16x16x32_bf16 v[104:107], v[140:143], v[182:185], v[104:107]
	v_mfma_f32_16x16x32_bf16 v[92:95], v[124:127], v[190:193], v[92:95]
	v_mfma_f32_16x16x32_bf16 v[88:91], v[140:143], v[190:193], v[88:91]
	v_mfma_f32_16x16x32_bf16 v[76:79], v[124:127], v[198:201], v[76:79]
	v_mfma_f32_16x16x32_bf16 v[72:75], v[140:143], v[198:201], v[72:75]
	v_mfma_f32_16x16x32_bf16 v[120:123], v[144:147], v[160:163], v[120:123]
	v_mfma_f32_16x16x32_bf16 v[116:119], v[152:155], v[160:163], v[116:119]
	v_mfma_f32_16x16x32_bf16 v[100:103], v[144:147], v[178:181], v[100:103]
	v_mfma_f32_16x16x32_bf16 v[96:99], v[152:155], v[178:181], v[96:99]
	v_mfma_f32_16x16x32_bf16 v[84:87], v[144:147], v[186:189], v[84:87]
	v_mfma_f32_16x16x32_bf16 v[80:83], v[152:155], v[186:189], v[80:83]
	v_mfma_f32_16x16x32_bf16 v[68:71], v[144:147], v[194:197], v[68:71]
	v_mfma_f32_16x16x32_bf16 v[64:67], v[152:155], v[194:197], v[64:67]
	v_mfma_f32_16x16x32_bf16 v[120:123], v[148:151], v[164:167], v[120:123]
	v_mfma_f32_16x16x32_bf16 v[116:119], v[156:159], v[164:167], v[116:119]
	v_mfma_f32_16x16x32_bf16 v[100:103], v[148:151], v[182:185], v[100:103]
	v_mfma_f32_16x16x32_bf16 v[96:99], v[156:159], v[182:185], v[96:99]
	v_mfma_f32_16x16x32_bf16 v[84:87], v[148:151], v[190:193], v[84:87]
	v_mfma_f32_16x16x32_bf16 v[80:83], v[156:159], v[190:193], v[80:83]
	v_mfma_f32_16x16x32_bf16 v[68:71], v[148:151], v[198:201], v[68:71]
	v_mfma_f32_16x16x32_bf16 v[64:67], v[156:159], v[198:201], v[64:67]
	s_setprio 0
	s_barrier
	s_mov_b32 m0, s1
	s_bitset1_b32 s55, 7
	buffer_load_dwordx4 v171, s[4:7], s55 offen lds
	s_mov_b32 m0, s35
	ds_read_b128 v[160:163], v177 offset:49152
	buffer_load_dwordx4 v173, s[4:7], s55 offen lds
	s_add_i32 s55, s55, s25
	s_mov_b32 m0, s43
	ds_read_b128 v[164:167], v177 offset:50176
	buffer_load_dwordx4 v171, s[4:7], s55 offen lds
	s_mov_b32 m0, s44
	ds_read_b128 v[178:181], v177 offset:51200
	buffer_load_dwordx4 v173, s[4:7], s55 offen lds
	s_mov_b32 m0, s41
	ds_read_b128 v[182:185], v177 offset:52224
	buffer_load_dwordx4 v170, s[36:39], s54 offen lds
	s_mov_b32 m0, s42
	ds_read_b128 v[186:189], v177 offset:53248
	buffer_load_dwordx4 v172, s[36:39], s54 offen lds
	ds_read_b128 v[190:193], v177 offset:54272
	ds_read_b128 v[194:197], v177 offset:55296
	ds_read_b128 v[198:201], v177 offset:56320
	s_waitcnt vmcnt(8)
	s_waitcnt lgkmcnt(0)
	s_barrier
	s_setprio 1
	v_mfma_f32_16x16x32_bf16 v[60:63], v[112:115], v[160:163], v[60:63]
	v_mfma_f32_16x16x32_bf16 v[56:59], v[136:139], v[160:163], v[56:59]
	v_mfma_f32_16x16x32_bf16 v[44:47], v[112:115], v[178:181], v[44:47]
	v_mfma_f32_16x16x32_bf16 v[40:43], v[136:139], v[178:181], v[40:43]
	v_mfma_f32_16x16x32_bf16 v[28:31], v[112:115], v[186:189], v[28:31]
	v_mfma_f32_16x16x32_bf16 v[24:27], v[136:139], v[186:189], v[24:27]
	v_mfma_f32_16x16x32_bf16 v[12:15], v[112:115], v[194:197], v[12:15]
	v_mfma_f32_16x16x32_bf16 v[8:11], v[136:139], v[194:197], v[8:11]
	v_mfma_f32_16x16x32_bf16 v[60:63], v[124:127], v[164:167], v[60:63]
	v_mfma_f32_16x16x32_bf16 v[56:59], v[140:143], v[164:167], v[56:59]
	v_mfma_f32_16x16x32_bf16 v[44:47], v[124:127], v[182:185], v[44:47]
	v_mfma_f32_16x16x32_bf16 v[40:43], v[140:143], v[182:185], v[40:43]
	v_mfma_f32_16x16x32_bf16 v[28:31], v[124:127], v[190:193], v[28:31]
	v_mfma_f32_16x16x32_bf16 v[24:27], v[140:143], v[190:193], v[24:27]
	v_mfma_f32_16x16x32_bf16 v[12:15], v[124:127], v[198:201], v[12:15]
	v_mfma_f32_16x16x32_bf16 v[8:11], v[140:143], v[198:201], v[8:11]
	v_mfma_f32_16x16x32_bf16 v[52:55], v[144:147], v[160:163], v[52:55]
	v_mfma_f32_16x16x32_bf16 v[48:51], v[152:155], v[160:163], v[48:51]
	v_mfma_f32_16x16x32_bf16 v[36:39], v[144:147], v[178:181], v[36:39]
	v_mfma_f32_16x16x32_bf16 v[32:35], v[152:155], v[178:181], v[32:35]
	v_mfma_f32_16x16x32_bf16 v[20:23], v[144:147], v[186:189], v[20:23]
	v_mfma_f32_16x16x32_bf16 v[16:19], v[152:155], v[186:189], v[16:19]
	v_mfma_f32_16x16x32_bf16 v[4:7], v[144:147], v[194:197], v[4:7]
	v_mfma_f32_16x16x32_bf16 v[0:3], v[152:155], v[194:197], v[0:3]
	v_mfma_f32_16x16x32_bf16 v[52:55], v[148:151], v[164:167], v[52:55]
	v_mfma_f32_16x16x32_bf16 v[48:51], v[156:159], v[164:167], v[48:51]
	v_mfma_f32_16x16x32_bf16 v[36:39], v[148:151], v[182:185], v[36:39]
	v_mfma_f32_16x16x32_bf16 v[32:35], v[156:159], v[182:185], v[32:35]
	v_mfma_f32_16x16x32_bf16 v[20:23], v[148:151], v[190:193], v[20:23]
	v_mfma_f32_16x16x32_bf16 v[16:19], v[156:159], v[190:193], v[16:19]
	v_mfma_f32_16x16x32_bf16 v[4:7], v[148:151], v[198:201], v[4:7]
	v_mfma_f32_16x16x32_bf16 v[0:3], v[156:159], v[198:201], v[0:3]
	s_setprio 0
	s_barrier
	s_add_i32 s67, s67, 2
	s_addk_i32 s65, 0x100
	s_addk_i32 s66, 0x100
	s_cmp_ge_i32 s67, s47
	s_cbranch_scc0 .LBB0_1701

;     __device__ __forceinline__ unsigned a_off(const Unit& u, const Gemm& g) const { return (unsigned)u.pm * (unsigned)(BM * 2) * (unsigned)g.K; }
;     __device__ __forceinline__ unsigned b_off(const Unit& u, const Gemm& g) const { return (unsigned)u.pn * (unsigned)(BM * 2) * (unsigned)g.K; }
;     __device__ __forceinline__ bool next(int i, Unit& u) const { return so.next(i, u); }
;     __device__ __forceinline__ unsigned a_off(const Unit& u, const Gemm& g) const { return (unsigned)u.pm * (unsigned)(BM * 2) * (unsigned)g.K; }
; #define PG8_WAIT_V(n) asm volatile("s_waitcnt vmcnt(" #n ")" ::: "memory")
; #define PG8_BAR __builtin_amdgcn_s_barrier()
; template <class Epi, class Sched, bool ALIGN_EPI = false, bool SP2 = false, bool FP8 = false>
; __device__ __forceinline__ void gemm_phase(LAS unsigned char* lds, const Gemm g, const Sched& S, const Epi& E, int wbase) {
;     ...
;     for (;;) {
;         const bool has_next = S.next(ui + 1, nxt);
;         const unsigned nA = has_next ? S.a_off(nxt, g) : cA, nB = has_next ? S.b_off(nxt, g) : cB;
;         const rsrc_t rAn = (Sched::TWO && has_next) ? (nxt.part ? rA1 : rA0) : rAc, rBn = (Sched::TWO && has_next) ? (nxt.part ? rB1 : rB0) : rBc;
;         float pre_[8] = {0.f, 0.f, 0.f, 0.f, 0.f, 0.f, 0.f, 0.f};
;         if constexpr (Epi::HAS_PRE) E.pre_load(pre_, cur, wr);
;         for (int t = 0; t < nt; t += 2) {
;             const bool last = (t == nt - 2);
;             const unsigned a1 = cA + (unsigned)(t + 1) * kstep;
;             const unsigned a2 = last ? nA : cA + (unsigned)(t + 2) * kstep, b2 = last ? nB : cB + (unsigned)(t + 2) * kstep; const rsrc_t rA2 = (Sched::TWO && last) ? rAn : rAc, rB2 = (Sched::TWO && last) ? rBn : rBc;
;             const unsigned a3 = a2 + kstep, b3 = b2 + kstep;
;             if (last && has_next) S.a_ready(nxt);
;             if constexpr (SP2) {
;             PG8_LDB(B0, 0, 0); PG8_LDB(B1, 0, 1); PG8_SCHED; PG8_LDA(At, 0, 0); PG8_STAGE(PG8_SA(1, 1), rAc, a1 + hstep, voffA);
;             PG8_WAIT_V(8); PG8_WAIT_L(0); PG8_BAR; PG8_MMA(0, 0, At, B0); PG8_MMA(0, 1, At, B1); PG8_BAR; PG8_SCHED;
;             PG8_LDA(At, 0, 1); PG8_STAGE(PG8_SB(0, 0), rB2, b2, voffB); PG8_STAGE(PG8_SB(0, 1), rB2, b2 + hstep, voffB); PG8_STAGE(PG8_SA(0, 0), rA2, a2, voffA);
;             PG8_WAIT_V(8); PG8_WAIT_L(0); PG8_BAR; PG8_MMA(1, 0, At, B0); PG8_MMA(1, 1, At, B1); PG8_BAR; PG8_SCHED;
.LBB0_1779:
	s_lshl_b32 s53, s52, 18
	s_andn2_b64 vcc, exec, s[14:15]
	s_lshl_b32 s56, s48, 18
	s_cbranch_vccnz .LBB0_1783
	s_and_b64 s[6:7], s[18:19], exec
	s_waitcnt vmcnt(37)
	s_waitcnt vmcnt(35)
	s_waitcnt vmcnt(31)
	s_waitcnt vmcnt(27)
	s_waitcnt vmcnt(23)
	s_waitcnt vmcnt(22)
	v_mov_b32_e32 v225, 1
	v_mov_b32_e32 v223, v233
	v_mov_b32_e32 v222, 0x358637bd
	s_cselect_b32 s59, s53, s55
	s_cselect_b32 s60, s56, s54
	s_add_i32 s61, s55, 0x80
	s_add_i32 s62, s54, 0x100
	s_mov_b32 s63, 0
	v_add_u32_e32 v140, 0x10000, v154
	v_add_u32_e32 v144, 0x14000, v154
	ds_read_b128 v[128:131], v140
	ds_read_b128 v[132:135], v140 offset:1024
	ds_read_b128 v[136:139], v140 offset:2048
	ds_read_b128 v[140:143], v140 offset:3072
	ds_read_b128 v[156:159], v144
	ds_read_b128 v[160:163], v144 offset:1024
	ds_read_b128 v[164:167], v144 offset:2048
	ds_read_b128 v[168:171], v144 offset:3072
	s_add_i32 s6, s61, 0x80
	s_cmp_eq_u32 s45, s63
	s_cselect_b32 s65, s59, s6
	s_cselect_b32 s55, s60, s62
	s_or_b32 s54, s65, 0x80
	s_add_i32 s6, s21, s61
	s_mov_b32 m0, s46
	ds_read_b128 v[172:175], v155
	ds_read_b128 v[176:179], v155 offset:1024
	ds_read_b128 v[180:183], v155 offset:2048
	ds_read_b128 v[184:187], v155 offset:3072
	ds_read_b128 v[194:197], v155 offset:4096
	ds_read_b128 v[198:201], v155 offset:5120
	ds_read_b128 v[202:205], v155 offset:6144
	ds_read_b128 v[206:209], v155 offset:7168
	buffer_load_dwordx4 v148, s[36:39], s6 offen lds
	s_mov_b32 m0, s47
	s_nop 0
	buffer_load_dwordx4 v150, s[36:39], s6 offen lds
	s_waitcnt vmcnt(8)
	s_waitcnt lgkmcnt(0)
	s_barrier
	s_setprio 1
	v_mfma_f32_16x16x128_f8f6f4 v[120:123], v[128:135], v[172:179], 0
	v_mfma_f32_16x16x128_f8f6f4 v[124:127], v[136:143], v[172:179], 0
	v_mfma_f32_16x16x128_f8f6f4 v[104:107], v[128:135], v[180:187], 0
	v_mfma_f32_16x16x128_f8f6f4 v[108:111], v[136:143], v[180:187], 0
	v_mfma_f32_16x16x128_f8f6f4 v[144:147], v[128:135], v[194:201], 0
	v_mfma_f32_16x16x128_f8f6f4 v[188:191], v[136:143], v[194:201], 0
	v_mfma_f32_16x16x128_f8f6f4 v[210:213], v[128:135], v[202:209], 0
	v_mfma_f32_16x16x128_f8f6f4 v[214:217], v[136:143], v[202:209], 0
	v_mfma_f32_16x16x128_f8f6f4 v[112:115], v[156:163], v[172:179], 0
	v_mfma_f32_16x16x128_f8f6f4 v[116:119], v[164:171], v[172:179], 0
	v_mfma_f32_16x16x128_f8f6f4 v[96:99], v[156:163], v[180:187], 0
	v_mfma_f32_16x16x128_f8f6f4 v[100:103], v[164:171], v[180:187], 0
	v_mfma_f32_16x16x128_f8f6f4 v[172:175], v[156:163], v[194:201], 0
	v_mfma_f32_16x16x128_f8f6f4 v[176:179], v[164:171], v[194:201], 0
	v_mfma_f32_16x16x128_f8f6f4 v[180:183], v[156:163], v[202:209], 0
	v_mfma_f32_16x16x128_f8f6f4 v[184:187], v[164:171], v[202:209], 0
	s_setprio 0
	s_barrier
	s_mov_b32 m0, s23
	s_mov_b32 s6, s38
	s_mov_b32 s7, s39
	s_nop 0
	buffer_load_dwordx4 v149, s[4:7], s55 offen lds
	s_mov_b32 m0, s24
	ds_read_b128 v[64:67], v155 offset:16384
	s_add_i32 s66, s55, s21
	buffer_load_dwordx4 v151, s[4:7], s55 offen lds
	s_mov_b32 m0, s22
	ds_read_b128 v[68:71], v155 offset:17408
	buffer_load_dwordx4 v148, s[36:39], s65 offen lds
	s_mov_b32 m0, s27
	ds_read_b128 v[72:75], v155 offset:18432
	buffer_load_dwordx4 v150, s[36:39], s65 offen lds
	ds_read_b128 v[76:79], v155 offset:19456
	ds_read_b128 v[80:83], v155 offset:20480
	ds_read_b128 v[84:87], v155 offset:21504
	ds_read_b128 v[88:91], v155 offset:22528
	ds_read_b128 v[92:95], v155 offset:23552
	s_waitcnt vmcnt(6)
	s_waitcnt lgkmcnt(0)
	s_barrier
	s_setprio 1
	v_mfma_f32_16x16x128_f8f6f4 v[56:59], v[128:135], v[64:71], 0
	v_mfma_f32_16x16x128_f8f6f4 v[60:63], v[136:143], v[64:71], 0
	v_mfma_f32_16x16x128_f8f6f4 v[8:11], v[128:135], v[88:95], 0
	v_mfma_f32_16x16x128_f8f6f4 v[192:195], v[128:135], v[72:79], 0
	v_mfma_f32_16x16x128_f8f6f4 v[196:199], v[136:143], v[72:79], 0
	v_mfma_f32_16x16x128_f8f6f4 v[200:203], v[128:135], v[80:87], 0
	v_mfma_f32_16x16x128_f8f6f4 v[204:207], v[136:143], v[80:87], 0
	v_mfma_f32_16x16x128_f8f6f4 v[218:221], v[136:143], v[88:95], 0
	v_mfma_f32_16x16x128_f8f6f4 v[52:55], v[164:171], v[64:71], 0
	v_mfma_f32_16x16x128_f8f6f4 v[226:229], v[156:163], v[64:71], 0
	v_mfma_f32_16x16x128_f8f6f4 v[230:233], v[156:163], v[72:79], 0
	v_mfma_f32_16x16x128_f8f6f4 v[234:237], v[164:171], v[72:79], 0
	v_mfma_f32_16x16x128_f8f6f4 v[238:241], v[156:163], v[80:87], 0
	v_mfma_f32_16x16x128_f8f6f4 v[242:245], v[164:171], v[80:87], 0
	v_mfma_f32_16x16x128_f8f6f4 v[246:249], v[156:163], v[88:95], 0
	v_mfma_f32_16x16x128_f8f6f4 v[250:253], v[164:171], v[88:95], 0
	s_setprio 0
	s_barrier
	s_mov_b32 m0, s25
	s_nop 0
	buffer_load_dwordx4 v149, s[4:7], s66 offen lds
	s_mov_b32 m0, s26
	s_nop 0
	buffer_load_dwordx4 v151, s[4:7], s66 offen lds
	s_nop 1
	v_add_u32_e32 v16, 0x18000, v154
	v_add_u32_e32 v20, 0x1c000, v154
	s_nop 0
	ds_read_b128 v[0:3], v16
	ds_read_b128 v[4:7], v16 offset:1024
	ds_read_b128 v[12:15], v16 offset:2048
	ds_read_b128 v[16:19], v16 offset:3072
	ds_read_b128 v[128:131], v20
	ds_read_b128 v[132:135], v20 offset:1024
	ds_read_b128 v[136:139], v20 offset:2048
	ds_read_b128 v[140:143], v20 offset:3072
	s_add_i32 s65, s65, s21
	s_mov_b32 m0, s28
	ds_read_b128 v[20:23], v155 offset:32768
	ds_read_b128 v[24:27], v155 offset:33792
	ds_read_b128 v[28:31], v155 offset:34816
	ds_read_b128 v[32:35], v155 offset:35840
	ds_read_b128 v[36:39], v155 offset:36864
	ds_read_b128 v[40:43], v155 offset:37888
	ds_read_b128 v[44:47], v155 offset:38912
	ds_read_b128 v[48:51], v155 offset:39936
	buffer_load_dwordx4 v148, s[36:39], s65 offen lds
	s_mov_b32 m0, s29
	s_nop 0
	buffer_load_dwordx4 v150, s[36:39], s65 offen lds
	s_waitcnt vmcnt(8)
	s_waitcnt lgkmcnt(0)
	s_barrier
; #define PG8_STAGE(bufoff, rs_, soff_, voff) do { _Pragma("unroll") for (int _i = 0; _i < 2; ++_i) \
;         __builtin_amdgcn_raw_ptr_buffer_load_lds(rs_, (LAS void*)(lds + (bufoff) + ldsw + _i * 8192), 16, (int)(voff)[_i], (int)(soff_), 0, 0); } while (0)
; #define PG8_LDA(dst, b, h) do { _Pragma("unroll") for (int m = 0; m < 4; ++m) dst[m] = PG8_LD2(lds + PG8_SA(b, h) + aoff + m * 2048); } while (0)
; #define PG8_LDB(dst, b, h) do { _Pragma("unroll") for (int n = 0; n < 2; ++n) dst[n] = PG8_LD2(lds + PG8_SB(b, h) + boff + n * 2048); } while (0)
; #define PG8_WAIT_V(n) asm volatile("s_waitcnt vmcnt(" #n ")" ::: "memory")
; #define PG8_WAIT_L(n) asm volatile("s_waitcnt lgkmcnt(" #n ")" ::: "memory")
; #define PG8_BAR __builtin_amdgcn_s_barrier()
; #define PG8_SCHED __builtin_amdgcn_sched_barrier(0)
; template <class Epi, class Sched, bool ALIGN_EPI = false, bool SP2 = false, bool FP8 = false>
; __device__ __forceinline__ void gemm_phase(LAS unsigned char* lds, const Gemm g, const Sched& S, const Epi& E, int wbase) {
;     ...
;         for (int t = 0; t < nt; t += 2) {
;             const bool last = (t == nt - 2);
;             const unsigned a1 = cA + (unsigned)(t + 1) * kstep;
;             const unsigned a2 = last ? nA : cA + (unsigned)(t + 2) * kstep, b2 = last ? nB : cB + (unsigned)(t + 2) * kstep; const rsrc_t rA2 = (Sched::TWO && last) ? rAn : rAc, rB2 = (Sched::TWO && last) ? rBn : rBc;
;             const unsigned a3 = a2 + kstep, b3 = b2 + kstep;
;             if (last && has_next) S.a_ready(nxt);
;             if constexpr (SP2) {
;             PG8_LDB(B0, 0, 0); PG8_LDB(B1, 0, 1); PG8_SCHED; PG8_LDA(At, 0, 0); PG8_STAGE(PG8_SA(1, 1), rAc, a1 + hstep, voffA);
;             PG8_WAIT_V(8); PG8_WAIT_L(0); PG8_BAR; PG8_MMA(0, 0, At, B0); PG8_MMA(0, 1, At, B1); PG8_BAR; PG8_SCHED;
;     ...
;             PG8_LDB(B0, 1, 0); PG8_LDB(B1, 1, 1); PG8_SCHED; PG8_LDA(At, 1, 0); PG8_STAGE(PG8_SA(0, 1), rA2, a2 + hstep, voffA);
;             PG8_WAIT_V(8); PG8_WAIT_L(0); PG8_BAR; PG8_MMA(0, 0, At, B0); PG8_MMA(0, 1, At, B1); PG8_BAR; PG8_SCHED;
;             PG8_LDA(At, 1, 1); PG8_STAGE(PG8_SB(1, 0), rB2, b3, voffB); PG8_STAGE(PG8_SB(1, 1), rB2, b3 + hstep, voffB); PG8_STAGE(PG8_SA(1, 0), rA2, a3, voffA);
;             PG8_WAIT_V(8); PG8_WAIT_L(0); PG8_BAR; PG8_MMA(1, 0, At, B0); PG8_MMA(1, 1, At, B1); PG8_BAR; PG8_SCHED;
	s_setprio 1
	v_mfma_f32_16x16x128_f8f6f4 v[120:123], v[0:7], v[20:27], v[120:123]
	v_mfma_f32_16x16x128_f8f6f4 v[124:127], v[12:19], v[20:27], v[124:127]
	v_mfma_f32_16x16x128_f8f6f4 v[104:107], v[0:7], v[28:35], v[104:107]
	v_mfma_f32_16x16x128_f8f6f4 v[108:111], v[12:19], v[28:35], v[108:111]
	v_mfma_f32_16x16x128_f8f6f4 v[88:91], v[0:7], v[36:43], v[144:147]
	v_mfma_f32_16x16x128_f8f6f4 v[92:95], v[12:19], v[36:43], v[188:191]
	v_mfma_f32_16x16x128_f8f6f4 v[72:75], v[0:7], v[44:51], v[210:213]
	v_mfma_f32_16x16x128_f8f6f4 v[76:79], v[12:19], v[44:51], v[214:217]
	v_mfma_f32_16x16x128_f8f6f4 v[112:115], v[128:135], v[20:27], v[112:115]
	v_mfma_f32_16x16x128_f8f6f4 v[116:119], v[136:143], v[20:27], v[116:119]
	v_mfma_f32_16x16x128_f8f6f4 v[96:99], v[128:135], v[28:35], v[96:99]
	v_mfma_f32_16x16x128_f8f6f4 v[100:103], v[136:143], v[28:35], v[100:103]
	v_mfma_f32_16x16x128_f8f6f4 v[80:83], v[128:135], v[36:43], v[172:175]
	v_mfma_f32_16x16x128_f8f6f4 v[84:87], v[136:143], v[36:43], v[176:179]
	v_mfma_f32_16x16x128_f8f6f4 v[64:67], v[128:135], v[44:51], v[180:183]
	v_mfma_f32_16x16x128_f8f6f4 v[68:71], v[136:143], v[44:51], v[184:187]
	s_setprio 0
	s_barrier
	s_mov_b32 m0, s30
	s_bitset1_b32 s55, 7
	buffer_load_dwordx4 v149, s[4:7], s55 offen lds
	s_mov_b32 m0, s31
	ds_read_b128 v[32:35], v155 offset:49152
	buffer_load_dwordx4 v151, s[4:7], s55 offen lds
	s_add_i32 s55, s55, s21
	s_mov_b32 m0, s35
	ds_read_b128 v[36:39], v155 offset:50176
	buffer_load_dwordx4 v149, s[4:7], s55 offen lds
	s_mov_b32 m0, s41
	ds_read_b128 v[156:159], v155 offset:51200
	buffer_load_dwordx4 v151, s[4:7], s55 offen lds
	s_mov_b32 m0, s33
	ds_read_b128 v[160:163], v155 offset:52224
	buffer_load_dwordx4 v148, s[36:39], s54 offen lds
	s_mov_b32 m0, s34
	ds_read_b128 v[164:167], v155 offset:53248
	buffer_load_dwordx4 v150, s[36:39], s54 offen lds
	ds_read_b128 v[168:171], v155 offset:54272
	ds_read_b128 v[172:175], v155 offset:55296
	ds_read_b128 v[176:179], v155 offset:56320
	s_waitcnt vmcnt(8)
	s_waitcnt lgkmcnt(0)
	s_barrier
	s_setprio 1
	v_mfma_f32_16x16x128_f8f6f4 v[56:59], v[0:7], v[32:39], v[56:59]
	v_mfma_f32_16x16x128_f8f6f4 v[60:63], v[12:19], v[32:39], v[60:63]
	v_mfma_f32_16x16x128_f8f6f4 v[40:43], v[0:7], v[156:163], v[192:195]
	v_mfma_f32_16x16x128_f8f6f4 v[44:47], v[12:19], v[156:163], v[196:199]
	v_mfma_f32_16x16x128_f8f6f4 v[24:27], v[0:7], v[164:171], v[200:203]
	v_mfma_f32_16x16x128_f8f6f4 v[28:31], v[12:19], v[164:171], v[204:207]
	v_mfma_f32_16x16x128_f8f6f4 v[8:11], v[0:7], v[172:179], v[8:11]
	v_mfma_f32_16x16x128_f8f6f4 v[12:15], v[12:19], v[172:179], v[218:221]
	v_mfma_f32_16x16x128_f8f6f4 v[48:51], v[128:135], v[32:39], v[226:229]
	v_mfma_f32_16x16x128_f8f6f4 v[52:55], v[136:143], v[32:39], v[52:55]
	v_mfma_f32_16x16x128_f8f6f4 v[32:35], v[128:135], v[156:163], v[230:233]
	v_mfma_f32_16x16x128_f8f6f4 v[36:39], v[136:143], v[156:163], v[234:237]
	v_mfma_f32_16x16x128_f8f6f4 v[16:19], v[128:135], v[164:171], v[238:241]
	v_mfma_f32_16x16x128_f8f6f4 v[20:23], v[136:143], v[164:171], v[242:245]
	v_mfma_f32_16x16x128_f8f6f4 v[4:7], v[128:135], v[172:179], v[246:249]
	v_mfma_f32_16x16x128_f8f6f4 v[0:3], v[136:143], v[172:179], v[250:253]
	s_setprio 0
	s_barrier
	s_add_i32 s63, s63, 2
	s_addk_i32 s61, 0x100
	s_addk_i32 s62, 0x100
	s_cmp_ge_i32 s63, s43
	s_cbranch_scc0 .LBB0_1781
	s_branch .Lzp_after_1781
.LBB0_1781:
	v_add_u32_e32 v140, 0x10000, v154
	v_add_u32_e32 v144, 0x14000, v154
	ds_read_b128 v[128:131], v140
	ds_read_b128 v[132:135], v140 offset:1024
	ds_read_b128 v[136:139], v140 offset:2048
	ds_read_b128 v[140:143], v140 offset:3072
	ds_read_b128 v[156:159], v144
	ds_read_b128 v[160:163], v144 offset:1024
	ds_read_b128 v[164:167], v144 offset:2048
	ds_read_b128 v[168:171], v144 offset:3072
	s_add_i32 s6, s61, 0x80
	s_cmp_eq_u32 s45, s63
	s_cselect_b32 s65, s59, s6
	s_cselect_b32 s55, s60, s62
	s_or_b32 s54, s65, 0x80
	s_add_i32 s6, s21, s61
	s_mov_b32 m0, s46
	ds_read_b128 v[172:175], v155
	ds_read_b128 v[176:179], v155 offset:1024
	ds_read_b128 v[180:183], v155 offset:2048
	ds_read_b128 v[184:187], v155 offset:3072
	ds_read_b128 v[194:197], v155 offset:4096
	ds_read_b128 v[198:201], v155 offset:5120
	ds_read_b128 v[202:205], v155 offset:6144
	ds_read_b128 v[206:209], v155 offset:7168
	buffer_load_dwordx4 v148, s[36:39], s6 offen lds
	s_mov_b32 m0, s47
	s_nop 0
	buffer_load_dwordx4 v150, s[36:39], s6 offen lds
	s_waitcnt vmcnt(8)
	s_waitcnt lgkmcnt(0)
	s_barrier
	s_setprio 1
	v_mfma_f32_16x16x128_f8f6f4 v[120:123], v[128:135], v[172:179], v[120:123]
	v_mfma_f32_16x16x128_f8f6f4 v[124:127], v[136:143], v[172:179], v[124:127]
	v_mfma_f32_16x16x128_f8f6f4 v[104:107], v[128:135], v[180:187], v[104:107]
	v_mfma_f32_16x16x128_f8f6f4 v[108:111], v[136:143], v[180:187], v[108:111]
	v_mfma_f32_16x16x128_f8f6f4 v[144:147], v[128:135], v[194:201], v[88:91]
	v_mfma_f32_16x16x128_f8f6f4 v[188:191], v[136:143], v[194:201], v[92:95]
	v_mfma_f32_16x16x128_f8f6f4 v[210:213], v[128:135], v[202:209], v[72:75]
	v_mfma_f32_16x16x128_f8f6f4 v[214:217], v[136:143], v[202:209], v[76:79]
	v_mfma_f32_16x16x128_f8f6f4 v[112:115], v[156:163], v[172:179], v[112:115]
	v_mfma_f32_16x16x128_f8f6f4 v[116:119], v[164:171], v[172:179], v[116:119]
	v_mfma_f32_16x16x128_f8f6f4 v[96:99], v[156:163], v[180:187], v[96:99]
	v_mfma_f32_16x16x128_f8f6f4 v[100:103], v[164:171], v[180:187], v[100:103]
	v_mfma_f32_16x16x128_f8f6f4 v[172:175], v[156:163], v[194:201], v[80:83]
	v_mfma_f32_16x16x128_f8f6f4 v[176:179], v[164:171], v[194:201], v[84:87]
	v_mfma_f32_16x16x128_f8f6f4 v[180:183], v[156:163], v[202:209], v[64:67]
	v_mfma_f32_16x16x128_f8f6f4 v[184:187], v[164:171], v[202:209], v[68:71]
	s_setprio 0
	s_barrier
; #define PG8_STAGE(bufoff, rs_, soff_, voff) do { _Pragma("unroll") for (int _i = 0; _i < 2; ++_i) \
;         __builtin_amdgcn_raw_ptr_buffer_load_lds(rs_, (LAS void*)(lds + (bufoff) + ldsw + _i * 8192), 16, (int)(voff)[_i], (int)(soff_), 0, 0); } while (0)
; #define PG8_LDA(dst, b, h) do { _Pragma("unroll") for (int m = 0; m < 4; ++m) dst[m] = PG8_LD2(lds + PG8_SA(b, h) + aoff + m * 2048); } while (0)
; #define PG8_LDB(dst, b, h) do { _Pragma("unroll") for (int n = 0; n < 2; ++n) dst[n] = PG8_LD2(lds + PG8_SB(b, h) + boff + n * 2048); } while (0)
; #define PG8_WAIT_V(n) asm volatile("s_waitcnt vmcnt(" #n ")" ::: "memory")
; #define PG8_WAIT_L(n) asm volatile("s_waitcnt lgkmcnt(" #n ")" ::: "memory")
; #define PG8_BAR __builtin_amdgcn_s_barrier()
; #define PG8_SCHED __builtin_amdgcn_sched_barrier(0)
; template <class Epi, class Sched, bool ALIGN_EPI = false, bool SP2 = false, bool FP8 = false>
; __device__ __forceinline__ void gemm_phase(LAS unsigned char* lds, const Gemm g, const Sched& S, const Epi& E, int wbase) {
;     ...
;             PG8_WAIT_V(8); PG8_WAIT_L(0); PG8_BAR; PG8_MMA(0, 0, At, B0); PG8_MMA(0, 1, At, B1); PG8_BAR; PG8_SCHED;
;             PG8_LDA(At, 0, 1); PG8_STAGE(PG8_SB(0, 0), rB2, b2, voffB); PG8_STAGE(PG8_SB(0, 1), rB2, b2 + hstep, voffB); PG8_STAGE(PG8_SA(0, 0), rA2, a2, voffA);
;             PG8_WAIT_V(8); PG8_WAIT_L(0); PG8_BAR; PG8_MMA(1, 0, At, B0); PG8_MMA(1, 1, At, B1); PG8_BAR; PG8_SCHED;
;             PG8_LDB(B0, 1, 0); PG8_LDB(B1, 1, 1); PG8_SCHED; PG8_LDA(At, 1, 0); PG8_STAGE(PG8_SA(0, 1), rA2, a2 + hstep, voffA);
;             PG8_WAIT_V(8); PG8_WAIT_L(0); PG8_BAR; PG8_MMA(0, 0, At, B0); PG8_MMA(0, 1, At, B1); PG8_BAR; PG8_SCHED;
;             PG8_LDA(At, 1, 1); PG8_STAGE(PG8_SB(1, 0), rB2, b3, voffB); PG8_STAGE(PG8_SB(1, 1), rB2, b3 + hstep, voffB); PG8_STAGE(PG8_SA(1, 0), rA2, a3, voffA);
;             PG8_WAIT_V(8); PG8_WAIT_L(0); PG8_BAR; PG8_MMA(1, 0, At, B0); PG8_MMA(1, 1, At, B1); PG8_BAR; PG8_SCHED;
	s_mov_b32 m0, s23
	s_mov_b32 s6, s38
	s_mov_b32 s7, s39
	s_nop 0
	buffer_load_dwordx4 v149, s[4:7], s55 offen lds
	s_mov_b32 m0, s24
	ds_read_b128 v[64:67], v155 offset:16384
	s_add_i32 s66, s55, s21
	buffer_load_dwordx4 v151, s[4:7], s55 offen lds
	s_mov_b32 m0, s22
	ds_read_b128 v[68:71], v155 offset:17408
	buffer_load_dwordx4 v148, s[36:39], s65 offen lds
	s_mov_b32 m0, s27
	ds_read_b128 v[72:75], v155 offset:18432
	buffer_load_dwordx4 v150, s[36:39], s65 offen lds
	ds_read_b128 v[76:79], v155 offset:19456
	ds_read_b128 v[80:83], v155 offset:20480
	ds_read_b128 v[84:87], v155 offset:21504
	ds_read_b128 v[88:91], v155 offset:22528
	ds_read_b128 v[92:95], v155 offset:23552
	s_waitcnt vmcnt(6)
	s_waitcnt lgkmcnt(0)
	s_barrier
	s_setprio 1
	v_mfma_f32_16x16x128_f8f6f4 v[56:59], v[128:135], v[64:71], v[56:59]
	v_mfma_f32_16x16x128_f8f6f4 v[60:63], v[136:143], v[64:71], v[60:63]
	v_mfma_f32_16x16x128_f8f6f4 v[8:11], v[128:135], v[88:95], v[8:11]
	v_mfma_f32_16x16x128_f8f6f4 v[192:195], v[128:135], v[72:79], v[40:43]
	v_mfma_f32_16x16x128_f8f6f4 v[196:199], v[136:143], v[72:79], v[44:47]
	v_mfma_f32_16x16x128_f8f6f4 v[200:203], v[128:135], v[80:87], v[24:27]
	v_mfma_f32_16x16x128_f8f6f4 v[204:207], v[136:143], v[80:87], v[28:31]
	v_mfma_f32_16x16x128_f8f6f4 v[218:221], v[136:143], v[88:95], v[12:15]
	v_mfma_f32_16x16x128_f8f6f4 v[52:55], v[164:171], v[64:71], v[52:55]
	v_mfma_f32_16x16x128_f8f6f4 v[226:229], v[156:163], v[64:71], v[48:51]
	v_mfma_f32_16x16x128_f8f6f4 v[230:233], v[156:163], v[72:79], v[32:35]
	v_mfma_f32_16x16x128_f8f6f4 v[234:237], v[164:171], v[72:79], v[36:39]
	v_mfma_f32_16x16x128_f8f6f4 v[238:241], v[156:163], v[80:87], v[16:19]
	v_mfma_f32_16x16x128_f8f6f4 v[242:245], v[164:171], v[80:87], v[20:23]
	v_mfma_f32_16x16x128_f8f6f4 v[246:249], v[156:163], v[88:95], v[4:7]
	v_mfma_f32_16x16x128_f8f6f4 v[250:253], v[164:171], v[88:95], v[0:3]
	s_setprio 0
	s_barrier
	s_mov_b32 m0, s25
	s_nop 0
	buffer_load_dwordx4 v149, s[4:7], s66 offen lds
	s_mov_b32 m0, s26
	s_nop 0
	buffer_load_dwordx4 v151, s[4:7], s66 offen lds
	s_nop 1
	v_add_u32_e32 v16, 0x18000, v154
	v_add_u32_e32 v20, 0x1c000, v154
	s_nop 0
	ds_read_b128 v[0:3], v16
	ds_read_b128 v[4:7], v16 offset:1024
	ds_read_b128 v[12:15], v16 offset:2048
	ds_read_b128 v[16:19], v16 offset:3072
	ds_read_b128 v[128:131], v20
	ds_read_b128 v[132:135], v20 offset:1024
	ds_read_b128 v[136:139], v20 offset:2048
	ds_read_b128 v[140:143], v20 offset:3072
	s_add_i32 s65, s65, s21
	s_mov_b32 m0, s28
	ds_read_b128 v[20:23], v155 offset:32768
	ds_read_b128 v[24:27], v155 offset:33792
	ds_read_b128 v[28:31], v155 offset:34816
	ds_read_b128 v[32:35], v155 offset:35840
	ds_read_b128 v[36:39], v155 offset:36864
	ds_read_b128 v[40:43], v155 offset:37888
	ds_read_b128 v[44:47], v155 offset:38912
	ds_read_b128 v[48:51], v155 offset:39936
	buffer_load_dwordx4 v148, s[36:39], s65 offen lds
	s_mov_b32 m0, s29
	s_nop 0
	buffer_load_dwordx4 v150, s[36:39], s65 offen lds
	s_waitcnt vmcnt(8)
	s_waitcnt lgkmcnt(0)
	s_barrier
	s_setprio 1
	v_mfma_f32_16x16x128_f8f6f4 v[120:123], v[0:7], v[20:27], v[120:123]
	v_mfma_f32_16x16x128_f8f6f4 v[124:127], v[12:19], v[20:27], v[124:127]
	v_mfma_f32_16x16x128_f8f6f4 v[104:107], v[0:7], v[28:35], v[104:107]
	v_mfma_f32_16x16x128_f8f6f4 v[108:111], v[12:19], v[28:35], v[108:111]
	v_mfma_f32_16x16x128_f8f6f4 v[88:91], v[0:7], v[36:43], v[144:147]
	v_mfma_f32_16x16x128_f8f6f4 v[92:95], v[12:19], v[36:43], v[188:191]
	v_mfma_f32_16x16x128_f8f6f4 v[72:75], v[0:7], v[44:51], v[210:213]
	v_mfma_f32_16x16x128_f8f6f4 v[76:79], v[12:19], v[44:51], v[214:217]
	v_mfma_f32_16x16x128_f8f6f4 v[112:115], v[128:135], v[20:27], v[112:115]
	v_mfma_f32_16x16x128_f8f6f4 v[116:119], v[136:143], v[20:27], v[116:119]
	v_mfma_f32_16x16x128_f8f6f4 v[96:99], v[128:135], v[28:35], v[96:99]
	v_mfma_f32_16x16x128_f8f6f4 v[100:103], v[136:143], v[28:35], v[100:103]
	v_mfma_f32_16x16x128_f8f6f4 v[80:83], v[128:135], v[36:43], v[172:175]
	v_mfma_f32_16x16x128_f8f6f4 v[84:87], v[136:143], v[36:43], v[176:179]
	v_mfma_f32_16x16x128_f8f6f4 v[64:67], v[128:135], v[44:51], v[180:183]
	v_mfma_f32_16x16x128_f8f6f4 v[68:71], v[136:143], v[44:51], v[184:187]
	s_setprio 0
	s_barrier
	s_mov_b32 m0, s30
	s_bitset1_b32 s55, 7
	buffer_load_dwordx4 v149, s[4:7], s55 offen lds
	s_mov_b32 m0, s31
	ds_read_b128 v[32:35], v155 offset:49152
	buffer_load_dwordx4 v151, s[4:7], s55 offen lds
	s_add_i32 s55, s55, s21
	s_mov_b32 m0, s35
	ds_read_b128 v[36:39], v155 offset:50176
	buffer_load_dwordx4 v149, s[4:7], s55 offen lds
	s_mov_b32 m0, s41
	ds_read_b128 v[156:159], v155 offset:51200
	buffer_load_dwordx4 v151, s[4:7], s55 offen lds
	s_mov_b32 m0, s33
	ds_read_b128 v[160:163], v155 offset:52224
	buffer_load_dwordx4 v148, s[36:39], s54 offen lds
	s_mov_b32 m0, s34
	ds_read_b128 v[164:167], v155 offset:53248
	buffer_load_dwordx4 v150, s[36:39], s54 offen lds
	ds_read_b128 v[168:171], v155 offset:54272
	ds_read_b128 v[172:175], v155 offset:55296
	ds_read_b128 v[176:179], v155 offset:56320
	s_waitcnt vmcnt(8)
	s_waitcnt lgkmcnt(0)
	s_barrier
	s_setprio 1
	v_mfma_f32_16x16x128_f8f6f4 v[56:59], v[0:7], v[32:39], v[56:59]
	v_mfma_f32_16x16x128_f8f6f4 v[60:63], v[12:19], v[32:39], v[60:63]
	v_mfma_f32_16x16x128_f8f6f4 v[40:43], v[0:7], v[156:163], v[192:195]
	v_mfma_f32_16x16x128_f8f6f4 v[44:47], v[12:19], v[156:163], v[196:199]
	v_mfma_f32_16x16x128_f8f6f4 v[24:27], v[0:7], v[164:171], v[200:203]
	v_mfma_f32_16x16x128_f8f6f4 v[28:31], v[12:19], v[164:171], v[204:207]
	v_mfma_f32_16x16x128_f8f6f4 v[8:11], v[0:7], v[172:179], v[8:11]
	v_mfma_f32_16x16x128_f8f6f4 v[12:15], v[12:19], v[172:179], v[218:221]
	v_mfma_f32_16x16x128_f8f6f4 v[48:51], v[128:135], v[32:39], v[226:229]
	v_mfma_f32_16x16x128_f8f6f4 v[52:55], v[136:143], v[32:39], v[52:55]
	v_mfma_f32_16x16x128_f8f6f4 v[32:35], v[128:135], v[156:163], v[230:233]
	v_mfma_f32_16x16x128_f8f6f4 v[36:39], v[136:143], v[156:163], v[234:237]
	v_mfma_f32_16x16x128_f8f6f4 v[16:19], v[128:135], v[164:171], v[238:241]
	v_mfma_f32_16x16x128_f8f6f4 v[20:23], v[136:143], v[164:171], v[242:245]
	v_mfma_f32_16x16x128_f8f6f4 v[4:7], v[128:135], v[172:179], v[246:249]
	v_mfma_f32_16x16x128_f8f6f4 v[0:3], v[136:143], v[172:179], v[250:253]
	s_setprio 0
	s_barrier
	s_add_i32 s63, s63, 2
	s_addk_i32 s61, 0x100
	s_addk_i32 s62, 0x100
	s_cmp_ge_i32 s63, s43
	s_cbranch_scc0 .LBB0_1781

;     __device__ __forceinline__ bool next(int i, Unit& u) const { return so.next(i, u); }
; template <class Epi, class Sched, bool ALIGN_EPI = false, bool SP2 = false, bool FP8 = false>
; __device__ __forceinline__ void gemm_phase(LAS unsigned char* lds, const Gemm g, const Sched& S, const Epi& E, int wbase) {
;     ...
;     for (;;) {
;         const bool has_next = S.next(ui + 1, nxt);
;         const unsigned nA = has_next ? S.a_off(nxt, g) : cA, nB = has_next ? S.b_off(nxt, g) : cB;
;         const rsrc_t rAn = (Sched::TWO && has_next) ? (nxt.part ? rA1 : rA0) : rAc, rBn = (Sched::TWO && has_next) ? (nxt.part ? rB1 : rB0) : rBc;
;         float pre_[8] = {0.f, 0.f, 0.f, 0.f, 0.f, 0.f, 0.f, 0.f};
;         if constexpr (Epi::HAS_PRE) E.pre_load(pre_, cur, wr);
;         for (int t = 0; t < nt; t += 2) {
;             const bool last = (t == nt - 2);
;             const unsigned a1 = cA + (unsigned)(t + 1) * kstep;
;             const unsigned a2 = last ? nA : cA + (unsigned)(t + 2) * kstep, b2 = last ? nB : cB + (unsigned)(t + 2) * kstep; const rsrc_t rA2 = (Sched::TWO && last) ? rAn : rAc, rB2 = (Sched::TWO && last) ? rBn : rBc;
;             const unsigned a3 = a2 + kstep, b3 = b2 + kstep;
;             if (last && has_next) S.a_ready(nxt);
;             if constexpr (SP2) {
;             PG8_LDB(B0, 0, 0); PG8_LDB(B1, 0, 1); PG8_SCHED; PG8_LDA(At, 0, 0); PG8_STAGE(PG8_SA(1, 1), rAc, a1 + hstep, voffA);
;             PG8_WAIT_V(8); PG8_WAIT_L(0); PG8_BAR; PG8_MMA(0, 0, At, B0); PG8_MMA(0, 1, At, B1); PG8_BAR; PG8_SCHED;
;             PG8_LDA(At, 0, 1); PG8_STAGE(PG8_SB(0, 0), rB2, b2, voffB); PG8_STAGE(PG8_SB(0, 1), rB2, b2 + hstep, voffB); PG8_STAGE(PG8_SA(0, 0), rA2, a2, voffA);
;             PG8_WAIT_V(8); PG8_WAIT_L(0); PG8_BAR; PG8_MMA(1, 0, At, B0); PG8_MMA(1, 1, At, B1); PG8_BAR; PG8_SCHED;
;             PG8_LDB(B0, 1, 0); PG8_LDB(B1, 1, 1); PG8_SCHED; PG8_LDA(At, 1, 0); PG8_STAGE(PG8_SA(0, 1), rA2, a2 + hstep, voffA);
;             PG8_WAIT_V(8); PG8_WAIT_L(0); PG8_BAR; PG8_MMA(0, 0, At, B0); PG8_MMA(0, 1, At, B1); PG8_BAR; PG8_SCHED;
;             PG8_LDA(At, 1, 1); PG8_STAGE(PG8_SB(1, 0), rB2, b3, voffB); PG8_STAGE(PG8_SB(1, 1), rB2, b3 + hstep, voffB); PG8_STAGE(PG8_SA(1, 0), rA2, a3, voffA);
;             PG8_WAIT_V(8); PG8_WAIT_L(0); PG8_BAR; PG8_MMA(1, 0, At, B0); PG8_MMA(1, 1, At, B1); PG8_BAR; PG8_SCHED;
.LBB0_1852:
	s_mul_i32 s61, s60, 0xe0000
	s_andn2_b64 vcc, exec, s[14:15]
	s_mul_i32 s62, s59, 0xe0000
	s_cbranch_vccnz .LBB0_1856
	s_and_b64 s[6:7], s[18:19], exec
	s_waitcnt vmcnt(37)
	s_waitcnt vmcnt(36)
	s_waitcnt vmcnt(35)
	s_waitcnt vmcnt(32)
	s_waitcnt vmcnt(31)
	s_waitcnt vmcnt(28)
	s_waitcnt vmcnt(27)
	s_waitcnt vmcnt(24)
	s_waitcnt vmcnt(23)
	s_waitcnt vmcnt(22)
	v_mov_b32_e32 v223, 0xff61b1e6
	v_mov_b32_e32 v222, 1
	v_mov_b32_e32 v169, v233
	v_mov_b32_e32 v168, 0x358637bd
	s_cselect_b32 s21, s61, s55
	s_cselect_b32 s63, s62, s54
	s_add_i32 s65, s55, 0x80
	s_add_i32 s66, s54, 0x100
	s_mov_b32 s67, 0
	v_add_u32_e32 v140, 0x10000, v176
	v_add_u32_e32 v156, 0x14000, v176
	ds_read_b128 v[128:131], v140
	ds_read_b128 v[132:135], v140 offset:1024
	ds_read_b128 v[136:139], v140 offset:2048
	ds_read_b128 v[140:143], v140 offset:3072
	ds_read_b128 v[144:147], v156
	ds_read_b128 v[148:151], v156 offset:1024
	ds_read_b128 v[152:155], v156 offset:2048
	ds_read_b128 v[156:159], v156 offset:3072
	s_add_i32 s6, s65, 0x80
	s_cmp_eq_u32 s52, s67
	s_cselect_b32 s68, s21, s6
	s_cselect_b32 s55, s63, s66
	s_or_b32 s54, s68, 0x80
	s_add_i32 s6, s24, s65
	s_mov_b32 m0, s53
	ds_read_b128 v[160:163], v177
	ds_read_b128 v[164:167], v177 offset:1024
	ds_read_b128 v[178:181], v177 offset:2048
	ds_read_b128 v[182:185], v177 offset:3072
	ds_read_b128 v[194:197], v177 offset:4096
	ds_read_b128 v[198:201], v177 offset:5120
	ds_read_b128 v[202:205], v177 offset:6144
	ds_read_b128 v[206:209], v177 offset:7168
	buffer_load_dwordx4 v170, s[36:39], s6 offen lds
	s_mov_b32 m0, s56
	s_nop 0
	buffer_load_dwordx4 v172, s[36:39], s6 offen lds
	s_waitcnt vmcnt(8)
	s_waitcnt lgkmcnt(0)
	s_barrier
	s_setprio 1
	v_mfma_f32_16x16x128_f8f6f4 v[124:127], v[128:135], v[160:167], 0
	v_mfma_f32_16x16x128_f8f6f4 v[120:123], v[136:143], v[160:167], 0
	v_mfma_f32_16x16x128_f8f6f4 v[108:111], v[128:135], v[178:185], 0
	v_mfma_f32_16x16x128_f8f6f4 v[104:107], v[136:143], v[178:185], 0
	v_mfma_f32_16x16x128_f8f6f4 v[186:189], v[128:135], v[194:201], 0
	v_mfma_f32_16x16x128_f8f6f4 v[190:193], v[136:143], v[194:201], 0
	v_mfma_f32_16x16x128_f8f6f4 v[210:213], v[128:135], v[202:209], 0
	v_mfma_f32_16x16x128_f8f6f4 v[214:217], v[136:143], v[202:209], 0
	v_mfma_f32_16x16x128_f8f6f4 v[116:119], v[144:151], v[160:167], 0
	v_mfma_f32_16x16x128_f8f6f4 v[112:115], v[152:159], v[160:167], 0
	v_mfma_f32_16x16x128_f8f6f4 v[100:103], v[144:151], v[178:185], 0
	v_mfma_f32_16x16x128_f8f6f4 v[96:99], v[152:159], v[178:185], 0
	v_mfma_f32_16x16x128_f8f6f4 v[160:163], v[144:151], v[194:201], 0
	v_mfma_f32_16x16x128_f8f6f4 v[164:167], v[152:159], v[194:201], 0
	v_mfma_f32_16x16x128_f8f6f4 v[178:181], v[144:151], v[202:209], 0
	v_mfma_f32_16x16x128_f8f6f4 v[182:185], v[152:159], v[202:209], 0
	s_setprio 0
	s_barrier
	s_mov_b32 m0, s26
	s_mov_b32 s6, s38
	s_mov_b32 s7, s39
	s_nop 1
	buffer_load_dwordx4 v171, s[4:7], s55 offen lds
	s_mov_b32 m0, s27
	ds_read_b128 v[64:67], v177 offset:16384
	s_add_i32 s69, s55, s24
	buffer_load_dwordx4 v173, s[4:7], s55 offen lds
	s_mov_b32 m0, s25
	ds_read_b128 v[68:71], v177 offset:17408
	buffer_load_dwordx4 v170, s[36:39], s68 offen lds
	s_mov_b32 m0, s30
	ds_read_b128 v[72:75], v177 offset:18432
	buffer_load_dwordx4 v172, s[36:39], s68 offen lds
	ds_read_b128 v[76:79], v177 offset:19456
	ds_read_b128 v[80:83], v177 offset:20480
	ds_read_b128 v[84:87], v177 offset:21504
	ds_read_b128 v[88:91], v177 offset:22528
	ds_read_b128 v[92:95], v177 offset:23552
	s_waitcnt vmcnt(6)
	s_waitcnt lgkmcnt(0)
	s_barrier
	s_setprio 1
	v_mfma_f32_16x16x128_f8f6f4 v[60:63], v[128:135], v[64:71], 0
	v_mfma_f32_16x16x128_f8f6f4 v[56:59], v[136:143], v[64:71], 0
	v_mfma_f32_16x16x128_f8f6f4 v[194:197], v[128:135], v[72:79], 0
	v_mfma_f32_16x16x128_f8f6f4 v[198:201], v[136:143], v[72:79], 0
	v_mfma_f32_16x16x128_f8f6f4 v[202:205], v[128:135], v[80:87], 0
	v_mfma_f32_16x16x128_f8f6f4 v[206:209], v[136:143], v[80:87], 0
	v_mfma_f32_16x16x128_f8f6f4 v[218:221], v[128:135], v[88:95], 0
	v_mfma_f32_16x16x128_f8f6f4 v[226:229], v[136:143], v[88:95], 0
	v_mfma_f32_16x16x128_f8f6f4 v[52:55], v[144:151], v[64:71], 0
	v_mfma_f32_16x16x128_f8f6f4 v[48:51], v[152:159], v[64:71], 0
	v_mfma_f32_16x16x128_f8f6f4 v[230:233], v[144:151], v[72:79], 0
	v_mfma_f32_16x16x128_f8f6f4 v[234:237], v[152:159], v[72:79], 0
	v_mfma_f32_16x16x128_f8f6f4 v[238:241], v[144:151], v[80:87], 0
	v_mfma_f32_16x16x128_f8f6f4 v[242:245], v[152:159], v[80:87], 0
	v_mfma_f32_16x16x128_f8f6f4 v[246:249], v[144:151], v[88:95], 0
	v_mfma_f32_16x16x128_f8f6f4 v[250:253], v[152:159], v[88:95], 0
	s_setprio 0
	s_barrier
	s_mov_b32 m0, s28
	s_nop 0
	buffer_load_dwordx4 v171, s[4:7], s69 offen lds
	s_mov_b32 m0, s29
	s_nop 0
	buffer_load_dwordx4 v173, s[4:7], s69 offen lds
	v_add_u32_e32 v8, 0x18000, v176
	s_nop 3
	ds_read_b128 v[0:3], v8
	ds_read_b128 v[4:7], v8 offset:1024
	ds_read_b128 v[16:19], v8 offset:2048
	ds_read_b128 v[20:23], v8 offset:3072
	v_add_u32_e32 v8, 0x1c000, v176
	ds_read_b128 v[128:131], v8
	ds_read_b128 v[132:135], v8 offset:1024
	ds_read_b128 v[136:139], v8 offset:2048
	ds_read_b128 v[140:143], v8 offset:3072
	s_add_i32 s68, s68, s24
	s_mov_b32 m0, s31
	ds_read_b128 v[8:11], v177 offset:32768
	ds_read_b128 v[12:15], v177 offset:33792
	ds_read_b128 v[24:27], v177 offset:34816
	ds_read_b128 v[28:31], v177 offset:35840
	ds_read_b128 v[32:35], v177 offset:36864
	ds_read_b128 v[36:39], v177 offset:37888
	ds_read_b128 v[40:43], v177 offset:38912
	ds_read_b128 v[44:47], v177 offset:39936
	buffer_load_dwordx4 v170, s[36:39], s68 offen lds
	s_mov_b32 m0, s33
	s_nop 0
	buffer_load_dwordx4 v172, s[36:39], s68 offen lds
	s_waitcnt vmcnt(8)
	s_waitcnt lgkmcnt(0)
	s_barrier
; #define PG8_STAGE(bufoff, rs_, soff_, voff) do { _Pragma("unroll") for (int _i = 0; _i < 2; ++_i) \
;         __builtin_amdgcn_raw_ptr_buffer_load_lds(rs_, (LAS void*)(lds + (bufoff) + ldsw + _i * 8192), 16, (int)(voff)[_i], (int)(soff_), 0, 0); } while (0)
; #define PG8_LDA(dst, b, h) do { _Pragma("unroll") for (int m = 0; m < 4; ++m) dst[m] = PG8_LD2(lds + PG8_SA(b, h) + aoff + m * 2048); } while (0)
; #define PG8_LDB(dst, b, h) do { _Pragma("unroll") for (int n = 0; n < 2; ++n) dst[n] = PG8_LD2(lds + PG8_SB(b, h) + boff + n * 2048); } while (0)
; #define PG8_WAIT_V(n) asm volatile("s_waitcnt vmcnt(" #n ")" ::: "memory")
; #define PG8_WAIT_L(n) asm volatile("s_waitcnt lgkmcnt(" #n ")" ::: "memory")
; #define PG8_BAR __builtin_amdgcn_s_barrier()
; #define PG8_SCHED __builtin_amdgcn_sched_barrier(0)
; template <class Epi, class Sched, bool ALIGN_EPI = false, bool SP2 = false, bool FP8 = false>
; __device__ __forceinline__ void gemm_phase(LAS unsigned char* lds, const Gemm g, const Sched& S, const Epi& E, int wbase) {
;     ...
;         for (int t = 0; t < nt; t += 2) {
;             const bool last = (t == nt - 2);
;             const unsigned a1 = cA + (unsigned)(t + 1) * kstep;
;             const unsigned a2 = last ? nA : cA + (unsigned)(t + 2) * kstep, b2 = last ? nB : cB + (unsigned)(t + 2) * kstep; const rsrc_t rA2 = (Sched::TWO && last) ? rAn : rAc, rB2 = (Sched::TWO && last) ? rBn : rBc;
;             const unsigned a3 = a2 + kstep, b3 = b2 + kstep;
;             if (last && has_next) S.a_ready(nxt);
;             if constexpr (SP2) {
;             PG8_LDB(B0, 0, 0); PG8_LDB(B1, 0, 1); PG8_SCHED; PG8_LDA(At, 0, 0); PG8_STAGE(PG8_SA(1, 1), rAc, a1 + hstep, voffA);
;             PG8_WAIT_V(8); PG8_WAIT_L(0); PG8_BAR; PG8_MMA(0, 0, At, B0); PG8_MMA(0, 1, At, B1); PG8_BAR; PG8_SCHED;
;     ...
;             PG8_LDB(B0, 1, 0); PG8_LDB(B1, 1, 1); PG8_SCHED; PG8_LDA(At, 1, 0); PG8_STAGE(PG8_SA(0, 1), rA2, a2 + hstep, voffA);
;             PG8_WAIT_V(8); PG8_WAIT_L(0); PG8_BAR; PG8_MMA(0, 0, At, B0); PG8_MMA(0, 1, At, B1); PG8_BAR; PG8_SCHED;
;             PG8_LDA(At, 1, 1); PG8_STAGE(PG8_SB(1, 0), rB2, b3, voffB); PG8_STAGE(PG8_SB(1, 1), rB2, b3 + hstep, voffB); PG8_STAGE(PG8_SA(1, 0), rA2, a3, voffA);
;             PG8_WAIT_V(8); PG8_WAIT_L(0); PG8_BAR; PG8_MMA(1, 0, At, B0); PG8_MMA(1, 1, At, B1); PG8_BAR; PG8_SCHED;
	s_setprio 1
	v_mfma_f32_16x16x128_f8f6f4 v[124:127], v[0:7], v[8:15], v[124:127]
	v_mfma_f32_16x16x128_f8f6f4 v[120:123], v[16:23], v[8:15], v[120:123]
	v_mfma_f32_16x16x128_f8f6f4 v[108:111], v[0:7], v[24:31], v[108:111]
	v_mfma_f32_16x16x128_f8f6f4 v[104:107], v[16:23], v[24:31], v[104:107]
	v_mfma_f32_16x16x128_f8f6f4 v[92:95], v[0:7], v[32:39], v[186:189]
	v_mfma_f32_16x16x128_f8f6f4 v[88:91], v[16:23], v[32:39], v[190:193]
	v_mfma_f32_16x16x128_f8f6f4 v[76:79], v[0:7], v[40:47], v[210:213]
	v_mfma_f32_16x16x128_f8f6f4 v[72:75], v[16:23], v[40:47], v[214:217]
	v_mfma_f32_16x16x128_f8f6f4 v[116:119], v[128:135], v[8:15], v[116:119]
	v_mfma_f32_16x16x128_f8f6f4 v[112:115], v[136:143], v[8:15], v[112:115]
	v_mfma_f32_16x16x128_f8f6f4 v[100:103], v[128:135], v[24:31], v[100:103]
	v_mfma_f32_16x16x128_f8f6f4 v[96:99], v[136:143], v[24:31], v[96:99]
	v_mfma_f32_16x16x128_f8f6f4 v[84:87], v[128:135], v[32:39], v[160:163]
	v_mfma_f32_16x16x128_f8f6f4 v[80:83], v[136:143], v[32:39], v[164:167]
	v_mfma_f32_16x16x128_f8f6f4 v[68:71], v[128:135], v[40:47], v[178:181]
	v_mfma_f32_16x16x128_f8f6f4 v[64:67], v[136:143], v[40:47], v[182:185]
	s_setprio 0
	s_barrier
	s_mov_b32 m0, s34
	s_bitset1_b32 s55, 7
	buffer_load_dwordx4 v171, s[4:7], s55 offen lds
	s_mov_b32 m0, s35
	ds_read_b128 v[32:35], v177 offset:49152
	buffer_load_dwordx4 v173, s[4:7], s55 offen lds
	s_add_i32 s55, s55, s24
	s_mov_b32 m0, s43
	ds_read_b128 v[36:39], v177 offset:50176
	buffer_load_dwordx4 v171, s[4:7], s55 offen lds
	s_mov_b32 m0, s44
	ds_read_b128 v[144:147], v177 offset:51200
	buffer_load_dwordx4 v173, s[4:7], s55 offen lds
	s_mov_b32 m0, s41
	ds_read_b128 v[148:151], v177 offset:52224
	buffer_load_dwordx4 v170, s[36:39], s54 offen lds
	s_mov_b32 m0, s42
	ds_read_b128 v[152:155], v177 offset:53248
	buffer_load_dwordx4 v172, s[36:39], s54 offen lds
	ds_read_b128 v[156:159], v177 offset:54272
	ds_read_b128 v[160:163], v177 offset:55296
	ds_read_b128 v[164:167], v177 offset:56320
	s_waitcnt vmcnt(8)
	s_waitcnt lgkmcnt(0)
	s_barrier
	s_setprio 1
	v_mfma_f32_16x16x128_f8f6f4 v[60:63], v[0:7], v[32:39], v[60:63]
	v_mfma_f32_16x16x128_f8f6f4 v[56:59], v[16:23], v[32:39], v[56:59]
	v_mfma_f32_16x16x128_f8f6f4 v[44:47], v[0:7], v[144:151], v[194:197]
	v_mfma_f32_16x16x128_f8f6f4 v[40:43], v[16:23], v[144:151], v[198:201]
	v_mfma_f32_16x16x128_f8f6f4 v[28:31], v[0:7], v[152:159], v[202:205]
	v_mfma_f32_16x16x128_f8f6f4 v[24:27], v[16:23], v[152:159], v[206:209]
	v_mfma_f32_16x16x128_f8f6f4 v[12:15], v[0:7], v[160:167], v[218:221]
	v_mfma_f32_16x16x128_f8f6f4 v[8:11], v[16:23], v[160:167], v[226:229]
	v_mfma_f32_16x16x128_f8f6f4 v[52:55], v[128:135], v[32:39], v[52:55]
	v_mfma_f32_16x16x128_f8f6f4 v[48:51], v[136:143], v[32:39], v[48:51]
	v_mfma_f32_16x16x128_f8f6f4 v[36:39], v[128:135], v[144:151], v[230:233]
	v_mfma_f32_16x16x128_f8f6f4 v[32:35], v[136:143], v[144:151], v[234:237]
	v_mfma_f32_16x16x128_f8f6f4 v[20:23], v[128:135], v[152:159], v[238:241]
	v_mfma_f32_16x16x128_f8f6f4 v[16:19], v[136:143], v[152:159], v[242:245]
	v_mfma_f32_16x16x128_f8f6f4 v[4:7], v[128:135], v[160:167], v[246:249]
	v_mfma_f32_16x16x128_f8f6f4 v[0:3], v[136:143], v[160:167], v[250:253]
	s_setprio 0
	s_barrier
	s_add_i32 s67, s67, 2
	s_addk_i32 s65, 0x100
	s_addk_i32 s66, 0x100
	s_cmp_ge_i32 s67, s47
	s_cbranch_scc0 .LBB0_1854
	s_branch .Lzp_after_1854
.LBB0_1854:
	v_add_u32_e32 v140, 0x10000, v176
	v_add_u32_e32 v156, 0x14000, v176
	ds_read_b128 v[128:131], v140
	ds_read_b128 v[132:135], v140 offset:1024
	ds_read_b128 v[136:139], v140 offset:2048
	ds_read_b128 v[140:143], v140 offset:3072
	ds_read_b128 v[144:147], v156
	ds_read_b128 v[148:151], v156 offset:1024
	ds_read_b128 v[152:155], v156 offset:2048
	ds_read_b128 v[156:159], v156 offset:3072
	s_add_i32 s6, s65, 0x80
	s_cmp_eq_u32 s52, s67
	s_cselect_b32 s68, s21, s6
	s_cselect_b32 s55, s63, s66
	s_or_b32 s54, s68, 0x80
	s_add_i32 s6, s24, s65
	s_mov_b32 m0, s53
	ds_read_b128 v[160:163], v177
	ds_read_b128 v[164:167], v177 offset:1024
	ds_read_b128 v[178:181], v177 offset:2048
	ds_read_b128 v[182:185], v177 offset:3072
	ds_read_b128 v[194:197], v177 offset:4096
	ds_read_b128 v[198:201], v177 offset:5120
	ds_read_b128 v[202:205], v177 offset:6144
	ds_read_b128 v[206:209], v177 offset:7168
	buffer_load_dwordx4 v170, s[36:39], s6 offen lds
	s_mov_b32 m0, s56
	s_nop 0
	buffer_load_dwordx4 v172, s[36:39], s6 offen lds
	s_waitcnt vmcnt(8)
	s_waitcnt lgkmcnt(0)
	s_barrier
	s_setprio 1
	v_mfma_f32_16x16x128_f8f6f4 v[124:127], v[128:135], v[160:167], v[124:127]
	v_mfma_f32_16x16x128_f8f6f4 v[120:123], v[136:143], v[160:167], v[120:123]
	v_mfma_f32_16x16x128_f8f6f4 v[108:111], v[128:135], v[178:185], v[108:111]
	v_mfma_f32_16x16x128_f8f6f4 v[104:107], v[136:143], v[178:185], v[104:107]
	v_mfma_f32_16x16x128_f8f6f4 v[186:189], v[128:135], v[194:201], v[92:95]
	v_mfma_f32_16x16x128_f8f6f4 v[190:193], v[136:143], v[194:201], v[88:91]
	v_mfma_f32_16x16x128_f8f6f4 v[210:213], v[128:135], v[202:209], v[76:79]
	v_mfma_f32_16x16x128_f8f6f4 v[214:217], v[136:143], v[202:209], v[72:75]
	v_mfma_f32_16x16x128_f8f6f4 v[116:119], v[144:151], v[160:167], v[116:119]
	v_mfma_f32_16x16x128_f8f6f4 v[112:115], v[152:159], v[160:167], v[112:115]
	v_mfma_f32_16x16x128_f8f6f4 v[100:103], v[144:151], v[178:185], v[100:103]
	v_mfma_f32_16x16x128_f8f6f4 v[96:99], v[152:159], v[178:185], v[96:99]
	v_mfma_f32_16x16x128_f8f6f4 v[160:163], v[144:151], v[194:201], v[84:87]
	v_mfma_f32_16x16x128_f8f6f4 v[164:167], v[152:159], v[194:201], v[80:83]
	v_mfma_f32_16x16x128_f8f6f4 v[178:181], v[144:151], v[202:209], v[68:71]
	v_mfma_f32_16x16x128_f8f6f4 v[182:185], v[152:159], v[202:209], v[64:67]
	s_setprio 0
	s_barrier
; #define PG8_STAGE(bufoff, rs_, soff_, voff) do { _Pragma("unroll") for (int _i = 0; _i < 2; ++_i) \
;         __builtin_amdgcn_raw_ptr_buffer_load_lds(rs_, (LAS void*)(lds + (bufoff) + ldsw + _i * 8192), 16, (int)(voff)[_i], (int)(soff_), 0, 0); } while (0)
; #define PG8_LDA(dst, b, h) do { _Pragma("unroll") for (int m = 0; m < 4; ++m) dst[m] = PG8_LD2(lds + PG8_SA(b, h) + aoff + m * 2048); } while (0)
; #define PG8_LDB(dst, b, h) do { _Pragma("unroll") for (int n = 0; n < 2; ++n) dst[n] = PG8_LD2(lds + PG8_SB(b, h) + boff + n * 2048); } while (0)
; #define PG8_WAIT_V(n) asm volatile("s_waitcnt vmcnt(" #n ")" ::: "memory")
; #define PG8_WAIT_L(n) asm volatile("s_waitcnt lgkmcnt(" #n ")" ::: "memory")
; #define PG8_BAR __builtin_amdgcn_s_barrier()
; #define PG8_SCHED __builtin_amdgcn_sched_barrier(0)
; template <class Epi, class Sched, bool ALIGN_EPI = false, bool SP2 = false, bool FP8 = false>
; __device__ __forceinline__ void gemm_phase(LAS unsigned char* lds, const Gemm g, const Sched& S, const Epi& E, int wbase) {
;     ...
;             PG8_WAIT_V(8); PG8_WAIT_L(0); PG8_BAR; PG8_MMA(0, 0, At, B0); PG8_MMA(0, 1, At, B1); PG8_BAR; PG8_SCHED;
;             PG8_LDA(At, 0, 1); PG8_STAGE(PG8_SB(0, 0), rB2, b2, voffB); PG8_STAGE(PG8_SB(0, 1), rB2, b2 + hstep, voffB); PG8_STAGE(PG8_SA(0, 0), rA2, a2, voffA);
;             PG8_WAIT_V(8); PG8_WAIT_L(0); PG8_BAR; PG8_MMA(1, 0, At, B0); PG8_MMA(1, 1, At, B1); PG8_BAR; PG8_SCHED;
;             PG8_LDB(B0, 1, 0); PG8_LDB(B1, 1, 1); PG8_SCHED; PG8_LDA(At, 1, 0); PG8_STAGE(PG8_SA(0, 1), rA2, a2 + hstep, voffA);
;             PG8_WAIT_V(8); PG8_WAIT_L(0); PG8_BAR; PG8_MMA(0, 0, At, B0); PG8_MMA(0, 1, At, B1); PG8_BAR; PG8_SCHED;
;             PG8_LDA(At, 1, 1); PG8_STAGE(PG8_SB(1, 0), rB2, b3, voffB); PG8_STAGE(PG8_SB(1, 1), rB2, b3 + hstep, voffB); PG8_STAGE(PG8_SA(1, 0), rA2, a3, voffA);
;             PG8_WAIT_V(8); PG8_WAIT_L(0); PG8_BAR; PG8_MMA(1, 0, At, B0); PG8_MMA(1, 1, At, B1); PG8_BAR; PG8_SCHED;
	s_mov_b32 m0, s26
	s_mov_b32 s6, s38
	s_mov_b32 s7, s39
	s_nop 1
	buffer_load_dwordx4 v171, s[4:7], s55 offen lds
	s_mov_b32 m0, s27
	ds_read_b128 v[64:67], v177 offset:16384
	s_add_i32 s69, s55, s24
	buffer_load_dwordx4 v173, s[4:7], s55 offen lds
	s_mov_b32 m0, s25
	ds_read_b128 v[68:71], v177 offset:17408
	buffer_load_dwordx4 v170, s[36:39], s68 offen lds
	s_mov_b32 m0, s30
	ds_read_b128 v[72:75], v177 offset:18432
	buffer_load_dwordx4 v172, s[36:39], s68 offen lds
	ds_read_b128 v[76:79], v177 offset:19456
	ds_read_b128 v[80:83], v177 offset:20480
	ds_read_b128 v[84:87], v177 offset:21504
	ds_read_b128 v[88:91], v177 offset:22528
	ds_read_b128 v[92:95], v177 offset:23552
	s_waitcnt vmcnt(6)
	s_waitcnt lgkmcnt(0)
	s_barrier
	s_setprio 1
	v_mfma_f32_16x16x128_f8f6f4 v[60:63], v[128:135], v[64:71], v[60:63]
	v_mfma_f32_16x16x128_f8f6f4 v[56:59], v[136:143], v[64:71], v[56:59]
	v_mfma_f32_16x16x128_f8f6f4 v[194:197], v[128:135], v[72:79], v[44:47]
	v_mfma_f32_16x16x128_f8f6f4 v[198:201], v[136:143], v[72:79], v[40:43]
	v_mfma_f32_16x16x128_f8f6f4 v[202:205], v[128:135], v[80:87], v[28:31]
	v_mfma_f32_16x16x128_f8f6f4 v[206:209], v[136:143], v[80:87], v[24:27]
	v_mfma_f32_16x16x128_f8f6f4 v[218:221], v[128:135], v[88:95], v[12:15]
	v_mfma_f32_16x16x128_f8f6f4 v[226:229], v[136:143], v[88:95], v[8:11]
	v_mfma_f32_16x16x128_f8f6f4 v[52:55], v[144:151], v[64:71], v[52:55]
	v_mfma_f32_16x16x128_f8f6f4 v[48:51], v[152:159], v[64:71], v[48:51]
	v_mfma_f32_16x16x128_f8f6f4 v[230:233], v[144:151], v[72:79], v[36:39]
	v_mfma_f32_16x16x128_f8f6f4 v[234:237], v[152:159], v[72:79], v[32:35]
	v_mfma_f32_16x16x128_f8f6f4 v[238:241], v[144:151], v[80:87], v[20:23]
	v_mfma_f32_16x16x128_f8f6f4 v[242:245], v[152:159], v[80:87], v[16:19]
	v_mfma_f32_16x16x128_f8f6f4 v[246:249], v[144:151], v[88:95], v[4:7]
	v_mfma_f32_16x16x128_f8f6f4 v[250:253], v[152:159], v[88:95], v[0:3]
	s_setprio 0
	s_barrier
	s_mov_b32 m0, s28
	s_nop 0
	buffer_load_dwordx4 v171, s[4:7], s69 offen lds
	s_mov_b32 m0, s29
	s_nop 0
	buffer_load_dwordx4 v173, s[4:7], s69 offen lds
	v_add_u32_e32 v8, 0x18000, v176
	s_nop 3
	ds_read_b128 v[0:3], v8
	ds_read_b128 v[4:7], v8 offset:1024
	ds_read_b128 v[16:19], v8 offset:2048
	ds_read_b128 v[20:23], v8 offset:3072
	v_add_u32_e32 v8, 0x1c000, v176
	ds_read_b128 v[128:131], v8
	ds_read_b128 v[132:135], v8 offset:1024
	ds_read_b128 v[136:139], v8 offset:2048
	ds_read_b128 v[140:143], v8 offset:3072
	s_add_i32 s68, s68, s24
	s_mov_b32 m0, s31
	ds_read_b128 v[8:11], v177 offset:32768
	ds_read_b128 v[12:15], v177 offset:33792
	ds_read_b128 v[24:27], v177 offset:34816
	ds_read_b128 v[28:31], v177 offset:35840
	ds_read_b128 v[32:35], v177 offset:36864
	ds_read_b128 v[36:39], v177 offset:37888
	ds_read_b128 v[40:43], v177 offset:38912
	ds_read_b128 v[44:47], v177 offset:39936
	buffer_load_dwordx4 v170, s[36:39], s68 offen lds
	s_mov_b32 m0, s33
	s_nop 0
	buffer_load_dwordx4 v172, s[36:39], s68 offen lds
	s_waitcnt vmcnt(8)
	s_waitcnt lgkmcnt(0)
	s_barrier
	s_setprio 1
	v_mfma_f32_16x16x128_f8f6f4 v[124:127], v[0:7], v[8:15], v[124:127]
	v_mfma_f32_16x16x128_f8f6f4 v[120:123], v[16:23], v[8:15], v[120:123]
	v_mfma_f32_16x16x128_f8f6f4 v[108:111], v[0:7], v[24:31], v[108:111]
	v_mfma_f32_16x16x128_f8f6f4 v[104:107], v[16:23], v[24:31], v[104:107]
	v_mfma_f32_16x16x128_f8f6f4 v[92:95], v[0:7], v[32:39], v[186:189]
	v_mfma_f32_16x16x128_f8f6f4 v[88:91], v[16:23], v[32:39], v[190:193]
	v_mfma_f32_16x16x128_f8f6f4 v[76:79], v[0:7], v[40:47], v[210:213]
	v_mfma_f32_16x16x128_f8f6f4 v[72:75], v[16:23], v[40:47], v[214:217]
	v_mfma_f32_16x16x128_f8f6f4 v[116:119], v[128:135], v[8:15], v[116:119]
	v_mfma_f32_16x16x128_f8f6f4 v[112:115], v[136:143], v[8:15], v[112:115]
	v_mfma_f32_16x16x128_f8f6f4 v[100:103], v[128:135], v[24:31], v[100:103]
	v_mfma_f32_16x16x128_f8f6f4 v[96:99], v[136:143], v[24:31], v[96:99]
	v_mfma_f32_16x16x128_f8f6f4 v[84:87], v[128:135], v[32:39], v[160:163]
	v_mfma_f32_16x16x128_f8f6f4 v[80:83], v[136:143], v[32:39], v[164:167]
	v_mfma_f32_16x16x128_f8f6f4 v[68:71], v[128:135], v[40:47], v[178:181]
	v_mfma_f32_16x16x128_f8f6f4 v[64:67], v[136:143], v[40:47], v[182:185]
	s_setprio 0
	s_barrier
	s_mov_b32 m0, s34
	s_bitset1_b32 s55, 7
	buffer_load_dwordx4 v171, s[4:7], s55 offen lds
	s_mov_b32 m0, s35
	ds_read_b128 v[32:35], v177 offset:49152
	buffer_load_dwordx4 v173, s[4:7], s55 offen lds
	s_add_i32 s55, s55, s24
	s_mov_b32 m0, s43
	ds_read_b128 v[36:39], v177 offset:50176
	buffer_load_dwordx4 v171, s[4:7], s55 offen lds
	s_mov_b32 m0, s44
	ds_read_b128 v[144:147], v177 offset:51200
	buffer_load_dwordx4 v173, s[4:7], s55 offen lds
	s_mov_b32 m0, s41
	ds_read_b128 v[148:151], v177 offset:52224
	buffer_load_dwordx4 v170, s[36:39], s54 offen lds
	s_mov_b32 m0, s42
	ds_read_b128 v[152:155], v177 offset:53248
	buffer_load_dwordx4 v172, s[36:39], s54 offen lds
	ds_read_b128 v[156:159], v177 offset:54272
	ds_read_b128 v[160:163], v177 offset:55296
	ds_read_b128 v[164:167], v177 offset:56320
	s_waitcnt vmcnt(8)
	s_waitcnt lgkmcnt(0)
	s_barrier
	s_setprio 1
	v_mfma_f32_16x16x128_f8f6f4 v[60:63], v[0:7], v[32:39], v[60:63]
	v_mfma_f32_16x16x128_f8f6f4 v[56:59], v[16:23], v[32:39], v[56:59]
	v_mfma_f32_16x16x128_f8f6f4 v[44:47], v[0:7], v[144:151], v[194:197]
	v_mfma_f32_16x16x128_f8f6f4 v[40:43], v[16:23], v[144:151], v[198:201]
	v_mfma_f32_16x16x128_f8f6f4 v[28:31], v[0:7], v[152:159], v[202:205]
	v_mfma_f32_16x16x128_f8f6f4 v[24:27], v[16:23], v[152:159], v[206:209]
	v_mfma_f32_16x16x128_f8f6f4 v[12:15], v[0:7], v[160:167], v[218:221]
	v_mfma_f32_16x16x128_f8f6f4 v[8:11], v[16:23], v[160:167], v[226:229]
	v_mfma_f32_16x16x128_f8f6f4 v[52:55], v[128:135], v[32:39], v[52:55]
	v_mfma_f32_16x16x128_f8f6f4 v[48:51], v[136:143], v[32:39], v[48:51]
	v_mfma_f32_16x16x128_f8f6f4 v[36:39], v[128:135], v[144:151], v[230:233]
	v_mfma_f32_16x16x128_f8f6f4 v[32:35], v[136:143], v[144:151], v[234:237]
	v_mfma_f32_16x16x128_f8f6f4 v[20:23], v[128:135], v[152:159], v[238:241]
	v_mfma_f32_16x16x128_f8f6f4 v[16:19], v[136:143], v[152:159], v[242:245]
	v_mfma_f32_16x16x128_f8f6f4 v[4:7], v[128:135], v[160:167], v[246:249]
	v_mfma_f32_16x16x128_f8f6f4 v[0:3], v[136:143], v[160:167], v[250:253]
	s_setprio 0
	s_barrier
	s_add_i32 s67, s67, 2
	s_addk_i32 s65, 0x100
	s_addk_i32 s66, 0x100
	s_cmp_ge_i32 s67, s47
	s_cbranch_scc0 .LBB0_1854

;     __device__ __forceinline__ unsigned a_off(const Unit& u, const Gemm& g) const { return (unsigned)u.pm * (unsigned)(BM * 2) * (unsigned)g.K; }
;     __device__ __forceinline__ unsigned b_off(const Unit& u, const Gemm& g) const { return (unsigned)u.pn * (unsigned)(BM * 2) * (unsigned)g.K; }
;     __device__ __forceinline__ bool next(int i, Unit& u) const { return so.next(i, u); }
;     __device__ __forceinline__ unsigned a_off(const Unit& u, const Gemm& g) const { return (unsigned)u.pm * (unsigned)(BM * 2) * (unsigned)g.K; }
; #define PG8_WAIT_V(n) asm volatile("s_waitcnt vmcnt(" #n ")" ::: "memory")
; #define PG8_BAR __builtin_amdgcn_s_barrier()
; template <class Epi, class Sched, bool ALIGN_EPI = false, bool SP2 = false, bool FP8 = false>
; __device__ __forceinline__ void gemm_phase(LAS unsigned char* lds, const Gemm g, const Sched& S, const Epi& E, int wbase) {
;     ...
;     for (;;) {
;         const bool has_next = S.next(ui + 1, nxt);
;         const unsigned nA = has_next ? S.a_off(nxt, g) : cA, nB = has_next ? S.b_off(nxt, g) : cB;
;         const rsrc_t rAn = (Sched::TWO && has_next) ? (nxt.part ? rA1 : rA0) : rAc, rBn = (Sched::TWO && has_next) ? (nxt.part ? rB1 : rB0) : rBc;
;         float pre_[8] = {0.f, 0.f, 0.f, 0.f, 0.f, 0.f, 0.f, 0.f};
;         if constexpr (Epi::HAS_PRE) E.pre_load(pre_, cur, wr);
;         for (int t = 0; t < nt; t += 2) {
;             const bool last = (t == nt - 2);
;             const unsigned a1 = cA + (unsigned)(t + 1) * kstep;
;             const unsigned a2 = last ? nA : cA + (unsigned)(t + 2) * kstep, b2 = last ? nB : cB + (unsigned)(t + 2) * kstep; const rsrc_t rA2 = (Sched::TWO && last) ? rAn : rAc, rB2 = (Sched::TWO && last) ? rBn : rBc;
;             const unsigned a3 = a2 + kstep, b3 = b2 + kstep;
;             if (last && has_next) S.a_ready(nxt);
;             if constexpr (SP2) {
;             PG8_LDB(B0, 0, 0); PG8_LDB(B1, 0, 1); PG8_SCHED; PG8_LDA(At, 0, 0); PG8_STAGE(PG8_SA(1, 1), rAc, a1 + hstep, voffA);
;             PG8_WAIT_V(8); PG8_WAIT_L(0); PG8_BAR; PG8_MMA(0, 0, At, B0); PG8_MMA(0, 1, At, B1); PG8_BAR; PG8_SCHED;
;             PG8_LDA(At, 0, 1); PG8_STAGE(PG8_SB(0, 0), rB2, b2, voffB); PG8_STAGE(PG8_SB(0, 1), rB2, b2 + hstep, voffB); PG8_STAGE(PG8_SA(0, 0), rA2, a2, voffA);
;             PG8_WAIT_V(8); PG8_WAIT_L(0); PG8_BAR; PG8_MMA(1, 0, At, B0); PG8_MMA(1, 1, At, B1); PG8_BAR; PG8_SCHED;
.LBB0_1942:
	s_mov_b32 s68, s94
	s_lshl_b32 s85, s84, 19
	s_andn2_b64 vcc, exec, s[22:23]
	s_lshl_b32 s94, s83, 19
	s_cbranch_vccnz .LBB0_1966
	s_and_b64 s[6:7], s[26:27], exec
	s_waitcnt vmcnt(37)
	s_waitcnt vmcnt(36)
	s_waitcnt vmcnt(35)
	s_waitcnt vmcnt(32)
	s_waitcnt vmcnt(31)
	s_waitcnt vmcnt(28)
	s_waitcnt vmcnt(27)
	s_waitcnt vmcnt(24)
	s_waitcnt vmcnt(23)
	s_cselect_b32 s29, s85, s55
	s_cselect_b32 s60, s94, s54
	s_add_i32 s61, s55, 0x80
	s_add_i32 s62, s54, 0x100
	s_mov_b32 s63, 0
	s_waitcnt vmcnt(0)
	v_add_u32_e32 v136, 0x10000, v174
	v_add_u32_e32 v156, 0x14000, v174
	ds_read_b128 v[120:123], v136
	ds_read_b128 v[124:127], v136 offset:1024
	ds_read_b128 v[132:135], v136 offset:2048
	ds_read_b128 v[136:139], v136 offset:3072
	ds_read_b128 v[144:147], v156
	ds_read_b128 v[148:151], v156 offset:1024
	ds_read_b128 v[152:155], v156 offset:2048
	ds_read_b128 v[156:159], v156 offset:3072
	s_add_i32 s6, s61, 0x80
	s_cmp_eq_u32 s77, s63
	s_cselect_b32 s66, s29, s6
	s_cselect_b32 s55, s60, s62
	s_or_b32 s54, s66, 0x80
	s_add_i32 s6, s33, s61
	s_mov_b32 m0, s79
	ds_read_b128 v[160:163], v175
	ds_read_b128 v[164:167], v175 offset:1024
	ds_read_b128 v[176:179], v175 offset:2048
	ds_read_b128 v[180:183], v175 offset:3072
	ds_read_b128 v[184:187], v175 offset:4096
	ds_read_b128 v[188:191], v175 offset:5120
	ds_read_b128 v[192:195], v175 offset:6144
	ds_read_b128 v[196:199], v175 offset:7168
	buffer_load_dwordx4 v168, s[36:39], s6 offen lds
	s_mov_b32 m0, s82
	s_nop 0
	buffer_load_dwordx4 v170, s[36:39], s6 offen lds
	s_waitcnt vmcnt(8)
	s_waitcnt lgkmcnt(0)
	s_barrier
	s_setprio 1
	v_mfma_f32_16x16x32_bf16 v[140:143], v[120:123], v[160:163], 0
	v_mfma_f32_16x16x32_bf16 v[128:131], v[132:135], v[160:163], 0
	v_mfma_f32_16x16x32_bf16 v[108:111], v[120:123], v[176:179], 0
	v_mfma_f32_16x16x32_bf16 v[104:107], v[132:135], v[176:179], 0
	v_mfma_f32_16x16x32_bf16 v[92:95], v[120:123], v[184:187], 0
	v_mfma_f32_16x16x32_bf16 v[88:91], v[132:135], v[184:187], 0
	v_mfma_f32_16x16x32_bf16 v[76:79], v[120:123], v[192:195], 0
	v_mfma_f32_16x16x32_bf16 v[72:75], v[132:135], v[192:195], 0
	v_mfma_f32_16x16x32_bf16 v[140:143], v[124:127], v[164:167], v[140:143]
	v_mfma_f32_16x16x32_bf16 v[128:131], v[136:139], v[164:167], v[128:131]
	v_mfma_f32_16x16x32_bf16 v[108:111], v[124:127], v[180:183], v[108:111]
	v_mfma_f32_16x16x32_bf16 v[104:107], v[136:139], v[180:183], v[104:107]
	v_mfma_f32_16x16x32_bf16 v[92:95], v[124:127], v[188:191], v[92:95]
	v_mfma_f32_16x16x32_bf16 v[88:91], v[136:139], v[188:191], v[88:91]
	v_mfma_f32_16x16x32_bf16 v[76:79], v[124:127], v[196:199], v[76:79]
	v_mfma_f32_16x16x32_bf16 v[72:75], v[136:139], v[196:199], v[72:75]
	v_mfma_f32_16x16x32_bf16 v[116:119], v[144:147], v[160:163], 0
	v_mfma_f32_16x16x32_bf16 v[112:115], v[152:155], v[160:163], 0
	v_mfma_f32_16x16x32_bf16 v[100:103], v[144:147], v[176:179], 0
	v_mfma_f32_16x16x32_bf16 v[96:99], v[152:155], v[176:179], 0
	v_mfma_f32_16x16x32_bf16 v[84:87], v[144:147], v[184:187], 0
	v_mfma_f32_16x16x32_bf16 v[80:83], v[152:155], v[184:187], 0
	v_mfma_f32_16x16x32_bf16 v[68:71], v[144:147], v[192:195], 0
	v_mfma_f32_16x16x32_bf16 v[64:67], v[152:155], v[192:195], 0
	v_mfma_f32_16x16x32_bf16 v[116:119], v[148:151], v[164:167], v[116:119]
	v_mfma_f32_16x16x32_bf16 v[112:115], v[156:159], v[164:167], v[112:115]
	v_mfma_f32_16x16x32_bf16 v[100:103], v[148:151], v[180:183], v[100:103]
	v_mfma_f32_16x16x32_bf16 v[96:99], v[156:159], v[180:183], v[96:99]
	v_mfma_f32_16x16x32_bf16 v[84:87], v[148:151], v[188:191], v[84:87]
	v_mfma_f32_16x16x32_bf16 v[80:83], v[156:159], v[188:191], v[80:83]
	v_mfma_f32_16x16x32_bf16 v[68:71], v[148:151], v[196:199], v[68:71]
	v_mfma_f32_16x16x32_bf16 v[64:67], v[156:159], v[196:199], v[64:67]
	s_setprio 0
	s_barrier
	s_mov_b32 m0, s35
	s_mov_b32 s6, s38
	s_mov_b32 s7, s39
	buffer_load_dwordx4 v169, s[4:7], s55 offen lds
	s_mov_b32 m0, s41
	ds_read_b128 v[160:163], v175 offset:16384
	s_add_i32 s67, s55, s33
	buffer_load_dwordx4 v171, s[4:7], s55 offen lds
	s_mov_b32 m0, s34
	ds_read_b128 v[164:167], v175 offset:17408
	buffer_load_dwordx4 v168, s[36:39], s66 offen lds
	s_mov_b32 m0, s44
	ds_read_b128 v[176:179], v175 offset:18432
	buffer_load_dwordx4 v170, s[36:39], s66 offen lds
	ds_read_b128 v[180:183], v175 offset:19456
	ds_read_b128 v[184:187], v175 offset:20480
	ds_read_b128 v[188:191], v175 offset:21504
	ds_read_b128 v[192:195], v175 offset:22528
	ds_read_b128 v[196:199], v175 offset:23552
	s_waitcnt vmcnt(6)
	s_waitcnt lgkmcnt(0)
	s_barrier
	s_setprio 1
	v_mfma_f32_16x16x32_bf16 v[60:63], v[120:123], v[160:163], 0
	v_mfma_f32_16x16x32_bf16 v[56:59], v[132:135], v[160:163], 0
	v_mfma_f32_16x16x32_bf16 v[44:47], v[120:123], v[176:179], 0
	v_mfma_f32_16x16x32_bf16 v[40:43], v[132:135], v[176:179], 0
	v_mfma_f32_16x16x32_bf16 v[28:31], v[120:123], v[184:187], 0
	v_mfma_f32_16x16x32_bf16 v[24:27], v[132:135], v[184:187], 0
	v_mfma_f32_16x16x32_bf16 v[12:15], v[120:123], v[192:195], 0
	v_mfma_f32_16x16x32_bf16 v[8:11], v[132:135], v[192:195], 0
	v_mfma_f32_16x16x32_bf16 v[60:63], v[124:127], v[164:167], v[60:63]
	v_mfma_f32_16x16x32_bf16 v[56:59], v[136:139], v[164:167], v[56:59]
	v_mfma_f32_16x16x32_bf16 v[44:47], v[124:127], v[180:183], v[44:47]
	v_mfma_f32_16x16x32_bf16 v[40:43], v[136:139], v[180:183], v[40:43]
	v_mfma_f32_16x16x32_bf16 v[28:31], v[124:127], v[188:191], v[28:31]
	v_mfma_f32_16x16x32_bf16 v[24:27], v[136:139], v[188:191], v[24:27]
	v_mfma_f32_16x16x32_bf16 v[12:15], v[124:127], v[196:199], v[12:15]
	v_mfma_f32_16x16x32_bf16 v[8:11], v[136:139], v[196:199], v[8:11]
	v_mfma_f32_16x16x32_bf16 v[52:55], v[144:147], v[160:163], 0
	v_mfma_f32_16x16x32_bf16 v[48:51], v[152:155], v[160:163], 0
	v_mfma_f32_16x16x32_bf16 v[36:39], v[144:147], v[176:179], 0
	v_mfma_f32_16x16x32_bf16 v[32:35], v[152:155], v[176:179], 0
	v_mfma_f32_16x16x32_bf16 v[20:23], v[144:147], v[184:187], 0
	v_mfma_f32_16x16x32_bf16 v[16:19], v[152:155], v[184:187], 0
	v_mfma_f32_16x16x32_bf16 v[4:7], v[144:147], v[192:195], 0
	v_mfma_f32_16x16x32_bf16 v[0:3], v[152:155], v[192:195], 0
	v_mfma_f32_16x16x32_bf16 v[52:55], v[148:151], v[164:167], v[52:55]
	v_mfma_f32_16x16x32_bf16 v[48:51], v[156:159], v[164:167], v[48:51]
	v_mfma_f32_16x16x32_bf16 v[36:39], v[148:151], v[180:183], v[36:39]
	v_mfma_f32_16x16x32_bf16 v[32:35], v[156:159], v[180:183], v[32:35]
	v_mfma_f32_16x16x32_bf16 v[20:23], v[148:151], v[188:191], v[20:23]
	v_mfma_f32_16x16x32_bf16 v[16:19], v[156:159], v[188:191], v[16:19]
	v_mfma_f32_16x16x32_bf16 v[4:7], v[148:151], v[196:199], v[4:7]
	v_mfma_f32_16x16x32_bf16 v[0:3], v[156:159], v[196:199], v[0:3]
	s_setprio 0
	s_barrier
; #define PG8_STAGE(bufoff, rs_, soff_, voff) do { _Pragma("unroll") for (int _i = 0; _i < 2; ++_i) \
;         __builtin_amdgcn_raw_ptr_buffer_load_lds(rs_, (LAS void*)(lds + (bufoff) + ldsw + _i * 8192), 16, (int)(voff)[_i], (int)(soff_), 0, 0); } while (0)
; #define PG8_LDA(dst, b, h) do { _Pragma("unroll") for (int m = 0; m < 4; ++m) dst[m] = PG8_LD2(lds + PG8_SA(b, h) + aoff + m * 2048); } while (0)
; #define PG8_LDB(dst, b, h) do { _Pragma("unroll") for (int n = 0; n < 2; ++n) dst[n] = PG8_LD2(lds + PG8_SB(b, h) + boff + n * 2048); } while (0)
; #define PG8_WAIT_V(n) asm volatile("s_waitcnt vmcnt(" #n ")" ::: "memory")
; #define PG8_WAIT_L(n) asm volatile("s_waitcnt lgkmcnt(" #n ")" ::: "memory")
; #define PG8_BAR __builtin_amdgcn_s_barrier()
; #define PG8_SCHED __builtin_amdgcn_sched_barrier(0)
; template <class Epi, class Sched, bool ALIGN_EPI = false, bool SP2 = false, bool FP8 = false>
; __device__ __forceinline__ void gemm_phase(LAS unsigned char* lds, const Gemm g, const Sched& S, const Epi& E, int wbase) {
;     ...
;         for (int t = 0; t < nt; t += 2) {
;     ...
;             PG8_LDB(B0, 1, 0); PG8_LDB(B1, 1, 1); PG8_SCHED; PG8_LDA(At, 1, 0); PG8_STAGE(PG8_SA(0, 1), rA2, a2 + hstep, voffA);
;             PG8_WAIT_V(8); PG8_WAIT_L(0); PG8_BAR; PG8_MMA(0, 0, At, B0); PG8_MMA(0, 1, At, B1); PG8_BAR; PG8_SCHED;
;             PG8_LDA(At, 1, 1); PG8_STAGE(PG8_SB(1, 0), rB2, b3, voffB); PG8_STAGE(PG8_SB(1, 1), rB2, b3 + hstep, voffB); PG8_STAGE(PG8_SA(1, 0), rA2, a3, voffA);
;             PG8_WAIT_V(8); PG8_WAIT_L(0); PG8_BAR; PG8_MMA(1, 0, At, B0); PG8_MMA(1, 1, At, B1); PG8_BAR; PG8_SCHED;
	s_mov_b32 m0, s42
	s_nop 0
	buffer_load_dwordx4 v169, s[4:7], s67 offen lds
	s_mov_b32 m0, s43
	s_nop 0
	buffer_load_dwordx4 v171, s[4:7], s67 offen lds
	v_add_u32_e32 v136, 0x18000, v174
	v_add_u32_e32 v156, 0x1c000, v174
	ds_read_b128 v[120:123], v136
	ds_read_b128 v[124:127], v136 offset:1024
	ds_read_b128 v[132:135], v136 offset:2048
	ds_read_b128 v[136:139], v136 offset:3072
	ds_read_b128 v[144:147], v156
	ds_read_b128 v[148:151], v156 offset:1024
	ds_read_b128 v[152:155], v156 offset:2048
	ds_read_b128 v[156:159], v156 offset:3072
	s_add_i32 s66, s66, s33
	s_mov_b32 m0, s45
	ds_read_b128 v[160:163], v175 offset:32768
	ds_read_b128 v[164:167], v175 offset:33792
	ds_read_b128 v[176:179], v175 offset:34816
	ds_read_b128 v[180:183], v175 offset:35840
	ds_read_b128 v[184:187], v175 offset:36864
	ds_read_b128 v[188:191], v175 offset:37888
	ds_read_b128 v[192:195], v175 offset:38912
	ds_read_b128 v[196:199], v175 offset:39936
	buffer_load_dwordx4 v168, s[36:39], s66 offen lds
	s_mov_b32 m0, s46
	s_nop 0
	buffer_load_dwordx4 v170, s[36:39], s66 offen lds
	s_waitcnt vmcnt(8)
	s_waitcnt lgkmcnt(0)
	s_barrier
	s_setprio 1
	v_mfma_f32_16x16x32_bf16 v[140:143], v[120:123], v[160:163], v[140:143]
	v_mfma_f32_16x16x32_bf16 v[128:131], v[132:135], v[160:163], v[128:131]
	v_mfma_f32_16x16x32_bf16 v[108:111], v[120:123], v[176:179], v[108:111]
	v_mfma_f32_16x16x32_bf16 v[104:107], v[132:135], v[176:179], v[104:107]
	v_mfma_f32_16x16x32_bf16 v[92:95], v[120:123], v[184:187], v[92:95]
	v_mfma_f32_16x16x32_bf16 v[88:91], v[132:135], v[184:187], v[88:91]
	v_mfma_f32_16x16x32_bf16 v[76:79], v[120:123], v[192:195], v[76:79]
	v_mfma_f32_16x16x32_bf16 v[72:75], v[132:135], v[192:195], v[72:75]
	v_mfma_f32_16x16x32_bf16 v[140:143], v[124:127], v[164:167], v[140:143]
	v_mfma_f32_16x16x32_bf16 v[128:131], v[136:139], v[164:167], v[128:131]
	v_mfma_f32_16x16x32_bf16 v[108:111], v[124:127], v[180:183], v[108:111]
	v_mfma_f32_16x16x32_bf16 v[104:107], v[136:139], v[180:183], v[104:107]
	v_mfma_f32_16x16x32_bf16 v[92:95], v[124:127], v[188:191], v[92:95]
	v_mfma_f32_16x16x32_bf16 v[88:91], v[136:139], v[188:191], v[88:91]
	v_mfma_f32_16x16x32_bf16 v[76:79], v[124:127], v[196:199], v[76:79]
	v_mfma_f32_16x16x32_bf16 v[72:75], v[136:139], v[196:199], v[72:75]
	v_mfma_f32_16x16x32_bf16 v[116:119], v[144:147], v[160:163], v[116:119]
	v_mfma_f32_16x16x32_bf16 v[112:115], v[152:155], v[160:163], v[112:115]
	v_mfma_f32_16x16x32_bf16 v[100:103], v[144:147], v[176:179], v[100:103]
	v_mfma_f32_16x16x32_bf16 v[96:99], v[152:155], v[176:179], v[96:99]
	v_mfma_f32_16x16x32_bf16 v[84:87], v[144:147], v[184:187], v[84:87]
	v_mfma_f32_16x16x32_bf16 v[80:83], v[152:155], v[184:187], v[80:83]
	v_mfma_f32_16x16x32_bf16 v[68:71], v[144:147], v[192:195], v[68:71]
	v_mfma_f32_16x16x32_bf16 v[64:67], v[152:155], v[192:195], v[64:67]
	v_mfma_f32_16x16x32_bf16 v[116:119], v[148:151], v[164:167], v[116:119]
	v_mfma_f32_16x16x32_bf16 v[112:115], v[156:159], v[164:167], v[112:115]
	v_mfma_f32_16x16x32_bf16 v[100:103], v[148:151], v[180:183], v[100:103]
	v_mfma_f32_16x16x32_bf16 v[96:99], v[156:159], v[180:183], v[96:99]
	v_mfma_f32_16x16x32_bf16 v[84:87], v[148:151], v[188:191], v[84:87]
	v_mfma_f32_16x16x32_bf16 v[80:83], v[156:159], v[188:191], v[80:83]
	v_mfma_f32_16x16x32_bf16 v[68:71], v[148:151], v[196:199], v[68:71]
	v_mfma_f32_16x16x32_bf16 v[64:67], v[156:159], v[196:199], v[64:67]
	s_setprio 0
	s_barrier
	s_mov_b32 m0, s47
	s_bitset1_b32 s55, 7
	buffer_load_dwordx4 v169, s[4:7], s55 offen lds
	s_mov_b32 m0, s48
	ds_read_b128 v[160:163], v175 offset:49152
	buffer_load_dwordx4 v171, s[4:7], s55 offen lds
	s_add_i32 s55, s55, s33
	s_mov_b32 m0, s56
	ds_read_b128 v[164:167], v175 offset:50176
	buffer_load_dwordx4 v169, s[4:7], s55 offen lds
	s_mov_b32 m0, s57
	ds_read_b128 v[176:179], v175 offset:51200
	buffer_load_dwordx4 v171, s[4:7], s55 offen lds
	s_mov_b32 m0, s52
	ds_read_b128 v[180:183], v175 offset:52224
	buffer_load_dwordx4 v168, s[36:39], s54 offen lds
	s_mov_b32 m0, s53
	ds_read_b128 v[184:187], v175 offset:53248
	buffer_load_dwordx4 v170, s[36:39], s54 offen lds
	ds_read_b128 v[188:191], v175 offset:54272
	ds_read_b128 v[192:195], v175 offset:55296
	ds_read_b128 v[196:199], v175 offset:56320
	s_waitcnt vmcnt(8)
	s_waitcnt lgkmcnt(0)
	s_barrier
	s_setprio 1
	v_mfma_f32_16x16x32_bf16 v[60:63], v[120:123], v[160:163], v[60:63]
	v_mfma_f32_16x16x32_bf16 v[56:59], v[132:135], v[160:163], v[56:59]
	v_mfma_f32_16x16x32_bf16 v[44:47], v[120:123], v[176:179], v[44:47]
	v_mfma_f32_16x16x32_bf16 v[40:43], v[132:135], v[176:179], v[40:43]
	v_mfma_f32_16x16x32_bf16 v[28:31], v[120:123], v[184:187], v[28:31]
	v_mfma_f32_16x16x32_bf16 v[24:27], v[132:135], v[184:187], v[24:27]
	v_mfma_f32_16x16x32_bf16 v[12:15], v[120:123], v[192:195], v[12:15]
	v_mfma_f32_16x16x32_bf16 v[8:11], v[132:135], v[192:195], v[8:11]
	v_mfma_f32_16x16x32_bf16 v[60:63], v[124:127], v[164:167], v[60:63]
	v_mfma_f32_16x16x32_bf16 v[56:59], v[136:139], v[164:167], v[56:59]
	v_mfma_f32_16x16x32_bf16 v[44:47], v[124:127], v[180:183], v[44:47]
	v_mfma_f32_16x16x32_bf16 v[40:43], v[136:139], v[180:183], v[40:43]
	v_mfma_f32_16x16x32_bf16 v[28:31], v[124:127], v[188:191], v[28:31]
	v_mfma_f32_16x16x32_bf16 v[24:27], v[136:139], v[188:191], v[24:27]
	v_mfma_f32_16x16x32_bf16 v[12:15], v[124:127], v[196:199], v[12:15]
	v_mfma_f32_16x16x32_bf16 v[8:11], v[136:139], v[196:199], v[8:11]
	v_mfma_f32_16x16x32_bf16 v[52:55], v[144:147], v[160:163], v[52:55]
	v_mfma_f32_16x16x32_bf16 v[48:51], v[152:155], v[160:163], v[48:51]
	v_mfma_f32_16x16x32_bf16 v[36:39], v[144:147], v[176:179], v[36:39]
	v_mfma_f32_16x16x32_bf16 v[32:35], v[152:155], v[176:179], v[32:35]
	v_mfma_f32_16x16x32_bf16 v[20:23], v[144:147], v[184:187], v[20:23]
	v_mfma_f32_16x16x32_bf16 v[16:19], v[152:155], v[184:187], v[16:19]
	v_mfma_f32_16x16x32_bf16 v[4:7], v[144:147], v[192:195], v[4:7]
	v_mfma_f32_16x16x32_bf16 v[0:3], v[152:155], v[192:195], v[0:3]
	v_mfma_f32_16x16x32_bf16 v[52:55], v[148:151], v[164:167], v[52:55]
	v_mfma_f32_16x16x32_bf16 v[48:51], v[156:159], v[164:167], v[48:51]
	v_mfma_f32_16x16x32_bf16 v[36:39], v[148:151], v[180:183], v[36:39]
	v_mfma_f32_16x16x32_bf16 v[32:35], v[156:159], v[180:183], v[32:35]
	v_mfma_f32_16x16x32_bf16 v[20:23], v[148:151], v[188:191], v[20:23]
	v_mfma_f32_16x16x32_bf16 v[16:19], v[156:159], v[188:191], v[16:19]
	v_mfma_f32_16x16x32_bf16 v[4:7], v[148:151], v[196:199], v[4:7]
	v_mfma_f32_16x16x32_bf16 v[0:3], v[156:159], v[196:199], v[0:3]
	s_setprio 0
	s_barrier
	s_add_i32 s63, s63, 2
	s_addk_i32 s61, 0x100
	s_addk_i32 s62, 0x100
	s_cmp_ge_i32 s63, s65
	s_cbranch_scc0 .LBB0_1944
	s_branch .Lzp_after_1944
; #define PG8_STAGE(bufoff, rs_, soff_, voff) do { _Pragma("unroll") for (int _i = 0; _i < 2; ++_i) \
;         __builtin_amdgcn_raw_ptr_buffer_load_lds(rs_, (LAS void*)(lds + (bufoff) + ldsw + _i * 8192), 16, (int)(voff)[_i], (int)(soff_), 0, 0); } while (0)
; #define PG8_LDA(dst, b, h) do { _Pragma("unroll") for (int m = 0; m < 4; ++m) dst[m] = PG8_LD2(lds + PG8_SA(b, h) + aoff + m * 2048); } while (0)
; #define PG8_LDB(dst, b, h) do { _Pragma("unroll") for (int n = 0; n < 2; ++n) dst[n] = PG8_LD2(lds + PG8_SB(b, h) + boff + n * 2048); } while (0)
; #define PG8_WAIT_V(n) asm volatile("s_waitcnt vmcnt(" #n ")" ::: "memory")
; #define PG8_WAIT_L(n) asm volatile("s_waitcnt lgkmcnt(" #n ")" ::: "memory")
; #define PG8_BAR __builtin_amdgcn_s_barrier()
; #define PG8_SCHED __builtin_amdgcn_sched_barrier(0)
; template <class Epi, class Sched, bool ALIGN_EPI = false, bool SP2 = false, bool FP8 = false>
; __device__ __forceinline__ void gemm_phase(LAS unsigned char* lds, const Gemm g, const Sched& S, const Epi& E, int wbase) {
;     ...
;         for (int t = 0; t < nt; t += 2) {
;             const bool last = (t == nt - 2);
;             const unsigned a1 = cA + (unsigned)(t + 1) * kstep;
;             const unsigned a2 = last ? nA : cA + (unsigned)(t + 2) * kstep, b2 = last ? nB : cB + (unsigned)(t + 2) * kstep; const rsrc_t rA2 = (Sched::TWO && last) ? rAn : rAc, rB2 = (Sched::TWO && last) ? rBn : rBc;
;             const unsigned a3 = a2 + kstep, b3 = b2 + kstep;
;             if (last && has_next) S.a_ready(nxt);
;             if constexpr (SP2) {
;             PG8_LDB(B0, 0, 0); PG8_LDB(B1, 0, 1); PG8_SCHED; PG8_LDA(At, 0, 0); PG8_STAGE(PG8_SA(1, 1), rAc, a1 + hstep, voffA);
;             PG8_WAIT_V(8); PG8_WAIT_L(0); PG8_BAR; PG8_MMA(0, 0, At, B0); PG8_MMA(0, 1, At, B1); PG8_BAR; PG8_SCHED;
;             PG8_LDA(At, 0, 1); PG8_STAGE(PG8_SB(0, 0), rB2, b2, voffB); PG8_STAGE(PG8_SB(0, 1), rB2, b2 + hstep, voffB); PG8_STAGE(PG8_SA(0, 0), rA2, a2, voffA);
;             PG8_WAIT_V(8); PG8_WAIT_L(0); PG8_BAR; PG8_MMA(1, 0, At, B0); PG8_MMA(1, 1, At, B1); PG8_BAR; PG8_SCHED;
.LBB0_1944:
	v_add_u32_e32 v136, 0x10000, v174
	v_add_u32_e32 v156, 0x14000, v174
	ds_read_b128 v[120:123], v136
	ds_read_b128 v[124:127], v136 offset:1024
	ds_read_b128 v[132:135], v136 offset:2048
	ds_read_b128 v[136:139], v136 offset:3072
	ds_read_b128 v[144:147], v156
	ds_read_b128 v[148:151], v156 offset:1024
	ds_read_b128 v[152:155], v156 offset:2048
	ds_read_b128 v[156:159], v156 offset:3072
	s_add_i32 s6, s61, 0x80
	s_cmp_eq_u32 s77, s63
	s_cselect_b32 s66, s29, s6
	s_cselect_b32 s55, s60, s62
	s_or_b32 s54, s66, 0x80
	s_add_i32 s6, s33, s61
	s_mov_b32 m0, s79
	ds_read_b128 v[160:163], v175
	ds_read_b128 v[164:167], v175 offset:1024
	ds_read_b128 v[176:179], v175 offset:2048
	ds_read_b128 v[180:183], v175 offset:3072
	ds_read_b128 v[184:187], v175 offset:4096
	ds_read_b128 v[188:191], v175 offset:5120
	ds_read_b128 v[192:195], v175 offset:6144
	ds_read_b128 v[196:199], v175 offset:7168
	buffer_load_dwordx4 v168, s[36:39], s6 offen lds
	s_mov_b32 m0, s82
	s_nop 0
	buffer_load_dwordx4 v170, s[36:39], s6 offen lds
	s_waitcnt vmcnt(8)
	s_waitcnt lgkmcnt(0)
	s_barrier
	s_setprio 1
	v_mfma_f32_16x16x32_bf16 v[140:143], v[120:123], v[160:163], v[140:143]
	v_mfma_f32_16x16x32_bf16 v[128:131], v[132:135], v[160:163], v[128:131]
	v_mfma_f32_16x16x32_bf16 v[108:111], v[120:123], v[176:179], v[108:111]
	v_mfma_f32_16x16x32_bf16 v[104:107], v[132:135], v[176:179], v[104:107]
	v_mfma_f32_16x16x32_bf16 v[92:95], v[120:123], v[184:187], v[92:95]
	v_mfma_f32_16x16x32_bf16 v[88:91], v[132:135], v[184:187], v[88:91]
	v_mfma_f32_16x16x32_bf16 v[76:79], v[120:123], v[192:195], v[76:79]
	v_mfma_f32_16x16x32_bf16 v[72:75], v[132:135], v[192:195], v[72:75]
	v_mfma_f32_16x16x32_bf16 v[140:143], v[124:127], v[164:167], v[140:143]
	v_mfma_f32_16x16x32_bf16 v[128:131], v[136:139], v[164:167], v[128:131]
	v_mfma_f32_16x16x32_bf16 v[108:111], v[124:127], v[180:183], v[108:111]
	v_mfma_f32_16x16x32_bf16 v[104:107], v[136:139], v[180:183], v[104:107]
	v_mfma_f32_16x16x32_bf16 v[92:95], v[124:127], v[188:191], v[92:95]
	v_mfma_f32_16x16x32_bf16 v[88:91], v[136:139], v[188:191], v[88:91]
	v_mfma_f32_16x16x32_bf16 v[76:79], v[124:127], v[196:199], v[76:79]
	v_mfma_f32_16x16x32_bf16 v[72:75], v[136:139], v[196:199], v[72:75]
	v_mfma_f32_16x16x32_bf16 v[116:119], v[144:147], v[160:163], v[116:119]
	v_mfma_f32_16x16x32_bf16 v[112:115], v[152:155], v[160:163], v[112:115]
	v_mfma_f32_16x16x32_bf16 v[100:103], v[144:147], v[176:179], v[100:103]
	v_mfma_f32_16x16x32_bf16 v[96:99], v[152:155], v[176:179], v[96:99]
	v_mfma_f32_16x16x32_bf16 v[84:87], v[144:147], v[184:187], v[84:87]
	v_mfma_f32_16x16x32_bf16 v[80:83], v[152:155], v[184:187], v[80:83]
	v_mfma_f32_16x16x32_bf16 v[68:71], v[144:147], v[192:195], v[68:71]
	v_mfma_f32_16x16x32_bf16 v[64:67], v[152:155], v[192:195], v[64:67]
	v_mfma_f32_16x16x32_bf16 v[116:119], v[148:151], v[164:167], v[116:119]
	v_mfma_f32_16x16x32_bf16 v[112:115], v[156:159], v[164:167], v[112:115]
	v_mfma_f32_16x16x32_bf16 v[100:103], v[148:151], v[180:183], v[100:103]
	v_mfma_f32_16x16x32_bf16 v[96:99], v[156:159], v[180:183], v[96:99]
	v_mfma_f32_16x16x32_bf16 v[84:87], v[148:151], v[188:191], v[84:87]
	v_mfma_f32_16x16x32_bf16 v[80:83], v[156:159], v[188:191], v[80:83]
	v_mfma_f32_16x16x32_bf16 v[68:71], v[148:151], v[196:199], v[68:71]
	v_mfma_f32_16x16x32_bf16 v[64:67], v[156:159], v[196:199], v[64:67]
	s_setprio 0
	s_barrier
	s_mov_b32 m0, s35
	s_mov_b32 s6, s38
	s_mov_b32 s7, s39
	buffer_load_dwordx4 v169, s[4:7], s55 offen lds
	s_mov_b32 m0, s41
	ds_read_b128 v[160:163], v175 offset:16384
	s_add_i32 s67, s55, s33
	buffer_load_dwordx4 v171, s[4:7], s55 offen lds
	s_mov_b32 m0, s34
	ds_read_b128 v[164:167], v175 offset:17408
	buffer_load_dwordx4 v168, s[36:39], s66 offen lds
	s_mov_b32 m0, s44
	ds_read_b128 v[176:179], v175 offset:18432
	buffer_load_dwordx4 v170, s[36:39], s66 offen lds
	ds_read_b128 v[180:183], v175 offset:19456
	ds_read_b128 v[184:187], v175 offset:20480
	ds_read_b128 v[188:191], v175 offset:21504
	ds_read_b128 v[192:195], v175 offset:22528
	ds_read_b128 v[196:199], v175 offset:23552
	s_waitcnt vmcnt(6)
	s_waitcnt lgkmcnt(0)
	s_barrier
	s_setprio 1
	v_mfma_f32_16x16x32_bf16 v[60:63], v[120:123], v[160:163], v[60:63]
	v_mfma_f32_16x16x32_bf16 v[56:59], v[132:135], v[160:163], v[56:59]
	v_mfma_f32_16x16x32_bf16 v[44:47], v[120:123], v[176:179], v[44:47]
	v_mfma_f32_16x16x32_bf16 v[40:43], v[132:135], v[176:179], v[40:43]
	v_mfma_f32_16x16x32_bf16 v[28:31], v[120:123], v[184:187], v[28:31]
	v_mfma_f32_16x16x32_bf16 v[24:27], v[132:135], v[184:187], v[24:27]
	v_mfma_f32_16x16x32_bf16 v[12:15], v[120:123], v[192:195], v[12:15]
	v_mfma_f32_16x16x32_bf16 v[8:11], v[132:135], v[192:195], v[8:11]
	v_mfma_f32_16x16x32_bf16 v[60:63], v[124:127], v[164:167], v[60:63]
	v_mfma_f32_16x16x32_bf16 v[56:59], v[136:139], v[164:167], v[56:59]
	v_mfma_f32_16x16x32_bf16 v[44:47], v[124:127], v[180:183], v[44:47]
	v_mfma_f32_16x16x32_bf16 v[40:43], v[136:139], v[180:183], v[40:43]
	v_mfma_f32_16x16x32_bf16 v[28:31], v[124:127], v[188:191], v[28:31]
	v_mfma_f32_16x16x32_bf16 v[24:27], v[136:139], v[188:191], v[24:27]
	v_mfma_f32_16x16x32_bf16 v[12:15], v[124:127], v[196:199], v[12:15]
	v_mfma_f32_16x16x32_bf16 v[8:11], v[136:139], v[196:199], v[8:11]
	v_mfma_f32_16x16x32_bf16 v[52:55], v[144:147], v[160:163], v[52:55]
	v_mfma_f32_16x16x32_bf16 v[48:51], v[152:155], v[160:163], v[48:51]
	v_mfma_f32_16x16x32_bf16 v[36:39], v[144:147], v[176:179], v[36:39]
	v_mfma_f32_16x16x32_bf16 v[32:35], v[152:155], v[176:179], v[32:35]
	v_mfma_f32_16x16x32_bf16 v[20:23], v[144:147], v[184:187], v[20:23]
	v_mfma_f32_16x16x32_bf16 v[16:19], v[152:155], v[184:187], v[16:19]
	v_mfma_f32_16x16x32_bf16 v[4:7], v[144:147], v[192:195], v[4:7]
	v_mfma_f32_16x16x32_bf16 v[0:3], v[152:155], v[192:195], v[0:3]
	v_mfma_f32_16x16x32_bf16 v[52:55], v[148:151], v[164:167], v[52:55]
	v_mfma_f32_16x16x32_bf16 v[48:51], v[156:159], v[164:167], v[48:51]
	v_mfma_f32_16x16x32_bf16 v[36:39], v[148:151], v[180:183], v[36:39]
	v_mfma_f32_16x16x32_bf16 v[32:35], v[156:159], v[180:183], v[32:35]
	v_mfma_f32_16x16x32_bf16 v[20:23], v[148:151], v[188:191], v[20:23]
	v_mfma_f32_16x16x32_bf16 v[16:19], v[156:159], v[188:191], v[16:19]
	v_mfma_f32_16x16x32_bf16 v[4:7], v[148:151], v[196:199], v[4:7]
	v_mfma_f32_16x16x32_bf16 v[0:3], v[156:159], v[196:199], v[0:3]
	s_setprio 0
	s_barrier
; #define PG8_STAGE(bufoff, rs_, soff_, voff) do { _Pragma("unroll") for (int _i = 0; _i < 2; ++_i) \
;         __builtin_amdgcn_raw_ptr_buffer_load_lds(rs_, (LAS void*)(lds + (bufoff) + ldsw + _i * 8192), 16, (int)(voff)[_i], (int)(soff_), 0, 0); } while (0)
; #define PG8_LDA(dst, b, h) do { _Pragma("unroll") for (int m = 0; m < 4; ++m) dst[m] = PG8_LD2(lds + PG8_SA(b, h) + aoff + m * 2048); } while (0)
; #define PG8_LDB(dst, b, h) do { _Pragma("unroll") for (int n = 0; n < 2; ++n) dst[n] = PG8_LD2(lds + PG8_SB(b, h) + boff + n * 2048); } while (0)
; #define PG8_WAIT_V(n) asm volatile("s_waitcnt vmcnt(" #n ")" ::: "memory")
; #define PG8_WAIT_L(n) asm volatile("s_waitcnt lgkmcnt(" #n ")" ::: "memory")
; #define PG8_BAR __builtin_amdgcn_s_barrier()
; #define PG8_SCHED __builtin_amdgcn_sched_barrier(0)
; template <class Epi, class Sched, bool ALIGN_EPI = false, bool SP2 = false, bool FP8 = false>
; __device__ __forceinline__ void gemm_phase(LAS unsigned char* lds, const Gemm g, const Sched& S, const Epi& E, int wbase) {
;     ...
;         for (int t = 0; t < nt; t += 2) {
;             const bool last = (t == nt - 2);
;             const unsigned a1 = cA + (unsigned)(t + 1) * kstep;
;     ...
;             PG8_LDA(At, 0, 1); PG8_STAGE(PG8_SB(0, 0), rB2, b2, voffB); PG8_STAGE(PG8_SB(0, 1), rB2, b2 + hstep, voffB); PG8_STAGE(PG8_SA(0, 0), rA2, a2, voffA);
;             PG8_WAIT_V(8); PG8_WAIT_L(0); PG8_BAR; PG8_MMA(1, 0, At, B0); PG8_MMA(1, 1, At, B1); PG8_BAR; PG8_SCHED;
;             PG8_LDB(B0, 1, 0); PG8_LDB(B1, 1, 1); PG8_SCHED; PG8_LDA(At, 1, 0); PG8_STAGE(PG8_SA(0, 1), rA2, a2 + hstep, voffA);
;             PG8_WAIT_V(8); PG8_WAIT_L(0); PG8_BAR; PG8_MMA(0, 0, At, B0); PG8_MMA(0, 1, At, B1); PG8_BAR; PG8_SCHED;
;             PG8_LDA(At, 1, 1); PG8_STAGE(PG8_SB(1, 0), rB2, b3, voffB); PG8_STAGE(PG8_SB(1, 1), rB2, b3 + hstep, voffB); PG8_STAGE(PG8_SA(1, 0), rA2, a3, voffA);
;             PG8_WAIT_V(8); PG8_WAIT_L(0); PG8_BAR; PG8_MMA(1, 0, At, B0); PG8_MMA(1, 1, At, B1); PG8_BAR; PG8_SCHED;
	s_mov_b32 m0, s42
	s_nop 0
	buffer_load_dwordx4 v169, s[4:7], s67 offen lds
	s_mov_b32 m0, s43
	s_nop 0
	buffer_load_dwordx4 v171, s[4:7], s67 offen lds
	v_add_u32_e32 v136, 0x18000, v174
	v_add_u32_e32 v156, 0x1c000, v174
	ds_read_b128 v[120:123], v136
	ds_read_b128 v[124:127], v136 offset:1024
	ds_read_b128 v[132:135], v136 offset:2048
	ds_read_b128 v[136:139], v136 offset:3072
	ds_read_b128 v[144:147], v156
	ds_read_b128 v[148:151], v156 offset:1024
	ds_read_b128 v[152:155], v156 offset:2048
	ds_read_b128 v[156:159], v156 offset:3072
	s_add_i32 s66, s66, s33
	s_mov_b32 m0, s45
	ds_read_b128 v[160:163], v175 offset:32768
	ds_read_b128 v[164:167], v175 offset:33792
	ds_read_b128 v[176:179], v175 offset:34816
	ds_read_b128 v[180:183], v175 offset:35840
	ds_read_b128 v[184:187], v175 offset:36864
	ds_read_b128 v[188:191], v175 offset:37888
	ds_read_b128 v[192:195], v175 offset:38912
	ds_read_b128 v[196:199], v175 offset:39936
	buffer_load_dwordx4 v168, s[36:39], s66 offen lds
	s_mov_b32 m0, s46
	s_nop 0
	buffer_load_dwordx4 v170, s[36:39], s66 offen lds
	s_waitcnt vmcnt(8)
	s_waitcnt lgkmcnt(0)
	s_barrier
	s_setprio 1
	v_mfma_f32_16x16x32_bf16 v[140:143], v[120:123], v[160:163], v[140:143]
	v_mfma_f32_16x16x32_bf16 v[128:131], v[132:135], v[160:163], v[128:131]
	v_mfma_f32_16x16x32_bf16 v[108:111], v[120:123], v[176:179], v[108:111]
	v_mfma_f32_16x16x32_bf16 v[104:107], v[132:135], v[176:179], v[104:107]
	v_mfma_f32_16x16x32_bf16 v[92:95], v[120:123], v[184:187], v[92:95]
	v_mfma_f32_16x16x32_bf16 v[88:91], v[132:135], v[184:187], v[88:91]
	v_mfma_f32_16x16x32_bf16 v[76:79], v[120:123], v[192:195], v[76:79]
	v_mfma_f32_16x16x32_bf16 v[72:75], v[132:135], v[192:195], v[72:75]
	v_mfma_f32_16x16x32_bf16 v[140:143], v[124:127], v[164:167], v[140:143]
	v_mfma_f32_16x16x32_bf16 v[128:131], v[136:139], v[164:167], v[128:131]
	v_mfma_f32_16x16x32_bf16 v[108:111], v[124:127], v[180:183], v[108:111]
	v_mfma_f32_16x16x32_bf16 v[104:107], v[136:139], v[180:183], v[104:107]
	v_mfma_f32_16x16x32_bf16 v[92:95], v[124:127], v[188:191], v[92:95]
	v_mfma_f32_16x16x32_bf16 v[88:91], v[136:139], v[188:191], v[88:91]
	v_mfma_f32_16x16x32_bf16 v[76:79], v[124:127], v[196:199], v[76:79]
	v_mfma_f32_16x16x32_bf16 v[72:75], v[136:139], v[196:199], v[72:75]
	v_mfma_f32_16x16x32_bf16 v[116:119], v[144:147], v[160:163], v[116:119]
	v_mfma_f32_16x16x32_bf16 v[112:115], v[152:155], v[160:163], v[112:115]
	v_mfma_f32_16x16x32_bf16 v[100:103], v[144:147], v[176:179], v[100:103]
	v_mfma_f32_16x16x32_bf16 v[96:99], v[152:155], v[176:179], v[96:99]
	v_mfma_f32_16x16x32_bf16 v[84:87], v[144:147], v[184:187], v[84:87]
	v_mfma_f32_16x16x32_bf16 v[80:83], v[152:155], v[184:187], v[80:83]
	v_mfma_f32_16x16x32_bf16 v[68:71], v[144:147], v[192:195], v[68:71]
	v_mfma_f32_16x16x32_bf16 v[64:67], v[152:155], v[192:195], v[64:67]
	v_mfma_f32_16x16x32_bf16 v[116:119], v[148:151], v[164:167], v[116:119]
	v_mfma_f32_16x16x32_bf16 v[112:115], v[156:159], v[164:167], v[112:115]
	v_mfma_f32_16x16x32_bf16 v[100:103], v[148:151], v[180:183], v[100:103]
	v_mfma_f32_16x16x32_bf16 v[96:99], v[156:159], v[180:183], v[96:99]
	v_mfma_f32_16x16x32_bf16 v[84:87], v[148:151], v[188:191], v[84:87]
	v_mfma_f32_16x16x32_bf16 v[80:83], v[156:159], v[188:191], v[80:83]
	v_mfma_f32_16x16x32_bf16 v[68:71], v[148:151], v[196:199], v[68:71]
	v_mfma_f32_16x16x32_bf16 v[64:67], v[156:159], v[196:199], v[64:67]
	s_setprio 0
	s_barrier
	s_mov_b32 m0, s47
	s_bitset1_b32 s55, 7
	buffer_load_dwordx4 v169, s[4:7], s55 offen lds
	s_mov_b32 m0, s48
	ds_read_b128 v[160:163], v175 offset:49152
	buffer_load_dwordx4 v171, s[4:7], s55 offen lds
	s_add_i32 s55, s55, s33
	s_mov_b32 m0, s56
	ds_read_b128 v[164:167], v175 offset:50176
	buffer_load_dwordx4 v169, s[4:7], s55 offen lds
	s_mov_b32 m0, s57
	ds_read_b128 v[176:179], v175 offset:51200
	buffer_load_dwordx4 v171, s[4:7], s55 offen lds
	s_mov_b32 m0, s52
	ds_read_b128 v[180:183], v175 offset:52224
	buffer_load_dwordx4 v168, s[36:39], s54 offen lds
	s_mov_b32 m0, s53
	ds_read_b128 v[184:187], v175 offset:53248
	buffer_load_dwordx4 v170, s[36:39], s54 offen lds
	ds_read_b128 v[188:191], v175 offset:54272
	ds_read_b128 v[192:195], v175 offset:55296
	ds_read_b128 v[196:199], v175 offset:56320
	s_waitcnt vmcnt(8)
	s_waitcnt lgkmcnt(0)
	s_barrier
	s_setprio 1
	v_mfma_f32_16x16x32_bf16 v[60:63], v[120:123], v[160:163], v[60:63]
	v_mfma_f32_16x16x32_bf16 v[56:59], v[132:135], v[160:163], v[56:59]
	v_mfma_f32_16x16x32_bf16 v[44:47], v[120:123], v[176:179], v[44:47]
	v_mfma_f32_16x16x32_bf16 v[40:43], v[132:135], v[176:179], v[40:43]
	v_mfma_f32_16x16x32_bf16 v[28:31], v[120:123], v[184:187], v[28:31]
	v_mfma_f32_16x16x32_bf16 v[24:27], v[132:135], v[184:187], v[24:27]
	v_mfma_f32_16x16x32_bf16 v[12:15], v[120:123], v[192:195], v[12:15]
	v_mfma_f32_16x16x32_bf16 v[8:11], v[132:135], v[192:195], v[8:11]
	v_mfma_f32_16x16x32_bf16 v[60:63], v[124:127], v[164:167], v[60:63]
	v_mfma_f32_16x16x32_bf16 v[56:59], v[136:139], v[164:167], v[56:59]
	v_mfma_f32_16x16x32_bf16 v[44:47], v[124:127], v[180:183], v[44:47]
	v_mfma_f32_16x16x32_bf16 v[40:43], v[136:139], v[180:183], v[40:43]
	v_mfma_f32_16x16x32_bf16 v[28:31], v[124:127], v[188:191], v[28:31]
	v_mfma_f32_16x16x32_bf16 v[24:27], v[136:139], v[188:191], v[24:27]
	v_mfma_f32_16x16x32_bf16 v[12:15], v[124:127], v[196:199], v[12:15]
	v_mfma_f32_16x16x32_bf16 v[8:11], v[136:139], v[196:199], v[8:11]
	v_mfma_f32_16x16x32_bf16 v[52:55], v[144:147], v[160:163], v[52:55]
	v_mfma_f32_16x16x32_bf16 v[48:51], v[152:155], v[160:163], v[48:51]
	v_mfma_f32_16x16x32_bf16 v[36:39], v[144:147], v[176:179], v[36:39]
	v_mfma_f32_16x16x32_bf16 v[32:35], v[152:155], v[176:179], v[32:35]
	v_mfma_f32_16x16x32_bf16 v[20:23], v[144:147], v[184:187], v[20:23]
	v_mfma_f32_16x16x32_bf16 v[16:19], v[152:155], v[184:187], v[16:19]
	v_mfma_f32_16x16x32_bf16 v[4:7], v[144:147], v[192:195], v[4:7]
	v_mfma_f32_16x16x32_bf16 v[0:3], v[152:155], v[192:195], v[0:3]
	v_mfma_f32_16x16x32_bf16 v[52:55], v[148:151], v[164:167], v[52:55]
	v_mfma_f32_16x16x32_bf16 v[48:51], v[156:159], v[164:167], v[48:51]
	v_mfma_f32_16x16x32_bf16 v[36:39], v[148:151], v[180:183], v[36:39]
	v_mfma_f32_16x16x32_bf16 v[32:35], v[156:159], v[180:183], v[32:35]
	v_mfma_f32_16x16x32_bf16 v[20:23], v[148:151], v[188:191], v[20:23]
	v_mfma_f32_16x16x32_bf16 v[16:19], v[156:159], v[188:191], v[16:19]
	v_mfma_f32_16x16x32_bf16 v[4:7], v[148:151], v[196:199], v[4:7]
	v_mfma_f32_16x16x32_bf16 v[0:3], v[156:159], v[196:199], v[0:3]
	s_setprio 0
	s_barrier
	s_add_i32 s63, s63, 2
	s_addk_i32 s61, 0x100
	s_addk_i32 s62, 0x100
	s_cmp_ge_i32 s63, s65
	s_cbranch_scc0 .LBB0_1944

; #define PG8_STAGE(bufoff, rs_, soff_, voff) do { _Pragma("unroll") for (int _i = 0; _i < 2; ++_i) \
;         __builtin_amdgcn_raw_ptr_buffer_load_lds(rs_, (LAS void*)(lds + (bufoff) + ldsw + _i * 8192), 16, (int)(voff)[_i], (int)(soff_), 0, 0); } while (0)
; #define PG8_LDA(dst, b, h) do { _Pragma("unroll") for (int m = 0; m < 4; ++m) dst[m] = PG8_LD2(lds + PG8_SA(b, h) + aoff + m * 2048); } while (0)
; #define PG8_LDB(dst, b, h) do { _Pragma("unroll") for (int n = 0; n < 2; ++n) dst[n] = PG8_LD2(lds + PG8_SB(b, h) + boff + n * 2048); } while (0)
; #define PG8_WAIT_V(n) asm volatile("s_waitcnt vmcnt(" #n ")" ::: "memory")
; #define PG8_WAIT_L(n) asm volatile("s_waitcnt lgkmcnt(" #n ")" ::: "memory")
; #define PG8_BAR __builtin_amdgcn_s_barrier()
; #define PG8_SCHED __builtin_amdgcn_sched_barrier(0)
; template <class Epi, class Sched, bool ALIGN_EPI = false, bool SP2 = false, bool FP8 = false>
; __device__ __forceinline__ void gemm_phase(LAS unsigned char* lds, const Gemm g, const Sched& S, const Epi& E, int wbase) {
;     ...
;     if constexpr (SP2) {
;         PG8_STAGE(PG8_SB(0, 0), rBc, cB, voffB); PG8_STAGE(PG8_SB(0, 1), rBc, cB + hstep, voffB); PG8_STAGE(PG8_SA(0, 0), rAc, cA, voffA); PG8_STAGE(PG8_SA(0, 1), rAc, cA + hstep, voffA);
;         if (wr == 1) PG8_BAR;
;         PG8_WAIT_V(2); PG8_BAR;
;         PG8_STAGE(PG8_SB(1, 0), rBc, cB + kstep, voffB); PG8_STAGE(PG8_SA(1, 0), rAc, cA + kstep, voffA); PG8_STAGE(PG8_SB(1, 1), rBc, cB + hstep + kstep, voffB);
;         PG8_WAIT_V(6); PG8_BAR;
;     ...
;             PG8_LDB(B0, 0, 0); PG8_LDB(B1, 0, 1); PG8_SCHED; PG8_LDA(At, 0, 0); PG8_STAGE(PG8_SA(1, 1), rAc, a1 + hstep, voffA);
;             PG8_WAIT_V(8); PG8_WAIT_L(0); PG8_BAR; PG8_MMA(0, 0, At, B0); PG8_MMA(0, 1, At, B1); PG8_BAR; PG8_SCHED;
;             PG8_LDA(At, 0, 1); PG8_STAGE(PG8_SB(0, 0), rB2, b2, voffB); PG8_STAGE(PG8_SB(0, 1), rB2, b2 + hstep, voffB); PG8_STAGE(PG8_SA(0, 0), rA2, a2, voffA);
;             PG8_WAIT_V(8); PG8_WAIT_L(0); PG8_BAR; PG8_MMA(1, 0, At, B0); PG8_MMA(1, 1, At, B1); PG8_BAR; PG8_SCHED;
;             PG8_LDB(B0, 1, 0); PG8_LDB(B1, 1, 1); PG8_SCHED; PG8_LDA(At, 1, 0); PG8_STAGE(PG8_SA(0, 1), rA2, a2 + hstep, voffA);
.LBB0_1988:
	s_lshl_b32 s95, s94, 18
	s_andn2_b64 vcc, exec, s[26:27]
	s_lshl_b32 s96, s9, 18
	s_cbranch_vccnz .LBB0_1992
	s_and_b64 s[2:3], s[34:35], exec
	s_waitcnt vmcnt(37)
	s_waitcnt vmcnt(36)
	s_waitcnt vmcnt(35)
	s_waitcnt vmcnt(32)
	s_waitcnt vmcnt(31)
	s_waitcnt vmcnt(28)
	s_waitcnt vmcnt(27)
	s_waitcnt vmcnt(24)
	s_waitcnt vmcnt(23)
	v_mov_b32_e32 v223, 0xff61b1e6
	v_mov_b32_e32 v222, 1
	v_mov_b32_e32 v173, v233
	v_mov_b32_e32 v172, 0x358637bd
	s_cselect_b32 s2, s95, s4
	s_cselect_b32 s3, s96, s5
	s_addk_i32 s4, 0x80
	s_addk_i32 s5, 0x100
	s_mov_b32 s61, 0
	s_waitcnt vmcnt(0)
	v_add_u32_e32 v136, 0x10000, v180
	v_add_u32_e32 v156, 0x14000, v180
	ds_read_b128 v[120:123], v136
	ds_read_b128 v[124:127], v136 offset:1024
	ds_read_b128 v[132:135], v136 offset:2048
	ds_read_b128 v[136:139], v136 offset:3072
	ds_read_b128 v[144:147], v156
	ds_read_b128 v[148:151], v156 offset:1024
	ds_read_b128 v[152:155], v156 offset:2048
	ds_read_b128 v[156:159], v156 offset:3072
	s_add_i32 s14, s4, 0x80
	s_cmp_eq_u32 s84, s61
	s_cselect_b32 s62, s2, s14
	s_cselect_b32 s55, s3, s5
	s_or_b32 s54, s62, 0x80
	s_add_i32 s14, s42, s4
	s_mov_b32 m0, s85
	ds_read_b128 v[160:163], v181
	ds_read_b128 v[164:167], v181 offset:1024
	ds_read_b128 v[182:185], v181 offset:2048
	ds_read_b128 v[186:189], v181 offset:3072
	ds_read_b128 v[194:197], v181 offset:4096
	ds_read_b128 v[198:201], v181 offset:5120
	ds_read_b128 v[202:205], v181 offset:6144
	ds_read_b128 v[206:209], v181 offset:7168
	buffer_load_dwordx4 v174, s[36:39], s14 offen lds
	s_mov_b32 m0, s8
	s_nop 0
	buffer_load_dwordx4 v176, s[36:39], s14 offen lds
	s_waitcnt vmcnt(8)
	s_waitcnt lgkmcnt(0)
	s_barrier
	s_setprio 1
	v_mfma_f32_16x16x128_f8f6f4 v[140:143], v[120:127], v[160:167], 0
	v_mfma_f32_16x16x128_f8f6f4 v[128:131], v[132:139], v[160:167], 0
	v_mfma_f32_16x16x128_f8f6f4 v[108:111], v[120:127], v[182:189], 0
	v_mfma_f32_16x16x128_f8f6f4 v[104:107], v[132:139], v[182:189], 0
	v_mfma_f32_16x16x128_f8f6f4 v[168:171], v[120:127], v[194:201], 0
	v_mfma_f32_16x16x128_f8f6f4 v[190:193], v[132:139], v[194:201], 0
	v_mfma_f32_16x16x128_f8f6f4 v[210:213], v[120:127], v[202:209], 0
	v_mfma_f32_16x16x128_f8f6f4 v[214:217], v[132:139], v[202:209], 0
	v_mfma_f32_16x16x128_f8f6f4 v[116:119], v[144:151], v[160:167], 0
	v_mfma_f32_16x16x128_f8f6f4 v[112:115], v[152:159], v[160:167], 0
	v_mfma_f32_16x16x128_f8f6f4 v[100:103], v[144:151], v[182:189], 0
	v_mfma_f32_16x16x128_f8f6f4 v[96:99], v[152:159], v[182:189], 0
	v_mfma_f32_16x16x128_f8f6f4 v[160:163], v[144:151], v[194:201], 0
	v_mfma_f32_16x16x128_f8f6f4 v[164:167], v[152:159], v[194:201], 0
	v_mfma_f32_16x16x128_f8f6f4 v[182:185], v[144:151], v[202:209], 0
	v_mfma_f32_16x16x128_f8f6f4 v[186:189], v[152:159], v[202:209], 0
	s_setprio 0
	s_barrier
	s_mov_b32 m0, s44
	s_mov_b32 s14, s38
	s_mov_b32 s15, s39
	s_nop 1
	buffer_load_dwordx4 v175, s[12:15], s55 offen lds
	s_mov_b32 m0, s45
	ds_read_b128 v[64:67], v181 offset:16384
	s_add_i32 s63, s55, s42
	buffer_load_dwordx4 v177, s[12:15], s55 offen lds
	s_mov_b32 m0, s43
	ds_read_b128 v[68:71], v181 offset:17408
	buffer_load_dwordx4 v174, s[36:39], s62 offen lds
	s_mov_b32 m0, s48
	ds_read_b128 v[72:75], v181 offset:18432
	buffer_load_dwordx4 v176, s[36:39], s62 offen lds
	ds_read_b128 v[76:79], v181 offset:19456
	ds_read_b128 v[80:83], v181 offset:20480
	ds_read_b128 v[84:87], v181 offset:21504
	ds_read_b128 v[88:91], v181 offset:22528
	ds_read_b128 v[92:95], v181 offset:23552
	s_waitcnt vmcnt(6)
	s_waitcnt lgkmcnt(0)
	s_barrier
	s_setprio 1
	v_mfma_f32_16x16x128_f8f6f4 v[60:63], v[120:127], v[64:71], 0
	v_mfma_f32_16x16x128_f8f6f4 v[56:59], v[132:139], v[64:71], 0
	v_mfma_f32_16x16x128_f8f6f4 v[194:197], v[120:127], v[72:79], 0
	v_mfma_f32_16x16x128_f8f6f4 v[198:201], v[132:139], v[72:79], 0
	v_mfma_f32_16x16x128_f8f6f4 v[202:205], v[120:127], v[80:87], 0
	v_mfma_f32_16x16x128_f8f6f4 v[206:209], v[132:139], v[80:87], 0
	v_mfma_f32_16x16x128_f8f6f4 v[218:221], v[120:127], v[88:95], 0
	v_mfma_f32_16x16x128_f8f6f4 v[226:229], v[132:139], v[88:95], 0
	v_mfma_f32_16x16x128_f8f6f4 v[52:55], v[144:151], v[64:71], 0
	v_mfma_f32_16x16x128_f8f6f4 v[48:51], v[152:159], v[64:71], 0
	v_mfma_f32_16x16x128_f8f6f4 v[230:233], v[144:151], v[72:79], 0
	v_mfma_f32_16x16x128_f8f6f4 v[234:237], v[152:159], v[72:79], 0
	v_mfma_f32_16x16x128_f8f6f4 v[238:241], v[144:151], v[80:87], 0
	v_mfma_f32_16x16x128_f8f6f4 v[242:245], v[152:159], v[80:87], 0
	v_mfma_f32_16x16x128_f8f6f4 v[246:249], v[144:151], v[88:95], 0
	v_mfma_f32_16x16x128_f8f6f4 v[250:253], v[152:159], v[88:95], 0
	s_setprio 0
	s_barrier
	s_mov_b32 m0, s46
	s_nop 0
	buffer_load_dwordx4 v175, s[12:15], s63 offen lds
	s_mov_b32 m0, s47
	s_nop 0
	buffer_load_dwordx4 v177, s[12:15], s63 offen lds
	v_add_u32_e32 v8, 0x18000, v180
	s_nop 3
	ds_read_b128 v[0:3], v8
	ds_read_b128 v[4:7], v8 offset:1024
	ds_read_b128 v[16:19], v8 offset:2048
	ds_read_b128 v[20:23], v8 offset:3072
	v_add_u32_e32 v8, 0x1c000, v180
	ds_read_b128 v[120:123], v8
	ds_read_b128 v[124:127], v8 offset:1024
	ds_read_b128 v[132:135], v8 offset:2048
	ds_read_b128 v[136:139], v8 offset:3072
	s_add_i32 s62, s62, s42
	s_mov_b32 m0, s52
	ds_read_b128 v[8:11], v181 offset:32768
	ds_read_b128 v[12:15], v181 offset:33792
	ds_read_b128 v[24:27], v181 offset:34816
	ds_read_b128 v[28:31], v181 offset:35840
	ds_read_b128 v[32:35], v181 offset:36864
	ds_read_b128 v[36:39], v181 offset:37888
	ds_read_b128 v[40:43], v181 offset:38912
	ds_read_b128 v[44:47], v181 offset:39936
	buffer_load_dwordx4 v174, s[36:39], s62 offen lds
	s_mov_b32 m0, s53
	s_nop 0
	buffer_load_dwordx4 v176, s[36:39], s62 offen lds
	s_waitcnt vmcnt(8)
	s_waitcnt lgkmcnt(0)
	s_barrier
; #define PG8_STAGE(bufoff, rs_, soff_, voff) do { _Pragma("unroll") for (int _i = 0; _i < 2; ++_i) \
;         __builtin_amdgcn_raw_ptr_buffer_load_lds(rs_, (LAS void*)(lds + (bufoff) + ldsw + _i * 8192), 16, (int)(voff)[_i], (int)(soff_), 0, 0); } while (0)
; #define PG8_LDA(dst, b, h) do { _Pragma("unroll") for (int m = 0; m < 4; ++m) dst[m] = PG8_LD2(lds + PG8_SA(b, h) + aoff + m * 2048); } while (0)
; #define PG8_LDB(dst, b, h) do { _Pragma("unroll") for (int n = 0; n < 2; ++n) dst[n] = PG8_LD2(lds + PG8_SB(b, h) + boff + n * 2048); } while (0)
; #define PG8_WAIT_V(n) asm volatile("s_waitcnt vmcnt(" #n ")" ::: "memory")
; #define PG8_WAIT_L(n) asm volatile("s_waitcnt lgkmcnt(" #n ")" ::: "memory")
; #define PG8_BAR __builtin_amdgcn_s_barrier()
; #define PG8_SCHED __builtin_amdgcn_sched_barrier(0)
; template <class Epi, class Sched, bool ALIGN_EPI = false, bool SP2 = false, bool FP8 = false>
; __device__ __forceinline__ void gemm_phase(LAS unsigned char* lds, const Gemm g, const Sched& S, const Epi& E, int wbase) {
;     ...
;         for (int t = 0; t < nt; t += 2) {
;             const bool last = (t == nt - 2);
;             const unsigned a1 = cA + (unsigned)(t + 1) * kstep;
;     ...
;             PG8_WAIT_V(8); PG8_WAIT_L(0); PG8_BAR; PG8_MMA(1, 0, At, B0); PG8_MMA(1, 1, At, B1); PG8_BAR; PG8_SCHED;
;             PG8_LDB(B0, 1, 0); PG8_LDB(B1, 1, 1); PG8_SCHED; PG8_LDA(At, 1, 0); PG8_STAGE(PG8_SA(0, 1), rA2, a2 + hstep, voffA);
;             PG8_WAIT_V(8); PG8_WAIT_L(0); PG8_BAR; PG8_MMA(0, 0, At, B0); PG8_MMA(0, 1, At, B1); PG8_BAR; PG8_SCHED;
;             PG8_LDA(At, 1, 1); PG8_STAGE(PG8_SB(1, 0), rB2, b3, voffB); PG8_STAGE(PG8_SB(1, 1), rB2, b3 + hstep, voffB); PG8_STAGE(PG8_SA(1, 0), rA2, a3, voffA);
;             PG8_WAIT_V(8); PG8_WAIT_L(0); PG8_BAR; PG8_MMA(1, 0, At, B0); PG8_MMA(1, 1, At, B1); PG8_BAR; PG8_SCHED;
	s_setprio 1
	v_mfma_f32_16x16x128_f8f6f4 v[140:143], v[0:7], v[8:15], v[140:143]
	v_mfma_f32_16x16x128_f8f6f4 v[128:131], v[16:23], v[8:15], v[128:131]
	v_mfma_f32_16x16x128_f8f6f4 v[108:111], v[0:7], v[24:31], v[108:111]
	v_mfma_f32_16x16x128_f8f6f4 v[104:107], v[16:23], v[24:31], v[104:107]
	v_mfma_f32_16x16x128_f8f6f4 v[92:95], v[0:7], v[32:39], v[168:171]
	v_mfma_f32_16x16x128_f8f6f4 v[88:91], v[16:23], v[32:39], v[190:193]
	v_mfma_f32_16x16x128_f8f6f4 v[76:79], v[0:7], v[40:47], v[210:213]
	v_mfma_f32_16x16x128_f8f6f4 v[72:75], v[16:23], v[40:47], v[214:217]
	v_mfma_f32_16x16x128_f8f6f4 v[116:119], v[120:127], v[8:15], v[116:119]
	v_mfma_f32_16x16x128_f8f6f4 v[112:115], v[132:139], v[8:15], v[112:115]
	v_mfma_f32_16x16x128_f8f6f4 v[100:103], v[120:127], v[24:31], v[100:103]
	v_mfma_f32_16x16x128_f8f6f4 v[96:99], v[132:139], v[24:31], v[96:99]
	v_mfma_f32_16x16x128_f8f6f4 v[84:87], v[120:127], v[32:39], v[160:163]
	v_mfma_f32_16x16x128_f8f6f4 v[80:83], v[132:139], v[32:39], v[164:167]
	v_mfma_f32_16x16x128_f8f6f4 v[68:71], v[120:127], v[40:47], v[182:185]
	v_mfma_f32_16x16x128_f8f6f4 v[64:67], v[132:139], v[40:47], v[186:189]
	s_setprio 0
	s_barrier
	s_mov_b32 m0, s56
	s_bitset1_b32 s55, 7
	buffer_load_dwordx4 v175, s[12:15], s55 offen lds
	s_mov_b32 m0, s57
	ds_read_b128 v[32:35], v181 offset:49152
	buffer_load_dwordx4 v177, s[12:15], s55 offen lds
	s_add_i32 s55, s55, s42
	s_mov_b32 m0, s65
	ds_read_b128 v[36:39], v181 offset:50176
	buffer_load_dwordx4 v175, s[12:15], s55 offen lds
	s_mov_b32 m0, s76
	ds_read_b128 v[144:147], v181 offset:51200
	buffer_load_dwordx4 v177, s[12:15], s55 offen lds
	s_mov_b32 m0, s58
	ds_read_b128 v[148:151], v181 offset:52224
	buffer_load_dwordx4 v174, s[36:39], s54 offen lds
	s_mov_b32 m0, s59
	ds_read_b128 v[152:155], v181 offset:53248
	buffer_load_dwordx4 v176, s[36:39], s54 offen lds
	ds_read_b128 v[156:159], v181 offset:54272
	ds_read_b128 v[160:163], v181 offset:55296
	ds_read_b128 v[164:167], v181 offset:56320
	s_waitcnt vmcnt(8)
	s_waitcnt lgkmcnt(0)
	s_barrier
	s_setprio 1
	v_mfma_f32_16x16x128_f8f6f4 v[60:63], v[0:7], v[32:39], v[60:63]
	v_mfma_f32_16x16x128_f8f6f4 v[56:59], v[16:23], v[32:39], v[56:59]
	v_mfma_f32_16x16x128_f8f6f4 v[44:47], v[0:7], v[144:151], v[194:197]
	v_mfma_f32_16x16x128_f8f6f4 v[40:43], v[16:23], v[144:151], v[198:201]
	v_mfma_f32_16x16x128_f8f6f4 v[28:31], v[0:7], v[152:159], v[202:205]
	v_mfma_f32_16x16x128_f8f6f4 v[24:27], v[16:23], v[152:159], v[206:209]
	v_mfma_f32_16x16x128_f8f6f4 v[12:15], v[0:7], v[160:167], v[218:221]
	v_mfma_f32_16x16x128_f8f6f4 v[8:11], v[16:23], v[160:167], v[226:229]
	v_mfma_f32_16x16x128_f8f6f4 v[52:55], v[120:127], v[32:39], v[52:55]
	v_mfma_f32_16x16x128_f8f6f4 v[48:51], v[132:139], v[32:39], v[48:51]
	v_mfma_f32_16x16x128_f8f6f4 v[36:39], v[120:127], v[144:151], v[230:233]
	v_mfma_f32_16x16x128_f8f6f4 v[32:35], v[132:139], v[144:151], v[234:237]
	v_mfma_f32_16x16x128_f8f6f4 v[20:23], v[120:127], v[152:159], v[238:241]
	v_mfma_f32_16x16x128_f8f6f4 v[16:19], v[132:139], v[152:159], v[242:245]
	v_mfma_f32_16x16x128_f8f6f4 v[4:7], v[120:127], v[160:167], v[246:249]
	v_mfma_f32_16x16x128_f8f6f4 v[0:3], v[132:139], v[160:167], v[250:253]
	s_setprio 0
	s_barrier
	s_add_i32 s61, s61, 2
	s_addk_i32 s4, 0x100
	s_addk_i32 s5, 0x100
	s_cmp_ge_i32 s61, s82
	s_cbranch_scc0 .LBB0_1990
	s_branch .Lzp_after_1990
.LBB0_1990:
	v_add_u32_e32 v136, 0x10000, v180
	v_add_u32_e32 v156, 0x14000, v180
	ds_read_b128 v[120:123], v136
	ds_read_b128 v[124:127], v136 offset:1024
	ds_read_b128 v[132:135], v136 offset:2048
	ds_read_b128 v[136:139], v136 offset:3072
	ds_read_b128 v[144:147], v156
	ds_read_b128 v[148:151], v156 offset:1024
	ds_read_b128 v[152:155], v156 offset:2048
	ds_read_b128 v[156:159], v156 offset:3072
	s_add_i32 s14, s4, 0x80
	s_cmp_eq_u32 s84, s61
	s_cselect_b32 s62, s2, s14
	s_cselect_b32 s55, s3, s5
	s_or_b32 s54, s62, 0x80
	s_add_i32 s14, s42, s4
	s_mov_b32 m0, s85
	ds_read_b128 v[160:163], v181
	ds_read_b128 v[164:167], v181 offset:1024
	ds_read_b128 v[182:185], v181 offset:2048
	ds_read_b128 v[186:189], v181 offset:3072
	ds_read_b128 v[194:197], v181 offset:4096
	ds_read_b128 v[198:201], v181 offset:5120
	ds_read_b128 v[202:205], v181 offset:6144
	ds_read_b128 v[206:209], v181 offset:7168
	buffer_load_dwordx4 v174, s[36:39], s14 offen lds
	s_mov_b32 m0, s8
	s_nop 0
	buffer_load_dwordx4 v176, s[36:39], s14 offen lds
	s_waitcnt vmcnt(8)
	s_waitcnt lgkmcnt(0)
	s_barrier
	s_setprio 1
	v_mfma_f32_16x16x128_f8f6f4 v[140:143], v[120:127], v[160:167], v[140:143]
	v_mfma_f32_16x16x128_f8f6f4 v[128:131], v[132:139], v[160:167], v[128:131]
	v_mfma_f32_16x16x128_f8f6f4 v[108:111], v[120:127], v[182:189], v[108:111]
	v_mfma_f32_16x16x128_f8f6f4 v[104:107], v[132:139], v[182:189], v[104:107]
	v_mfma_f32_16x16x128_f8f6f4 v[168:171], v[120:127], v[194:201], v[92:95]
	v_mfma_f32_16x16x128_f8f6f4 v[190:193], v[132:139], v[194:201], v[88:91]
	v_mfma_f32_16x16x128_f8f6f4 v[210:213], v[120:127], v[202:209], v[76:79]
	v_mfma_f32_16x16x128_f8f6f4 v[214:217], v[132:139], v[202:209], v[72:75]
	v_mfma_f32_16x16x128_f8f6f4 v[116:119], v[144:151], v[160:167], v[116:119]
	v_mfma_f32_16x16x128_f8f6f4 v[112:115], v[152:159], v[160:167], v[112:115]
	v_mfma_f32_16x16x128_f8f6f4 v[100:103], v[144:151], v[182:189], v[100:103]
	v_mfma_f32_16x16x128_f8f6f4 v[96:99], v[152:159], v[182:189], v[96:99]
	v_mfma_f32_16x16x128_f8f6f4 v[160:163], v[144:151], v[194:201], v[84:87]
	v_mfma_f32_16x16x128_f8f6f4 v[164:167], v[152:159], v[194:201], v[80:83]
	v_mfma_f32_16x16x128_f8f6f4 v[182:185], v[144:151], v[202:209], v[68:71]
	v_mfma_f32_16x16x128_f8f6f4 v[186:189], v[152:159], v[202:209], v[64:67]
	s_setprio 0
	s_barrier
; #define PG8_STAGE(bufoff, rs_, soff_, voff) do { _Pragma("unroll") for (int _i = 0; _i < 2; ++_i) \
;         __builtin_amdgcn_raw_ptr_buffer_load_lds(rs_, (LAS void*)(lds + (bufoff) + ldsw + _i * 8192), 16, (int)(voff)[_i], (int)(soff_), 0, 0); } while (0)
; #define PG8_LDA(dst, b, h) do { _Pragma("unroll") for (int m = 0; m < 4; ++m) dst[m] = PG8_LD2(lds + PG8_SA(b, h) + aoff + m * 2048); } while (0)
; #define PG8_LDB(dst, b, h) do { _Pragma("unroll") for (int n = 0; n < 2; ++n) dst[n] = PG8_LD2(lds + PG8_SB(b, h) + boff + n * 2048); } while (0)
; #define PG8_WAIT_V(n) asm volatile("s_waitcnt vmcnt(" #n ")" ::: "memory")
; #define PG8_WAIT_L(n) asm volatile("s_waitcnt lgkmcnt(" #n ")" ::: "memory")
; #define PG8_BAR __builtin_amdgcn_s_barrier()
; #define PG8_SCHED __builtin_amdgcn_sched_barrier(0)
; template <class Epi, class Sched, bool ALIGN_EPI = false, bool SP2 = false, bool FP8 = false>
; __device__ __forceinline__ void gemm_phase(LAS unsigned char* lds, const Gemm g, const Sched& S, const Epi& E, int wbase) {
;     ...
;         for (int t = 0; t < nt; t += 2) {
;             const bool last = (t == nt - 2);
;             const unsigned a1 = cA + (unsigned)(t + 1) * kstep;
;     ...
;             PG8_LDA(At, 0, 1); PG8_STAGE(PG8_SB(0, 0), rB2, b2, voffB); PG8_STAGE(PG8_SB(0, 1), rB2, b2 + hstep, voffB); PG8_STAGE(PG8_SA(0, 0), rA2, a2, voffA);
;             PG8_WAIT_V(8); PG8_WAIT_L(0); PG8_BAR; PG8_MMA(1, 0, At, B0); PG8_MMA(1, 1, At, B1); PG8_BAR; PG8_SCHED;
;             PG8_LDB(B0, 1, 0); PG8_LDB(B1, 1, 1); PG8_SCHED; PG8_LDA(At, 1, 0); PG8_STAGE(PG8_SA(0, 1), rA2, a2 + hstep, voffA);
;             PG8_WAIT_V(8); PG8_WAIT_L(0); PG8_BAR; PG8_MMA(0, 0, At, B0); PG8_MMA(0, 1, At, B1); PG8_BAR; PG8_SCHED;
;             PG8_LDA(At, 1, 1); PG8_STAGE(PG8_SB(1, 0), rB2, b3, voffB); PG8_STAGE(PG8_SB(1, 1), rB2, b3 + hstep, voffB); PG8_STAGE(PG8_SA(1, 0), rA2, a3, voffA);
;             PG8_WAIT_V(8); PG8_WAIT_L(0); PG8_BAR; PG8_MMA(1, 0, At, B0); PG8_MMA(1, 1, At, B1); PG8_BAR; PG8_SCHED;
	s_mov_b32 m0, s44
	s_mov_b32 s14, s38
	s_mov_b32 s15, s39
	s_nop 1
	buffer_load_dwordx4 v175, s[12:15], s55 offen lds
	s_mov_b32 m0, s45
	ds_read_b128 v[64:67], v181 offset:16384
	s_add_i32 s63, s55, s42
	buffer_load_dwordx4 v177, s[12:15], s55 offen lds
	s_mov_b32 m0, s43
	ds_read_b128 v[68:71], v181 offset:17408
	buffer_load_dwordx4 v174, s[36:39], s62 offen lds
	s_mov_b32 m0, s48
	ds_read_b128 v[72:75], v181 offset:18432
	buffer_load_dwordx4 v176, s[36:39], s62 offen lds
	ds_read_b128 v[76:79], v181 offset:19456
	ds_read_b128 v[80:83], v181 offset:20480
	ds_read_b128 v[84:87], v181 offset:21504
	ds_read_b128 v[88:91], v181 offset:22528
	ds_read_b128 v[92:95], v181 offset:23552
	s_waitcnt vmcnt(6)
	s_waitcnt lgkmcnt(0)
	s_barrier
	s_setprio 1
	v_mfma_f32_16x16x128_f8f6f4 v[60:63], v[120:127], v[64:71], v[60:63]
	v_mfma_f32_16x16x128_f8f6f4 v[56:59], v[132:139], v[64:71], v[56:59]
	v_mfma_f32_16x16x128_f8f6f4 v[194:197], v[120:127], v[72:79], v[44:47]
	v_mfma_f32_16x16x128_f8f6f4 v[198:201], v[132:139], v[72:79], v[40:43]
	v_mfma_f32_16x16x128_f8f6f4 v[202:205], v[120:127], v[80:87], v[28:31]
	v_mfma_f32_16x16x128_f8f6f4 v[206:209], v[132:139], v[80:87], v[24:27]
	v_mfma_f32_16x16x128_f8f6f4 v[218:221], v[120:127], v[88:95], v[12:15]
	v_mfma_f32_16x16x128_f8f6f4 v[226:229], v[132:139], v[88:95], v[8:11]
	v_mfma_f32_16x16x128_f8f6f4 v[52:55], v[144:151], v[64:71], v[52:55]
	v_mfma_f32_16x16x128_f8f6f4 v[48:51], v[152:159], v[64:71], v[48:51]
	v_mfma_f32_16x16x128_f8f6f4 v[230:233], v[144:151], v[72:79], v[36:39]
	v_mfma_f32_16x16x128_f8f6f4 v[234:237], v[152:159], v[72:79], v[32:35]
	v_mfma_f32_16x16x128_f8f6f4 v[238:241], v[144:151], v[80:87], v[20:23]
	v_mfma_f32_16x16x128_f8f6f4 v[242:245], v[152:159], v[80:87], v[16:19]
	v_mfma_f32_16x16x128_f8f6f4 v[246:249], v[144:151], v[88:95], v[4:7]
	v_mfma_f32_16x16x128_f8f6f4 v[250:253], v[152:159], v[88:95], v[0:3]
	s_setprio 0
	s_barrier
	s_mov_b32 m0, s46
	s_nop 0
	buffer_load_dwordx4 v175, s[12:15], s63 offen lds
	s_mov_b32 m0, s47
	s_nop 0
	buffer_load_dwordx4 v177, s[12:15], s63 offen lds
	v_add_u32_e32 v8, 0x18000, v180
	s_nop 3
	ds_read_b128 v[0:3], v8
	ds_read_b128 v[4:7], v8 offset:1024
	ds_read_b128 v[16:19], v8 offset:2048
	ds_read_b128 v[20:23], v8 offset:3072
	v_add_u32_e32 v8, 0x1c000, v180
	ds_read_b128 v[120:123], v8
	ds_read_b128 v[124:127], v8 offset:1024
	ds_read_b128 v[132:135], v8 offset:2048
	ds_read_b128 v[136:139], v8 offset:3072
	s_add_i32 s62, s62, s42
	s_mov_b32 m0, s52
	ds_read_b128 v[8:11], v181 offset:32768
	ds_read_b128 v[12:15], v181 offset:33792
	ds_read_b128 v[24:27], v181 offset:34816
	ds_read_b128 v[28:31], v181 offset:35840
	ds_read_b128 v[32:35], v181 offset:36864
	ds_read_b128 v[36:39], v181 offset:37888
	ds_read_b128 v[40:43], v181 offset:38912
	ds_read_b128 v[44:47], v181 offset:39936
	buffer_load_dwordx4 v174, s[36:39], s62 offen lds
	s_mov_b32 m0, s53
	s_nop 0
	buffer_load_dwordx4 v176, s[36:39], s62 offen lds
	s_waitcnt vmcnt(8)
	s_waitcnt lgkmcnt(0)
	s_barrier
	s_setprio 1
	v_mfma_f32_16x16x128_f8f6f4 v[140:143], v[0:7], v[8:15], v[140:143]
	v_mfma_f32_16x16x128_f8f6f4 v[128:131], v[16:23], v[8:15], v[128:131]
	v_mfma_f32_16x16x128_f8f6f4 v[108:111], v[0:7], v[24:31], v[108:111]
	v_mfma_f32_16x16x128_f8f6f4 v[104:107], v[16:23], v[24:31], v[104:107]
	v_mfma_f32_16x16x128_f8f6f4 v[92:95], v[0:7], v[32:39], v[168:171]
	v_mfma_f32_16x16x128_f8f6f4 v[88:91], v[16:23], v[32:39], v[190:193]
	v_mfma_f32_16x16x128_f8f6f4 v[76:79], v[0:7], v[40:47], v[210:213]
	v_mfma_f32_16x16x128_f8f6f4 v[72:75], v[16:23], v[40:47], v[214:217]
	v_mfma_f32_16x16x128_f8f6f4 v[116:119], v[120:127], v[8:15], v[116:119]
	v_mfma_f32_16x16x128_f8f6f4 v[112:115], v[132:139], v[8:15], v[112:115]
	v_mfma_f32_16x16x128_f8f6f4 v[100:103], v[120:127], v[24:31], v[100:103]
	v_mfma_f32_16x16x128_f8f6f4 v[96:99], v[132:139], v[24:31], v[96:99]
	v_mfma_f32_16x16x128_f8f6f4 v[84:87], v[120:127], v[32:39], v[160:163]
	v_mfma_f32_16x16x128_f8f6f4 v[80:83], v[132:139], v[32:39], v[164:167]
	v_mfma_f32_16x16x128_f8f6f4 v[68:71], v[120:127], v[40:47], v[182:185]
	v_mfma_f32_16x16x128_f8f6f4 v[64:67], v[132:139], v[40:47], v[186:189]
	s_setprio 0
	s_barrier
	s_mov_b32 m0, s56
	s_bitset1_b32 s55, 7
	buffer_load_dwordx4 v175, s[12:15], s55 offen lds
	s_mov_b32 m0, s57
	ds_read_b128 v[32:35], v181 offset:49152
	buffer_load_dwordx4 v177, s[12:15], s55 offen lds
	s_add_i32 s55, s55, s42
	s_mov_b32 m0, s65
	ds_read_b128 v[36:39], v181 offset:50176
	buffer_load_dwordx4 v175, s[12:15], s55 offen lds
	s_mov_b32 m0, s76
	ds_read_b128 v[144:147], v181 offset:51200
	buffer_load_dwordx4 v177, s[12:15], s55 offen lds
	s_mov_b32 m0, s58
	ds_read_b128 v[148:151], v181 offset:52224
	buffer_load_dwordx4 v174, s[36:39], s54 offen lds
	s_mov_b32 m0, s59
	ds_read_b128 v[152:155], v181 offset:53248
	buffer_load_dwordx4 v176, s[36:39], s54 offen lds
	ds_read_b128 v[156:159], v181 offset:54272
	ds_read_b128 v[160:163], v181 offset:55296
	ds_read_b128 v[164:167], v181 offset:56320
	s_waitcnt vmcnt(8)
	s_waitcnt lgkmcnt(0)
	s_barrier
	s_setprio 1
	v_mfma_f32_16x16x128_f8f6f4 v[60:63], v[0:7], v[32:39], v[60:63]
	v_mfma_f32_16x16x128_f8f6f4 v[56:59], v[16:23], v[32:39], v[56:59]
	v_mfma_f32_16x16x128_f8f6f4 v[44:47], v[0:7], v[144:151], v[194:197]
	v_mfma_f32_16x16x128_f8f6f4 v[40:43], v[16:23], v[144:151], v[198:201]
	v_mfma_f32_16x16x128_f8f6f4 v[28:31], v[0:7], v[152:159], v[202:205]
	v_mfma_f32_16x16x128_f8f6f4 v[24:27], v[16:23], v[152:159], v[206:209]
	v_mfma_f32_16x16x128_f8f6f4 v[12:15], v[0:7], v[160:167], v[218:221]
	v_mfma_f32_16x16x128_f8f6f4 v[8:11], v[16:23], v[160:167], v[226:229]
	v_mfma_f32_16x16x128_f8f6f4 v[52:55], v[120:127], v[32:39], v[52:55]
	v_mfma_f32_16x16x128_f8f6f4 v[48:51], v[132:139], v[32:39], v[48:51]
	v_mfma_f32_16x16x128_f8f6f4 v[36:39], v[120:127], v[144:151], v[230:233]
	v_mfma_f32_16x16x128_f8f6f4 v[32:35], v[132:139], v[144:151], v[234:237]
	v_mfma_f32_16x16x128_f8f6f4 v[20:23], v[120:127], v[152:159], v[238:241]
	v_mfma_f32_16x16x128_f8f6f4 v[16:19], v[132:139], v[152:159], v[242:245]
	v_mfma_f32_16x16x128_f8f6f4 v[4:7], v[120:127], v[160:167], v[246:249]
	v_mfma_f32_16x16x128_f8f6f4 v[0:3], v[132:139], v[160:167], v[250:253]
	s_setprio 0
	s_barrier
	s_add_i32 s61, s61, 2
	s_addk_i32 s4, 0x100
	s_addk_i32 s5, 0x100
	s_cmp_ge_i32 s61, s82
	s_cbranch_scc0 .LBB0_1990
